# attention: K d-step-1 and V fragments prefetched into two spare 8-VGPR buffers (counted lgkmcnt), dead fp8-pack seed moves removed
# speedup vs baseline: 1.0072x; 1.0014x over previous
; #define LAS __attribute__((address_space(3)))
; #define LDS_WAIT() asm volatile("s_waitcnt lgkmcnt(0)" ::: "memory")
; __device__ __forceinline__ unsigned cvt_pk4_fp8(float a, float b, float c, float d) { int w; asm("" : "=v"(w));     w = __builtin_amdgcn_cvt_pk_fp8_f32(a, b, w, false); w = __builtin_amdgcn_cvt_pk_fp8_f32(c, d, w, true); return (unsigned)w; }
; __device__ __forceinline__ void transpose_item_fp8(const float* W, int N, int k0, int n0, unsigned char* WT, int ldk, int dst_row0, LAS float* scr, int lane, const float* kgain) {
;     float v[64];
; #pragma unroll
;     for (int i = 0; i < 64; ++i) v[i] = W[(size_t)(k0 + 2 * i + (lane >> 5)) * N + n0 + (lane & 31)];
; #pragma unroll
;     for (int i = 0; i < 64; ++i) { const int kk = 2 * i + (lane >> 5); scr[kk * 32 + ((lane & 31) ^ ((kk >> 4) << 2))] = v[i] * W8_SCALE; }
;     LDS_WAIT(); asm volatile("" ::: "memory");
;     const int c = lane & 7;
;     f32x4 g[4];
; #pragma unroll
;     for (int q = 0; q < 4; ++q) g[q] = kgain ? *(const f32x4*)(kgain + k0 + 16 * c + 4 * q) : (f32x4){1.f, 1.f, 1.f, 1.f};
; #pragma unroll
;     for (int j = 0; j < 4; ++j) { const int n = (lane >> 3) + 8 * j; const LAS float* s = scr + (16 * c) * 32 + (n ^ (c << 2));
;         u32x4 o; o.x = cvt_pk4_fp8(s[0 * 32] * g[0][0], s[1 * 32] * g[0][1], s[2 * 32] * g[0][2], s[3 * 32] * g[0][3]); o.y = cvt_pk4_fp8(s[4 * 32] * g[1][0], s[5 * 32] * g[1][1], s[6 * 32] * g[1][2], s[7 * 32] * g[1][3]);
;         o.z = cvt_pk4_fp8(s[8 * 32] * g[2][0], s[9 * 32] * g[2][1], s[10 * 32] * g[2][2], s[11 * 32] * g[2][3]); o.w = cvt_pk4_fp8(s[12 * 32] * g[3][0], s[13 * 32] * g[3][1], s[14 * 32] * g[3][2], s[15 * 32] * g[3][3]);
;         *(u32x4*)(WT + (size_t)(dst_row0 + n) * ldk + k0 + 16 * c) = o; }
;     LDS_WAIT(); asm volatile("" ::: "memory");
.LBB0_12:
	ds_read2_b32 v[16:17], v201 offset1:32
	ds_read2_b32 v[34:35], v201 offset0:64 offset1:96
	s_add_u32 s4, s3, s24
	s_waitcnt vmcnt(0) lgkmcnt(1)
	v_mul_f32_e32 v16, v4, v16
	v_mul_f32_e32 v17, v5, v17
	v_cvt_pk_fp8_f32 v32, v16, v17
	ds_read2_b32 v[16:17], v201 offset0:128 offset1:160
	s_waitcnt lgkmcnt(1)
	v_mul_f32_e32 v18, v6, v34
	v_mul_f32_e32 v24, v7, v35
	v_cvt_pk_fp8_f32 v32, v18, v24 op_sel:[0,0,1]
	s_waitcnt lgkmcnt(0)
	v_mul_f32_e32 v18, v0, v16
	v_mul_f32_e32 v24, v1, v17
	ds_read2_b32 v[16:17], v201 offset0:192 offset1:224
	v_cvt_pk_fp8_f32 v33, v18, v24
	v_add_u32_e32 v18, 0x400, v201
	ds_read2_b32 v[34:35], v18 offset1:32
	ds_read2_b32 v[36:37], v18 offset0:128 offset1:160
	s_waitcnt lgkmcnt(2)
	v_mul_f32_e32 v24, v2, v16
	v_mul_f32_e32 v29, v3, v17
	ds_read2_b32 v[16:17], v18 offset0:64 offset1:96
	v_cvt_pk_fp8_f32 v33, v24, v29 op_sel:[0,0,1]
	s_waitcnt lgkmcnt(2)
	v_mul_f32_e32 v24, v12, v34
	v_mul_f32_e32 v29, v13, v35
	s_waitcnt lgkmcnt(0)
	v_mul_f32_e32 v38, v14, v16
	v_mul_f32_e32 v39, v15, v17
	ds_read2_b32 v[16:17], v18 offset0:192 offset1:224
	v_cvt_pk_fp8_f32 v34, v24, v29
	v_mul_f32_e32 v24, v8, v36
	v_mul_f32_e32 v18, v9, v37
	v_cvt_pk_fp8_f32 v35, v24, v18
	s_waitcnt lgkmcnt(0)
	v_mul_f32_e32 v16, v10, v16
	v_mul_f32_e32 v17, v11, v17
	s_addc_u32 s5, s1, s25
	v_cvt_pk_fp8_f32 v35, v16, v17 op_sel:[0,0,1]
	v_ashrrev_i32_e32 v16, 31, v208
	v_mul_lo_u32 v18, s12, v16
	ds_read2_b32 v[16:17], v202 offset1:32
	v_lshl_add_u64 v[30:31], s[4:5], 0, v[26:27]
	v_cvt_pk_fp8_f32 v34, v38, v39 op_sel:[0,0,1]
	v_mad_u64_u32 v[38:39], s[4:5], s12, v208, v[30:31]
	v_mul_lo_u32 v24, s13, v208
	v_add3_u32 v39, v24, v39, v18
	s_waitcnt lgkmcnt(0)
	v_mul_f32_e32 v18, v4, v16
	v_mul_f32_e32 v24, v5, v17
	ds_read2_b32 v[16:17], v202 offset0:64 offset1:96
	ds_read2_b32 v[40:41], v202 offset0:128 offset1:160
	v_cvt_pk_fp8_f32 v36, v18, v24
	s_waitcnt lgkmcnt(1)
	v_mul_f32_e32 v16, v6, v16
	v_mul_f32_e32 v17, v7, v17
	s_waitcnt lgkmcnt(0)
	v_mul_f32_e32 v18, v0, v40
	v_mul_f32_e32 v24, v1, v41
	v_cvt_pk_fp8_f32 v36, v16, v17 op_sel:[0,0,1]
	ds_read2_b32 v[16:17], v202 offset0:192 offset1:224
	v_cvt_pk_fp8_f32 v37, v18, v24
	v_add_u32_e32 v18, 0x400, v202
	global_store_dwordx4 v[38:39], v[32:35], off
	ds_read2_b32 v[32:33], v18 offset1:32
	s_waitcnt lgkmcnt(1)
	v_mul_f32_e32 v24, v2, v16
	v_mul_f32_e32 v29, v3, v17
	ds_read2_b32 v[16:17], v18 offset0:64 offset1:96
	v_cvt_pk_fp8_f32 v37, v24, v29 op_sel:[0,0,1]
	s_waitcnt lgkmcnt(1)
	v_mul_f32_e32 v24, v12, v32
	v_mul_f32_e32 v29, v13, v33
	ds_read2_b32 v[32:33], v18 offset0:128 offset1:160
	s_waitcnt lgkmcnt(1)
	v_mul_f32_e32 v34, v14, v16
	v_mul_f32_e32 v35, v15, v17
	ds_read2_b32 v[16:17], v18 offset0:192 offset1:224
	v_cvt_pk_fp8_f32 v38, v24, v29
	s_waitcnt lgkmcnt(1)
	v_mul_f32_e32 v24, v8, v32
	v_mul_f32_e32 v18, v9, v33
	v_cvt_pk_fp8_f32 v39, v24, v18
	s_waitcnt lgkmcnt(0)
	v_mul_f32_e32 v16, v10, v16
	v_mul_f32_e32 v17, v11, v17
	v_cvt_pk_fp8_f32 v38, v34, v35 op_sel:[0,0,1]
	v_cvt_pk_fp8_f32 v39, v16, v17 op_sel:[0,0,1]
	v_ashrrev_i32_e32 v16, 31, v207
	v_mul_lo_u32 v18, s12, v16
	ds_read2_b32 v[16:17], v203 offset1:32
	v_mad_u64_u32 v[34:35], s[4:5], s12, v207, v[30:31]
	v_mul_lo_u32 v24, s13, v207
	v_add3_u32 v35, v24, v35, v18
	s_waitcnt lgkmcnt(0)
	v_mul_f32_e32 v18, v4, v16
	v_mul_f32_e32 v24, v5, v17
	ds_read2_b32 v[16:17], v203 offset0:64 offset1:96
	v_cvt_pk_fp8_f32 v32, v18, v24
	ds_read2_b32 v[40:41], v203 offset0:128 offset1:160
	s_waitcnt lgkmcnt(1)
	v_mul_f32_e32 v16, v6, v16
	v_mul_f32_e32 v17, v7, v17
	v_cvt_pk_fp8_f32 v32, v16, v17 op_sel:[0,0,1]
	ds_read2_b32 v[16:17], v203 offset0:192 offset1:224
	s_waitcnt lgkmcnt(1)
	v_mul_f32_e32 v18, v0, v40
	v_mul_f32_e32 v24, v1, v41
	v_cvt_pk_fp8_f32 v33, v18, v24
	v_add_u32_e32 v18, 0x400, v203
	global_store_dwordx4 v[34:35], v[36:39], off
	ds_read2_b32 v[34:35], v18 offset1:32
	s_waitcnt lgkmcnt(1)
	v_mul_f32_e32 v24, v2, v16
	v_mul_f32_e32 v29, v3, v17
	ds_read2_b32 v[16:17], v18 offset0:64 offset1:96
	ds_read2_b32 v[36:37], v18 offset0:128 offset1:160
	v_cvt_pk_fp8_f32 v33, v24, v29 op_sel:[0,0,1]
	s_waitcnt lgkmcnt(2)
	v_mul_f32_e32 v24, v12, v34
	v_mul_f32_e32 v29, v13, v35
	s_waitcnt lgkmcnt(1)
	v_mul_f32_e32 v38, v14, v16
	v_mul_f32_e32 v39, v15, v17
	ds_read2_b32 v[16:17], v18 offset0:192 offset1:224
	v_cvt_pk_fp8_f32 v34, v24, v29
	s_waitcnt lgkmcnt(1)
	v_mul_f32_e32 v24, v8, v36
	v_mul_f32_e32 v18, v9, v37
	v_cvt_pk_fp8_f32 v35, v24, v18
	s_waitcnt lgkmcnt(0)
	v_mul_f32_e32 v16, v10, v16
	v_mul_f32_e32 v17, v11, v17
	v_mad_u64_u32 v[36:37], s[4:5], s12, v206, v[30:31]
	v_cvt_pk_fp8_f32 v35, v16, v17 op_sel:[0,0,1]
	v_ashrrev_i32_e32 v16, 31, v206
	v_mul_lo_u32 v18, s12, v16
	ds_read2_b32 v[16:17], v204 offset1:32
	v_mul_lo_u32 v24, s13, v206
	v_add3_u32 v37, v24, v37, v18
	v_cvt_pk_fp8_f32 v34, v38, v39 op_sel:[0,0,1]
	ds_read2_b32 v[38:39], v204 offset0:128 offset1:160
	s_waitcnt lgkmcnt(1)
	v_mul_f32_e32 v18, v4, v16
	v_mul_f32_e32 v17, v5, v17
	ds_read2_b32 v[4:5], v204 offset0:64 offset1:96
	v_cvt_pk_fp8_f32 v16, v18, v17
	v_add_u32_e32 v24, 0x400, v204
	s_waitcnt lgkmcnt(0)
	v_mul_f32_e32 v4, v6, v4
	v_mul_f32_e32 v5, v7, v5
	v_cvt_pk_fp8_f32 v16, v4, v5 op_sel:[0,0,1]
	v_mul_f32_e32 v4, v0, v38
	v_mul_f32_e32 v5, v1, v39
	ds_read2_b32 v[0:1], v204 offset0:192 offset1:224
	v_cvt_pk_fp8_f32 v17, v4, v5
	ds_read2_b32 v[4:5], v24 offset1:32
	ds_read2_b32 v[6:7], v24 offset0:64 offset1:96
	s_waitcnt lgkmcnt(2)
	v_mul_f32_e32 v0, v2, v0
	v_mul_f32_e32 v1, v3, v1
	v_cvt_pk_fp8_f32 v17, v0, v1 op_sel:[0,0,1]
	ds_read2_b32 v[0:1], v24 offset0:128 offset1:160
	s_waitcnt lgkmcnt(2)
	v_mul_f32_e32 v2, v12, v4
	v_mul_f32_e32 v3, v13, v5
	v_cvt_pk_fp8_f32 v18, v2, v3
	ds_read2_b32 v[2:3], v24 offset0:192 offset1:224
	s_waitcnt lgkmcnt(1)
	v_mul_f32_e32 v0, v8, v0
	v_mul_f32_e32 v1, v9, v1
	v_cvt_pk_fp8_f32 v19, v0, v1
	v_mul_f32_e32 v4, v14, v6
	v_mul_f32_e32 v5, v15, v7
	s_waitcnt lgkmcnt(0)
	v_mul_f32_e32 v0, v10, v2
	v_mul_f32_e32 v1, v11, v3
	v_cvt_pk_fp8_f32 v18, v4, v5 op_sel:[0,0,1]
	v_cvt_pk_fp8_f32 v19, v0, v1 op_sel:[0,0,1]
	v_ashrrev_i32_e32 v0, 31, v205
	v_mul_lo_u32 v2, s12, v0
	v_mad_u64_u32 v[0:1], s[4:5], s12, v205, v[30:31]
	v_mul_lo_u32 v3, s13, v205
	v_add3_u32 v1, v3, v1, v2
	global_store_dwordx4 v[36:37], v[32:35], off
	global_store_dwordx4 v[0:1], v[16:19], off
	s_waitcnt lgkmcnt(0)

; __device__ __forceinline__ unsigned cvt_pk_bf16(float lo, float hi) { unsigned r; asm volatile("v_cvt_pk_bf16_f32 %0, %1, %2" : "=v"(r) : "v"(lo), "v"(hi)); return r; }
; __device__ __forceinline__ unsigned cvt_pk4_fp8(float a, float b, float c, float d) { int w; asm("" : "=v"(w));     w = __builtin_amdgcn_cvt_pk_fp8_f32(a, b, w, false); w = __builtin_amdgcn_cvt_pk_fp8_f32(c, d, w, true); return (unsigned)w; }
; __global__ void __launch_bounds__(512, 2) fwd_kernel(Params p) {
;     ...
;         for (int m = gw; m < T; m += NGW) {
;             const f32x4* xr = (const f32x4*)(p.in[I_X] + (size_t)m * DM) + lane; const f32x4* gr = (const f32x4*)p.in[I_GMIX] + lane;
;             f32x4 v[8]; float s = 0.f;
; #pragma unroll
;             for (int j = 0; j < 8; ++j) { v[j] = xr[64 * j]; s += (v[j].x * v[j].x + v[j].y * v[j].y) + (v[j].z * v[j].z + v[j].w * v[j].w); }
;             const float rstd = rsqrtf(wave_sum(s) * (1.f / DM) + RMS_EPS);
;             u32x2* o8 = (u32x2*)(Hb + (size_t)m * DM) + lane; unsigned* o4 = (unsigned*)(H8 + (size_t)m * DM) + lane;
; #pragma unroll
;             for (int j = 0; j < 8; ++j) { const f32x4 g = gr[64 * j]; const f32x4 hv = v[j] * rstd * g; u32x2 w; w.x = cvt_pk_bf16(hv.x, hv.y); w.y = cvt_pk_bf16(hv.z, hv.w); o8[64 * j] = w; o4[64 * j] = cvt_pk4_fp8(hv.x, hv.y, hv.z, hv.w); }
;         }
.LBB0_46:
	v_add_co_u32_e32 v60, vcc, 0xfffff000, v30
	global_load_dwordx4 v[12:15], v[30:31], off offset:-3072
	global_load_dwordx4 v[8:11], v[30:31], off offset:-2048
	global_load_dwordx4 v[4:7], v[30:31], off offset:-1024
	v_addc_co_u32_e32 v61, vcc, -1, v31, vcc
	global_load_dwordx4 v[40:43], v[60:61], off offset:-3072
	global_load_dwordx4 v[44:47], v[60:61], off offset:-2048
	global_load_dwordx4 v[48:51], v[60:61], off offset:-1024
	global_load_dwordx4 v[52:55], v[30:31], off offset:-4096
	global_load_dwordx4 v[0:3], v[30:31], off
	global_load_dwordx4 v[56:59], v[16:17], off
	s_add_i32 s12, s12, s18
	s_cmpk_gt_i32 s12, 0x3fff
	v_lshl_add_u64 v[30:31], v[30:31], 0, s[10:11]
	s_waitcnt vmcnt(5)
	v_mov_b32_e32 v70, v41
	v_pk_mul_f32 v[60:61], v[10:11], v[10:11]
	v_pk_mul_f32 v[62:63], v[8:9], v[8:9]
	v_mul_f32_e32 v64, v5, v5
	v_mul_f32_e32 v66, v7, v7
	s_waitcnt vmcnt(1)
	v_mul_f32_e32 v81, v2, v2
	v_mul_f32_e32 v88, v3, v3
	v_pk_mov_b32 v[68:69], v[62:63], v[60:61] op_sel:[1,0]
	v_mov_b32_e32 v63, v61
	v_pk_fma_f32 v[60:61], v[4:5], v[4:5], v[64:65] op_sel_hi:[1,1,0]
	v_pk_fma_f32 v[64:65], v[6:7], v[6:7], v[66:67] op_sel_hi:[1,1,0]
	v_mov_b32_e32 v71, v45
	v_mov_b32_e32 v74, v43
	v_mov_b32_e32 v75, v47
	v_mov_b32_e32 v66, v40
	v_mov_b32_e32 v67, v44
	v_mov_b32_e32 v72, v42
	v_mov_b32_e32 v73, v46
	v_pk_mul_f32 v[76:77], v[50:51], v[50:51]
	v_pk_mul_f32 v[78:79], v[48:49], v[48:49]
	v_pk_add_f32 v[62:63], v[68:69], v[62:63]
	v_mov_b32_e32 v61, v81
	v_mov_b32_e32 v65, v88
	v_pk_mul_f32 v[68:69], v[70:71], v[70:71]
	v_pk_mul_f32 v[70:71], v[74:75], v[74:75]
	v_pk_mov_b32 v[74:75], v[78:79], v[76:77] op_sel:[1,0]
	v_mov_b32_e32 v79, v77
	v_pk_add_f32 v[60:61], v[60:61], v[64:65]
	v_pk_fma_f32 v[64:65], v[66:67], v[66:67], v[68:69]
	v_pk_fma_f32 v[66:67], v[72:73], v[72:73], v[70:71]
	v_mul_f32_e32 v83, v13, v13
	v_mul_f32_e32 v80, v53, v53
	v_mul_f32_e32 v82, v55, v55
	v_pk_add_f32 v[68:69], v[74:75], v[78:79]
	v_pk_add_f32 v[64:65], v[64:65], v[66:67]
	v_mul_f32_e32 v39, v12, v12
	v_mul_f32_e32 v84, v14, v14
	v_mul_f32_e32 v85, v15, v15
	v_pk_fma_f32 v[76:77], v[52:53], v[52:53], v[80:81] op_sel_hi:[1,1,0]
	v_pk_fma_f32 v[80:81], v[54:55], v[54:55], v[82:83] op_sel_hi:[1,1,0]
	v_pk_add_f32 v[66:67], v[68:69], v[68:69] op_sel:[0,1] op_sel_hi:[1,0]
	v_pk_add_f32 v[64:65], v[64:65], v[64:65] op_sel:[0,1] op_sel_hi:[1,0]
	v_mov_b32_e32 v77, v84
	v_mov_b32_e32 v81, v85
	v_mov_b32_e32 v67, v83
	v_mov_b32_e32 v65, v39
	v_pk_add_f32 v[68:69], v[76:77], v[80:81]
	v_pk_add_f32 v[64:65], v[64:65], v[66:67]
	v_mul_f32_e32 v86, v0, v0
	v_pk_add_f32 v[64:65], v[64:65], v[68:69]
	v_mul_f32_e32 v87, v1, v1
	v_pk_add_f32 v[62:63], v[62:63], v[62:63] op_sel:[0,1] op_sel_hi:[1,0]
	v_pk_add_f32 v[64:65], v[64:65], v[64:65] op_sel:[0,1] op_sel_hi:[1,0]
	v_mov_b32_e32 v63, v87
	v_mov_b32_e32 v65, v86
	v_pk_add_f32 v[62:63], v[64:65], v[62:63]
	s_nop 0
	v_pk_add_f32 v[60:61], v[62:63], v[60:61]
	v_add_f32_e32 v39, v60, v61
	ds_bpermute_b32 v60, v32, v39
	s_waitcnt lgkmcnt(0)
	v_add_f32_e32 v39, v39, v60
	ds_bpermute_b32 v60, v33, v39
	s_waitcnt lgkmcnt(0)
	v_add_f32_e32 v39, v39, v60
	ds_bpermute_b32 v62, v34, v39
	v_lshl_add_u64 v[60:61], s[28:29], 0, v[20:21]
	v_add_co_u32_e32 v60, vcc, s1, v60
	v_lshl_add_u64 v[20:21], v[20:21], 0, s[8:9]
	s_waitcnt lgkmcnt(0)
	v_add_f32_e32 v39, v39, v62
	ds_bpermute_b32 v64, v35, v39
	v_addc_co_u32_e32 v61, vcc, 0, v61, vcc
	v_lshl_add_u64 v[62:63], s[28:29], 0, v[28:29]
	v_add_co_u32_e64 v62, s[4:5], s3, v62
	s_waitcnt lgkmcnt(0)
	v_add_f32_e32 v39, v39, v64
	ds_bpermute_b32 v64, v36, v39
	v_lshl_add_u64 v[28:29], v[28:29], 0, s[6:7]
	s_waitcnt lgkmcnt(0)
	v_add_f32_e32 v39, v39, v64
	ds_bpermute_b32 v64, v37, v39
	s_waitcnt lgkmcnt(0)
	v_add_f32_e32 v39, v39, v64
	v_fmamk_f32 v39, v39, 0x3a000000, v38
	v_mul_f32_e32 v64, 0x4b800000, v39
	v_cmp_gt_f32_e32 vcc, s0, v39
	s_nop 1
	v_cndmask_b32_e32 v39, v39, v64, vcc
	v_rsq_f32_e32 v39, v39
	s_nop 0
	v_mul_f32_e32 v64, 0x45800000, v39
	v_cndmask_b32_e32 v64, v39, v64, vcc
	v_pk_mul_f32 v[40:41], v[64:65], v[40:41] op_sel_hi:[0,1]
	s_waitcnt vmcnt(0)
; __device__ __forceinline__ unsigned cvt_pk_bf16(float lo, float hi) { unsigned r; asm volatile("v_cvt_pk_bf16_f32 %0, %1, %2" : "=v"(r) : "v"(lo), "v"(hi)); return r; }
; __device__ __forceinline__ unsigned cvt_pk4_fp8(float a, float b, float c, float d) { int w; asm("" : "=v"(w));     w = __builtin_amdgcn_cvt_pk_fp8_f32(a, b, w, false); w = __builtin_amdgcn_cvt_pk_fp8_f32(c, d, w, true); return (unsigned)w; }
; __global__ void __launch_bounds__(512, 2) fwd_kernel(Params p) {
;     ...
;             const float rstd = rsqrtf(wave_sum(s) * (1.f / DM) + RMS_EPS);
;             u32x2* o8 = (u32x2*)(Hb + (size_t)m * DM) + lane; unsigned* o4 = (unsigned*)(H8 + (size_t)m * DM) + lane;
; #pragma unroll
;             for (int j = 0; j < 8; ++j) { const f32x4 g = gr[64 * j]; const f32x4 hv = v[j] * rstd * g; u32x2 w; w.x = cvt_pk_bf16(hv.x, hv.y); w.y = cvt_pk_bf16(hv.z, hv.w); o8[64 * j] = w; o4[64 * j] = cvt_pk4_fp8(hv.x, hv.y, hv.z, hv.w); }
;         }
	v_pk_mul_f32 v[40:41], v[56:57], v[40:41]
	v_pk_mul_f32 v[42:43], v[64:65], v[42:43] op_sel_hi:[0,1]
	v_cvt_pk_fp8_f32 v66, v40, v41
	v_pk_mul_f32 v[42:43], v[58:59], v[42:43]
	v_cvt_pk_bf16_f32 v40, v40, v41
	v_addc_co_u32_e64 v63, vcc, 0, v63, s[4:5]
	v_cvt_pk_fp8_f32 v66, v42, v43 op_sel:[0,0,1]
	v_cvt_pk_bf16_f32 v41, v42, v43
	global_store_dwordx2 v[60:61], v[40:41], off
	global_store_dword v[62:63], v66, off
	global_load_dwordx4 v[40:43], v[16:17], off offset:1024
	v_pk_mul_f32 v[44:45], v[64:65], v[44:45] op_sel_hi:[0,1]
	v_pk_mul_f32 v[12:13], v[64:65], v[12:13] op_sel_hi:[0,1]
	v_pk_mul_f32 v[14:15], v[64:65], v[14:15] op_sel_hi:[0,1]
	v_pk_mul_f32 v[8:9], v[64:65], v[8:9] op_sel_hi:[0,1]
	v_pk_mul_f32 v[10:11], v[64:65], v[10:11] op_sel_hi:[0,1]
	v_pk_mul_f32 v[4:5], v[64:65], v[4:5] op_sel_hi:[0,1]
	v_pk_mul_f32 v[6:7], v[64:65], v[6:7] op_sel_hi:[0,1]
	v_pk_mul_f32 v[0:1], v[64:65], v[0:1] op_sel_hi:[0,1]
	s_waitcnt vmcnt(0)
	v_pk_mul_f32 v[40:41], v[40:41], v[44:45]
	s_nop 0
	v_cvt_pk_fp8_f32 v39, v40, v41
	v_pk_mul_f32 v[44:45], v[64:65], v[46:47] op_sel_hi:[0,1]
	v_pk_mul_f32 v[42:43], v[42:43], v[44:45]
	v_cvt_pk_bf16_f32 v40, v40, v41
	v_pk_mul_f32 v[44:45], v[64:65], v[48:49] op_sel_hi:[0,1]
	v_cvt_pk_fp8_f32 v39, v42, v43 op_sel:[0,0,1]
	v_cvt_pk_bf16_f32 v41, v42, v43
	global_store_dwordx2 v[60:61], v[40:41], off offset:512
	global_store_dword v[62:63], v39, off offset:256
	global_load_dwordx4 v[40:43], v[16:17], off offset:2048
	s_waitcnt vmcnt(0)
	v_pk_mul_f32 v[40:41], v[40:41], v[44:45]
	s_nop 0
	v_cvt_pk_fp8_f32 v39, v40, v41
	v_pk_mul_f32 v[44:45], v[64:65], v[50:51] op_sel_hi:[0,1]
	v_pk_mul_f32 v[42:43], v[42:43], v[44:45]
	v_cvt_pk_bf16_f32 v40, v40, v41
	v_pk_mul_f32 v[44:45], v[64:65], v[52:53] op_sel_hi:[0,1]
	v_cvt_pk_fp8_f32 v39, v42, v43 op_sel:[0,0,1]
	v_cvt_pk_bf16_f32 v41, v42, v43
	global_store_dwordx2 v[60:61], v[40:41], off offset:1024
	global_store_dword v[62:63], v39, off offset:512
	global_load_dwordx4 v[40:43], v[16:17], off offset:3072
	s_waitcnt vmcnt(0)
	v_pk_mul_f32 v[40:41], v[40:41], v[44:45]
	s_nop 0
	v_cvt_pk_fp8_f32 v39, v40, v41
	v_pk_mul_f32 v[44:45], v[64:65], v[54:55] op_sel_hi:[0,1]
	v_pk_mul_f32 v[42:43], v[42:43], v[44:45]
	v_cvt_pk_bf16_f32 v40, v40, v41
	s_nop 0
	v_cvt_pk_fp8_f32 v39, v42, v43 op_sel:[0,0,1]
	v_cvt_pk_bf16_f32 v41, v42, v43
	global_store_dwordx2 v[60:61], v[40:41], off offset:1536
	global_store_dword v[62:63], v39, off offset:768
	global_load_dwordx4 v[40:43], v[18:19], off
	s_waitcnt vmcnt(0)
	v_pk_mul_f32 v[12:13], v[40:41], v[12:13]
	s_nop 0
	v_cvt_pk_fp8_f32 v39, v12, v13
	v_pk_mul_f32 v[14:15], v[42:43], v[14:15]
	v_cvt_pk_bf16_f32 v12, v12, v13
	s_nop 0
	v_cvt_pk_fp8_f32 v39, v14, v15 op_sel:[0,0,1]
	v_cvt_pk_bf16_f32 v13, v14, v15
	global_store_dwordx2 v[60:61], v[12:13], off offset:2048
	global_store_dword v[62:63], v39, off offset:1024
	global_load_dwordx4 v[12:15], v[22:23], off
	s_waitcnt vmcnt(0)
	v_pk_mul_f32 v[8:9], v[12:13], v[8:9]
	s_nop 0
	v_cvt_pk_fp8_f32 v39, v8, v9
	v_pk_mul_f32 v[10:11], v[14:15], v[10:11]
	v_cvt_pk_bf16_f32 v8, v8, v9
	v_cvt_pk_fp8_f32 v39, v10, v11 op_sel:[0,0,1]
	v_cvt_pk_bf16_f32 v9, v10, v11
	global_store_dwordx2 v[60:61], v[8:9], off offset:2560
	global_store_dword v[62:63], v39, off offset:1280
	global_load_dwordx4 v[8:11], v[24:25], off
	s_waitcnt vmcnt(0)
	v_pk_mul_f32 v[4:5], v[8:9], v[4:5]
	s_nop 0
	v_cvt_pk_fp8_f32 v12, v4, v5
	v_pk_mul_f32 v[6:7], v[10:11], v[6:7]
	v_cvt_pk_bf16_f32 v4, v4, v5
	s_nop 0
	v_cvt_pk_fp8_f32 v12, v6, v7 op_sel:[0,0,1]
	v_cvt_pk_bf16_f32 v5, v6, v7
	global_store_dwordx2 v[60:61], v[4:5], off offset:3072
	global_store_dword v[62:63], v12, off offset:1536
	global_load_dwordx4 v[4:7], v[26:27], off
	s_waitcnt vmcnt(0)
	v_pk_mul_f32 v[0:1], v[4:5], v[0:1]
	s_nop 0
	v_cvt_pk_fp8_f32 v65, v0, v1
	v_cvt_pk_bf16_f32 v0, v0, v1
	v_pk_mul_f32 v[2:3], v[64:65], v[2:3] op_sel_hi:[0,1]
	v_pk_mul_f32 v[2:3], v[6:7], v[2:3]
	s_nop 0
	v_cvt_pk_fp8_f32 v65, v2, v3 op_sel:[0,0,1]
	v_cvt_pk_bf16_f32 v1, v2, v3
	global_store_dwordx2 v[60:61], v[0:1], off offset:3584
	global_store_dword v[62:63], v65, off offset:1792
	s_cbranch_scc0 .LBB0_46

; __device__ __forceinline__ unsigned cvt_pk4_fp8(float a, float b, float c, float d) { int w; asm("" : "=v"(w));     w = __builtin_amdgcn_cvt_pk_fp8_f32(a, b, w, false); w = __builtin_amdgcn_cvt_pk_fp8_f32(c, d, w, true); return (unsigned)w; }
;     __device__ __forceinline__ void operator()(const f32x4 (&acc)[2][2][4][2], const Unit& u, int wr, int wc, int fr, int fq) const {
;         const int row0 = u.pm * BM + wr * 64 + fr, col0 = u.pn * BM + wc * 32 + 8 * fq;
; #pragma unroll
;         for (int ai = 0; ai < 2; ++ai)
; #pragma unroll
;             for (int m = 0; m < 4; ++m) { const size_t r = (size_t)(row0 + ai * HALF + m * 16);
; #pragma unroll
;                 for (int bj = 0; bj < 2; ++bj) { const f32x4 v0 = acc[ai][bj][m][0] * sc, v1 = acc[ai][bj][m][1] * sc;
;                     u32x2 z; z.x = cvt_pk4_fp8(v0[0], v0[1], v0[2], v0[3]); z.y = cvt_pk4_fp8(v1[0], v1[1], v1[2], v1[3]); *(u32x2*)(Z8 + r * 1024 + col0 + bj * HALF) = z; } }
;     }
.LBB0_145:
	v_pk_mul_f32 v[146:147], v[120:121], s[10:11] op_sel_hi:[1,0]
	v_pk_mul_f32 v[122:123], v[122:123], s[10:11] op_sel_hi:[1,0]
	v_cvt_pk_fp8_f32 v149, v146, v147
	v_pk_mul_f32 v[116:117], v[116:117], s[10:11] op_sel_hi:[1,0]
	v_pk_mul_f32 v[108:109], v[108:109], s[10:11] op_sel_hi:[1,0]
	v_pk_mul_f32 v[104:105], v[104:105], s[10:11] op_sel_hi:[1,0]
	v_cvt_pk_fp8_f32 v149, v122, v123 op_sel:[0,0,1]
	v_cvt_pk_fp8_f32 v122, v116, v117
	v_cvt_pk_fp8_f32 v116, v108, v109
	v_cvt_pk_fp8_f32 v117, v104, v105
	v_pk_mul_f32 v[104:105], v[110:111], s[10:11] op_sel_hi:[1,0]
	v_pk_mul_f32 v[96:97], v[96:97], s[10:11] op_sel_hi:[1,0]
	v_cvt_pk_fp8_f32 v116, v104, v105 op_sel:[0,0,1]
	v_cvt_pk_fp8_f32 v105, v96, v97
	v_pk_mul_f32 v[98:99], v[98:99], s[10:11] op_sel_hi:[1,0]
	v_pk_mul_f32 v[92:93], v[92:93], s[10:11] op_sel_hi:[1,0]
	v_pk_mul_f32 v[112:113], v[112:113], s[10:11] op_sel_hi:[1,0]
	v_cvt_pk_fp8_f32 v105, v98, v99 op_sel:[0,0,1]
	v_cvt_pk_fp8_f32 v98, v92, v93
	v_pk_mul_f32 v[88:89], v[88:89], s[10:11] op_sel_hi:[1,0]
	v_pk_mul_f32 v[124:125], v[124:125], s[10:11] op_sel_hi:[1,0]
	v_cvt_pk_fp8_f32 v123, v112, v113
	v_cvt_pk_fp8_f32 v99, v88, v89
	v_pk_mul_f32 v[88:89], v[94:95], s[10:11] op_sel_hi:[1,0]
	s_lshl_b32 s47, s52, 8
	v_cvt_pk_fp8_f32 v148, v124, v125
	v_pk_mul_f32 v[100:101], v[100:101], s[10:11] op_sel_hi:[1,0]
	v_cvt_pk_fp8_f32 v98, v88, v89 op_sel:[0,0,1]
	v_pk_mul_f32 v[80:81], v[80:81], s[10:11] op_sel_hi:[1,0]
	s_add_i32 s47, s47, s34
	v_cvt_pk_fp8_f32 v104, v100, v101
	v_cvt_pk_fp8_f32 v89, v80, v81
	v_mbcnt_lo_u32_b32 v137, -1, 0
	v_mbcnt_hi_u32_b32 v137, -1, v137
	v_pk_mul_f32 v[114:115], v[114:115], s[10:11] op_sel_hi:[1,0]
	v_and_or_b32 v140, v137, 15, s47
	s_lshl_b32 s47, s75, 8
	v_ashrrev_i32_e32 v137, 1, v137
	v_pk_mul_f32 v[124:125], v[126:127], s[10:11] op_sel_hi:[1,0]
	v_cvt_pk_fp8_f32 v123, v114, v115 op_sel:[0,0,1]
	v_or_b32_e32 v114, 16, v140
	v_pk_mul_f32 v[106:107], v[106:107], s[10:11] op_sel_hi:[1,0]
	s_or_b32 s47, s47, s84
	v_and_b32_e32 v137, -8, v137
	v_ashrrev_i32_e32 v141, 31, v140
	v_cvt_pk_fp8_f32 v148, v124, v125 op_sel:[0,0,1]
	v_pk_mul_f32 v[112:113], v[118:119], s[10:11] op_sel_hi:[1,0]
	v_ashrrev_i32_e32 v115, 31, v114
	v_cvt_pk_fp8_f32 v117, v106, v107 op_sel:[0,0,1]
	v_pk_mul_f32 v[96:97], v[102:103], s[10:11] op_sel_hi:[1,0]
	v_pk_mul_f32 v[82:83], v[82:83], s[10:11] op_sel_hi:[1,0]
	v_add_u32_e32 v142, s47, v137
	v_lshlrev_b64 v[144:145], 10, v[140:141]
	v_cvt_pk_fp8_f32 v122, v112, v113 op_sel:[0,0,1]
	v_lshlrev_b64 v[114:115], 10, v[114:115]
	v_cvt_pk_fp8_f32 v104, v96, v97 op_sel:[0,0,1]
	v_pk_mul_f32 v[84:85], v[84:85], s[10:11] op_sel_hi:[1,0]
	v_cvt_pk_fp8_f32 v89, v82, v83 op_sel:[0,0,1]
	v_pk_mul_f32 v[76:77], v[76:77], s[10:11] op_sel_hi:[1,0]
	v_ashrrev_i32_e32 v143, 31, v142
	v_lshl_add_u64 v[112:113], s[22:23], 0, v[144:145]
	v_lshl_add_u64 v[96:97], s[22:23], 0, v[114:115]
	v_cvt_pk_fp8_f32 v88, v84, v85
	v_cvt_pk_fp8_f32 v82, v76, v77
	v_lshl_add_u64 v[112:113], v[112:113], 0, v[142:143]
	v_lshl_add_u64 v[96:97], v[96:97], 0, v[142:143]
	global_store_dwordx2 v[112:113], v[148:149], off
	global_store_dwordx2 v[112:113], v[122:123], off offset:128
	global_store_dwordx2 v[96:97], v[116:117], off
	global_store_dwordx2 v[96:97], v[104:105], off offset:128
	v_or_b32_e32 v96, 32, v140
	v_pk_mul_f32 v[90:91], v[90:91], s[10:11] op_sel_hi:[1,0]
	v_pk_mul_f32 v[72:73], v[72:73], s[10:11] op_sel_hi:[1,0]
	v_ashrrev_i32_e32 v97, 31, v96
	v_cvt_pk_fp8_f32 v99, v90, v91 op_sel:[0,0,1]
	v_pk_mul_f32 v[80:81], v[86:87], s[10:11] op_sel_hi:[1,0]
	v_cvt_pk_fp8_f32 v83, v72, v73
	v_pk_mul_f32 v[72:73], v[78:79], s[10:11] op_sel_hi:[1,0]
	v_lshlrev_b64 v[96:97], 10, v[96:97]
	v_cvt_pk_fp8_f32 v88, v80, v81 op_sel:[0,0,1]
	v_cvt_pk_fp8_f32 v82, v72, v73 op_sel:[0,0,1]
	v_pk_mul_f32 v[68:69], v[68:69], s[10:11] op_sel_hi:[1,0]
	v_pk_mul_f32 v[64:65], v[64:65], s[10:11] op_sel_hi:[1,0]
	v_lshl_add_u64 v[80:81], s[22:23], 0, v[96:97]
	v_cvt_pk_fp8_f32 v72, v68, v69
	v_cvt_pk_fp8_f32 v73, v64, v65
	v_lshl_add_u64 v[80:81], v[80:81], 0, v[142:143]
	global_store_dwordx2 v[80:81], v[98:99], off
	global_store_dwordx2 v[80:81], v[88:89], off offset:128
	v_or_b32_e32 v80, 48, v140
	v_pk_mul_f32 v[74:75], v[74:75], s[10:11] op_sel_hi:[1,0]
	v_ashrrev_i32_e32 v81, 31, v80
	v_cvt_pk_fp8_f32 v83, v74, v75 op_sel:[0,0,1]
	v_pk_mul_f32 v[64:65], v[70:71], s[10:11] op_sel_hi:[1,0]
	v_pk_mul_f32 v[66:67], v[66:67], s[10:11] op_sel_hi:[1,0]
	v_lshlrev_b64 v[80:81], 10, v[80:81]
	v_cvt_pk_fp8_f32 v72, v64, v65 op_sel:[0,0,1]
; __device__ __forceinline__ unsigned cvt_pk4_fp8(float a, float b, float c, float d) { int w; asm("" : "=v"(w));     w = __builtin_amdgcn_cvt_pk_fp8_f32(a, b, w, false); w = __builtin_amdgcn_cvt_pk_fp8_f32(c, d, w, true); return (unsigned)w; }
; __device__ __forceinline__ int lane_id() { int l; asm volatile("v_mbcnt_lo_u32_b32 %0, -1, 0\n\tv_mbcnt_hi_u32_b32 %0, -1, %0" : "=v"(l)); return l; }
; #define PG8_BAR __builtin_amdgcn_s_barrier()
;     __device__ __forceinline__ void operator()(const f32x4 (&acc)[2][2][4][2], const Unit& u, int wr, int wc, int fr, int fq) const {
;         const int row0 = u.pm * BM + wr * 64 + fr, col0 = u.pn * BM + wc * 32 + 8 * fq;
; #pragma unroll
;         for (int ai = 0; ai < 2; ++ai)
; #pragma unroll
;             for (int m = 0; m < 4; ++m) { const size_t r = (size_t)(row0 + ai * HALF + m * 16);
; #pragma unroll
;                 for (int bj = 0; bj < 2; ++bj) { const f32x4 v0 = acc[ai][bj][m][0] * sc, v1 = acc[ai][bj][m][1] * sc;
;                     u32x2 z; z.x = cvt_pk4_fp8(v0[0], v0[1], v0[2], v0[3]); z.y = cvt_pk4_fp8(v1[0], v1[1], v1[2], v1[3]); *(u32x2*)(Z8 + r * 1024 + col0 + bj * HALF) = z; } }
;     }
; template <bool FP8 = false, class Epi, class Sched>
; __device__ __forceinline__ void gemm_phase(LAS unsigned char* lds, const int K, const int lda, const int ldb, const Sched& S, const Epi& E, const int wid) {
;     ...
;         if (wr == 0) PG8_BAR;
;         { const int l2 = lane_id(); E(acc, cur, wr, wc, l2 & 15, l2 >> 4); }
;         if (!has_next) break;
; #pragma unroll
;         for (int a = 0; a < 2; ++a)
; #pragma unroll
;             for (int b = 0; b < 2; ++b)
; #pragma unroll
;                 for (int m = 0; m < 4; ++m)
; #pragma unroll
;                     for (int n = 0; n < 2; ++n) acc[a][b][m][n] = (f32x4){0.f, 0.f, 0.f, 0.f};
;         cur = nxt; cA = nA; cB = nB; ++ui;
;         if (wr == 1) PG8_BAR;
	v_cvt_pk_fp8_f32 v73, v66, v67 op_sel:[0,0,1]
	v_lshl_add_u64 v[64:65], s[22:23], 0, v[80:81]
	v_lshl_add_u64 v[64:65], v[64:65], 0, v[142:143]
	global_store_dwordx2 v[64:65], v[82:83], off
	global_store_dwordx2 v[64:65], v[72:73], off offset:128
	v_pk_mul_f32 v[56:57], v[56:57], s[10:11] op_sel_hi:[1,0]
	v_cvt_pk_fp8_f32 v65, v56, v57
	v_pk_mul_f32 v[58:59], v[58:59], s[10:11] op_sel_hi:[1,0]
	v_pk_mul_f32 v[44:45], v[44:45], s[10:11] op_sel_hi:[1,0]
	v_pk_mul_f32 v[60:61], v[60:61], s[10:11] op_sel_hi:[1,0]
	v_cvt_pk_fp8_f32 v65, v58, v59 op_sel:[0,0,1]
	v_cvt_pk_fp8_f32 v59, v44, v45
	v_cvt_pk_fp8_f32 v64, v60, v61
	v_pk_mul_f32 v[52:53], v[52:53], s[10:11] op_sel_hi:[1,0]
	v_cvt_pk_fp8_f32 v58, v52, v53
	v_pk_mul_f32 v[46:47], v[46:47], s[10:11] op_sel_hi:[1,0]
	v_pk_mul_f32 v[56:57], v[62:63], s[10:11] op_sel_hi:[1,0]
	v_cvt_pk_fp8_f32 v59, v46, v47 op_sel:[0,0,1]
	v_pk_mul_f32 v[40:41], v[40:41], s[10:11] op_sel_hi:[1,0]
	v_cvt_pk_fp8_f32 v64, v56, v57 op_sel:[0,0,1]
	v_pk_mul_f32 v[44:45], v[54:55], s[10:11] op_sel_hi:[1,0]
	v_cvt_pk_fp8_f32 v47, v40, v41
	v_cvt_pk_fp8_f32 v58, v44, v45 op_sel:[0,0,1]
	v_add_co_u32_e32 v44, vcc, s70, v112
	v_pk_mul_f32 v[42:43], v[42:43], s[10:11] op_sel_hi:[1,0]
	s_nop 0
	v_addc_co_u32_e32 v45, vcc, 0, v113, vcc
	v_lshl_add_u64 v[56:57], v[112:113], 0, s[12:13]
	global_store_dwordx2 v[44:45], v[64:65], off
	global_store_dwordx2 v[56:57], v[58:59], off offset:128
	v_pk_mul_f32 v[44:45], v[48:49], s[10:11] op_sel_hi:[1,0]
	v_cvt_pk_fp8_f32 v47, v42, v43 op_sel:[0,0,1]
	v_pk_mul_f32 v[28:29], v[28:29], s[10:11] op_sel_hi:[1,0]
	v_cvt_pk_fp8_f32 v46, v44, v45
	v_pk_mul_f32 v[36:37], v[36:37], s[10:11] op_sel_hi:[1,0]
	v_cvt_pk_fp8_f32 v43, v28, v29
	v_cvt_pk_fp8_f32 v42, v36, v37
	v_pk_mul_f32 v[40:41], v[50:51], s[10:11] op_sel_hi:[1,0]
	v_pk_mul_f32 v[30:31], v[30:31], s[10:11] op_sel_hi:[1,0]
	v_cvt_pk_fp8_f32 v46, v40, v41 op_sel:[0,0,1]
	v_pk_mul_f32 v[28:29], v[38:39], s[10:11] op_sel_hi:[1,0]
	v_cvt_pk_fp8_f32 v43, v30, v31 op_sel:[0,0,1]
	v_pk_mul_f32 v[24:25], v[24:25], s[10:11] op_sel_hi:[1,0]
	v_cvt_pk_fp8_f32 v42, v28, v29 op_sel:[0,0,1]
	v_cvt_pk_fp8_f32 v31, v24, v25
	v_add_co_u32_e32 v28, vcc, s71, v112
	v_lshl_add_u64 v[40:41], v[112:113], 0, s[14:15]
	s_nop 0
	v_addc_co_u32_e32 v29, vcc, 0, v113, vcc
	global_store_dwordx2 v[28:29], v[46:47], off
	global_store_dwordx2 v[40:41], v[42:43], off offset:128
	v_pk_mul_f32 v[28:29], v[32:33], s[10:11] op_sel_hi:[1,0]
	v_pk_mul_f32 v[26:27], v[26:27], s[10:11] op_sel_hi:[1,0]
	v_cvt_pk_fp8_f32 v30, v28, v29
	v_cvt_pk_fp8_f32 v31, v26, v27 op_sel:[0,0,1]
	v_pk_mul_f32 v[20:21], v[20:21], s[10:11] op_sel_hi:[1,0]
	v_pk_mul_f32 v[12:13], v[12:13], s[10:11] op_sel_hi:[1,0]
	v_cvt_pk_fp8_f32 v26, v20, v21
	v_cvt_pk_fp8_f32 v27, v12, v13
	v_pk_mul_f32 v[24:25], v[34:35], s[10:11] op_sel_hi:[1,0]
	v_pk_mul_f32 v[12:13], v[22:23], s[10:11] op_sel_hi:[1,0]
	v_cvt_pk_fp8_f32 v30, v24, v25 op_sel:[0,0,1]
	v_pk_mul_f32 v[14:15], v[14:15], s[10:11] op_sel_hi:[1,0]
	v_cvt_pk_fp8_f32 v26, v12, v13 op_sel:[0,0,1]
	v_cvt_pk_fp8_f32 v27, v14, v15 op_sel:[0,0,1]
	v_add_co_u32_e32 v12, vcc, s72, v112
	v_lshl_add_u64 v[24:25], v[112:113], 0, s[24:25]
	s_nop 0
	v_addc_co_u32_e32 v13, vcc, 0, v113, vcc
	global_store_dwordx2 v[12:13], v[30:31], off
	global_store_dwordx2 v[24:25], v[26:27], off offset:128
	v_pk_mul_f32 v[12:13], v[16:17], s[10:11] op_sel_hi:[1,0]
	v_pk_mul_f32 v[8:9], v[8:9], s[10:11] op_sel_hi:[1,0]
	v_cvt_pk_fp8_f32 v14, v12, v13
	v_cvt_pk_fp8_f32 v15, v8, v9
	v_pk_mul_f32 v[4:5], v[4:5], s[10:11] op_sel_hi:[1,0]
	v_pk_mul_f32 v[0:1], v[0:1], s[10:11] op_sel_hi:[1,0]
	v_cvt_pk_fp8_f32 v120, v4, v5
	v_cvt_pk_fp8_f32 v121, v0, v1
	v_pk_mul_f32 v[8:9], v[18:19], s[10:11] op_sel_hi:[1,0]
	v_pk_mul_f32 v[10:11], v[10:11], s[10:11] op_sel_hi:[1,0]
	v_cvt_pk_fp8_f32 v14, v8, v9 op_sel:[0,0,1]
	v_cvt_pk_fp8_f32 v15, v10, v11 op_sel:[0,0,1]
	v_pk_mul_f32 v[0:1], v[6:7], s[10:11] op_sel_hi:[1,0]
	v_pk_mul_f32 v[2:3], v[2:3], s[10:11] op_sel_hi:[1,0]
	v_cvt_pk_fp8_f32 v120, v0, v1 op_sel:[0,0,1]
	v_cvt_pk_fp8_f32 v121, v2, v3 op_sel:[0,0,1]
	v_add_co_u32_e32 v0, vcc, s73, v112
	v_readlane_b32 s78, v252, 14
	s_nop 0
	v_addc_co_u32_e32 v1, vcc, 0, v113, vcc
	s_andn2_b64 vcc, exec, s[44:45]
	s_mov_b64 s[44:45], -1
	v_lshl_add_u64 v[8:9], v[112:113], 0, s[26:27]
	global_store_dwordx2 v[0:1], v[14:15], off
	global_store_dwordx2 v[8:9], v[120:121], off offset:128
	s_cbranch_vccnz .LBB0_134
	s_andn2_b64 vcc, exec, s[6:7]
	s_cbranch_vccnz .LBB0_133
	s_barrier
	s_branch .LBB0_133

; __device__ __forceinline__ unsigned cvt_pk4_fp8(float a, float b, float c, float d) { int w; asm("" : "=v"(w));     w = __builtin_amdgcn_cvt_pk_fp8_f32(a, b, w, false); w = __builtin_amdgcn_cvt_pk_fp8_f32(c, d, w, true); return (unsigned)w; }
;     __device__ __forceinline__ void operator()(const f32x4 (&acc)[2][2][4][2], const Unit& u, int wr, int wc, int fr, int fq) const {
;         const int row0 = u.pm * BM + wr * 64 + fr, col0 = u.pn * BM + wc * 32 + 8 * fq;
; #pragma unroll
;         for (int ai = 0; ai < 2; ++ai)
; #pragma unroll
;             for (int m = 0; m < 4; ++m) { const int r = row0 + ai * HALF + m * 16; const float c = rs[r] * (1.0f / W8_SCALE);     unsigned char* rowp = O + (size_t)r * ldc + col0;
; #pragma unroll
;                 for (int bj = 0; bj < 2; ++bj) { const f32x4 v0 = acc[ai][bj][m][0] * c, v1 = acc[ai][bj][m][1] * c;
;                     u32x2 w; w.x = cvt_pk4_fp8(v0[0], v0[1], v0[2], v0[3]); w.y = cvt_pk4_fp8(v1[0], v1[1], v1[2], v1[3]);
;                     *(u32x2*)(rowp + bj * HALF) = w; } }
;     }
.LBB0_374:
	s_lshl_b32 s15, s50, 8
	s_add_i32 s15, s15, s34
	v_mbcnt_lo_u32_b32 v132, -1, 0
	v_mbcnt_hi_u32_b32 v132, -1, v132
	v_readlane_b32 s46, v252, 21
	v_and_or_b32 v128, v132, 15, s15
	v_ashrrev_i32_e32 v129, 31, v128
	v_lshl_add_u64 v[136:137], v[128:129], 2, s[6:7]
	global_load_dword v129, v[136:137], off
	global_load_dword v240, v[136:137], off offset:64
	global_load_dword v241, v[136:137], off offset:128
	global_load_dword v242, v[136:137], off offset:192
	global_load_dword v243, v[136:137], off offset:512
	global_load_dword v244, v[136:137], off offset:576
	global_load_dword v245, v[136:137], off offset:640
	global_load_dword v246, v[136:137], off offset:704
	s_lshl_b32 s15, s76, 8
	v_ashrrev_i32_e32 v132, 1, v132
	s_or_b32 s15, s15, s84
	v_and_b32_e32 v132, -8, v132
	v_add_u32_e32 v134, s15, v132
	v_readlane_b32 s47, v252, 22
	v_or_b32_e32 v154, 16, v128
	v_ashrrev_i32_e32 v135, 31, v134
	v_mov_b64_e32 v[130:131], s[46:47]
	v_mad_i64_i32 v[152:153], s[52:53], v128, s74, v[130:131]
	v_ashrrev_i32_e32 v155, 31, v154
	s_andn2_b64 vcc, exec, s[48:49]
	s_waitcnt vmcnt(0)
	v_mul_f32_e32 v132, 0x3c800000, v129
	v_pk_mul_f32 v[124:125], v[124:125], v[132:133] op_sel_hi:[1,0]
	v_pk_mul_f32 v[120:121], v[120:121], v[132:133] op_sel_hi:[1,0]
	v_pk_mul_f32 v[116:117], v[116:117], v[132:133] op_sel_hi:[1,0]
	v_pk_mul_f32 v[112:113], v[112:113], v[132:133] op_sel_hi:[1,0]
	v_cvt_pk_fp8_f32 v148, v124, v125
	v_cvt_pk_fp8_f32 v149, v120, v121
	v_cvt_pk_fp8_f32 v150, v116, v117
	v_cvt_pk_fp8_f32 v151, v112, v113
	v_pk_mul_f32 v[126:127], v[126:127], v[132:133] op_sel_hi:[1,0]
	v_pk_mul_f32 v[122:123], v[122:123], v[132:133] op_sel_hi:[1,0]
	v_pk_mul_f32 v[118:119], v[118:119], v[132:133] op_sel_hi:[1,0]
	v_pk_mul_f32 v[114:115], v[114:115], v[132:133] op_sel_hi:[1,0]
	v_cvt_pk_fp8_f32 v148, v126, v127 op_sel:[0,0,1]
	v_cvt_pk_fp8_f32 v149, v122, v123 op_sel:[0,0,1]
	v_cvt_pk_fp8_f32 v150, v118, v119 op_sel:[0,0,1]
	v_cvt_pk_fp8_f32 v151, v114, v115 op_sel:[0,0,1]
	v_lshl_add_u64 v[112:113], v[152:153], 0, v[134:135]
	v_lshl_add_u64 v[114:115], v[154:155], 2, s[6:7]
	global_store_dwordx2 v[112:113], v[148:149], off
	global_store_dwordx2 v[112:113], v[150:151], off offset:128
	v_mov_b32_e32 v120, v240
	v_or_b32_e32 v116, 32, v128
	v_mad_i64_i32 v[118:119], s[52:53], v154, s74, v[130:131]
	v_ashrrev_i32_e32 v117, 31, v116
	v_mul_f32_e32 v120, 0x3c800000, v120
	v_pk_mul_f32 v[108:109], v[108:109], v[120:121] op_sel_hi:[1,0]
	v_pk_mul_f32 v[104:105], v[104:105], v[120:121] op_sel_hi:[1,0]
	v_pk_mul_f32 v[100:101], v[100:101], v[120:121] op_sel_hi:[1,0]
	v_pk_mul_f32 v[96:97], v[96:97], v[120:121] op_sel_hi:[1,0]
	v_cvt_pk_fp8_f32 v112, v108, v109
	v_cvt_pk_fp8_f32 v113, v104, v105
	v_cvt_pk_fp8_f32 v114, v100, v101
	v_cvt_pk_fp8_f32 v115, v96, v97
	v_pk_mul_f32 v[110:111], v[110:111], v[120:121] op_sel_hi:[1,0]
	v_pk_mul_f32 v[106:107], v[106:107], v[120:121] op_sel_hi:[1,0]
	v_pk_mul_f32 v[102:103], v[102:103], v[120:121] op_sel_hi:[1,0]
	v_pk_mul_f32 v[98:99], v[98:99], v[120:121] op_sel_hi:[1,0]
	v_cvt_pk_fp8_f32 v112, v110, v111 op_sel:[0,0,1]
	v_cvt_pk_fp8_f32 v113, v106, v107 op_sel:[0,0,1]
	v_cvt_pk_fp8_f32 v114, v102, v103 op_sel:[0,0,1]
	v_cvt_pk_fp8_f32 v115, v98, v99 op_sel:[0,0,1]
	v_lshl_add_u64 v[96:97], v[118:119], 0, v[134:135]
	v_lshl_add_u64 v[98:99], v[116:117], 2, s[6:7]
	global_store_dwordx2 v[96:97], v[112:113], off
	global_store_dwordx2 v[96:97], v[114:115], off offset:128
	v_mov_b32_e32 v104, v241
	v_or_b32_e32 v100, 48, v128
	v_mad_i64_i32 v[102:103], s[52:53], v116, s74, v[130:131]
	v_ashrrev_i32_e32 v101, 31, v100
	v_mul_f32_e32 v104, 0x3c800000, v104
	v_pk_mul_f32 v[92:93], v[92:93], v[104:105] op_sel_hi:[1,0]
	v_pk_mul_f32 v[88:89], v[88:89], v[104:105] op_sel_hi:[1,0]
	v_pk_mul_f32 v[84:85], v[84:85], v[104:105] op_sel_hi:[1,0]
	v_pk_mul_f32 v[80:81], v[80:81], v[104:105] op_sel_hi:[1,0]
	v_cvt_pk_fp8_f32 v96, v92, v93
	v_cvt_pk_fp8_f32 v97, v88, v89
	v_cvt_pk_fp8_f32 v98, v84, v85
	v_cvt_pk_fp8_f32 v99, v80, v81
	v_pk_mul_f32 v[94:95], v[94:95], v[104:105] op_sel_hi:[1,0]
	v_pk_mul_f32 v[90:91], v[90:91], v[104:105] op_sel_hi:[1,0]
	v_pk_mul_f32 v[86:87], v[86:87], v[104:105] op_sel_hi:[1,0]
	v_pk_mul_f32 v[82:83], v[82:83], v[104:105] op_sel_hi:[1,0]
	v_cvt_pk_fp8_f32 v96, v94, v95 op_sel:[0,0,1]
	v_cvt_pk_fp8_f32 v97, v90, v91 op_sel:[0,0,1]
	v_cvt_pk_fp8_f32 v98, v86, v87 op_sel:[0,0,1]
	v_cvt_pk_fp8_f32 v99, v82, v83 op_sel:[0,0,1]
	v_lshl_add_u64 v[80:81], v[102:103], 0, v[134:135]
	v_lshl_add_u64 v[82:83], v[100:101], 2, s[6:7]
	global_store_dwordx2 v[80:81], v[96:97], off
	global_store_dwordx2 v[80:81], v[98:99], off offset:128
	v_mov_b32_e32 v84, v242
	v_mul_f32_e32 v84, 0x3c800000, v84
	v_pk_mul_f32 v[76:77], v[76:77], v[84:85] op_sel_hi:[1,0]
	v_pk_mul_f32 v[72:73], v[72:73], v[84:85] op_sel_hi:[1,0]
	v_pk_mul_f32 v[68:69], v[68:69], v[84:85] op_sel_hi:[1,0]
	v_pk_mul_f32 v[64:65], v[64:65], v[84:85] op_sel_hi:[1,0]
	v_cvt_pk_fp8_f32 v80, v76, v77
	v_cvt_pk_fp8_f32 v81, v72, v73
	v_cvt_pk_fp8_f32 v82, v68, v69
	v_cvt_pk_fp8_f32 v83, v64, v65
; __device__ __forceinline__ unsigned cvt_pk4_fp8(float a, float b, float c, float d) { int w; asm("" : "=v"(w));     w = __builtin_amdgcn_cvt_pk_fp8_f32(a, b, w, false); w = __builtin_amdgcn_cvt_pk_fp8_f32(c, d, w, true); return (unsigned)w; }
;     __device__ __forceinline__ void operator()(const f32x4 (&acc)[2][2][4][2], const Unit& u, int wr, int wc, int fr, int fq) const {
;         const int row0 = u.pm * BM + wr * 64 + fr, col0 = u.pn * BM + wc * 32 + 8 * fq;
; #pragma unroll
;         for (int ai = 0; ai < 2; ++ai)
; #pragma unroll
;             for (int m = 0; m < 4; ++m) { const int r = row0 + ai * HALF + m * 16; const float c = rs[r] * (1.0f / W8_SCALE);     unsigned char* rowp = O + (size_t)r * ldc + col0;
; #pragma unroll
;                 for (int bj = 0; bj < 2; ++bj) { const f32x4 v0 = acc[ai][bj][m][0] * c, v1 = acc[ai][bj][m][1] * c;
;                     u32x2 w; w.x = cvt_pk4_fp8(v0[0], v0[1], v0[2], v0[3]); w.y = cvt_pk4_fp8(v1[0], v1[1], v1[2], v1[3]);
;                     *(u32x2*)(rowp + bj * HALF) = w; } }
;     }
	v_pk_mul_f32 v[78:79], v[78:79], v[84:85] op_sel_hi:[1,0]
	v_pk_mul_f32 v[74:75], v[74:75], v[84:85] op_sel_hi:[1,0]
	v_pk_mul_f32 v[70:71], v[70:71], v[84:85] op_sel_hi:[1,0]
	v_pk_mul_f32 v[66:67], v[66:67], v[84:85] op_sel_hi:[1,0]
	v_cvt_pk_fp8_f32 v80, v78, v79 op_sel:[0,0,1]
	v_cvt_pk_fp8_f32 v81, v74, v75 op_sel:[0,0,1]
	v_cvt_pk_fp8_f32 v82, v70, v71 op_sel:[0,0,1]
	v_cvt_pk_fp8_f32 v83, v66, v67 op_sel:[0,0,1]
	v_mad_i64_i32 v[64:65], s[52:53], v100, s74, v[130:131]
	v_lshl_add_u64 v[64:65], v[64:65], 0, v[134:135]
	global_store_dwordx2 v[64:65], v[80:81], off
	global_store_dwordx2 v[64:65], v[82:83], off offset:128
	v_mov_b32_e32 v68, v243
	v_add_u32_e32 v69, 0x80, v128
	v_mul_f32_e32 v68, 0x3c800000, v68
	v_pk_mul_f32 v[60:61], v[60:61], v[68:69] op_sel_hi:[1,0]
	v_pk_mul_f32 v[56:57], v[56:57], v[68:69] op_sel_hi:[1,0]
	v_pk_mul_f32 v[52:53], v[52:53], v[68:69] op_sel_hi:[1,0]
	v_pk_mul_f32 v[48:49], v[48:49], v[68:69] op_sel_hi:[1,0]
	v_cvt_pk_fp8_f32 v64, v60, v61
	v_cvt_pk_fp8_f32 v65, v56, v57
	v_cvt_pk_fp8_f32 v66, v52, v53
	v_cvt_pk_fp8_f32 v67, v48, v49
	v_pk_mul_f32 v[62:63], v[62:63], v[68:69] op_sel_hi:[1,0]
	v_pk_mul_f32 v[58:59], v[58:59], v[68:69] op_sel_hi:[1,0]
	v_pk_mul_f32 v[54:55], v[54:55], v[68:69] op_sel_hi:[1,0]
	v_pk_mul_f32 v[50:51], v[50:51], v[68:69] op_sel_hi:[1,0]
	v_cvt_pk_fp8_f32 v64, v62, v63 op_sel:[0,0,1]
	v_cvt_pk_fp8_f32 v65, v58, v59 op_sel:[0,0,1]
	v_cvt_pk_fp8_f32 v66, v54, v55 op_sel:[0,0,1]
	v_cvt_pk_fp8_f32 v67, v50, v51 op_sel:[0,0,1]
	v_mad_i64_i32 v[48:49], s[52:53], v69, s74, v[130:131]
	v_lshl_add_u64 v[48:49], v[48:49], 0, v[134:135]
	global_store_dwordx2 v[48:49], v[64:65], off
	global_store_dwordx2 v[48:49], v[66:67], off offset:128
	v_mov_b32_e32 v52, v244
	v_add_u32_e32 v53, 0x90, v128
	v_mul_f32_e32 v52, 0x3c800000, v52
	v_pk_mul_f32 v[44:45], v[44:45], v[52:53] op_sel_hi:[1,0]
	v_pk_mul_f32 v[40:41], v[40:41], v[52:53] op_sel_hi:[1,0]
	v_pk_mul_f32 v[36:37], v[36:37], v[52:53] op_sel_hi:[1,0]
	v_pk_mul_f32 v[32:33], v[32:33], v[52:53] op_sel_hi:[1,0]
	v_cvt_pk_fp8_f32 v48, v44, v45
	v_cvt_pk_fp8_f32 v49, v40, v41
	v_cvt_pk_fp8_f32 v50, v36, v37
	v_cvt_pk_fp8_f32 v51, v32, v33
	v_pk_mul_f32 v[46:47], v[46:47], v[52:53] op_sel_hi:[1,0]
	v_pk_mul_f32 v[42:43], v[42:43], v[52:53] op_sel_hi:[1,0]
	v_pk_mul_f32 v[38:39], v[38:39], v[52:53] op_sel_hi:[1,0]
	v_pk_mul_f32 v[34:35], v[34:35], v[52:53] op_sel_hi:[1,0]
	v_cvt_pk_fp8_f32 v48, v46, v47 op_sel:[0,0,1]
	v_cvt_pk_fp8_f32 v49, v42, v43 op_sel:[0,0,1]
	v_cvt_pk_fp8_f32 v50, v38, v39 op_sel:[0,0,1]
	v_cvt_pk_fp8_f32 v51, v34, v35 op_sel:[0,0,1]
	v_mad_i64_i32 v[32:33], s[52:53], v53, s74, v[130:131]
	v_lshl_add_u64 v[32:33], v[32:33], 0, v[134:135]
	global_store_dwordx2 v[32:33], v[48:49], off
	global_store_dwordx2 v[32:33], v[50:51], off offset:128
	v_mov_b32_e32 v36, v245
	v_add_u32_e32 v37, 0xa0, v128
	v_mul_f32_e32 v36, 0x3c800000, v36
	v_pk_mul_f32 v[28:29], v[28:29], v[36:37] op_sel_hi:[1,0]
	v_pk_mul_f32 v[24:25], v[24:25], v[36:37] op_sel_hi:[1,0]
	v_pk_mul_f32 v[20:21], v[20:21], v[36:37] op_sel_hi:[1,0]
	v_pk_mul_f32 v[16:17], v[16:17], v[36:37] op_sel_hi:[1,0]
	v_cvt_pk_fp8_f32 v32, v28, v29
	v_cvt_pk_fp8_f32 v33, v24, v25
	v_cvt_pk_fp8_f32 v34, v20, v21
	v_cvt_pk_fp8_f32 v35, v16, v17
	v_pk_mul_f32 v[30:31], v[30:31], v[36:37] op_sel_hi:[1,0]
	v_pk_mul_f32 v[26:27], v[26:27], v[36:37] op_sel_hi:[1,0]
	v_pk_mul_f32 v[22:23], v[22:23], v[36:37] op_sel_hi:[1,0]
	v_pk_mul_f32 v[18:19], v[18:19], v[36:37] op_sel_hi:[1,0]
	v_cvt_pk_fp8_f32 v32, v30, v31 op_sel:[0,0,1]
	v_cvt_pk_fp8_f32 v33, v26, v27 op_sel:[0,0,1]
	v_cvt_pk_fp8_f32 v34, v22, v23 op_sel:[0,0,1]
	v_cvt_pk_fp8_f32 v35, v18, v19 op_sel:[0,0,1]
	v_mad_i64_i32 v[16:17], s[52:53], v37, s74, v[130:131]
	v_lshl_add_u64 v[16:17], v[16:17], 0, v[134:135]
	global_store_dwordx2 v[16:17], v[32:33], off
	global_store_dwordx2 v[16:17], v[34:35], off offset:128
	v_mov_b32_e32 v18, v246
	v_add_u32_e32 v19, 0xb0, v128
	v_mul_f32_e32 v18, 0x3c800000, v18
	v_pk_mul_f32 v[12:13], v[12:13], v[18:19] op_sel_hi:[1,0]
	v_pk_mul_f32 v[8:9], v[8:9], v[18:19] op_sel_hi:[1,0]
	v_pk_mul_f32 v[4:5], v[4:5], v[18:19] op_sel_hi:[1,0]
	v_pk_mul_f32 v[0:1], v[0:1], v[18:19] op_sel_hi:[1,0]
	v_cvt_pk_fp8_f32 v16, v12, v13
	v_cvt_pk_fp8_f32 v17, v8, v9
	v_cvt_pk_fp8_f32 v132, v4, v5
	v_cvt_pk_fp8_f32 v133, v0, v1
	v_pk_mul_f32 v[14:15], v[14:15], v[18:19] op_sel_hi:[1,0]
	v_pk_mul_f32 v[10:11], v[10:11], v[18:19] op_sel_hi:[1,0]
	v_pk_mul_f32 v[6:7], v[6:7], v[18:19] op_sel_hi:[1,0]
	v_pk_mul_f32 v[2:3], v[2:3], v[18:19] op_sel_hi:[1,0]
	v_cvt_pk_fp8_f32 v16, v14, v15 op_sel:[0,0,1]
	v_cvt_pk_fp8_f32 v17, v10, v11 op_sel:[0,0,1]
	v_cvt_pk_fp8_f32 v132, v6, v7 op_sel:[0,0,1]
	v_cvt_pk_fp8_f32 v133, v2, v3 op_sel:[0,0,1]
	v_mad_i64_i32 v[0:1], s[48:49], v19, s74, v[130:131]
	v_lshl_add_u64 v[0:1], v[0:1], 0, v[134:135]
	s_mov_b64 s[48:49], -1
	global_store_dwordx2 v[0:1], v[16:17], off
	global_store_dwordx2 v[0:1], v[132:133], off offset:128
	s_cbranch_vccnz .LBB0_367
	s_andn2_b64 vcc, exec, s[4:5]
	s_cbranch_vccnz .LBB0_366
	s_barrier
	s_branch .LBB0_366

; #define LAS __attribute__((address_space(3)))
; __device__ __forceinline__ unsigned cvt_pk4_fp8(float a, float b, float c, float d) { int w; asm("" : "=v"(w));     w = __builtin_amdgcn_cvt_pk_fp8_f32(a, b, w, false); w = __builtin_amdgcn_cvt_pk_fp8_f32(c, d, w, true); return (unsigned)w; }
;     __device__ __forceinline__ void operator()(const f32x4 (&acc)[2][2][4][2], const Unit& u, int wr, int wc, int fr, int fq) const {
;     ...
;         asm volatile("s_waitcnt lgkmcnt(0)" ::: "memory"); __builtin_amdgcn_s_barrier(); asm volatile("" ::: "memory");
;         const f32x4 g0 = *(const f32x4*)(gk + dl0) * *(const f32x4*)(gq + dl0), g1 = *(const f32x4*)(gk + dl0 + 4) * *(const f32x4*)(gq + dl0 + 4);
;         const int kpos = 64 * (wc >> 1) + 32 * (fq & 1) + 8 * ((2 * wc + (fq >> 1)) & 3);
; #pragma unroll
;         for (int ai = 0; ai < 2; ++ai)
; #pragma unroll
;             for (int m = 0; m < 4; ++m) { const int rl = rl0 + ai * HALF + m; const float c = rs[u.pm * BM + rl] * (1.0f / W8_SCALE);
;                 const f32x4 pq = *(const LAS f32x4*)(xch + rl * 4); const float rstd = rsqrtf(((pq[0] + pq[1]) + (pq[2] + pq[3])) * (1.0f / 128.0f) + RMS_EPS) * c;
;                 const f32x4 v0 = acc[ai][0][m][0] * (rstd * KSC_) * g0, v1 = acc[ai][0][m][1] * (rstd * KSC_) * g1;
;                 u32x2 w; w.x = cvt_pk4_fp8(v0[0], v0[1], v0[2], v0[3]); w.y = cvt_pk4_fp8(v1[0], v1[1], v1[2], v1[3]);
;                 *(u32x2*)(K8 + (size_t)(u.pm * BM + rl) * 2048 + u.pn * 128 + kpos) = w; }
.LBB0_417:
	s_or_b64 exec, exec, s[4:5]
	s_waitcnt lgkmcnt(0)
	s_barrier
	s_load_dwordx2 s[4:5], s[88:89], 0x50
	v_ashrrev_i32_e32 v128, 4, v128
	v_lshl_add_u32 v130, v128, 3, s41
	s_waitcnt lgkmcnt(0)
	v_ashrrev_i32_e32 v131, 31, v130
	v_lshlrev_b64 v[140:141], 2, v[130:131]
	v_lshl_add_u64 v[136:137], s[4:5], 0, v[140:141]
	global_load_dwordx4 v[194:197], v[136:137], off offset:16
	s_nop 0
	global_load_dwordx4 v[136:139], v[136:137], off
	s_load_dwordx2 s[4:5], s[88:89], 0x40
	v_lshlrev_b32_e32 v186, 5, v128
	v_lshl_add_u32 v128, v128, 2, s83
	v_and_b32_e32 v131, 32, v186
	v_and_b32_e32 v128, 24, v128
	s_waitcnt lgkmcnt(0)
	v_lshl_add_u64 v[140:141], s[4:5], 0, v[140:141]
	global_load_dwordx4 v[198:201], v[140:141], off offset:16
	global_load_dwordx4 v[202:205], v[140:141], off
	v_or3_b32 v128, v131, s82, v128
	v_mov_b32_e32 v131, v240
	s_lshl_b32 s60, s0, 7
	s_add_i32 s0, 0, 0x20000
	v_lshlrev_b64 v[152:153], 11, v[152:153]
	s_ashr_i32 s61, s60, 31
	v_lshl_add_u64 v[152:153], s[48:49], 0, v[152:153]
	v_lshl_add_u64 v[152:153], v[152:153], 0, s[60:61]
	s_mov_b32 s4, 0x358637bd
	s_ashr_i32 s59, s58, 31
	s_lshr_b32 s1, s59, 19
	s_add_i32 s1, s58, s1
	s_and_b32 s1, s1, 0xffffe000
	s_sub_i32 s1, s58, s1
	s_ashr_i32 s1, s1, 6
	s_waitcnt vmcnt(0)
	v_pk_mul_f32 v[140:141], v[138:139], v[204:205]
	v_pk_mul_f32 v[142:143], v[136:137], v[202:203]
	v_mul_f32_e32 v193, 0x3c800000, v131
	v_lshl_add_u32 v131, v185, 4, s0
	v_pk_mul_f32 v[136:137], v[196:197], v[200:201]
	v_pk_mul_f32 v[138:139], v[194:195], v[198:199]
	ds_read_b128 v[194:197], v131
	s_waitcnt lgkmcnt(0)
	v_mov_b32_e32 v170, v195
	v_mov_b32_e32 v171, v196
	v_mov_b32_e32 v195, v197
	v_pk_add_f32 v[198:199], v[170:171], v[194:195]
	v_lshl_add_u64 v[170:171], v[152:153], 0, v[128:129]
	v_lshl_add_u32 v152, v172, 4, s0
	ds_read_b128 v[194:197], v152
	v_mov_b32_e32 v173, v198
	s_waitcnt lgkmcnt(0)
	v_mov_b32_e32 v152, v195
	v_mov_b32_e32 v153, v196
	v_mov_b32_e32 v195, v197
	v_pk_add_f32 v[152:153], v[152:153], v[194:195]
	s_nop 0
	v_mov_b32_e32 v172, v152
	v_mov_b32_e32 v198, v153
	v_pk_add_f32 v[172:173], v[172:173], v[198:199]
	v_mov_b64_e32 v[152:153], s[4:5]
	v_pk_fma_f32 v[172:173], v[172:173], s[22:23], v[152:153] op_sel_hi:[1,0,0]
	s_nop 0
	v_mul_f32_e32 v194, 0x4b800000, v173
	v_cmp_gt_f32_e64 s[4:5], s86, v173
	v_cmp_gt_f32_e32 vcc, s86, v172
	s_nop 0
	v_cndmask_b32_e64 v173, v173, v194, s[4:5]
	v_rsq_f32_e32 v173, v173
	s_nop 0
	v_mul_f32_e32 v194, 0x45800000, v173
	v_cndmask_b32_e64 v173, v173, v194, s[4:5]
	v_mul_f32_e32 v173, v193, v173
	v_mul_f32_e32 v194, 0x3ed53b94, v173
	v_pk_mul_f32 v[124:125], v[124:125], v[194:195] op_sel_hi:[1,0]
	v_pk_mul_f32 v[196:197], v[120:121], v[194:195] op_sel_hi:[1,0]
	v_pk_mul_f32 v[126:127], v[126:127], v[194:195] op_sel_hi:[1,0]
	v_pk_mul_f32 v[124:125], v[142:143], v[124:125]
	v_pk_mul_f32 v[120:121], v[122:123], v[194:195] op_sel_hi:[1,0]
	v_pk_mul_f32 v[122:123], v[138:139], v[196:197]
	v_cvt_pk_fp8_f32 v194, v124, v125
	v_cvt_pk_fp8_f32 v195, v122, v123
	v_pk_mul_f32 v[126:127], v[140:141], v[126:127]
	v_pk_mul_f32 v[120:121], v[136:137], v[120:121]
	v_cvt_pk_fp8_f32 v194, v126, v127 op_sel:[0,0,1]
	v_cvt_pk_fp8_f32 v195, v120, v121 op_sel:[0,0,1]
	v_mul_f32_e32 v121, 0x4b800000, v172
	v_cndmask_b32_e32 v121, v172, v121, vcc
	v_rsq_f32_e32 v121, v121
	global_store_dwordx2 v[170:171], v[194:195], off
	v_mov_b32_e32 v120, v241
	v_mul_f32_e32 v122, 0x45800000, v121
	v_cndmask_b32_e32 v121, v121, v122, vcc
	v_mul_f32_e32 v120, 0x3c800000, v120
	v_mul_f32_e32 v120, v120, v121
	v_mul_f32_e32 v120, 0x3ed53b94, v120
	v_pk_mul_f32 v[116:117], v[116:117], v[120:121] op_sel_hi:[1,0]
	v_pk_mul_f32 v[112:113], v[112:113], v[120:121] op_sel_hi:[1,0]
	v_pk_mul_f32 v[118:119], v[118:119], v[120:121] op_sel_hi:[1,0]
	v_pk_mul_f32 v[116:117], v[142:143], v[116:117]
	v_pk_mul_f32 v[114:115], v[114:115], v[120:121] op_sel_hi:[1,0]
	v_pk_mul_f32 v[112:113], v[138:139], v[112:113]
	v_cvt_pk_fp8_f32 v120, v116, v117
	v_cvt_pk_fp8_f32 v121, v112, v113
	v_pk_mul_f32 v[118:119], v[140:141], v[118:119]
	v_pk_mul_f32 v[114:115], v[136:137], v[114:115]
	v_cvt_pk_fp8_f32 v120, v118, v119 op_sel:[0,0,1]
	v_cvt_pk_fp8_f32 v121, v114, v115 op_sel:[0,0,1]
	v_lshlrev_b64 v[112:113], 11, v[166:167]
	v_lshl_add_u64 v[112:113], s[48:49], 0, v[112:113]
	v_lshl_add_u64 v[112:113], v[112:113], 0, s[60:61]
	v_lshl_add_u64 v[112:113], v[112:113], 0, v[128:129]
	global_store_dwordx2 v[112:113], v[120:121], off
	v_mov_b32_e32 v112, v242
	v_mul_f32_e32 v122, 0x3c800000, v112
	v_lshl_add_u32 v112, v191, 4, s0
	ds_read_b128 v[112:115], v112
	s_waitcnt lgkmcnt(0)
	v_mov_b32_e32 v116, v113
	v_mov_b32_e32 v117, v114
	v_mov_b32_e32 v113, v115
	v_pk_add_f32 v[116:117], v[116:117], v[112:113]
	v_lshlrev_b64 v[112:113], 11, v[162:163]
	v_lshl_add_u64 v[112:113], s[48:49], 0, v[112:113]
	v_lshl_add_u64 v[112:113], v[112:113], 0, s[60:61]
	v_lshl_add_u64 v[118:119], v[112:113], 0, v[128:129]
	v_lshl_add_u32 v112, v192, 4, s0
	ds_read_b128 v[112:115], v112
	s_waitcnt lgkmcnt(0)
; #define LAS __attribute__((address_space(3)))
; __device__ __forceinline__ unsigned cvt_pk4_fp8(float a, float b, float c, float d) { int w; asm("" : "=v"(w));     w = __builtin_amdgcn_cvt_pk_fp8_f32(a, b, w, false); w = __builtin_amdgcn_cvt_pk_fp8_f32(c, d, w, true); return (unsigned)w; }
;     __device__ __forceinline__ void operator()(const f32x4 (&acc)[2][2][4][2], const Unit& u, int wr, int wc, int fr, int fq) const {
;     ...
;         for (int ai = 0; ai < 2; ++ai)
; #pragma unroll
;             for (int m = 0; m < 4; ++m) { const int rl = rl0 + ai * HALF + m; const float c = rs[u.pm * BM + rl] * (1.0f / W8_SCALE);
;                 const f32x4 pq = *(const LAS f32x4*)(xch + rl * 4); const float rstd = rsqrtf(((pq[0] + pq[1]) + (pq[2] + pq[3])) * (1.0f / 128.0f) + RMS_EPS) * c;
;                 const f32x4 v0 = acc[ai][0][m][0] * (rstd * KSC_) * g0, v1 = acc[ai][0][m][1] * (rstd * KSC_) * g1;
;                 u32x2 w; w.x = cvt_pk4_fp8(v0[0], v0[1], v0[2], v0[3]); w.y = cvt_pk4_fp8(v1[0], v1[1], v1[2], v1[3]);
;                 *(u32x2*)(K8 + (size_t)(u.pm * BM + rl) * 2048 + u.pn * 128 + kpos) = w; }
	v_mov_b32_e32 v120, v113
	v_mov_b32_e32 v121, v114
	v_mov_b32_e32 v113, v115
	v_pk_add_f32 v[112:113], v[120:121], v[112:113]
	v_mov_b32_e32 v115, v116
	v_mov_b32_e32 v114, v112
	v_mov_b32_e32 v116, v113
	v_pk_add_f32 v[112:113], v[114:115], v[116:117]
	s_nop 0
	v_pk_fma_f32 v[112:113], v[112:113], s[22:23], v[152:153] op_sel_hi:[1,0,0]
	s_nop 0
	v_mul_f32_e32 v114, 0x4b800000, v113
	v_cmp_gt_f32_e64 s[4:5], s86, v113
	v_cmp_gt_f32_e32 vcc, s86, v112
	s_nop 0
	v_cndmask_b32_e64 v113, v113, v114, s[4:5]
	v_rsq_f32_e32 v113, v113
	s_nop 0
	v_mul_f32_e32 v114, 0x45800000, v113
	v_cndmask_b32_e64 v113, v113, v114, s[4:5]
	v_mul_f32_e32 v113, v122, v113
	v_mul_f32_e32 v114, 0x3ed53b94, v113
	v_pk_mul_f32 v[108:109], v[108:109], v[114:115] op_sel_hi:[1,0]
	v_pk_mul_f32 v[104:105], v[104:105], v[114:115] op_sel_hi:[1,0]
	v_pk_mul_f32 v[110:111], v[110:111], v[114:115] op_sel_hi:[1,0]
	v_pk_mul_f32 v[108:109], v[142:143], v[108:109]
	v_pk_mul_f32 v[106:107], v[106:107], v[114:115] op_sel_hi:[1,0]
	v_pk_mul_f32 v[104:105], v[138:139], v[104:105]
	v_cvt_pk_fp8_f32 v114, v108, v109
	v_cvt_pk_fp8_f32 v115, v104, v105
	v_pk_mul_f32 v[110:111], v[140:141], v[110:111]
	v_pk_mul_f32 v[106:107], v[136:137], v[106:107]
	v_cvt_pk_fp8_f32 v114, v110, v111 op_sel:[0,0,1]
	v_cvt_pk_fp8_f32 v115, v106, v107 op_sel:[0,0,1]
	v_mul_f32_e32 v105, 0x4b800000, v112
	v_cndmask_b32_e32 v105, v112, v105, vcc
	v_rsq_f32_e32 v105, v105
	global_store_dwordx2 v[118:119], v[114:115], off
	v_mov_b32_e32 v104, v243
	v_mul_f32_e32 v106, 0x45800000, v105
	v_cndmask_b32_e32 v105, v105, v106, vcc
	v_mul_f32_e32 v104, 0x3c800000, v104
	v_mul_f32_e32 v104, v104, v105
	v_mul_f32_e32 v104, 0x3ed53b94, v104
	v_pk_mul_f32 v[100:101], v[100:101], v[104:105] op_sel_hi:[1,0]
	v_pk_mul_f32 v[96:97], v[96:97], v[104:105] op_sel_hi:[1,0]
	v_pk_mul_f32 v[102:103], v[102:103], v[104:105] op_sel_hi:[1,0]
	v_pk_mul_f32 v[100:101], v[142:143], v[100:101]
	v_pk_mul_f32 v[98:99], v[98:99], v[104:105] op_sel_hi:[1,0]
	v_pk_mul_f32 v[96:97], v[138:139], v[96:97]
	v_cvt_pk_fp8_f32 v104, v100, v101
	v_cvt_pk_fp8_f32 v105, v96, v97
	v_pk_mul_f32 v[102:103], v[140:141], v[102:103]
	v_pk_mul_f32 v[98:99], v[136:137], v[98:99]
	v_cvt_pk_fp8_f32 v104, v102, v103 op_sel:[0,0,1]
	v_cvt_pk_fp8_f32 v105, v98, v99 op_sel:[0,0,1]
	v_lshlrev_b64 v[96:97], 11, v[158:159]
	v_lshl_add_u64 v[96:97], s[48:49], 0, v[96:97]
	v_lshl_add_u64 v[96:97], v[96:97], 0, s[60:61]
	v_lshl_add_u64 v[96:97], v[96:97], 0, v[128:129]
	global_store_dwordx2 v[96:97], v[104:105], off
	v_mov_b32_e32 v96, v244
	v_mul_f32_e32 v106, 0x3c800000, v96
	v_lshl_add_u32 v96, v189, 4, s0
	ds_read_b128 v[96:99], v96
	s_waitcnt lgkmcnt(0)
	v_mov_b32_e32 v100, v97
	v_mov_b32_e32 v101, v98
	v_mov_b32_e32 v97, v99
	v_pk_add_f32 v[100:101], v[100:101], v[96:97]
	v_lshlrev_b64 v[96:97], 11, v[154:155]
	v_lshl_add_u64 v[96:97], s[48:49], 0, v[96:97]
	v_lshl_add_u64 v[96:97], v[96:97], 0, s[60:61]
	v_lshl_add_u64 v[102:103], v[96:97], 0, v[128:129]
	v_lshl_add_u32 v96, v190, 4, s0
	ds_read_b128 v[96:99], v96
	s_waitcnt lgkmcnt(0)
	v_mov_b32_e32 v104, v97
	v_mov_b32_e32 v105, v98
	v_mov_b32_e32 v97, v99
	v_pk_add_f32 v[96:97], v[104:105], v[96:97]
	v_mov_b32_e32 v99, v100
	v_mov_b32_e32 v98, v96
	v_mov_b32_e32 v100, v97
	v_pk_add_f32 v[96:97], v[98:99], v[100:101]
	s_nop 0
	v_pk_fma_f32 v[96:97], v[96:97], s[22:23], v[152:153] op_sel_hi:[1,0,0]
	s_nop 0
	v_mul_f32_e32 v98, 0x4b800000, v97
	v_cmp_gt_f32_e64 s[4:5], s86, v97
	v_cmp_gt_f32_e32 vcc, s86, v96
	s_nop 0
	v_cndmask_b32_e64 v97, v97, v98, s[4:5]
	v_rsq_f32_e32 v97, v97
	s_nop 0
	v_mul_f32_e32 v98, 0x45800000, v97
	v_cndmask_b32_e64 v97, v97, v98, s[4:5]
	v_mul_f32_e32 v97, v106, v97
	v_mul_f32_e32 v98, 0x3ed53b94, v97
	v_pk_mul_f32 v[92:93], v[92:93], v[98:99] op_sel_hi:[1,0]
	v_pk_mul_f32 v[88:89], v[88:89], v[98:99] op_sel_hi:[1,0]
	v_pk_mul_f32 v[94:95], v[94:95], v[98:99] op_sel_hi:[1,0]
	v_pk_mul_f32 v[92:93], v[142:143], v[92:93]
	v_pk_mul_f32 v[90:91], v[90:91], v[98:99] op_sel_hi:[1,0]
	v_pk_mul_f32 v[88:89], v[138:139], v[88:89]
	v_cvt_pk_fp8_f32 v98, v92, v93
	v_cvt_pk_fp8_f32 v99, v88, v89
	v_pk_mul_f32 v[94:95], v[140:141], v[94:95]
	v_pk_mul_f32 v[90:91], v[136:137], v[90:91]
	v_cvt_pk_fp8_f32 v98, v94, v95 op_sel:[0,0,1]
	v_cvt_pk_fp8_f32 v99, v90, v91 op_sel:[0,0,1]
	v_mul_f32_e32 v89, 0x4b800000, v96
	v_cndmask_b32_e32 v89, v96, v89, vcc
	v_rsq_f32_e32 v89, v89
	global_store_dwordx2 v[102:103], v[98:99], off
	v_mov_b32_e32 v88, v245
	v_mul_f32_e32 v90, 0x45800000, v89
	v_cndmask_b32_e32 v89, v89, v90, vcc
	v_mul_f32_e32 v88, 0x3c800000, v88
	v_mul_f32_e32 v88, v88, v89
	v_mul_f32_e32 v88, 0x3ed53b94, v88
	v_pk_mul_f32 v[84:85], v[84:85], v[88:89] op_sel_hi:[1,0]
	v_pk_mul_f32 v[80:81], v[80:81], v[88:89] op_sel_hi:[1,0]
	v_pk_mul_f32 v[86:87], v[86:87], v[88:89] op_sel_hi:[1,0]
	v_pk_mul_f32 v[84:85], v[142:143], v[84:85]
	v_pk_mul_f32 v[82:83], v[82:83], v[88:89] op_sel_hi:[1,0]
	v_pk_mul_f32 v[80:81], v[138:139], v[80:81]
	v_cvt_pk_fp8_f32 v88, v84, v85
	v_cvt_pk_fp8_f32 v89, v80, v81
	v_pk_mul_f32 v[86:87], v[140:141], v[86:87]
	v_pk_mul_f32 v[82:83], v[136:137], v[82:83]
	v_cvt_pk_fp8_f32 v88, v86, v87 op_sel:[0,0,1]
	v_cvt_pk_fp8_f32 v89, v82, v83 op_sel:[0,0,1]
	v_lshlrev_b64 v[80:81], 11, v[148:149]
	v_lshl_add_u64 v[80:81], s[48:49], 0, v[80:81]
	v_lshl_add_u64 v[80:81], v[80:81], 0, s[60:61]
	v_lshl_add_u64 v[80:81], v[80:81], 0, v[128:129]
	global_store_dwordx2 v[80:81], v[88:89], off
	v_mov_b32_e32 v80, v246
	v_mul_f32_e32 v90, 0x3c800000, v80
	v_lshl_add_u32 v80, v187, 4, s0
	ds_read_b128 v[80:83], v80
	s_waitcnt lgkmcnt(0)
; #define LAS __attribute__((address_space(3)))
; __device__ __forceinline__ unsigned cvt_pk4_fp8(float a, float b, float c, float d) { int w; asm("" : "=v"(w));     w = __builtin_amdgcn_cvt_pk_fp8_f32(a, b, w, false); w = __builtin_amdgcn_cvt_pk_fp8_f32(c, d, w, true); return (unsigned)w; }
;     __device__ __forceinline__ void operator()(const f32x4 (&acc)[2][2][4][2], const Unit& u, int wr, int wc, int fr, int fq) const {
;     ...
;             for (int m = 0; m < 4; ++m) { const int rl = rl0 + ai * HALF + m; const float c = rs[u.pm * BM + rl] * (1.0f / W8_SCALE);
;                 const f32x4 pq = *(const LAS f32x4*)(xch + rl * 4); const float rstd = rsqrtf(((pq[0] + pq[1]) + (pq[2] + pq[3])) * (1.0f / 128.0f) + RMS_EPS) * c;
;                 const f32x4 v0 = acc[ai][0][m][0] * (rstd * KSC_) * g0, v1 = acc[ai][0][m][1] * (rstd * KSC_) * g1;
;                 u32x2 w; w.x = cvt_pk4_fp8(v0[0], v0[1], v0[2], v0[3]); w.y = cvt_pk4_fp8(v1[0], v1[1], v1[2], v1[3]);
;                 *(u32x2*)(K8 + (size_t)(u.pm * BM + rl) * 2048 + u.pn * 128 + kpos) = w; }
;         const int t0 = u.pm * BM, bb = t0 / SEQ, tile0 = (t0 % SEQ) / 64 + wr;
; #pragma unroll
;         for (int ai = 0; ai < 2; ++ai) { unsigned char* tb = V8T + ((size_t)((bb * NH + u.pn) * (SEQ / 64) + tile0 + 2 * ai)) * 8192 + 4 * ((fr >> 1) & 3);
;             const f32x4 c4 = *(const f32x4*)(rs + u.pm * BM + rl0 + ai * HALF) * (1.0f / W8_SCALE);
; #pragma unroll
;             for (int e = 0; e < 8; ++e) { const int D = dl0 + e, ch = 2 * (fr & 1) + (fr >> 3);
;                 const unsigned w = cvt_pk4_fp8(acc[ai][1][0][e >> 2][e & 3] * c4[0], acc[ai][1][1][e >> 2][e & 3] * c4[1], acc[ai][1][2][e >> 2][e & 3] * c4[2], acc[ai][1][3][e >> 2][e & 3] * c4[3]);
;                 *(unsigned*)(tb + D * 64 + (((ch ^ (D >> 2)) & 3) << 4)) = w; } }
	v_mov_b32_e32 v84, v81
	v_mov_b32_e32 v85, v82
	v_mov_b32_e32 v81, v83
	v_pk_add_f32 v[84:85], v[84:85], v[80:81]
	v_lshlrev_b64 v[80:81], 11, v[144:145]
	v_lshl_add_u64 v[80:81], s[48:49], 0, v[80:81]
	v_lshl_add_u64 v[80:81], v[80:81], 0, s[60:61]
	v_lshl_add_u64 v[86:87], v[80:81], 0, v[128:129]
	v_add_u32_e32 v80, s0, v188
	ds_read_b128 v[80:83], v80
	s_ashr_i32 s0, s56, 31
	s_lshr_b32 s0, s0, 27
	s_add_i32 s0, s56, s0
	s_lshl_b32 s0, s0, 6
	s_waitcnt lgkmcnt(0)
	v_mov_b32_e32 v88, v81
	v_mov_b32_e32 v89, v82
	v_mov_b32_e32 v81, v83
	v_pk_add_f32 v[80:81], v[88:89], v[80:81]
	v_mov_b32_e32 v83, v84
	v_mov_b32_e32 v82, v80
	v_mov_b32_e32 v84, v81
	v_pk_add_f32 v[80:81], v[82:83], v[84:85]
	s_and_b32 s0, s0, 0xfffff800
	v_pk_fma_f32 v[80:81], v[80:81], s[22:23], v[152:153] op_sel_hi:[1,0,0]
	s_nop 0
	v_mul_f32_e32 v82, 0x4b800000, v81
	v_cmp_gt_f32_e64 s[4:5], s86, v81
	v_cmp_gt_f32_e32 vcc, s86, v80
	s_nop 0
	v_cndmask_b32_e64 v81, v81, v82, s[4:5]
	v_rsq_f32_e32 v81, v81
	s_nop 0
	v_mul_f32_e32 v82, 0x45800000, v81
	v_cndmask_b32_e64 v81, v81, v82, s[4:5]
	v_mul_f32_e32 v81, v90, v81
	v_mul_f32_e32 v82, 0x3ed53b94, v81
	v_pk_mul_f32 v[76:77], v[76:77], v[82:83] op_sel_hi:[1,0]
	v_pk_mul_f32 v[72:73], v[72:73], v[82:83] op_sel_hi:[1,0]
	v_pk_mul_f32 v[78:79], v[78:79], v[82:83] op_sel_hi:[1,0]
	v_pk_mul_f32 v[76:77], v[142:143], v[76:77]
	v_pk_mul_f32 v[74:75], v[74:75], v[82:83] op_sel_hi:[1,0]
	v_pk_mul_f32 v[72:73], v[138:139], v[72:73]
	v_cvt_pk_fp8_f32 v82, v76, v77
	v_cvt_pk_fp8_f32 v83, v72, v73
	v_pk_mul_f32 v[78:79], v[140:141], v[78:79]
	v_pk_mul_f32 v[74:75], v[136:137], v[74:75]
	v_cvt_pk_fp8_f32 v82, v78, v79 op_sel:[0,0,1]
	v_cvt_pk_fp8_f32 v83, v74, v75 op_sel:[0,0,1]
	v_mul_f32_e32 v73, 0x4b800000, v80
	v_cndmask_b32_e32 v73, v80, v73, vcc
	v_rsq_f32_e32 v73, v73
	global_store_dwordx2 v[86:87], v[82:83], off
	v_mov_b32_e32 v72, v247
	s_add_i32 s4, s60, s36
	v_mul_f32_e32 v74, 0x45800000, v73
	v_cndmask_b32_e32 v73, v73, v74, vcc
	s_add_i32 s0, s4, s0
	s_add_i32 s0, s0, s1
	s_lshl_b64 s[4:5], s[58:59], 2
	s_add_u32 s4, s12, s4
	s_addc_u32 s5, s13, s5
	v_lshrrev_b32_e32 v74, 3, v184
	s_ashr_i32 s1, s0, 31
	s_lshl_b64 s[0:1], s[0:1], 13
	s_andn2_b64 vcc, exec, s[26:27]
	v_mul_f32_e32 v72, 0x3c800000, v72
	v_mul_f32_e32 v72, v72, v73
	v_mul_f32_e32 v72, 0x3ed53b94, v72
	v_pk_mul_f32 v[68:69], v[68:69], v[72:73] op_sel_hi:[1,0]
	v_pk_mul_f32 v[64:65], v[64:65], v[72:73] op_sel_hi:[1,0]
	v_pk_mul_f32 v[70:71], v[70:71], v[72:73] op_sel_hi:[1,0]
	v_pk_mul_f32 v[68:69], v[142:143], v[68:69]
	v_pk_mul_f32 v[66:67], v[66:67], v[72:73] op_sel_hi:[1,0]
	v_pk_mul_f32 v[64:65], v[138:139], v[64:65]
	v_cvt_pk_fp8_f32 v72, v68, v69
	v_cvt_pk_fp8_f32 v73, v64, v65
	v_pk_mul_f32 v[70:71], v[140:141], v[70:71]
	v_pk_mul_f32 v[66:67], v[136:137], v[66:67]
	v_cvt_pk_fp8_f32 v72, v70, v71 op_sel:[0,0,1]
	v_cvt_pk_fp8_f32 v73, v66, v67 op_sel:[0,0,1]
	v_lshlrev_b64 v[64:65], 11, v[132:133]
	v_lshl_add_u64 v[64:65], s[48:49], 0, v[64:65]
	v_lshl_add_u64 v[64:65], v[64:65], 0, s[60:61]
	v_lshl_add_u64 v[64:65], v[64:65], 0, v[128:129]
	global_store_dwordx2 v[64:65], v[72:73], off
	v_lshlrev_b32_e32 v72, 2, v185
	v_mov_b32_e32 v66, v240
	v_mov_b32_e32 v67, v241
	v_mov_b32_e32 v68, v242
	v_mov_b32_e32 v69, v243
	v_lshlrev_b32_e32 v73, 1, v184
	v_or_b32_e32 v75, v73, v74
	v_and_b32_e32 v128, 12, v73
	v_lshl_add_u64 v[64:65], s[50:51], 0, v[128:129]
	v_lshl_add_u64 v[64:65], v[64:65], 0, s[0:1]
	s_mov_b64 s[0:1], 0x4000
	v_pk_mul_f32 v[70:71], v[66:67], s[20:21] op_sel_hi:[1,0]
	s_nop 0
	v_mul_f32_e32 v60, v60, v70
	v_mul_f32_e32 v56, v56, v71
	v_cvt_pk_fp8_f32 v78, v60, v56
	v_pk_mul_f32 v[68:69], v[68:69], s[20:21] op_sel_hi:[1,0]
	v_mul_f32_e32 v52, v52, v68
	v_mul_f32_e32 v48, v48, v69
	v_cvt_pk_fp8_f32 v78, v52, v48 op_sel:[0,0,1]
	v_lshlrev_b32_e32 v48, 4, v75
	v_bitop3_b32 v128, v186, 48, v48 bitop3:0x48
	v_mul_f32_e32 v48, v61, v70
	v_mul_f32_e32 v52, v57, v71
	v_cvt_pk_fp8_f32 v56, v48, v52
	v_mul_f32_e32 v53, v53, v68
	v_mul_f32_e32 v49, v49, v69
	v_mul_f32_e32 v48, v62, v70
	v_cvt_pk_fp8_f32 v56, v53, v49 op_sel:[0,0,1]
	v_mul_f32_e32 v49, v58, v71
	v_cvt_pk_fp8_f32 v53, v48, v49
	v_mul_f32_e32 v52, v54, v68
	v_mul_f32_e32 v50, v50, v69
	v_mul_f32_e32 v48, v63, v70
	v_cvt_pk_fp8_f32 v53, v52, v50 op_sel:[0,0,1]
	v_mul_f32_e32 v49, v59, v71
	v_cvt_pk_fp8_f32 v52, v48, v49
	v_mul_f32_e32 v44, v44, v70
	v_mul_f32_e32 v40, v40, v71
	v_cvt_pk_fp8_f32 v54, v44, v40
	v_mul_f32_e32 v50, v55, v68
	v_mul_f32_e32 v51, v51, v69
	v_cvt_pk_fp8_f32 v52, v50, v51 op_sel:[0,0,1]
	v_or_b32_e32 v50, 4, v130
	v_mul_f32_e32 v36, v36, v68
	v_mul_f32_e32 v32, v32, v69
	v_cvt_pk_fp8_f32 v54, v36, v32 op_sel:[0,0,1]
	v_lshrrev_b32_e32 v32, 2, v50
	v_bitop3_b32 v32, v32, v73, v74 bitop3:0x1e
	v_lshlrev_b32_e32 v32, 4, v32
	v_lshlrev_b32_e32 v48, 6, v50
	v_and_b32_e32 v50, 48, v32
	v_mul_f32_e32 v32, v45, v70
	v_mul_f32_e32 v40, v41, v71
	v_cvt_pk_fp8_f32 v44, v32, v40
; __device__ __forceinline__ unsigned cvt_pk4_fp8(float a, float b, float c, float d) { int w; asm("" : "=v"(w));     w = __builtin_amdgcn_cvt_pk_fp8_f32(a, b, w, false); w = __builtin_amdgcn_cvt_pk_fp8_f32(c, d, w, true); return (unsigned)w; }
;     __device__ __forceinline__ void operator()(const f32x4 (&acc)[2][2][4][2], const Unit& u, int wr, int wc, int fr, int fq) const {
;     ...
;         const int t0 = u.pm * BM, bb = t0 / SEQ, tile0 = (t0 % SEQ) / 64 + wr;
; #pragma unroll
;         for (int ai = 0; ai < 2; ++ai) { unsigned char* tb = V8T + ((size_t)((bb * NH + u.pn) * (SEQ / 64) + tile0 + 2 * ai)) * 8192 + 4 * ((fr >> 1) & 3);
;             const f32x4 c4 = *(const f32x4*)(rs + u.pm * BM + rl0 + ai * HALF) * (1.0f / W8_SCALE);
; #pragma unroll
;             for (int e = 0; e < 8; ++e) { const int D = dl0 + e, ch = 2 * (fr & 1) + (fr >> 3);
;                 const unsigned w = cvt_pk4_fp8(acc[ai][1][0][e >> 2][e & 3] * c4[0], acc[ai][1][1][e >> 2][e & 3] * c4[1], acc[ai][1][2][e >> 2][e & 3] * c4[2], acc[ai][1][3][e >> 2][e & 3] * c4[3]);
;                 *(unsigned*)(tb + D * 64 + (((ch ^ (D >> 2)) & 3) << 4)) = w; } }
;         asm volatile("s_waitcnt lgkmcnt(0)" ::: "memory"); __builtin_amdgcn_s_barrier(); asm volatile("" ::: "memory");
	v_or_b32_e32 v36, 5, v130
	v_mul_f32_e32 v37, v37, v68
	v_mul_f32_e32 v33, v33, v69
	v_lshlrev_b32_e32 v32, 6, v36
	v_lshrrev_b32_e32 v36, 2, v36
	v_cvt_pk_fp8_f32 v44, v37, v33 op_sel:[0,0,1]
	v_bitop3_b32 v36, v36, v73, v74 bitop3:0x1e
	v_ashrrev_i32_e32 v33, 31, v32
	v_lshlrev_b32_e32 v36, 4, v36
	v_lshl_add_u64 v[40:41], v[64:65], 0, v[32:33]
	v_and_b32_e32 v36, 48, v36
	v_mov_b32_e32 v37, v129
	v_lshl_add_u64 v[40:41], v[40:41], 0, v[36:37]
	global_store_dword v[40:41], v44, off
	v_mul_f32_e32 v40, v46, v70
	v_mul_f32_e32 v41, v42, v71
	v_cvt_pk_fp8_f32 v42, v40, v41
	v_lshlrev_b32_e32 v66, 6, v130
	v_ashrrev_i32_e32 v67, 31, v66
	v_lshl_add_u64 v[76:77], v[64:65], 0, v[66:67]
	v_or_b32_e32 v44, 6, v130
	v_mul_f32_e32 v38, v38, v68
	v_mul_f32_e32 v34, v34, v69
	v_lshl_add_u64 v[76:77], v[76:77], 0, v[128:129]
	v_ashrrev_i32_e32 v49, 31, v48
	v_cvt_pk_fp8_f32 v42, v38, v34 op_sel:[0,0,1]
	v_lshrrev_b32_e32 v34, 2, v44
	global_store_dword v[76:77], v53, off offset:128
	global_store_dword v[76:77], v52, off offset:192
	v_lshl_add_u64 v[52:53], v[64:65], 0, v[48:49]
	v_mov_b32_e32 v51, v129
	v_lshlrev_b32_e32 v40, 6, v44
	v_bitop3_b32 v34, v34, v73, v74 bitop3:0x1e
	v_lshl_add_u64 v[52:53], v[52:53], 0, v[50:51]
	v_ashrrev_i32_e32 v41, 31, v40
	v_lshlrev_b32_e32 v34, 4, v34
	global_store_dword v[52:53], v54, off
	v_lshl_add_u64 v[52:53], v[64:65], 0, v[40:41]
	v_and_b32_e32 v44, 48, v34
	v_mov_b32_e32 v45, v129
	v_lshl_add_u64 v[52:53], v[52:53], 0, v[44:45]
	global_store_dword v[52:53], v42, off
	v_mul_f32_e32 v38, v47, v70
	v_mul_f32_e32 v42, v43, v71
	v_cvt_pk_fp8_f32 v46, v38, v42
	v_or_b32_e32 v34, 7, v130
	v_mul_f32_e32 v39, v39, v68
	v_mul_f32_e32 v35, v35, v69
	v_lshlrev_b32_e32 v38, 6, v34
	v_lshrrev_b32_e32 v34, 2, v34
	v_cvt_pk_fp8_f32 v46, v39, v35 op_sel:[0,0,1]
	v_bitop3_b32 v34, v34, v73, v74 bitop3:0x1e
	v_ashrrev_i32_e32 v39, 31, v38
	v_lshlrev_b32_e32 v34, 4, v34
	v_lshl_add_u64 v[42:43], v[64:65], 0, v[38:39]
	v_and_b32_e32 v34, 48, v34
	v_mov_b32_e32 v35, v129
	v_lshl_add_u64 v[42:43], v[42:43], 0, v[34:35]
	global_store_dword v[76:77], v78, off
	global_store_dword v[76:77], v56, off offset:64
	global_store_dword v[42:43], v46, off
	v_mov_b32_e32 v52, v244
	v_mov_b32_e32 v53, v245
	v_mov_b32_e32 v54, v246
	v_mov_b32_e32 v55, v247
	v_lshl_add_u64 v[42:43], v[64:65], 0, s[0:1]
	s_mov_b64 s[4:5], -1
	v_pk_mul_f32 v[52:53], v[52:53], s[20:21] op_sel_hi:[1,0]
	s_nop 0
	v_mul_f32_e32 v28, v28, v52
	v_mul_f32_e32 v24, v24, v53
	v_cvt_pk_fp8_f32 v56, v28, v24
	v_pk_mul_f32 v[46:47], v[54:55], s[20:21] op_sel_hi:[1,0]
	v_mul_f32_e32 v20, v20, v46
	v_mul_f32_e32 v16, v16, v47
	v_cvt_pk_fp8_f32 v56, v20, v16 op_sel:[0,0,1]
	v_mul_f32_e32 v16, v29, v52
	v_mul_f32_e32 v20, v25, v53
	v_cvt_pk_fp8_f32 v24, v16, v20
	v_mul_f32_e32 v21, v21, v46
	v_mul_f32_e32 v17, v17, v47
	v_mul_f32_e32 v16, v30, v52
	v_cvt_pk_fp8_f32 v24, v21, v17 op_sel:[0,0,1]
	v_mul_f32_e32 v17, v26, v53
	v_cvt_pk_fp8_f32 v21, v16, v17
	v_mul_f32_e32 v20, v22, v46
	v_mul_f32_e32 v18, v18, v47
	v_mul_f32_e32 v16, v31, v52
	v_cvt_pk_fp8_f32 v21, v20, v18 op_sel:[0,0,1]
	v_mul_f32_e32 v17, v27, v53
	v_cvt_pk_fp8_f32 v20, v16, v17
	v_mul_f32_e32 v18, v23, v46
	v_mul_f32_e32 v19, v19, v47
	v_mul_f32_e32 v12, v12, v52
	v_cvt_pk_fp8_f32 v20, v18, v19 op_sel:[0,0,1]
	v_mul_f32_e32 v8, v8, v53
	v_cvt_pk_fp8_f32 v18, v12, v8
	v_mul_f32_e32 v4, v4, v46
	v_mul_f32_e32 v0, v0, v47
	v_cvt_pk_fp8_f32 v18, v4, v0 op_sel:[0,0,1]
	v_mul_f32_e32 v0, v13, v52
	v_mul_f32_e32 v4, v9, v53
	v_cvt_pk_fp8_f32 v8, v0, v4
	v_mul_f32_e32 v5, v5, v46
	v_mul_f32_e32 v1, v1, v47
	v_mul_f32_e32 v4, v6, v46
	v_cvt_pk_fp8_f32 v8, v5, v1 op_sel:[0,0,1]
	v_lshl_add_u64 v[0:1], v[42:43], 0, v[32:33]
	v_lshl_add_u64 v[0:1], v[0:1], 0, v[36:37]
	global_store_dword v[0:1], v8, off
	v_mul_f32_e32 v0, v14, v52
	v_mul_f32_e32 v1, v10, v53
	v_cvt_pk_fp8_f32 v5, v0, v1
	v_mul_f32_e32 v2, v2, v47
	v_lshl_add_u64 v[0:1], v[42:43], 0, v[40:41]
	v_lshl_add_u64 v[0:1], v[0:1], 0, v[44:45]
	v_cvt_pk_fp8_f32 v5, v4, v2 op_sel:[0,0,1]
	v_mul_f32_e32 v2, v7, v46
	v_mul_f32_e32 v3, v3, v47
	v_lshl_add_u64 v[54:55], v[42:43], 0, v[66:67]
	global_store_dword v[0:1], v5, off
	v_mul_f32_e32 v0, v15, v52
	v_mul_f32_e32 v1, v11, v53
	v_cvt_pk_fp8_f32 v131, v0, v1
	v_lshl_add_u64 v[16:17], v[42:43], 0, v[48:49]
	v_lshl_add_u64 v[0:1], v[42:43], 0, v[38:39]
	v_lshl_add_u64 v[54:55], v[54:55], 0, v[128:129]
	v_cvt_pk_fp8_f32 v131, v2, v3 op_sel:[0,0,1]
	v_lshl_add_u64 v[16:17], v[16:17], 0, v[50:51]
	v_lshl_add_u64 v[0:1], v[0:1], 0, v[34:35]
	global_store_dword v[54:55], v56, off
	global_store_dword v[54:55], v24, off offset:64
	global_store_dword v[54:55], v21, off offset:128
	global_store_dword v[54:55], v20, off offset:192
	global_store_dword v[16:17], v18, off
	global_store_dword v[0:1], v131, off
	s_waitcnt lgkmcnt(0)
	s_barrier
	s_cbranch_vccnz .LBB0_390
	s_andn2_b64 vcc, exec, s[6:7]
	s_cbranch_vccnz .LBB0_389
	s_barrier
	s_branch .LBB0_389

; __device__ __forceinline__ cgptr cuni(const void* p) { const unsigned long long v = (unsigned long long)p; const unsigned lo = __builtin_amdgcn_readfirstlane((unsigned)v), hi = __builtin_amdgcn_readfirstlane((unsigned)(v >> 32)); return (cgptr)(((unsigned long long)hi << 32) | lo); }
; __device__ __forceinline__ ConvItem conv_decode(int it, const float* wgu, const float* wd, unsigned char* WguT, unsigned char* WdT) {
;     constexpr int I_GU = NE * 16 * 128;
;     ConvItem c; int r = it, nbn, N; const float* src; unsigned char* dstp; bool gu;
;     if (r < I_GU) { const int e = r / (16 * 128); r -= e * (16 * 128); N = 4096; nbn = 128; src = wgu + (size_t)e * DM * 4096; dstp = WguT + (size_t)e * 4096 * DM; gu = true; }
;     else { r -= I_GU; const int e = r / (16 * 64); r -= e * (16 * 64); N = DM; nbn = 64; src = wd + (size_t)e * DFF * DM; dstp = WdT + (size_t)e * DM * DFF; gu = false; }
;     const int kb = r / nbn, nb = r - kb * nbn, n0 = nb * 32, k0 = kb * 128; int dst = n0;
;     if (gu) { const int j = n0 & 2047; dst = (j >> 7) * 256 + (j & 127) + ((n0 >= 2048) ? 128 : 0); }
;     c.src = cuni(src + (size_t)k0 * N + n0); c.dstp = cuni(dstp + (size_t)dst * DM + k0); c.N4 = (unsigned)N * 4u;
;     return c;
; }
.LBB0_487:
	v_cvt_f32_ubyte0_e32 v0, s10
	v_rcp_iflag_f32_e32 v0, v0
	s_sub_i32 s12, 0, s10
	s_abs_i32 s11, s9
	s_add_i32 s1, s3, s44
	v_mul_f32_e32 v0, 0x4f7ffffe, v0
	v_cvt_u32_f32_e32 v0, v0
	s_ashr_i32 s3, s9, 31
	v_readfirstlane_b32 s17, v0
	s_mul_i32 s12, s12, s17
	s_mul_hi_u32 s12, s17, s12
	s_add_i32 s17, s17, s12
	s_mul_hi_u32 s12, s11, s17
	s_mul_i32 s17, s12, s10
	s_sub_i32 s11, s11, s17
	s_add_i32 s24, s12, 1
	s_sub_i32 s17, s11, s10
	s_cmp_ge_u32 s11, s10
	s_cselect_b32 s12, s24, s12
	s_cselect_b32 s11, s17, s11
	s_add_i32 s17, s12, 1
	s_cmp_ge_u32 s11, s10
	s_cselect_b32 s11, s17, s12
	s_xor_b32 s11, s11, s3
	s_sub_i32 s3, s11, s3
	s_mul_i32 s10, s3, s10
	s_sub_i32 s11, s9, s10
	s_lshl_b32 s10, s11, 5
	s_lshl_b32 s9, s9, 6
	s_and_b32 s9, s9, 0xf00
	s_and_b32 s12, s10, 0x60
	s_or_b32 s9, s12, s9
	s_cmp_gt_i32 s11, 63
	s_cselect_b32 s11, 0x80, 0
	s_or_b32 s9, s9, s11
	s_and_b64 s[14:15], s[14:15], exec
	s_cselect_b32 s14, s9, s10
	s_lshl_b32 s3, s3, 7
	s_mul_hi_i32 s25, s3, s8
	s_mul_i32 s24, s3, s8
	s_ashr_i32 s9, s3, 31
	s_lshl_b64 s[24:25], s[24:25], 2
	s_add_u32 s12, s22, s24
	s_addc_u32 s15, s23, s25
	s_ashr_i32 s11, s10, 31
	s_lshl_b64 s[10:11], s[10:11], 2
	s_add_u32 s22, s12, s10
	s_addc_u32 s23, s15, s11
	s_ashr_i32 s15, s14, 31
	s_lshl_b64 s[10:11], s[14:15], 11
	s_add_u32 s10, s20, s10
	s_addc_u32 s11, s21, s11
	s_add_u32 s14, s10, s3
	s_addc_u32 s15, s11, s9
	s_lshl_b32 s3, s8, 5
	v_mul_lo_u32 v0, v130, s8
	s_add_u32 s10, s22, s3
	v_or_b32_e32 v56, v0, v131
	s_addc_u32 s11, s23, 0
	s_lshl_b32 s3, s8, 6
	global_load_dwordx4 v[4:7], v56, s[22:23] nt
	global_load_dwordx4 v[0:3], v56, s[10:11] nt
	s_add_u32 s10, s22, s3
	s_addc_u32 s11, s23, 0
	s_mul_i32 s3, s8, 0x60
	s_add_u32 s20, s22, s3
	s_addc_u32 s21, s23, 0
	s_lshl_b32 s3, s8, 7
	global_load_dwordx4 v[12:15], v56, s[10:11] nt
	global_load_dwordx4 v[8:11], v56, s[20:21] nt
	s_add_u32 s10, s22, s3
	s_addc_u32 s11, s23, 0
	s_mul_i32 s3, s8, 0xa0
	s_add_u32 s20, s22, s3
	s_addc_u32 s21, s23, 0
	s_mul_i32 s3, s8, 0xc0
	global_load_dwordx4 v[20:23], v56, s[10:11] nt
	global_load_dwordx4 v[16:19], v56, s[20:21] nt
	s_add_u32 s10, s22, s3
	s_addc_u32 s11, s23, 0
	s_mul_i32 s3, s8, 0xe0
	s_add_u32 s20, s22, s3
	s_addc_u32 s21, s23, 0
	s_lshl_b32 s3, s8, 8
	global_load_dwordx4 v[28:31], v56, s[10:11] nt
	global_load_dwordx4 v[24:27], v56, s[20:21] nt
	s_add_u32 s10, s22, s3
	s_addc_u32 s11, s23, 0
	s_mul_i32 s3, s8, 0x120
	s_add_u32 s20, s22, s3
	s_addc_u32 s21, s23, 0
	s_mul_i32 s3, s8, 0x140
	global_load_dwordx4 v[36:39], v56, s[10:11] nt
	global_load_dwordx4 v[32:35], v56, s[20:21] nt
	s_add_u32 s10, s22, s3
	s_addc_u32 s11, s23, 0
	s_mul_i32 s3, s8, 0x160
	s_add_u32 s20, s22, s3
	s_addc_u32 s21, s23, 0
	s_mul_i32 s3, s8, 0x180
	global_load_dwordx4 v[44:47], v56, s[10:11] nt
	global_load_dwordx4 v[40:43], v56, s[20:21] nt
	s_add_u32 s10, s22, s3
	s_addc_u32 s11, s23, 0
	s_mul_i32 s3, s8, 0x1a0
	s_add_u32 s20, s22, s3
	s_addc_u32 s21, s23, 0
	s_mul_i32 s3, s8, 0x1c0
	global_load_dwordx4 v[52:55], v56, s[10:11] nt
	global_load_dwordx4 v[48:51], v56, s[20:21] nt
	s_add_u32 s10, s22, s3
	s_addc_u32 s11, s23, 0
	s_mul_i32 s3, s8, 0x1e0
	s_add_u32 s8, s22, s3
	s_addc_u32 s9, s23, 0
	global_load_dwordx4 v[60:63], v56, s[10:11] nt
	s_nop 0
	global_load_dwordx4 v[56:59], v56, s[8:9] nt
	s_waitcnt vmcnt(35)
	v_pk_mul_f32 v[126:127], v[126:127], s[16:17] op_sel_hi:[1,0]
	v_pk_mul_f32 v[124:125], v[124:125], s[16:17] op_sel_hi:[1,0]
	s_waitcnt vmcnt(34)
	v_pk_mul_f32 v[118:119], v[118:119], s[16:17] op_sel_hi:[1,0]
	v_pk_mul_f32 v[116:117], v[116:117], s[16:17] op_sel_hi:[1,0]
	ds_write_b128 v132, v[124:127]
	ds_write_b128 v133, v[116:119]
	s_waitcnt vmcnt(33)
	v_pk_mul_f32 v[118:119], v[122:123], s[16:17] op_sel_hi:[1,0]
	v_pk_mul_f32 v[116:117], v[120:121], s[16:17] op_sel_hi:[1,0]
	s_waitcnt vmcnt(32)
	v_pk_mul_f32 v[110:111], v[110:111], s[16:17] op_sel_hi:[1,0]
	v_pk_mul_f32 v[108:109], v[108:109], s[16:17] op_sel_hi:[1,0]
	ds_write_b128 v134, v[116:119]
	ds_write_b128 v135, v[108:111]
	s_waitcnt vmcnt(31)
	v_pk_mul_f32 v[110:111], v[114:115], s[16:17] op_sel_hi:[1,0]
	v_pk_mul_f32 v[108:109], v[112:113], s[16:17] op_sel_hi:[1,0]
	s_waitcnt vmcnt(30)
	v_pk_mul_f32 v[102:103], v[102:103], s[16:17] op_sel_hi:[1,0]
	v_pk_mul_f32 v[100:101], v[100:101], s[16:17] op_sel_hi:[1,0]
	ds_write_b128 v136, v[108:111]
	ds_write_b128 v137, v[100:103]
	s_waitcnt vmcnt(29)
	v_pk_mul_f32 v[102:103], v[106:107], s[16:17] op_sel_hi:[1,0]
	v_pk_mul_f32 v[100:101], v[104:105], s[16:17] op_sel_hi:[1,0]
	s_waitcnt vmcnt(28)
	v_pk_mul_f32 v[94:95], v[94:95], s[16:17] op_sel_hi:[1,0]
	v_pk_mul_f32 v[92:93], v[92:93], s[16:17] op_sel_hi:[1,0]
	ds_write_b128 v138, v[100:103]
	ds_write_b128 v139, v[92:95]
	s_waitcnt vmcnt(27)
	v_pk_mul_f32 v[94:95], v[98:99], s[16:17] op_sel_hi:[1,0]
	v_pk_mul_f32 v[92:93], v[96:97], s[16:17] op_sel_hi:[1,0]
	s_waitcnt vmcnt(26)
	v_pk_mul_f32 v[86:87], v[86:87], s[16:17] op_sel_hi:[1,0]
	v_pk_mul_f32 v[84:85], v[84:85], s[16:17] op_sel_hi:[1,0]
	ds_write_b128 v140, v[92:95]
	ds_write_b128 v141, v[84:87]
	s_waitcnt vmcnt(25)
	v_pk_mul_f32 v[86:87], v[90:91], s[16:17] op_sel_hi:[1,0]
	v_pk_mul_f32 v[84:85], v[88:89], s[16:17] op_sel_hi:[1,0]
	s_waitcnt vmcnt(24)
	v_pk_mul_f32 v[78:79], v[78:79], s[16:17] op_sel_hi:[1,0]
	v_pk_mul_f32 v[76:77], v[76:77], s[16:17] op_sel_hi:[1,0]
	ds_write_b128 v142, v[84:87]
	ds_write_b128 v143, v[76:79]
	s_waitcnt vmcnt(23)
	v_pk_mul_f32 v[78:79], v[82:83], s[16:17] op_sel_hi:[1,0]
	v_pk_mul_f32 v[76:77], v[80:81], s[16:17] op_sel_hi:[1,0]
	s_waitcnt vmcnt(22)
	v_pk_mul_f32 v[70:71], v[70:71], s[16:17] op_sel_hi:[1,0]
	v_pk_mul_f32 v[68:69], v[68:69], s[16:17] op_sel_hi:[1,0]
	ds_write_b128 v144, v[76:79]
	ds_write_b128 v145, v[68:71]
	s_waitcnt vmcnt(21)
	v_pk_mul_f32 v[70:71], v[74:75], s[16:17] op_sel_hi:[1,0]
	v_pk_mul_f32 v[68:69], v[72:73], s[16:17] op_sel_hi:[1,0]
	s_waitcnt vmcnt(20)
	v_pk_mul_f32 v[66:67], v[66:67], s[16:17] op_sel_hi:[1,0]
	v_pk_mul_f32 v[64:65], v[64:65], s[16:17] op_sel_hi:[1,0]
	ds_write_b128 v146, v[68:71]
	ds_write_b128 v147, v[64:67]
	s_waitcnt lgkmcnt(0)
	ds_read2_b32 v[64:65], v148 offset1:32
	ds_read2_b32 v[72:73], v148 offset0:64 offset1:96
	ds_read2_b32 v[70:71], v148 offset0:128 offset1:160
	ds_read2_b32 v[74:75], v152 offset1:32
	s_waitcnt lgkmcnt(3)
	v_cvt_pk_fp8_f32 v68, v64, v65
	ds_read2_b32 v[64:65], v148 offset0:192 offset1:224
	ds_read2_b32 v[76:77], v152 offset0:64 offset1:96
	ds_read2_b32 v[78:79], v152 offset0:128 offset1:160
	s_waitcnt lgkmcnt(4)
	v_cvt_pk_fp8_f32 v69, v70, v71
	s_waitcnt lgkmcnt(3)
	v_cvt_pk_fp8_f32 v70, v74, v75
	ds_read2_b32 v[74:75], v152 offset0:192 offset1:224
	s_waitcnt lgkmcnt(1)
	v_cvt_pk_fp8_f32 v71, v78, v79
	v_cvt_pk_fp8_f32 v68, v72, v73 op_sel:[0,0,1]
	v_cvt_pk_fp8_f32 v69, v64, v65 op_sel:[0,0,1]
	v_cvt_pk_fp8_f32 v70, v76, v77 op_sel:[0,0,1]
	s_waitcnt lgkmcnt(0)
	v_cvt_pk_fp8_f32 v71, v74, v75 op_sel:[0,0,1]
	ds_read2_b32 v[72:73], v149 offset1:32
	v_lshl_add_u64 v[64:65], s[18:19], 0, v[128:129]
	ds_read2_b32 v[74:75], v153 offset1:32
	global_store_dwordx4 v[64:65], v[68:71], off nt
	ds_read2_b32 v[70:71], v149 offset0:128 offset1:160
	ds_read2_b32 v[64:65], v149 offset0:64 offset1:96
	s_waitcnt lgkmcnt(3)
	v_cvt_pk_fp8_f32 v68, v72, v73
	ds_read2_b32 v[72:73], v149 offset0:192 offset1:224
	ds_read2_b32 v[76:77], v153 offset0:64 offset1:96
	ds_read2_b32 v[78:79], v153 offset0:128 offset1:160
	s_waitcnt lgkmcnt(4)
	v_cvt_pk_fp8_f32 v69, v70, v71
	v_cvt_pk_fp8_f32 v70, v74, v75
	ds_read2_b32 v[74:75], v153 offset0:192 offset1:224
	s_waitcnt lgkmcnt(1)
	v_cvt_pk_fp8_f32 v71, v78, v79
	v_cvt_pk_fp8_f32 v68, v64, v65 op_sel:[0,0,1]
	v_cvt_pk_fp8_f32 v69, v72, v73 op_sel:[0,0,1]
	v_cvt_pk_fp8_f32 v70, v76, v77 op_sel:[0,0,1]
	s_waitcnt lgkmcnt(0)
	v_cvt_pk_fp8_f32 v71, v74, v75 op_sel:[0,0,1]
	s_add_u32 s8, s18, 0x4000
	ds_read2_b32 v[72:73], v150 offset1:32
	s_addc_u32 s9, s19, 0
	v_lshl_add_u64 v[64:65], s[8:9], 0, v[128:129]
	global_store_dwordx4 v[64:65], v[68:71], off nt
	ds_read2_b32 v[70:71], v150 offset0:128 offset1:160
	ds_read2_b32 v[74:75], v154 offset1:32
	ds_read2_b32 v[64:65], v150 offset0:64 offset1:96
	s_waitcnt lgkmcnt(3)
	v_cvt_pk_fp8_f32 v68, v72, v73
	ds_read2_b32 v[72:73], v150 offset0:192 offset1:224
	ds_read2_b32 v[76:77], v154 offset0:64 offset1:96
	ds_read2_b32 v[78:79], v154 offset0:128 offset1:160
	s_waitcnt lgkmcnt(5)
	v_cvt_pk_fp8_f32 v69, v70, v71
	s_waitcnt lgkmcnt(4)
	v_cvt_pk_fp8_f32 v70, v74, v75
	ds_read2_b32 v[74:75], v154 offset0:192 offset1:224
	s_waitcnt lgkmcnt(1)
	v_cvt_pk_fp8_f32 v71, v78, v79
	v_cvt_pk_fp8_f32 v68, v64, v65 op_sel:[0,0,1]
	v_cvt_pk_fp8_f32 v69, v72, v73 op_sel:[0,0,1]
	v_cvt_pk_fp8_f32 v70, v76, v77 op_sel:[0,0,1]
	s_waitcnt lgkmcnt(0)
	v_cvt_pk_fp8_f32 v71, v74, v75 op_sel:[0,0,1]
	s_add_u32 s8, s18, 0x8000
	s_addc_u32 s9, s19, 0
	v_lshl_add_u64 v[64:65], s[8:9], 0, v[128:129]
	ds_read2_b32 v[72:73], v151 offset1:32
	global_store_dwordx4 v[64:65], v[68:71], off nt
	ds_read2_b32 v[70:71], v151 offset0:128 offset1:160
	ds_read2_b32 v[74:75], v155 offset1:32
	ds_read2_b32 v[68:69], v151 offset0:64 offset1:96
	s_waitcnt lgkmcnt(3)
	v_cvt_pk_fp8_f32 v64, v72, v73
	ds_read2_b32 v[72:73], v151 offset0:192 offset1:224
	s_waitcnt lgkmcnt(3)
	v_cvt_pk_fp8_f32 v65, v70, v71
	ds_read2_b32 v[70:71], v155 offset0:128 offset1:160
	ds_read2_b32 v[76:77], v155 offset0:64 offset1:96
	s_waitcnt lgkmcnt(4)
	v_cvt_pk_fp8_f32 v66, v74, v75
	ds_read2_b32 v[74:75], v155 offset0:192 offset1:224
	s_waitcnt lgkmcnt(2)
	v_cvt_pk_fp8_f32 v67, v70, v71
	v_cvt_pk_fp8_f32 v64, v68, v69 op_sel:[0,0,1]
	v_cvt_pk_fp8_f32 v65, v72, v73 op_sel:[0,0,1]
	s_waitcnt lgkmcnt(1)
	v_cvt_pk_fp8_f32 v66, v76, v77 op_sel:[0,0,1]
	s_waitcnt lgkmcnt(0)
	v_cvt_pk_fp8_f32 v67, v74, v75 op_sel:[0,0,1]
	s_add_u32 s8, s18, 0xc000
	s_addc_u32 s9, s19, 0
	v_lshl_add_u64 v[68:69], s[8:9], 0, v[128:129]
	global_store_dwordx4 v[68:69], v[64:67], off nt
	s_waitcnt lgkmcnt(0)
	s_cmp_ge_i32 s1, s45
	s_cselect_b64 s[20:21], -1, 0

; __device__ __forceinline__ cgptr cuni(const void* p) { const unsigned long long v = (unsigned long long)p; const unsigned lo = __builtin_amdgcn_readfirstlane((unsigned)v), hi = __builtin_amdgcn_readfirstlane((unsigned)(v >> 32)); return (cgptr)(((unsigned long long)hi << 32) | lo); }
; #define CONV_LOAD(v, c) do { const unsigned lo_ = (unsigned)(lane >> 3) * (c).N4 + 16u * (unsigned)(lane & 7); _Pragma("unroll") for (int i = 0; i < 16; ++i) v[i] = __builtin_nontemporal_load((const GAS f32x4*)(cuni((const void*)((c).src + (size_t)(8 * i) * (c).N4)) + lo_)); } while (0)
; __device__ __forceinline__ ConvItem conv_decode(int it, const float* wgu, const float* wd, unsigned char* WguT, unsigned char* WdT) {
;     constexpr int I_GU = NE * 16 * 128;
;     ConvItem c; int r = it, nbn, N; const float* src; unsigned char* dstp; bool gu;
;     if (r < I_GU) { const int e = r / (16 * 128); r -= e * (16 * 128); N = 4096; nbn = 128; src = wgu + (size_t)e * DM * 4096; dstp = WguT + (size_t)e * 4096 * DM; gu = true; }
;     else { r -= I_GU; const int e = r / (16 * 64); r -= e * (16 * 64); N = DM; nbn = 64; src = wd + (size_t)e * DFF * DM; dstp = WdT + (size_t)e * DM * DFF; gu = false; }
;     const int kb = r / nbn, nb = r - kb * nbn, n0 = nb * 32, k0 = kb * 128; int dst = n0;
;     if (gu) { const int j = n0 & 2047; dst = (j >> 7) * 256 + (j & 127) + ((n0 >= 2048) ? 128 : 0); }
;     c.src = cuni(src + (size_t)k0 * N + n0); c.dstp = cuni(dstp + (size_t)dst * DM + k0); c.N4 = (unsigned)N * 4u;
;     return c;
; }
; __device__ __forceinline__ void convert_expert_weights(const float* wgu, const float* wd, unsigned char* WguT, unsigned char* WdT, LAS float* scr, int gw, int NGW, int NIT, int lane) {
;     ...
;         const bool ha = it + NGW < NIT; ca = conv_decode(ha ? it + NGW : it, wgu, wd, WguT, WdT); CONV_LOAD(va, ca);
;         CONV_STORE(vb, cb);
.LBB0_494:
	s_waitcnt vmcnt(4)
	v_cvt_f32_ubyte0_e32 v64, s10
	v_rcp_iflag_f32_e32 v64, v64
	s_sub_i32 s17, 0, s10
	s_abs_i32 s12, s9
	s_ashr_i32 s11, s9, 31
	v_mul_f32_e32 v64, 0x4f7ffffe, v64
	v_cvt_u32_f32_e32 v64, v64
	v_add_u32_e32 v152, 0x400, v148
	v_add_u32_e32 v153, 0x400, v149
	v_add_u32_e32 v154, 0x400, v150
	v_readfirstlane_b32 s26, v64
	s_mul_i32 s17, s17, s26
	s_mul_hi_u32 s17, s26, s17
	s_add_i32 s26, s26, s17
	s_mul_hi_u32 s17, s12, s26
	s_mul_i32 s26, s17, s10
	s_sub_i32 s12, s12, s26
	s_add_i32 s27, s17, 1
	s_sub_i32 s26, s12, s10
	s_cmp_ge_u32 s12, s10
	s_cselect_b32 s17, s27, s17
	s_cselect_b32 s12, s26, s12
	s_add_i32 s26, s17, 1
	s_cmp_ge_u32 s12, s10
	s_cselect_b32 s12, s26, s17
	s_xor_b32 s12, s12, s11
	s_sub_i32 s11, s12, s11
	s_mul_i32 s10, s11, s10
	s_lshl_b32 s17, s9, 6
	s_sub_i32 s9, s9, s10
	s_lshl_b32 s10, s9, 5
	s_and_b32 s12, s17, 0xf00
	s_and_b32 s17, s10, 0x60
	s_or_b32 s12, s17, s12
	s_cmp_gt_i32 s9, 63
	s_cselect_b32 s9, 0x80, 0
	s_or_b32 s9, s12, s9
	s_and_b64 s[18:19], s[18:19], exec
	s_cselect_b32 s18, s9, s10
	s_lshl_b32 s9, s11, 7
	s_mul_hi_i32 s27, s9, s8
	s_mul_i32 s26, s9, s8
	s_ashr_i32 s12, s9, 31
	s_lshl_b64 s[26:27], s[26:27], 2
	s_add_u32 s17, s24, s26
	s_addc_u32 s19, s25, s27
	s_ashr_i32 s11, s10, 31
	s_lshl_b64 s[10:11], s[10:11], 2
	s_add_u32 s24, s17, s10
	s_addc_u32 s25, s19, s11
	s_ashr_i32 s19, s18, 31
	s_lshl_b64 s[10:11], s[18:19], 11
	s_add_u32 s10, s22, s10
	s_addc_u32 s11, s23, s11
	s_add_u32 s18, s10, s9
	s_addc_u32 s19, s11, s12
	s_lshl_b32 s9, s8, 5
	v_mul_lo_u32 v64, v130, s8
	s_add_u32 s10, s24, s9
	v_or_b32_e32 v64, v64, v131
	s_addc_u32 s11, s25, 0
	s_lshl_b32 s9, s8, 6
	global_load_dwordx4 v[124:127], v64, s[24:25] nt
	global_load_dwordx4 v[116:119], v64, s[10:11] nt
	s_add_u32 s10, s24, s9
	s_addc_u32 s11, s25, 0
	s_mul_i32 s9, s8, 0x60
	s_add_u32 s22, s24, s9
	s_addc_u32 s23, s25, 0
	s_lshl_b32 s9, s8, 7
	global_load_dwordx4 v[120:123], v64, s[10:11] nt
	global_load_dwordx4 v[108:111], v64, s[22:23] nt
	s_add_u32 s10, s24, s9
	s_addc_u32 s11, s25, 0
	s_mul_i32 s9, s8, 0xa0
	s_add_u32 s22, s24, s9
	s_addc_u32 s23, s25, 0
	s_mul_i32 s9, s8, 0xc0
	global_load_dwordx4 v[112:115], v64, s[10:11] nt
	global_load_dwordx4 v[100:103], v64, s[22:23] nt
	s_add_u32 s10, s24, s9
	s_addc_u32 s11, s25, 0
	s_mul_i32 s9, s8, 0xe0
	s_add_u32 s22, s24, s9
	s_addc_u32 s23, s25, 0
	s_lshl_b32 s9, s8, 8
	global_load_dwordx4 v[104:107], v64, s[10:11] nt
	global_load_dwordx4 v[92:95], v64, s[22:23] nt
	s_add_u32 s10, s24, s9
	s_addc_u32 s11, s25, 0
	s_mul_i32 s9, s8, 0x120
	s_add_u32 s22, s24, s9
	s_addc_u32 s23, s25, 0
	s_mul_i32 s9, s8, 0x140
	global_load_dwordx4 v[96:99], v64, s[10:11] nt
	global_load_dwordx4 v[84:87], v64, s[22:23] nt
	s_add_u32 s10, s24, s9
	s_addc_u32 s11, s25, 0
	s_mul_i32 s9, s8, 0x160
	s_add_u32 s22, s24, s9
	s_addc_u32 s23, s25, 0
	s_mul_i32 s9, s8, 0x180
	global_load_dwordx4 v[88:91], v64, s[10:11] nt
	global_load_dwordx4 v[76:79], v64, s[22:23] nt
	s_add_u32 s10, s24, s9
	s_addc_u32 s11, s25, 0
	s_mul_i32 s9, s8, 0x1a0
	s_add_u32 s22, s24, s9
	s_addc_u32 s23, s25, 0
	s_mul_i32 s9, s8, 0x1c0
	global_load_dwordx4 v[80:83], v64, s[10:11] nt
	global_load_dwordx4 v[68:71], v64, s[22:23] nt
	s_add_u32 s10, s24, s9
	s_addc_u32 s11, s25, 0
	s_mulk_i32 s8, 0x1e0
	s_add_u32 s8, s24, s8
	s_waitcnt vmcnt(29)
	v_pk_mul_f32 v[6:7], v[6:7], s[16:17] op_sel_hi:[1,0]
	v_pk_mul_f32 v[4:5], v[4:5], s[16:17] op_sel_hi:[1,0]
	s_waitcnt vmcnt(28)
	v_pk_mul_f32 v[2:3], v[2:3], s[16:17] op_sel_hi:[1,0]
	v_pk_mul_f32 v[0:1], v[0:1], s[16:17] op_sel_hi:[1,0]
	s_addc_u32 s9, s25, 0
	global_load_dwordx4 v[72:75], v64, s[10:11] nt
	s_nop 0
	global_load_dwordx4 v[64:67], v64, s[8:9] nt
	ds_write_b128 v132, v[4:7]
	ds_write_b128 v133, v[0:3]
	s_waitcnt vmcnt(29)
	v_pk_mul_f32 v[2:3], v[14:15], s[16:17] op_sel_hi:[1,0]
	v_pk_mul_f32 v[0:1], v[12:13], s[16:17] op_sel_hi:[1,0]
	ds_write_b128 v134, v[0:3]
	s_waitcnt vmcnt(28)
	v_pk_mul_f32 v[2:3], v[10:11], s[16:17] op_sel_hi:[1,0]
	v_pk_mul_f32 v[0:1], v[8:9], s[16:17] op_sel_hi:[1,0]
	ds_write_b128 v135, v[0:3]
	s_waitcnt vmcnt(27)
	v_pk_mul_f32 v[2:3], v[22:23], s[16:17] op_sel_hi:[1,0]
	v_pk_mul_f32 v[0:1], v[20:21], s[16:17] op_sel_hi:[1,0]
	ds_write_b128 v136, v[0:3]
	s_waitcnt vmcnt(26)
	v_pk_mul_f32 v[2:3], v[18:19], s[16:17] op_sel_hi:[1,0]
	v_pk_mul_f32 v[0:1], v[16:17], s[16:17] op_sel_hi:[1,0]
	ds_write_b128 v137, v[0:3]
	s_waitcnt vmcnt(25)
	v_pk_mul_f32 v[2:3], v[30:31], s[16:17] op_sel_hi:[1,0]
	v_pk_mul_f32 v[0:1], v[28:29], s[16:17] op_sel_hi:[1,0]
	ds_write_b128 v138, v[0:3]
	s_waitcnt vmcnt(24)
	v_pk_mul_f32 v[2:3], v[26:27], s[16:17] op_sel_hi:[1,0]
	v_pk_mul_f32 v[0:1], v[24:25], s[16:17] op_sel_hi:[1,0]
	ds_write_b128 v139, v[0:3]
	s_waitcnt vmcnt(23)
	v_pk_mul_f32 v[2:3], v[38:39], s[16:17] op_sel_hi:[1,0]
	v_pk_mul_f32 v[0:1], v[36:37], s[16:17] op_sel_hi:[1,0]
	ds_write_b128 v140, v[0:3]
	s_waitcnt vmcnt(22)
	v_pk_mul_f32 v[2:3], v[34:35], s[16:17] op_sel_hi:[1,0]
	v_pk_mul_f32 v[0:1], v[32:33], s[16:17] op_sel_hi:[1,0]
	ds_write_b128 v141, v[0:3]
	s_waitcnt vmcnt(21)
	v_pk_mul_f32 v[2:3], v[46:47], s[16:17] op_sel_hi:[1,0]
	v_pk_mul_f32 v[0:1], v[44:45], s[16:17] op_sel_hi:[1,0]
	ds_write_b128 v142, v[0:3]
	s_waitcnt vmcnt(20)
; #define LAS __attribute__((address_space(3)))
; #define CONV_LOAD(v, c) do { const unsigned lo_ = (unsigned)(lane >> 3) * (c).N4 + 16u * (unsigned)(lane & 7); _Pragma("unroll") for (int i = 0; i < 16; ++i) v[i] = __builtin_nontemporal_load((const GAS f32x4*)(cuni((const void*)((c).src + (size_t)(8 * i) * (c).N4)) + lo_)); } while (0)
; __device__ __forceinline__ void convert_expert_weights(const float* wgu, const float* wd, unsigned char* WguT, unsigned char* WdT, LAS float* scr, int gw, int NGW, int NIT, int lane) {
;     int it = gw; if (it >= NIT) return;
;     f32x4 va[16], vb[16];
;     ConvItem ca = conv_decode(it, wgu, wd, WguT, WdT), cb = ca;
;     CONV_LOAD(va, ca);
;     for (;;) {
;         const bool hb = it + NGW < NIT; cb = conv_decode(hb ? it + NGW : it, wgu, wd, WguT, WdT); CONV_LOAD(vb, cb);
;         CONV_STORE(va, ca);
;         if (!hb) break;
;         it += NGW;
;         const bool ha = it + NGW < NIT; ca = conv_decode(ha ? it + NGW : it, wgu, wd, WguT, WdT); CONV_LOAD(va, ca);
;         CONV_STORE(vb, cb);
;         if (!ha) break;
;         it += NGW;
;     }
	v_pk_mul_f32 v[2:3], v[42:43], s[16:17] op_sel_hi:[1,0]
	v_pk_mul_f32 v[0:1], v[40:41], s[16:17] op_sel_hi:[1,0]
	ds_write_b128 v143, v[0:3]
	s_waitcnt vmcnt(19)
	v_pk_mul_f32 v[2:3], v[54:55], s[16:17] op_sel_hi:[1,0]
	v_pk_mul_f32 v[0:1], v[52:53], s[16:17] op_sel_hi:[1,0]
	ds_write_b128 v144, v[0:3]
	s_waitcnt vmcnt(18)
	v_pk_mul_f32 v[2:3], v[50:51], s[16:17] op_sel_hi:[1,0]
	v_pk_mul_f32 v[0:1], v[48:49], s[16:17] op_sel_hi:[1,0]
	ds_write_b128 v145, v[0:3]
	s_waitcnt vmcnt(17)
	v_pk_mul_f32 v[2:3], v[62:63], s[16:17] op_sel_hi:[1,0]
	v_pk_mul_f32 v[0:1], v[60:61], s[16:17] op_sel_hi:[1,0]
	ds_write_b128 v146, v[0:3]
	s_waitcnt vmcnt(16)
	v_pk_mul_f32 v[2:3], v[58:59], s[16:17] op_sel_hi:[1,0]
	v_pk_mul_f32 v[0:1], v[56:57], s[16:17] op_sel_hi:[1,0]
	ds_write_b128 v147, v[0:3]
	s_waitcnt lgkmcnt(0)
	ds_read2_b32 v[0:1], v148 offset1:32
	ds_read2_b32 v[8:9], v148 offset0:64 offset1:96
	s_add_u32 s8, s14, 0x4000
	s_waitcnt lgkmcnt(0)
	v_cvt_pk_fp8_f32 v4, v0, v1
	ds_read2_b32 v[0:1], v148 offset0:128 offset1:160
	ds_read2_b32 v[10:11], v148 offset0:192 offset1:224
	ds_read2_b32 v[12:13], v152 offset1:32
	s_waitcnt lgkmcnt(2)
	v_cvt_pk_fp8_f32 v5, v0, v1
	ds_read2_b32 v[0:1], v152 offset0:64 offset1:96
	ds_read2_b32 v[14:15], v152 offset0:128 offset1:160
	s_waitcnt lgkmcnt(2)
	v_cvt_pk_fp8_f32 v6, v12, v13
	ds_read2_b32 v[12:13], v152 offset0:192 offset1:224
	v_cvt_pk_fp8_f32 v4, v8, v9 op_sel:[0,0,1]
	s_waitcnt lgkmcnt(1)
	v_cvt_pk_fp8_f32 v7, v14, v15
	v_cvt_pk_fp8_f32 v5, v10, v11 op_sel:[0,0,1]
	v_cvt_pk_fp8_f32 v6, v0, v1 op_sel:[0,0,1]
	ds_read2_b32 v[0:1], v149 offset1:32
	s_waitcnt lgkmcnt(1)
	v_cvt_pk_fp8_f32 v7, v12, v13 op_sel:[0,0,1]
	v_lshl_add_u64 v[8:9], s[14:15], 0, v[128:129]
	s_addc_u32 s9, s15, 0
	v_add_u32_e32 v155, 0x400, v151
	global_store_dwordx4 v[8:9], v[4:7], off nt
	ds_read2_b32 v[8:9], v149 offset0:64 offset1:96
	s_waitcnt lgkmcnt(1)
	v_cvt_pk_fp8_f32 v4, v0, v1
	ds_read2_b32 v[0:1], v149 offset0:128 offset1:160
	ds_read2_b32 v[10:11], v149 offset0:192 offset1:224
	ds_read2_b32 v[12:13], v153 offset1:32
	s_waitcnt lgkmcnt(2)
	v_cvt_pk_fp8_f32 v5, v0, v1
	ds_read2_b32 v[0:1], v153 offset0:64 offset1:96
	ds_read2_b32 v[14:15], v153 offset0:128 offset1:160
	s_waitcnt lgkmcnt(2)
	v_cvt_pk_fp8_f32 v6, v12, v13
	ds_read2_b32 v[12:13], v153 offset0:192 offset1:224
	v_cvt_pk_fp8_f32 v4, v8, v9 op_sel:[0,0,1]
	s_waitcnt lgkmcnt(1)
	v_cvt_pk_fp8_f32 v7, v14, v15
	v_cvt_pk_fp8_f32 v5, v10, v11 op_sel:[0,0,1]
	v_cvt_pk_fp8_f32 v6, v0, v1 op_sel:[0,0,1]
	ds_read2_b32 v[0:1], v150 offset1:32
	s_waitcnt lgkmcnt(1)
	v_cvt_pk_fp8_f32 v7, v12, v13 op_sel:[0,0,1]
	v_lshl_add_u64 v[8:9], s[8:9], 0, v[128:129]
	s_add_u32 s8, s14, 0x8000
	s_addc_u32 s9, s15, 0
	global_store_dwordx4 v[8:9], v[4:7], off nt
	ds_read2_b32 v[8:9], v150 offset0:64 offset1:96
	s_nop 0
	s_waitcnt lgkmcnt(1)
	v_cvt_pk_fp8_f32 v4, v0, v1
	ds_read2_b32 v[0:1], v150 offset0:128 offset1:160
	ds_read2_b32 v[10:11], v150 offset0:192 offset1:224
	ds_read2_b32 v[12:13], v154 offset1:32
	s_waitcnt lgkmcnt(2)
	v_cvt_pk_fp8_f32 v5, v0, v1
	ds_read2_b32 v[0:1], v154 offset0:64 offset1:96
	ds_read2_b32 v[14:15], v154 offset0:128 offset1:160
	s_waitcnt lgkmcnt(2)
	v_cvt_pk_fp8_f32 v6, v12, v13
	ds_read2_b32 v[12:13], v154 offset0:192 offset1:224
	v_cvt_pk_fp8_f32 v4, v8, v9 op_sel:[0,0,1]
	s_waitcnt lgkmcnt(1)
	v_cvt_pk_fp8_f32 v7, v14, v15
	v_cvt_pk_fp8_f32 v5, v10, v11 op_sel:[0,0,1]
	v_cvt_pk_fp8_f32 v6, v0, v1 op_sel:[0,0,1]
	ds_read2_b32 v[8:9], v151 offset1:32
	s_waitcnt lgkmcnt(1)
	v_cvt_pk_fp8_f32 v7, v12, v13 op_sel:[0,0,1]
	v_lshl_add_u64 v[0:1], s[8:9], 0, v[128:129]
	s_add_u32 s8, s14, 0xc000
	s_addc_u32 s9, s15, 0
	global_store_dwordx4 v[0:1], v[4:7], off nt
	ds_read2_b32 v[4:5], v151 offset0:64 offset1:96
	s_waitcnt lgkmcnt(1)
	v_cvt_pk_fp8_f32 v0, v8, v9
	ds_read2_b32 v[6:7], v151 offset0:128 offset1:160
	ds_read2_b32 v[8:9], v151 offset0:192 offset1:224
	ds_read2_b32 v[10:11], v155 offset1:32
	s_waitcnt lgkmcnt(3)
	v_cvt_pk_fp8_f32 v0, v4, v5 op_sel:[0,0,1]
	s_waitcnt lgkmcnt(2)
	v_cvt_pk_fp8_f32 v1, v6, v7
	ds_read2_b32 v[6:7], v155 offset0:128 offset1:160
	ds_read2_b32 v[12:13], v155 offset0:64 offset1:96
	s_waitcnt lgkmcnt(2)
	v_cvt_pk_fp8_f32 v2, v10, v11
	ds_read2_b32 v[10:11], v155 offset0:192 offset1:224
	v_cvt_pk_fp8_f32 v1, v8, v9 op_sel:[0,0,1]
	s_waitcnt lgkmcnt(2)
	v_cvt_pk_fp8_f32 v3, v6, v7
	s_waitcnt lgkmcnt(1)
	v_cvt_pk_fp8_f32 v2, v12, v13 op_sel:[0,0,1]
	v_lshl_add_u64 v[4:5], s[8:9], 0, v[128:129]
	s_andn2_b64 vcc, exec, s[20:21]
	s_waitcnt lgkmcnt(0)
	v_cvt_pk_fp8_f32 v3, v10, v11 op_sel:[0,0,1]
	s_mov_b64 s[20:21], -1
	global_store_dwordx4 v[4:5], v[0:3], off nt
	s_waitcnt lgkmcnt(0)
	s_cbranch_vccnz .LBB0_488
	s_add_i32 s1, s0, s1
	s_cmp_lt_i32 s1, s45
	s_cselect_b32 s1, s1, s3
	s_cmp_lt_i32 s1, 0x10000
	s_cselect_b64 s[14:15], -1, 0
	s_cmp_gt_i32 s1, 0xffff
	s_mov_b64 s[24:25], -1
	s_cbranch_scc0 .LBB0_497
	s_add_i32 s8, s1, 0xffff0000
	s_lshr_b32 s12, s8, 10
	s_and_b32 s9, s1, 0x3ff
	s_lshl_b64 s[10:11], s[12:13], 22
	s_lshl_b64 s[20:21], s[12:13], 24
	s_add_u32 s22, s6, s20
	s_addc_u32 s23, s7, s21
	s_add_u32 s20, s77, s10
	v_readlane_b32 s8, v252, 33
	s_addc_u32 s21, s8, s11
	s_mov_b64 s[24:25], 0

; #define GAS __attribute__((address_space(1)))
; __device__ __forceinline__ unsigned cvt_pk_bf16(float lo, float hi) { unsigned r; asm volatile("v_cvt_pk_bf16_f32 %0, %1, %2" : "=v"(r) : "v"(lo), "v"(hi)); return r; }
; #define SBAR() __builtin_amdgcn_sched_barrier(0)
; __device__ __forceinline__ gptr uni(const GAS void* p) { const unsigned long long v = (unsigned long long)p; const unsigned lo = __builtin_amdgcn_readfirstlane((unsigned)v), hi = __builtin_amdgcn_readfirstlane((unsigned)(v >> 32)); return (gptr)(((unsigned long long)hi << 32) | lo); }
; #define QLOAD(ref) do { gptr qb_ = uni((const GAS void*)((ref).Q + (size_t)(wid * QBLK) * QS)); _Pragma("unroll") for (int d0 = 0; d0 < NQR; ++d0) S.qr[d0] = *reinterpret_cast<const GAS u32x2*>(qb_ + d0 * 16 + voff_q); } while (0)
; template <int AV>
; __device__ __forceinline__ void block(const BlockRef& cur, const BlockRef& nxt, char* lds, Seam& S, const int wid, const QNorm& QN) {
;     ...
;     SBAR(); QLOAD(nxt); v_read(vf, STGP(sc), ka); SBAR();
;     finishSM(pB0, pB1, pa); SBAR();
;     pv_mma(o, ol, vf, ones, pa);
;     S.g = INC6(sc, 1);
;     __builtin_amdgcn_s_setprio(0);
;     float rli[16];
; #pragma unroll
;     for (int r = 0; r < 16; ++r) rli[r] = __builtin_amdgcn_rcpf(ol[r]);
;     GAS char* Ow = (GAS char*)uni((const GAS void*)(cur.O + (size_t)(wid * QBLK) * OS));
;     const bool odd = (r32 & 1) != 0;
;     const unsigned voff_o = (unsigned)((4 * hi + (odd ? 1 : 0)) * OS + (r32 & ~1)) * 2u;
; #pragma unroll
;     for (int r = 0; r < 16; r += 2) { const int orow0 = (r & 3) + 8 * (r >> 2);
; #pragma unroll
;         for (int d0 = 0; d0 < 4; ++d0) { const float a = o[d0][r] * rli[r], b = o[d0][r + 1] * rli[r + 1];
;             const float send = odd ? a : b;
;             const float recv = __int_as_float(__builtin_amdgcn_mov_dpp(__float_as_int(send), 0xB1, 0xF, 0xF, true));
;             *(GAS unsigned*)(Ow + (size_t)orow0 * OS * 2 + d0 * 64 + voff_o) = cvt_pk_bf16(odd ? recv : a, odd ? b : recv); } }
.LBB0_506:
	s_add_u32 s6, s66, s95
	s_addc_u32 s7, s67, s11
	v_lshl_add_u64 v[80:81], s[6:7], 0, v[184:185]
	global_load_dwordx2 v[86:87], v[80:81], off
	global_load_dwordx2 v[84:85], v[80:81], off offset:16
	global_load_dwordx2 v[82:83], v[80:81], off offset:32
	s_nop 0
	global_load_dwordx2 v[80:81], v[80:81], off offset:48
	s_add_i32 s0, s92, 0
	v_add_u32_e32 v124, s0, v193
	v_add_u32_e32 v132, s0, v194
	ds_read_b128 v[88:91], v124 offset:12288
	ds_read_b128 v[112:115], v124 offset:14336
	ds_read_b128 v[92:95], v132 offset:12288
	ds_read_b128 v[116:119], v132 offset:14336
	ds_read_b128 v[120:123], v124 offset:16384
	ds_read_b128 v[128:131], v124 offset:18432
	ds_read_b128 v[124:127], v132 offset:16384
	ds_read_b128 v[132:135], v132 offset:18432
	v_exp_f32_e32 v136, v96
	v_exp_f32_e32 v97, v97
	v_exp_f32_e32 v137, v100
	v_exp_f32_e32 v138, v101
	v_exp_f32_e32 v139, v103
	v_exp_f32_e32 v98, v98
	v_exp_f32_e32 v99, v99
	v_exp_f32_e32 v102, v102
	v_cvt_pk_fp8_f32 v100, v136, v97
	v_cvt_pk_fp8_f32 v101, v137, v138
	v_exp_f32_e32 v104, v104
	v_exp_f32_e32 v105, v105
	v_exp_f32_e32 v108, v108
	v_exp_f32_e32 v109, v109
	v_cvt_pk_fp8_f32 v100, v98, v99 op_sel:[0,0,1]
	v_cvt_pk_fp8_f32 v101, v102, v139 op_sel:[0,0,1]
	v_exp_f32_e32 v106, v106
	v_exp_f32_e32 v107, v107
	v_exp_f32_e32 v110, v110
	v_exp_f32_e32 v111, v111
	v_cvt_pk_fp8_f32 v96, v215, v216
	v_cvt_pk_fp8_f32 v97, v211, v212
	v_cvt_pk_fp8_f32 v98, v207, v208
	v_cvt_pk_fp8_f32 v102, v104, v105
	v_cvt_pk_fp8_f32 v99, v203, v204
	v_cvt_pk_fp8_f32 v103, v108, v109
	v_cvt_pk_fp8_f32 v96, v213, v214 op_sel:[0,0,1]
	v_cvt_pk_fp8_f32 v97, v209, v210 op_sel:[0,0,1]
	v_cvt_pk_fp8_f32 v98, v205, v206 op_sel:[0,0,1]
	v_cvt_pk_fp8_f32 v102, v106, v107 op_sel:[0,0,1]
	v_cvt_pk_fp8_f32 v99, v201, v202 op_sel:[0,0,1]
	v_cvt_pk_fp8_f32 v103, v110, v111 op_sel:[0,0,1]
	s_cmp_gt_i32 s1, 4
	s_cselect_b32 s0, -5, 1
	s_add_i32 s41, s0, s1
	s_waitcnt lgkmcnt(5)
	v_mfma_f32_32x32x64_f8f6f4 v[48:63], v[96:103], v[88:95], v[48:63]
	s_waitcnt lgkmcnt(4)
	v_mfma_f32_32x32x64_f8f6f4 v[32:47], v[96:103], v[112:119], v[32:47]
	s_waitcnt lgkmcnt(1)
	v_mfma_f32_32x32x64_f8f6f4 v[16:31], v[96:103], v[120:127], v[16:31]
	s_waitcnt lgkmcnt(0)
	v_mfma_f32_32x32x64_f8f6f4 v[0:15], v[96:103], v[128:135], v[0:15]
	v_mfma_f32_32x32x64_f8f6f4 v[64:79], v[96:103], v[152:159], v[64:79]
	s_setprio 0
	s_nop 15
	s_nop 2
	v_rcp_f32_e32 v88, v64
	v_rcp_f32_e32 v89, v65
	v_and_b32_e32 v90, 1, v188
	v_cmp_eq_u32_e32 vcc, 0, v90
	v_mul_f32_e32 v48, v48, v88
	v_mul_f32_e32 v49, v49, v89
	v_or_b32_e32 v64, v189, v90
	v_cndmask_b32_e32 v90, v48, v49, vcc
	v_lshlrev_b32_e32 v65, 1, v188
	s_add_u32 s0, s76, s60
	v_mov_b32_dpp v90, v90 quad_perm:[1,0,3,2] row_mask:0xf bank_mask:0xf bound_ctrl:1
	v_and_b32_e32 v65, 60, v65
	v_cndmask_b32_e32 v48, v90, v48, vcc
	s_addc_u32 s1, s77, s61
	v_lshl_or_b32 v184, v64, 12, v65
	v_cndmask_b32_e32 v49, v49, v90, vcc
	v_cvt_pk_bf16_f32 v48, v48, v49
	v_mul_f32_e32 v32, v32, v88
	v_mul_f32_e32 v33, v33, v89
	global_store_dword v184, v48, s[0:1]
	v_cndmask_b32_e32 v48, v32, v33, vcc
	v_mul_f32_e32 v16, v16, v88
	v_mul_f32_e32 v17, v17, v89
	v_mov_b32_dpp v48, v48 quad_perm:[1,0,3,2] row_mask:0xf bank_mask:0xf bound_ctrl:1
	v_cndmask_b32_e32 v32, v48, v32, vcc
	v_cndmask_b32_e32 v33, v33, v48, vcc
	v_cvt_pk_bf16_f32 v32, v32, v33
	global_store_dword v184, v32, s[0:1] offset:64
	v_cndmask_b32_e32 v32, v16, v17, vcc
	v_mul_f32_e32 v0, v0, v88
	v_mul_f32_e32 v1, v1, v89
	v_mov_b32_dpp v32, v32 quad_perm:[1,0,3,2] row_mask:0xf bank_mask:0xf bound_ctrl:1
	v_cndmask_b32_e32 v16, v32, v16, vcc
	v_cndmask_b32_e32 v17, v17, v32, vcc
	v_cvt_pk_bf16_f32 v16, v16, v17
	v_rcp_f32_e32 v66, v66
	v_rcp_f32_e32 v67, v67
	global_store_dword v184, v16, s[0:1] offset:128
	v_cndmask_b32_e32 v16, v0, v1, vcc
	v_lshl_add_u64 v[64:65], s[0:1], 0, v[184:185]
	v_mul_f32_e32 v17, v35, v67
	v_mov_b32_dpp v16, v16 quad_perm:[1,0,3,2] row_mask:0xf bank_mask:0xf bound_ctrl:1
	v_cndmask_b32_e32 v0, v16, v0, vcc
	v_cndmask_b32_e32 v1, v1, v16, vcc
	v_cvt_pk_bf16_f32 v0, v0, v1
	global_store_dword v184, v0, s[0:1] offset:192
	v_mul_f32_e32 v0, v50, v66
	v_mul_f32_e32 v1, v51, v67
	v_cndmask_b32_e32 v16, v0, v1, vcc
	s_movk_i32 s0, 0x2000
	v_rcp_f32_e32 v68, v68
	v_mov_b32_dpp v16, v16 quad_perm:[1,0,3,2] row_mask:0xf bank_mask:0xf bound_ctrl:1
	v_cndmask_b32_e32 v0, v16, v0, vcc
	v_cndmask_b32_e32 v1, v1, v16, vcc
	v_cvt_pk_bf16_f32 v16, v0, v1
	v_add_co_u32_e64 v0, s[6:7], s0, v64
	v_rcp_f32_e32 v69, v69
	s_nop 0
	v_addc_co_u32_e64 v1, s[6:7], 0, v65, s[6:7]
	global_store_dword v[0:1], v16, off
	v_mul_f32_e32 v16, v34, v66
	v_cndmask_b32_e32 v32, v16, v17, vcc
	v_mul_f32_e32 v2, v2, v66
	v_mul_f32_e32 v3, v3, v67
	v_mov_b32_dpp v32, v32 quad_perm:[1,0,3,2] row_mask:0xf bank_mask:0xf bound_ctrl:1
	v_cndmask_b32_e32 v16, v32, v16, vcc
	v_cndmask_b32_e32 v17, v17, v32, vcc
	v_cvt_pk_bf16_f32 v16, v16, v17
	global_store_dword v[0:1], v16, off offset:64
	v_mul_f32_e32 v16, v18, v66
	v_mul_f32_e32 v17, v19, v67
	v_cndmask_b32_e32 v18, v16, v17, vcc
	s_mov_b32 s0, 0x8000
	v_rcp_f32_e32 v70, v70
	v_mov_b32_dpp v18, v18 quad_perm:[1,0,3,2] row_mask:0xf bank_mask:0xf bound_ctrl:1
	v_cndmask_b32_e32 v16, v18, v16, vcc
	v_cndmask_b32_e32 v17, v17, v18, vcc
	v_cvt_pk_bf16_f32 v16, v16, v17
	global_store_dword v[0:1], v16, off offset:128
	v_cndmask_b32_e32 v16, v2, v3, vcc
	v_rcp_f32_e32 v71, v71
	v_rcp_f32_e32 v72, v72
	v_mov_b32_dpp v16, v16 quad_perm:[1,0,3,2] row_mask:0xf bank_mask:0xf bound_ctrl:1
	v_cndmask_b32_e32 v2, v16, v2, vcc
	v_cndmask_b32_e32 v3, v3, v16, vcc
	v_cvt_pk_bf16_f32 v2, v2, v3
	global_store_dword v[0:1], v2, off offset:192
; #define GAS __attribute__((address_space(1)))
; __device__ __forceinline__ unsigned cvt_pk_bf16(float lo, float hi) { unsigned r; asm volatile("v_cvt_pk_bf16_f32 %0, %1, %2" : "=v"(r) : "v"(lo), "v"(hi)); return r; }
; template <int AV>
; __device__ __forceinline__ void block(const BlockRef& cur, const BlockRef& nxt, char* lds, Seam& S, const int wid, const QNorm& QN) {
;     ...
; #pragma unroll
;     for (int r = 0; r < 16; r += 2) { const int orow0 = (r & 3) + 8 * (r >> 2);
; #pragma unroll
;         for (int d0 = 0; d0 < 4; ++d0) { const float a = o[d0][r] * rli[r], b = o[d0][r + 1] * rli[r + 1];
;             const float send = odd ? a : b;
;             const float recv = __int_as_float(__builtin_amdgcn_mov_dpp(__float_as_int(send), 0xB1, 0xF, 0xF, true));
;             *(GAS unsigned*)(Ow + (size_t)orow0 * OS * 2 + d0 * 64 + voff_o) = cvt_pk_bf16(odd ? recv : a, odd ? b : recv); } }
	v_mul_f32_e32 v0, v52, v68
	v_mul_f32_e32 v1, v53, v69
	v_cndmask_b32_e32 v2, v0, v1, vcc
	v_mul_f32_e32 v3, v37, v69
	v_rcp_f32_e32 v73, v73
	v_mov_b32_dpp v2, v2 quad_perm:[1,0,3,2] row_mask:0xf bank_mask:0xf bound_ctrl:1
	v_cndmask_b32_e32 v0, v2, v0, vcc
	v_cndmask_b32_e32 v1, v1, v2, vcc
	v_cvt_pk_bf16_f32 v2, v0, v1
	v_add_co_u32_e64 v0, s[6:7], s0, v64
	s_mov_b32 s0, 0xa000
	s_nop 0
	v_addc_co_u32_e64 v1, s[6:7], 0, v65, s[6:7]
	global_store_dword v[0:1], v2, off
	v_mul_f32_e32 v2, v36, v68
	v_cndmask_b32_e32 v16, v2, v3, vcc
	v_rcp_f32_e32 v74, v74
	v_rcp_f32_e32 v75, v75
	v_mov_b32_dpp v16, v16 quad_perm:[1,0,3,2] row_mask:0xf bank_mask:0xf bound_ctrl:1
	v_cndmask_b32_e32 v2, v16, v2, vcc
	v_cndmask_b32_e32 v3, v3, v16, vcc
	v_cvt_pk_bf16_f32 v2, v2, v3
	global_store_dword v[0:1], v2, off offset:64
	v_mul_f32_e32 v2, v20, v68
	v_mul_f32_e32 v3, v21, v69
	v_cndmask_b32_e32 v16, v2, v3, vcc
	v_rcp_f32_e32 v76, v76
	v_rcp_f32_e32 v77, v77
	v_mov_b32_dpp v16, v16 quad_perm:[1,0,3,2] row_mask:0xf bank_mask:0xf bound_ctrl:1
	v_cndmask_b32_e32 v2, v16, v2, vcc
	v_cndmask_b32_e32 v3, v3, v16, vcc
	v_cvt_pk_bf16_f32 v2, v2, v3
	global_store_dword v[0:1], v2, off offset:128
	v_mul_f32_e32 v2, v4, v68
	v_mul_f32_e32 v3, v5, v69
	v_cndmask_b32_e32 v4, v2, v3, vcc
	v_rcp_f32_e32 v78, v78
	v_rcp_f32_e32 v79, v79
	v_mov_b32_dpp v4, v4 quad_perm:[1,0,3,2] row_mask:0xf bank_mask:0xf bound_ctrl:1
	v_cndmask_b32_e32 v2, v4, v2, vcc
	v_cndmask_b32_e32 v3, v3, v4, vcc
	v_cvt_pk_bf16_f32 v2, v2, v3
	global_store_dword v[0:1], v2, off offset:192
	v_mul_f32_e32 v0, v54, v70
	v_mul_f32_e32 v1, v55, v71
	v_cndmask_b32_e32 v2, v0, v1, vcc
	v_mul_f32_e32 v3, v39, v71
	s_mov_b32 s86, s54
	v_mov_b32_dpp v2, v2 quad_perm:[1,0,3,2] row_mask:0xf bank_mask:0xf bound_ctrl:1
	v_cndmask_b32_e32 v0, v2, v0, vcc
	v_cndmask_b32_e32 v1, v1, v2, vcc
	v_cvt_pk_bf16_f32 v2, v0, v1
	v_add_co_u32_e64 v0, s[6:7], s0, v64
	s_mov_b32 s0, 0x10000
	s_nop 0
	v_addc_co_u32_e64 v1, s[6:7], 0, v65, s[6:7]
	global_store_dword v[0:1], v2, off
	v_mul_f32_e32 v2, v38, v70
	v_cndmask_b32_e32 v4, v2, v3, vcc
	s_mov_b64 s[76:77], s[68:69]
	s_mov_b64 s[82:83], s[74:75]
	v_mov_b32_dpp v4, v4 quad_perm:[1,0,3,2] row_mask:0xf bank_mask:0xf bound_ctrl:1
	v_cndmask_b32_e32 v2, v4, v2, vcc
	v_cndmask_b32_e32 v3, v3, v4, vcc
	v_cvt_pk_bf16_f32 v2, v2, v3
	global_store_dword v[0:1], v2, off offset:64
	v_mul_f32_e32 v2, v22, v70
	v_mul_f32_e32 v3, v23, v71
	v_cndmask_b32_e32 v4, v2, v3, vcc
	s_mov_b64 s[80:81], s[72:73]
	s_mov_b64 s[78:79], s[70:71]
	v_mov_b32_dpp v4, v4 quad_perm:[1,0,3,2] row_mask:0xf bank_mask:0xf bound_ctrl:1
	v_cndmask_b32_e32 v2, v4, v2, vcc
	v_cndmask_b32_e32 v3, v3, v4, vcc
	v_cvt_pk_bf16_f32 v2, v2, v3
	global_store_dword v[0:1], v2, off offset:128
	v_mul_f32_e32 v2, v6, v70
	v_mul_f32_e32 v3, v7, v71
	v_cndmask_b32_e32 v4, v2, v3, vcc
	s_nop 1
	v_mov_b32_dpp v4, v4 quad_perm:[1,0,3,2] row_mask:0xf bank_mask:0xf bound_ctrl:1
	v_cndmask_b32_e32 v2, v4, v2, vcc
	v_cndmask_b32_e32 v3, v3, v4, vcc
	v_cvt_pk_bf16_f32 v2, v2, v3
	global_store_dword v[0:1], v2, off offset:192
	v_mul_f32_e32 v0, v56, v72
	v_mul_f32_e32 v1, v57, v73
	v_cndmask_b32_e32 v2, v0, v1, vcc
	v_mul_f32_e32 v3, v41, v73
	s_nop 0
	v_mov_b32_dpp v2, v2 quad_perm:[1,0,3,2] row_mask:0xf bank_mask:0xf bound_ctrl:1
	v_cndmask_b32_e32 v0, v2, v0, vcc
	v_cndmask_b32_e32 v1, v1, v2, vcc
	v_cvt_pk_bf16_f32 v2, v0, v1
	v_add_co_u32_e64 v0, s[6:7], s0, v64
	s_mov_b32 s0, 0x12000
	s_nop 0
	v_addc_co_u32_e64 v1, s[6:7], 0, v65, s[6:7]
	global_store_dword v[0:1], v2, off
	v_mul_f32_e32 v2, v40, v72
	v_cndmask_b32_e32 v4, v2, v3, vcc
	s_nop 1
	v_mov_b32_dpp v4, v4 quad_perm:[1,0,3,2] row_mask:0xf bank_mask:0xf bound_ctrl:1
	v_cndmask_b32_e32 v2, v4, v2, vcc
	v_cndmask_b32_e32 v3, v3, v4, vcc
	v_cvt_pk_bf16_f32 v2, v2, v3
	global_store_dword v[0:1], v2, off offset:64
	v_mul_f32_e32 v2, v24, v72
	v_mul_f32_e32 v3, v25, v73
	v_cndmask_b32_e32 v4, v2, v3, vcc
	s_nop 1
	v_mov_b32_dpp v4, v4 quad_perm:[1,0,3,2] row_mask:0xf bank_mask:0xf bound_ctrl:1
	v_cndmask_b32_e32 v2, v4, v2, vcc
	v_cndmask_b32_e32 v3, v3, v4, vcc
	v_cvt_pk_bf16_f32 v2, v2, v3
	global_store_dword v[0:1], v2, off offset:128
	v_mul_f32_e32 v2, v8, v72
	v_mul_f32_e32 v3, v9, v73
	v_cndmask_b32_e32 v4, v2, v3, vcc
	s_nop 1
	v_mov_b32_dpp v4, v4 quad_perm:[1,0,3,2] row_mask:0xf bank_mask:0xf bound_ctrl:1
	v_cndmask_b32_e32 v2, v4, v2, vcc
	v_cndmask_b32_e32 v3, v3, v4, vcc
; #define GAS __attribute__((address_space(1)))
; __device__ __forceinline__ unsigned cvt_pk_bf16(float lo, float hi) { unsigned r; asm volatile("v_cvt_pk_bf16_f32 %0, %1, %2" : "=v"(r) : "v"(lo), "v"(hi)); return r; }
; template <int AV>
; __device__ __forceinline__ void block(const BlockRef& cur, const BlockRef& nxt, char* lds, Seam& S, const int wid, const QNorm& QN) {
;     ...
; #pragma unroll
;     for (int r = 0; r < 16; r += 2) { const int orow0 = (r & 3) + 8 * (r >> 2);
; #pragma unroll
;         for (int d0 = 0; d0 < 4; ++d0) { const float a = o[d0][r] * rli[r], b = o[d0][r + 1] * rli[r + 1];
;             const float send = odd ? a : b;
;             const float recv = __int_as_float(__builtin_amdgcn_mov_dpp(__float_as_int(send), 0xB1, 0xF, 0xF, true));
;             *(GAS unsigned*)(Ow + (size_t)orow0 * OS * 2 + d0 * 64 + voff_o) = cvt_pk_bf16(odd ? recv : a, odd ? b : recv); } }
;     __syncthreads();
	v_cvt_pk_bf16_f32 v2, v2, v3
	global_store_dword v[0:1], v2, off offset:192
	v_mul_f32_e32 v0, v58, v74
	v_mul_f32_e32 v1, v59, v75
	v_cndmask_b32_e32 v2, v0, v1, vcc
	v_mul_f32_e32 v3, v43, v75
	s_nop 0
	v_mov_b32_dpp v2, v2 quad_perm:[1,0,3,2] row_mask:0xf bank_mask:0xf bound_ctrl:1
	v_cndmask_b32_e32 v0, v2, v0, vcc
	v_cndmask_b32_e32 v1, v1, v2, vcc
	v_cvt_pk_bf16_f32 v2, v0, v1
	v_add_co_u32_e64 v0, s[6:7], s0, v64
	s_mov_b32 s0, 0x18000
	s_nop 0
	v_addc_co_u32_e64 v1, s[6:7], 0, v65, s[6:7]
	global_store_dword v[0:1], v2, off
	v_mul_f32_e32 v2, v42, v74
	v_cndmask_b32_e32 v4, v2, v3, vcc
	s_nop 1
	v_mov_b32_dpp v4, v4 quad_perm:[1,0,3,2] row_mask:0xf bank_mask:0xf bound_ctrl:1
	v_cndmask_b32_e32 v2, v4, v2, vcc
	v_cndmask_b32_e32 v3, v3, v4, vcc
	v_cvt_pk_bf16_f32 v2, v2, v3
	global_store_dword v[0:1], v2, off offset:64
	v_mul_f32_e32 v2, v26, v74
	v_mul_f32_e32 v3, v27, v75
	v_cndmask_b32_e32 v4, v2, v3, vcc
	s_nop 1
	v_mov_b32_dpp v4, v4 quad_perm:[1,0,3,2] row_mask:0xf bank_mask:0xf bound_ctrl:1
	v_cndmask_b32_e32 v2, v4, v2, vcc
	v_cndmask_b32_e32 v3, v3, v4, vcc
	v_cvt_pk_bf16_f32 v2, v2, v3
	global_store_dword v[0:1], v2, off offset:128
	v_mul_f32_e32 v2, v10, v74
	v_mul_f32_e32 v3, v11, v75
	v_cndmask_b32_e32 v4, v2, v3, vcc
	s_nop 1
	v_mov_b32_dpp v4, v4 quad_perm:[1,0,3,2] row_mask:0xf bank_mask:0xf bound_ctrl:1
	v_cndmask_b32_e32 v2, v4, v2, vcc
	v_cndmask_b32_e32 v3, v3, v4, vcc
	v_cvt_pk_bf16_f32 v2, v2, v3
	global_store_dword v[0:1], v2, off offset:192
	v_mul_f32_e32 v0, v60, v76
	v_mul_f32_e32 v1, v61, v77
	v_cndmask_b32_e32 v2, v0, v1, vcc
	v_mul_f32_e32 v3, v45, v77
	s_nop 0
	v_mov_b32_dpp v2, v2 quad_perm:[1,0,3,2] row_mask:0xf bank_mask:0xf bound_ctrl:1
	v_cndmask_b32_e32 v0, v2, v0, vcc
	v_cndmask_b32_e32 v1, v1, v2, vcc
	v_cvt_pk_bf16_f32 v2, v0, v1
	v_add_co_u32_e64 v0, s[6:7], s0, v64
	s_mov_b32 s0, 0x1a000
	s_nop 0
	v_addc_co_u32_e64 v1, s[6:7], 0, v65, s[6:7]
	global_store_dword v[0:1], v2, off
	v_mul_f32_e32 v2, v44, v76
	v_cndmask_b32_e32 v4, v2, v3, vcc
	s_nop 1
	v_mov_b32_dpp v4, v4 quad_perm:[1,0,3,2] row_mask:0xf bank_mask:0xf bound_ctrl:1
	v_cndmask_b32_e32 v2, v4, v2, vcc
	v_cndmask_b32_e32 v3, v3, v4, vcc
	v_cvt_pk_bf16_f32 v2, v2, v3
	global_store_dword v[0:1], v2, off offset:64
	v_mul_f32_e32 v2, v28, v76
	v_mul_f32_e32 v3, v29, v77
	v_cndmask_b32_e32 v4, v2, v3, vcc
	s_nop 1
	v_mov_b32_dpp v4, v4 quad_perm:[1,0,3,2] row_mask:0xf bank_mask:0xf bound_ctrl:1
	v_cndmask_b32_e32 v2, v4, v2, vcc
	v_cndmask_b32_e32 v3, v3, v4, vcc
	v_cvt_pk_bf16_f32 v2, v2, v3
	global_store_dword v[0:1], v2, off offset:128
	v_mul_f32_e32 v2, v12, v76
	v_mul_f32_e32 v3, v13, v77
	v_cndmask_b32_e32 v4, v2, v3, vcc
	s_nop 1
	v_mov_b32_dpp v4, v4 quad_perm:[1,0,3,2] row_mask:0xf bank_mask:0xf bound_ctrl:1
	v_cndmask_b32_e32 v2, v4, v2, vcc
	v_cndmask_b32_e32 v3, v3, v4, vcc
	v_cvt_pk_bf16_f32 v2, v2, v3
	global_store_dword v[0:1], v2, off offset:192
	v_mul_f32_e32 v0, v62, v78
	v_mul_f32_e32 v1, v63, v79
	v_cndmask_b32_e32 v2, v0, v1, vcc
	v_mul_f32_e32 v3, v47, v79
	s_nop 0
	v_mov_b32_dpp v2, v2 quad_perm:[1,0,3,2] row_mask:0xf bank_mask:0xf bound_ctrl:1
	v_cndmask_b32_e32 v0, v2, v0, vcc
	v_cndmask_b32_e32 v1, v1, v2, vcc
	v_cvt_pk_bf16_f32 v2, v0, v1
	v_add_co_u32_e64 v0, s[6:7], s0, v64
	s_mov_b32 s0, s31
	s_nop 0
	v_addc_co_u32_e64 v1, s[6:7], 0, v65, s[6:7]
	global_store_dword v[0:1], v2, off
	v_mul_f32_e32 v2, v46, v78
	v_cndmask_b32_e32 v4, v2, v3, vcc
	s_mov_b64 s[6:7], s[66:67]
	s_nop 0
	v_mov_b32_dpp v4, v4 quad_perm:[1,0,3,2] row_mask:0xf bank_mask:0xf bound_ctrl:1
	v_cndmask_b32_e32 v2, v4, v2, vcc
	v_cndmask_b32_e32 v3, v3, v4, vcc
	v_cvt_pk_bf16_f32 v2, v2, v3
	global_store_dword v[0:1], v2, off offset:64
	v_mul_f32_e32 v2, v30, v78
	v_mul_f32_e32 v3, v31, v79
	v_cndmask_b32_e32 v4, v2, v3, vcc
	s_nop 1
	v_mov_b32_dpp v4, v4 quad_perm:[1,0,3,2] row_mask:0xf bank_mask:0xf bound_ctrl:1
	v_cndmask_b32_e32 v2, v4, v2, vcc
	v_cndmask_b32_e32 v3, v3, v4, vcc
	v_cvt_pk_bf16_f32 v2, v2, v3
	global_store_dword v[0:1], v2, off offset:128
	v_mul_f32_e32 v2, v14, v78
	v_mul_f32_e32 v3, v15, v79
	v_cndmask_b32_e32 v4, v2, v3, vcc
	s_nop 1
	v_mov_b32_dpp v4, v4 quad_perm:[1,0,3,2] row_mask:0xf bank_mask:0xf bound_ctrl:1
	v_cndmask_b32_e32 v2, v4, v2, vcc
	v_cndmask_b32_e32 v3, v3, v4, vcc
	s_andn2_b64 vcc, exec, s[64:65]
	v_cvt_pk_bf16_f32 v2, v2, v3
	global_store_dword v[0:1], v2, off offset:192
	s_barrier
	s_cbranch_vccz .LBB0_548

; __device__ __forceinline__ void qnorm_rope(const u32x2 (&q)[12], const QCoef& C, i32x8 (&qf)[3]) {
;     float sn = 0.f, sp = 0.f, v[8];
; #pragma unroll
;     for (int f = 0; f < 8; ++f) { unpk8(q[f], v);
; #pragma unroll
;         for (int e = 0; e < 8; ++e) sn += v[e] * v[e]; }
; #pragma unroll
;     for (int f = 8; f < 12; ++f) { unpk8(q[f], v);
; #pragma unroll
;         for (int e = 0; e < 8; ++e) sp += v[e] * v[e]; }
;     { auto rr = __builtin_amdgcn_permlane32_swap(__float_as_uint(sn), __float_as_uint(sn), false, false); sn = __uint_as_float(rr[0]) + __uint_as_float(rr[1]); }
.LBB0_513:
	s_waitcnt vmcnt(27)
	v_cvt_pk_f32_fp8_e32 v[174:175], v86
	v_cvt_pk_f32_fp8_sdwa v[168:169], v86 src0_sel:WORD_1
	s_add_i32 s0, s86, s40
	v_lshlrev_b32_e32 v189, 2, v88
	v_or_b32_e32 v88, s0, v196
	v_lshlrev_b32_e32 v89, 2, v188
	v_cvt_pk_f32_fp8_e32 v[172:173], v87
	v_mul_f32_e32 v86, v175, v175
	v_sub_u32_e32 v197, v88, v189
	v_and_b32_e32 v88, 32, v188
	v_and_b32_e32 v90, 48, v89
	v_lshlrev_b32_e32 v195, 6, v196
	v_cvt_pk_f32_fp8_sdwa v[166:167], v87 src0_sel:WORD_1
	v_pk_fma_f32 v[86:87], v[174:175], v[174:175], v[86:87] op_sel_hi:[1,1,0]
	v_bitop3_b32 v194, v89, v88, 48 bitop3:0x6c
	v_bitop3_b32 v193, v90, v195, v88 bitop3:0xde
	v_pk_fma_f32 v[86:87], v[168:169], v[168:169], v[86:87]
	v_mul_f32_e32 v88, v169, v169
	v_pk_add_f32 v[86:87], v[88:89], v[86:87] op_sel_hi:[0,1]
	v_pk_fma_f32 v[86:87], v[172:173], v[172:173], v[86:87]
	v_mul_f32_e32 v88, v173, v173
	s_waitcnt vmcnt(26)
	v_cvt_pk_f32_fp8_e32 v[170:171], v84
	v_pk_add_f32 v[86:87], v[88:89], v[86:87] op_sel_hi:[0,1]
	v_pk_fma_f32 v[86:87], v[166:167], v[166:167], v[86:87]
	v_mul_f32_e32 v88, v167, v167
	v_cvt_pk_f32_fp8_sdwa v[162:163], v84 src0_sel:WORD_1
	v_pk_add_f32 v[86:87], v[88:89], v[86:87] op_sel_hi:[0,1]
	v_cvt_pk_f32_fp8_e32 v[164:165], v85
	v_cvt_pk_f32_fp8_sdwa v[160:161], v85 src0_sel:WORD_1
	v_pk_fma_f32 v[84:85], v[170:171], v[170:171], v[86:87]
	v_mul_f32_e32 v86, v171, v171
	v_pk_add_f32 v[84:85], v[86:87], v[84:85] op_sel_hi:[0,1]
	v_pk_fma_f32 v[84:85], v[162:163], v[162:163], v[84:85]
	v_mul_f32_e32 v86, v163, v163
	v_pk_add_f32 v[84:85], v[86:87], v[84:85] op_sel_hi:[0,1]
	v_pk_fma_f32 v[84:85], v[164:165], v[164:165], v[84:85]
	v_mul_f32_e32 v86, v165, v165
	s_waitcnt vmcnt(25)
	v_cvt_pk_f32_fp8_e32 v[142:143], v82
	v_pk_add_f32 v[84:85], v[86:87], v[84:85] op_sel_hi:[0,1]
	v_pk_fma_f32 v[84:85], v[160:161], v[160:161], v[84:85]
	v_mul_f32_e32 v86, v161, v161
	v_cvt_pk_f32_fp8_sdwa v[138:139], v82 src0_sel:WORD_1
	v_pk_add_f32 v[84:85], v[86:87], v[84:85] op_sel_hi:[0,1]
	v_cvt_pk_f32_fp8_e32 v[140:141], v83
	v_cvt_pk_f32_fp8_sdwa v[136:137], v83 src0_sel:WORD_1
	v_pk_fma_f32 v[82:83], v[142:143], v[142:143], v[84:85]
	v_mul_f32_e32 v84, v143, v143
	v_pk_add_f32 v[82:83], v[84:85], v[82:83] op_sel_hi:[0,1]
	v_pk_fma_f32 v[82:83], v[138:139], v[138:139], v[82:83]
	v_mul_f32_e32 v84, v139, v139
	v_pk_add_f32 v[82:83], v[84:85], v[82:83] op_sel_hi:[0,1]
	v_pk_fma_f32 v[82:83], v[140:141], v[140:141], v[82:83]
	v_mul_f32_e32 v84, v141, v141
	s_waitcnt vmcnt(24)
	v_cvt_pk_f32_fp8_e32 v[134:135], v80
	v_pk_add_f32 v[82:83], v[84:85], v[82:83] op_sel_hi:[0,1]
	v_pk_fma_f32 v[82:83], v[136:137], v[136:137], v[82:83]
	v_mul_f32_e32 v84, v137, v137
	v_cvt_pk_f32_fp8_sdwa v[130:131], v80 src0_sel:WORD_1
	v_pk_add_f32 v[82:83], v[84:85], v[82:83] op_sel_hi:[0,1]
	v_cvt_pk_f32_fp8_e32 v[132:133], v81
	v_cvt_pk_f32_fp8_sdwa v[128:129], v81 src0_sel:WORD_1
	v_pk_fma_f32 v[80:81], v[134:135], v[134:135], v[82:83]
	v_mul_f32_e32 v82, v135, v135
	v_pk_add_f32 v[80:81], v[82:83], v[80:81] op_sel_hi:[0,1]
	v_pk_fma_f32 v[80:81], v[130:131], v[130:131], v[80:81]
	v_mul_f32_e32 v82, v131, v131
	v_pk_add_f32 v[80:81], v[82:83], v[80:81] op_sel_hi:[0,1]
	v_pk_fma_f32 v[80:81], v[132:133], v[132:133], v[80:81]
	v_mul_f32_e32 v82, v133, v133
	s_waitcnt vmcnt(23)
	v_cvt_pk_f32_fp8_e32 v[126:127], v78
	v_pk_add_f32 v[80:81], v[82:83], v[80:81] op_sel_hi:[0,1]
	v_pk_fma_f32 v[80:81], v[128:129], v[128:129], v[80:81]
	v_mul_f32_e32 v82, v129, v129
	v_cvt_pk_f32_fp8_sdwa v[122:123], v78 src0_sel:WORD_1
	v_pk_add_f32 v[80:81], v[82:83], v[80:81] op_sel_hi:[0,1]
	v_cvt_pk_f32_fp8_e32 v[124:125], v79
	v_cvt_pk_f32_fp8_sdwa v[120:121], v79 src0_sel:WORD_1
	v_pk_fma_f32 v[78:79], v[126:127], v[126:127], v[80:81]
	v_mul_f32_e32 v80, v127, v127
	v_pk_add_f32 v[78:79], v[80:81], v[78:79] op_sel_hi:[0,1]
	v_pk_fma_f32 v[78:79], v[122:123], v[122:123], v[78:79]
	v_mul_f32_e32 v80, v123, v123
	v_pk_add_f32 v[78:79], v[80:81], v[78:79] op_sel_hi:[0,1]
	v_pk_fma_f32 v[78:79], v[124:125], v[124:125], v[78:79]
	v_mul_f32_e32 v80, v125, v125
	s_waitcnt vmcnt(22)
	v_cvt_pk_f32_fp8_e32 v[118:119], v76
	v_pk_add_f32 v[78:79], v[80:81], v[78:79] op_sel_hi:[0,1]
	v_pk_fma_f32 v[78:79], v[120:121], v[120:121], v[78:79]
	v_mul_f32_e32 v80, v121, v121
	v_cvt_pk_f32_fp8_sdwa v[114:115], v76 src0_sel:WORD_1
	v_pk_add_f32 v[78:79], v[80:81], v[78:79] op_sel_hi:[0,1]
	v_cvt_pk_f32_fp8_e32 v[116:117], v77
	v_cvt_pk_f32_fp8_sdwa v[112:113], v77 src0_sel:WORD_1
	v_pk_fma_f32 v[76:77], v[118:119], v[118:119], v[78:79]
	v_mul_f32_e32 v78, v119, v119
	v_pk_add_f32 v[76:77], v[78:79], v[76:77] op_sel_hi:[0,1]
	v_pk_fma_f32 v[76:77], v[114:115], v[114:115], v[76:77]
	v_mul_f32_e32 v78, v115, v115
	v_pk_add_f32 v[76:77], v[78:79], v[76:77] op_sel_hi:[0,1]
	v_pk_fma_f32 v[76:77], v[116:117], v[116:117], v[76:77]
	v_mul_f32_e32 v78, v117, v117
	s_waitcnt vmcnt(21)
	v_cvt_pk_f32_fp8_e32 v[110:111], v74
	v_pk_add_f32 v[76:77], v[78:79], v[76:77] op_sel_hi:[0,1]
	v_pk_fma_f32 v[76:77], v[112:113], v[112:113], v[76:77]
	v_mul_f32_e32 v78, v113, v113
	v_cvt_pk_f32_fp8_sdwa v[106:107], v74 src0_sel:WORD_1
	s_waitcnt vmcnt(19)
; __device__ __forceinline__ unsigned cvt_pk4_fp8(float a, float b, float c, float d) { int w; asm("" : "=v"(w));     w = __builtin_amdgcn_cvt_pk_fp8_f32(a, b, w, false); w = __builtin_amdgcn_cvt_pk_fp8_f32(c, d, w, true); return (unsigned)w; }
; __device__ __forceinline__ void qnorm_rope(const u32x2 (&q)[12], const QCoef& C, i32x8 (&qf)[3]) {
;     float sn = 0.f, sp = 0.f, v[8];
; #pragma unroll
;     for (int f = 0; f < 8; ++f) { unpk8(q[f], v);
; #pragma unroll
;         for (int e = 0; e < 8; ++e) sn += v[e] * v[e]; }
; #pragma unroll
;     for (int f = 8; f < 12; ++f) { unpk8(q[f], v);
; #pragma unroll
;         for (int e = 0; e < 8; ++e) sp += v[e] * v[e]; }
;     { auto rr = __builtin_amdgcn_permlane32_swap(__float_as_uint(sn), __float_as_uint(sn), false, false); sn = __uint_as_float(rr[0]) + __uint_as_float(rr[1]); }
;     { auto rr = __builtin_amdgcn_permlane32_swap(__float_as_uint(sp), __float_as_uint(sp), false, false); sp = __uint_as_float(rr[0]) + __uint_as_float(rr[1]); }
;     const float rn = rsqrtf(sn * (1.f / 128.f) + RMS_EPS), rp = rsqrtf(sp * (1.f / 64.f) + RMS_EPS);
; #pragma unroll
;     for (int f = 0; f < 8; ++f) { unpk8(q[f], v);
; #pragma unroll
;         for (int e = 0; e < 8; ++e) v[e] *= rn * QSC;
;         qf[f >> 2][2 * (f & 3)] = (int)cvt_pk4_fp8(v[0], v[1], v[2], v[3]); qf[f >> 2][2 * (f & 3) + 1] = (int)cvt_pk4_fp8(v[4], v[5], v[6], v[7]); }
	v_cvt_pk_f32_fp8_e32 v[90:91], v66
	v_pk_add_f32 v[76:77], v[78:79], v[76:77] op_sel_hi:[0,1]
	v_cvt_pk_f32_fp8_e32 v[108:109], v75
	v_cvt_pk_f32_fp8_sdwa v[104:105], v75 src0_sel:WORD_1
	v_pk_fma_f32 v[74:75], v[110:111], v[110:111], v[76:77]
	v_mul_f32_e32 v76, v111, v111
	v_cvt_pk_f32_fp8_sdwa v[86:87], v66 src0_sel:WORD_1
	v_pk_add_f32 v[74:75], v[76:77], v[74:75] op_sel_hi:[0,1]
	v_pk_fma_f32 v[74:75], v[106:107], v[106:107], v[74:75]
	v_mul_f32_e32 v76, v107, v107
	v_cvt_pk_f32_fp8_e32 v[82:83], v67
	v_mul_f32_e32 v66, v91, v91
	v_pk_add_f32 v[74:75], v[76:77], v[74:75] op_sel_hi:[0,1]
	v_cvt_pk_f32_fp8_sdwa v[80:81], v67 src0_sel:WORD_1
	v_pk_fma_f32 v[66:67], v[90:91], v[90:91], v[66:67] op_sel_hi:[1,1,0]
	v_pk_fma_f32 v[74:75], v[108:109], v[108:109], v[74:75]
	v_mul_f32_e32 v76, v109, v109
	v_cvt_pk_f32_fp8_e32 v[102:103], v70
	v_cvt_pk_f32_fp8_sdwa v[98:99], v70 src0_sel:WORD_1
	v_pk_fma_f32 v[66:67], v[86:87], v[86:87], v[66:67]
	v_mul_f32_e32 v70, v87, v87
	v_pk_add_f32 v[74:75], v[76:77], v[74:75] op_sel_hi:[0,1]
	v_pk_add_f32 v[66:67], v[70:71], v[66:67] op_sel_hi:[0,1]
	v_pk_fma_f32 v[74:75], v[104:105], v[104:105], v[74:75]
	v_mul_f32_e32 v76, v105, v105
	v_pk_fma_f32 v[66:67], v[82:83], v[82:83], v[66:67]
	v_mul_f32_e32 v70, v83, v83
	v_pk_add_f32 v[176:177], v[76:77], v[74:75] op_sel_hi:[0,1]
	v_pk_add_f32 v[66:67], v[70:71], v[66:67] op_sel_hi:[0,1]
	s_waitcnt vmcnt(18)
	v_cvt_pk_f32_fp8_e32 v[74:75], v64
	v_pk_fma_f32 v[66:67], v[80:81], v[80:81], v[66:67]
	v_mul_f32_e32 v70, v81, v81
	v_cvt_pk_f32_fp8_e32 v[100:101], v71
	v_cvt_pk_f32_fp8_sdwa v[96:97], v71 src0_sel:WORD_1
	v_pk_add_f32 v[76:77], v[70:71], v[66:67] op_sel_hi:[0,1]
	v_cvt_pk_f32_fp8_sdwa v[70:71], v64 src0_sel:WORD_1
	v_cvt_pk_f32_fp8_e32 v[66:67], v65
	v_pk_fma_f32 v[76:77], v[74:75], v[74:75], v[76:77]
	v_mul_f32_e32 v78, v75, v75
	v_pk_add_f32 v[76:77], v[78:79], v[76:77] op_sel_hi:[0,1]
	v_cvt_pk_f32_fp8_sdwa v[64:65], v65 src0_sel:WORD_1
	v_pk_fma_f32 v[76:77], v[70:71], v[70:71], v[76:77]
	v_mul_f32_e32 v78, v71, v71
	v_pk_add_f32 v[76:77], v[78:79], v[76:77] op_sel_hi:[0,1]
	v_pk_fma_f32 v[76:77], v[66:67], v[66:67], v[76:77]
	v_mul_f32_e32 v78, v67, v67
	s_waitcnt vmcnt(17)
	v_cvt_pk_f32_fp8_e32 v[94:95], v72
	v_pk_add_f32 v[76:77], v[78:79], v[76:77] op_sel_hi:[0,1]
	v_pk_fma_f32 v[76:77], v[64:65], v[64:65], v[76:77]
	v_mul_f32_e32 v78, v65, v65
	v_cvt_pk_f32_fp8_sdwa v[92:93], v72 src0_sel:WORD_1
	v_pk_add_f32 v[76:77], v[78:79], v[76:77] op_sel_hi:[0,1]
	v_cvt_pk_f32_fp8_e32 v[88:89], v73
	v_cvt_pk_f32_fp8_sdwa v[84:85], v73 src0_sel:WORD_1
	v_pk_fma_f32 v[72:73], v[94:95], v[94:95], v[76:77]
	v_mul_f32_e32 v76, v95, v95
	v_pk_add_f32 v[72:73], v[76:77], v[72:73] op_sel_hi:[0,1]
	v_pk_fma_f32 v[72:73], v[92:93], v[92:93], v[72:73]
	v_mul_f32_e32 v76, v93, v93
	v_pk_add_f32 v[72:73], v[76:77], v[72:73] op_sel_hi:[0,1]
	v_pk_fma_f32 v[72:73], v[88:89], v[88:89], v[72:73]
	v_mul_f32_e32 v76, v89, v89
	v_pk_add_f32 v[72:73], v[76:77], v[72:73] op_sel_hi:[0,1]
	s_waitcnt vmcnt(16)
	v_cvt_pk_f32_fp8_e32 v[78:79], v68
	v_pk_fma_f32 v[72:73], v[84:85], v[84:85], v[72:73]
	v_mul_f32_e32 v76, v85, v85
	v_pk_add_f32 v[178:179], v[76:77], v[72:73] op_sel_hi:[0,1]
	v_cvt_pk_f32_fp8_sdwa v[76:77], v68 src0_sel:WORD_1
	v_cvt_pk_f32_fp8_e32 v[72:73], v69
	v_pk_fma_f32 v[178:179], v[78:79], v[78:79], v[178:179]
	v_mul_f32_e32 v180, v79, v79
	v_pk_add_f32 v[178:179], v[180:181], v[178:179] op_sel_hi:[0,1]
	v_cvt_pk_f32_fp8_sdwa v[68:69], v69 src0_sel:WORD_1
	v_pk_fma_f32 v[178:179], v[76:77], v[76:77], v[178:179]
	v_mul_f32_e32 v180, v77, v77
	v_pk_add_f32 v[178:179], v[180:181], v[178:179] op_sel_hi:[0,1]
	v_pk_fma_f32 v[178:179], v[72:73], v[72:73], v[178:179]
	v_mul_f32_e32 v180, v73, v73
	v_pk_add_f32 v[178:179], v[180:181], v[178:179] op_sel_hi:[0,1]
	v_pk_fma_f32 v[178:179], v[68:69], v[68:69], v[178:179]
	v_mul_f32_e32 v180, v69, v69
	v_pk_add_f32 v[178:179], v[180:181], v[178:179] op_sel_hi:[0,1]
	v_pk_fma_f32 v[176:177], v[102:103], v[102:103], v[176:177]
	v_mul_f32_e32 v180, v103, v103
	v_pk_add_f32 v[176:177], v[180:181], v[176:177] op_sel_hi:[0,1]
	v_pk_fma_f32 v[176:177], v[98:99], v[98:99], v[176:177]
	v_mul_f32_e32 v180, v99, v99
	v_pk_add_f32 v[176:177], v[180:181], v[176:177] op_sel_hi:[0,1]
	v_pk_fma_f32 v[176:177], v[100:101], v[100:101], v[176:177]
	v_mul_f32_e32 v180, v101, v101
	v_pk_add_f32 v[176:177], v[180:181], v[176:177] op_sel_hi:[0,1]
	v_pk_fma_f32 v[176:177], v[96:97], v[96:97], v[176:177]
	v_mul_f32_e32 v180, v97, v97
	v_pk_add_f32 v[176:177], v[180:181], v[176:177] op_sel_hi:[0,1]
	v_mov_b32_e32 v181, v176
	s_nop 1
	v_permlane32_swap_b32_e32 v176, v181
	v_mov_b32_e32 v180, v178
	s_nop 1
	v_permlane32_swap_b32_e32 v178, v180
	v_mov_b32_e32 v179, v176
	v_pk_add_f32 v[176:177], v[178:179], v[180:181]
	s_nop 0
	v_pk_fma_f32 v[176:177], v[176:177], s[62:63], v[186:187] op_sel_hi:[1,1,0]
	s_nop 0
	v_mul_f32_e32 v178, 0x4b800000, v177
	v_cmp_gt_f32_e64 s[6:7], s9, v177
	v_cmp_gt_f32_e32 vcc, s9, v176
	s_nop 0
	v_cndmask_b32_e64 v177, v177, v178, s[6:7]
	v_rsq_f32_e32 v177, v177
	s_nop 0
	v_mul_f32_e32 v178, 0x45800000, v177
	v_cndmask_b32_e64 v177, v177, v178, s[6:7]
	v_mul_f32_e32 v178, 0x4b800000, v176
	v_cndmask_b32_e32 v176, v176, v178, vcc
	v_mul_f32_e32 v182, 0x3e800000, v177
	v_rsq_f32_e32 v198, v176
	v_mul_f32_e32 v174, v174, v182
	v_mul_f32_e32 v175, v175, v182
	v_mul_f32_e32 v176, v168, v182
	v_mul_f32_e32 v177, v167, v182
	v_mul_f32_e32 v169, v169, v182
	v_cvt_pk_fp8_f32 v168, v174, v175
	v_mul_f32_e32 v172, v172, v182
	v_mul_f32_e32 v173, v173, v182
	v_mul_f32_e32 v166, v166, v182
	v_cvt_pk_fp8_f32 v168, v176, v169 op_sel:[0,0,1]
; __device__ __forceinline__ unsigned cvt_pk4_fp8(float a, float b, float c, float d) { int w; asm("" : "=v"(w));     w = __builtin_amdgcn_cvt_pk_fp8_f32(a, b, w, false); w = __builtin_amdgcn_cvt_pk_fp8_f32(c, d, w, true); return (unsigned)w; }
; __device__ __forceinline__ void qnorm_rope(const u32x2 (&q)[12], const QCoef& C, i32x8 (&qf)[3]) {
;     ...
;     for (int f = 0; f < 8; ++f) { unpk8(q[f], v);
; #pragma unroll
;         for (int e = 0; e < 8; ++e) v[e] *= rn * QSC;
;         qf[f >> 2][2 * (f & 3)] = (int)cvt_pk4_fp8(v[0], v[1], v[2], v[3]); qf[f >> 2][2 * (f & 3) + 1] = (int)cvt_pk4_fp8(v[4], v[5], v[6], v[7]); }
; #pragma unroll
;     for (int f = 0; f < 2; ++f) {
;         float t1[8], t2[8], o1[8], o2[8]; unpk8(q[8 + f], t1); unpk8(q[10 + f], t2);
; #pragma unroll
;         for (int e = 0; e < 8; ++e) { const int j = 2 * f + (e >> 2), k = e & 3; const float a = t1[e] * (rp * QSC) * C.ga[j][k], b = t2[e] * (rp * QSC) * C.gb[j][k]; o1[e] = a * C.c[j][k] - b * C.s[j][k]; o2[e] = b * C.c[j][k] + a * C.s[j][k]; }
;         qf[2][2 * f] = (int)cvt_pk4_fp8(o1[0], o1[1], o1[2], o1[3]); qf[2][2 * f + 1] = (int)cvt_pk4_fp8(o1[4], o1[5], o1[6], o1[7]);
;         qf[2][4 + 2 * f] = (int)cvt_pk4_fp8(o2[0], o2[1], o2[2], o2[3]); qf[2][5 + 2 * f] = (int)cvt_pk4_fp8(o2[4], o2[5], o2[6], o2[7]); }
	v_cvt_pk_fp8_f32 v169, v172, v173
	v_mul_f32_e32 v100, v100, v182
	v_mul_f32_e32 v101, v101, v182
	v_cvt_pk_fp8_f32 v169, v166, v177 op_sel:[0,0,1]
	v_mul_f32_e32 v166, v170, v182
	v_mul_f32_e32 v171, v171, v182
	v_mul_f32_e32 v162, v162, v182
	v_mul_f32_e32 v163, v163, v182
	v_mul_f32_e32 v164, v164, v182
	v_mul_f32_e32 v165, v165, v182
	v_mul_f32_e32 v160, v160, v182
	v_mul_f32_e32 v161, v161, v182
	v_mul_f32_e32 v142, v142, v182
	v_mul_f32_e32 v143, v143, v182
	v_mul_f32_e32 v138, v138, v182
	v_mul_f32_e32 v139, v139, v182
	v_mul_f32_e32 v140, v140, v182
	v_mul_f32_e32 v141, v141, v182
	v_mul_f32_e32 v136, v136, v182
	v_mul_f32_e32 v137, v137, v182
	v_mul_f32_e32 v134, v134, v182
	v_mul_f32_e32 v135, v135, v182
	v_mul_f32_e32 v130, v130, v182
	v_mul_f32_e32 v131, v131, v182
	v_mul_f32_e32 v132, v132, v182
	v_mul_f32_e32 v133, v133, v182
	v_mul_f32_e32 v128, v128, v182
	v_mul_f32_e32 v129, v129, v182
	v_mul_f32_e32 v126, v126, v182
	v_mul_f32_e32 v127, v127, v182
	v_mul_f32_e32 v122, v122, v182
	v_mul_f32_e32 v123, v123, v182
	v_mul_f32_e32 v124, v124, v182
	v_mul_f32_e32 v125, v125, v182
	v_mul_f32_e32 v120, v120, v182
	v_mul_f32_e32 v121, v121, v182
	v_mul_f32_e32 v118, v118, v182
	v_mul_f32_e32 v119, v119, v182
	v_mul_f32_e32 v114, v114, v182
	v_mul_f32_e32 v115, v115, v182
	v_mul_f32_e32 v116, v116, v182
	v_mul_f32_e32 v117, v117, v182
	v_mul_f32_e32 v112, v112, v182
	v_mul_f32_e32 v113, v113, v182
	v_mul_f32_e32 v110, v110, v182
	v_mul_f32_e32 v111, v111, v182
	v_mul_f32_e32 v106, v106, v182
	v_mul_f32_e32 v107, v107, v182
	v_mul_f32_e32 v108, v108, v182
	v_mul_f32_e32 v109, v109, v182
	v_mul_f32_e32 v104, v104, v182
	v_mul_f32_e32 v105, v105, v182
	v_mul_f32_e32 v102, v102, v182
	v_mul_f32_e32 v103, v103, v182
	v_mul_f32_e32 v98, v98, v182
	v_mul_f32_e32 v99, v99, v182
	v_mul_f32_e32 v96, v96, v182
	v_mul_f32_e32 v97, v97, v182
	v_cvt_pk_fp8_f32 v183, v100, v101
	v_cvt_pk_fp8_f32 v182, v102, v103
	v_mul_f32_e32 v199, 0x45800000, v198
	s_waitcnt vmcnt(8)
	v_mov_b32_e32 v100, v60
	v_cvt_pk_fp8_f32 v183, v96, v97 op_sel:[0,0,1]
	v_cndmask_b32_e32 v96, v198, v199, vcc
	v_cvt_pk_fp8_f32 v182, v98, v99 op_sel:[0,0,1]
	v_mul_f32_e32 v96, 0x3e800000, v96
	v_mov_b32_e32 v98, v94
	v_mov_b32_e32 v99, v90
	v_pk_mul_f32 v[98:99], v[98:99], v[96:97] op_sel_hi:[1,0]
	v_mov_b32_e32 v101, v56
	v_pk_mul_f32 v[98:99], v[100:101], v[98:99]
	v_mov_b32_e32 v100, v52
	v_mov_b32_e32 v101, v48
	v_pk_mul_f32 v[100:101], v[100:101], v[98:99]
	v_mov_b32_e32 v90, v95
	v_sub_f32_e32 v94, v101, v100
	v_mov_b32_e32 v100, v48
	v_mov_b32_e32 v101, v52
	v_pk_mul_f32 v[98:99], v[100:101], v[98:99]
	v_mov_b32_e32 v56, v61
	v_add_f32_e32 v97, v98, v99
	v_pk_mul_f32 v[90:91], v[90:91], v[96:97] op_sel_hi:[1,0]
	v_mov_b32_e32 v48, v53
	v_pk_mul_f32 v[56:57], v[56:57], v[90:91]
	v_mov_b32_e32 v52, v49
	v_pk_mul_f32 v[60:61], v[48:49], v[56:57]
	v_pk_mul_f32 v[48:49], v[52:53], v[56:57]
	v_mov_b32_e32 v52, v62
	v_add_f32_e32 v56, v48, v49
	v_mov_b32_e32 v48, v92
	v_mov_b32_e32 v49, v86
	v_pk_mul_f32 v[48:49], v[48:49], v[96:97] op_sel_hi:[1,0]
	v_mov_b32_e32 v53, v58
	v_pk_mul_f32 v[48:49], v[52:53], v[48:49]
	v_mov_b32_e32 v52, v54
	v_mov_b32_e32 v53, v50
	v_pk_mul_f32 v[52:53], v[52:53], v[48:49]
	v_mov_b32_e32 v86, v93
	v_sub_f32_e32 v57, v53, v52
	v_mov_b32_e32 v52, v50
	v_mov_b32_e32 v53, v54
	v_pk_mul_f32 v[48:49], v[52:53], v[48:49]
	v_sub_f32_e32 v60, v61, v60
	v_add_f32_e32 v61, v48, v49
	v_pk_mul_f32 v[48:49], v[86:87], v[96:97] op_sel_hi:[1,0]
	v_mov_b32_e32 v58, v63
	v_pk_mul_f32 v[48:49], v[58:59], v[48:49]
	v_mov_b32_e32 v50, v55
	v_mov_b32_e32 v54, v51
	v_pk_mul_f32 v[52:53], v[50:51], v[48:49]
	v_pk_mul_f32 v[48:49], v[54:55], v[48:49]
	v_sub_f32_e32 v52, v53, v52
	v_add_f32_e32 v53, v48, v49
	v_mov_b32_e32 v48, v88
	v_mov_b32_e32 v49, v82
	v_pk_mul_f32 v[48:49], v[48:49], v[96:97] op_sel_hi:[1,0]
	v_mov_b32_e32 v50, v44
	v_mov_b32_e32 v51, v40
	v_pk_mul_f32 v[48:49], v[50:51], v[48:49]
	v_mov_b32_e32 v50, v36
	v_mov_b32_e32 v51, v32
	v_pk_mul_f32 v[50:51], v[50:51], v[48:49]
	v_mov_b32_e32 v82, v89
	v_sub_f32_e32 v54, v51, v50
	v_mov_b32_e32 v50, v32
	v_mov_b32_e32 v51, v36
	v_pk_mul_f32 v[48:49], v[50:51], v[48:49]
	v_mov_b32_e32 v40, v45
	v_add_f32_e32 v50, v48, v49
	v_pk_mul_f32 v[48:49], v[82:83], v[96:97] op_sel_hi:[1,0]
	v_mov_b32_e32 v32, v37
	v_pk_mul_f32 v[40:41], v[40:41], v[48:49]
	v_mov_b32_e32 v36, v33
	v_pk_mul_f32 v[44:45], v[32:33], v[40:41]
	v_pk_mul_f32 v[32:33], v[36:37], v[40:41]
	v_add_f32_e32 v40, v32, v33
	v_mov_b32_e32 v32, v84
	v_mov_b32_e32 v33, v80
	v_cvt_pk_fp8_f32 v170, v166, v171
	v_pk_mul_f32 v[32:33], v[32:33], v[96:97] op_sel_hi:[1,0]
	v_mov_b32_e32 v36, v46
	v_mov_b32_e32 v37, v42
	v_cvt_pk_fp8_f32 v171, v164, v165
	v_pk_mul_f32 v[32:33], v[36:37], v[32:33]
	v_mov_b32_e32 v36, v38
	v_mov_b32_e32 v37, v34
	v_pk_mul_f32 v[36:37], v[36:37], v[32:33]
	v_mov_b32_e32 v80, v85
	v_sub_f32_e32 v41, v37, v36
	v_mov_b32_e32 v36, v34
	v_mov_b32_e32 v37, v38
	v_pk_mul_f32 v[32:33], v[36:37], v[32:33]
	v_cvt_pk_fp8_f32 v171, v160, v161 op_sel:[0,0,1]
	v_sub_f32_e32 v44, v45, v44
	v_add_f32_e32 v45, v32, v33
	v_pk_mul_f32 v[32:33], v[80:81], v[96:97] op_sel_hi:[1,0]
	v_mov_b32_e32 v42, v47
	v_cvt_pk_fp8_f32 v165, v50, v40
	v_pk_mul_f32 v[32:33], v[42:43], v[32:33]
	v_mov_b32_e32 v34, v39
	v_mov_b32_e32 v38, v35
	v_cvt_pk_fp8_f32 v161, v54, v44
	v_pk_mul_f32 v[36:37], v[34:35], v[32:33]
	v_pk_mul_f32 v[32:33], v[38:39], v[32:33]
	v_sub_f32_e32 v34, v37, v36
	v_add_f32_e32 v32, v32, v33
	v_cvt_pk_fp8_f32 v165, v45, v32 op_sel:[0,0,1]
	v_mov_b32_e32 v32, v78
	v_mov_b32_e32 v33, v74
	v_cvt_pk_fp8_f32 v161, v41, v34 op_sel:[0,0,1]
	v_pk_mul_f32 v[32:33], v[32:33], v[96:97] op_sel_hi:[1,0]
	s_waitcnt vmcnt(0)
; __device__ __forceinline__ unsigned cvt_pk4_fp8(float a, float b, float c, float d) { int w; asm("" : "=v"(w));     w = __builtin_amdgcn_cvt_pk_fp8_f32(a, b, w, false); w = __builtin_amdgcn_cvt_pk_fp8_f32(c, d, w, true); return (unsigned)w; }
; __device__ __forceinline__ void qkt(f32x16& p0, f32x16& p1, const char* stg, int ka, const i32x8* qf, const f32x16& minit) {
;     p0 = minit; p1 = minit;
; #pragma unroll
;     for (int s = 0; s < 3; ++s) { const char* a = stg + SOFF_K + s * 4096 + ka; const char* b = stg + SOFF_K + s * 4096 + (ka ^ 16);
;         const i32x4 a0 = *reinterpret_cast<const i32x4*>(a), a1 = *reinterpret_cast<const i32x4*>(b);
;         const i32x4 c0 = *reinterpret_cast<const i32x4*>(a + 2048), c1 = *reinterpret_cast<const i32x4*>(b + 2048);
;         p0 = __builtin_amdgcn_mfma_scale_f32_32x32x64_f8f6f4(__builtin_shufflevector(a0, a1, 0, 1, 2, 3, 4, 5, 6, 7), qf[s], p0, 0, 0, 0, 0, 0, 0);
;         p1 = __builtin_amdgcn_mfma_scale_f32_32x32x64_f8f6f4(__builtin_shufflevector(c0, c1, 0, 1, 2, 3, 4, 5, 6, 7), qf[s], p1, 0, 0, 0, 0, 0, 0); }
; }
; __device__ __forceinline__ void qnorm_rope(const u32x2 (&q)[12], const QCoef& C, i32x8 (&qf)[3]) {
;     ...
;     for (int f = 0; f < 2; ++f) {
;         float t1[8], t2[8], o1[8], o2[8]; unpk8(q[8 + f], t1); unpk8(q[10 + f], t2);
; #pragma unroll
;         for (int e = 0; e < 8; ++e) { const int j = 2 * f + (e >> 2), k = e & 3; const float a = t1[e] * (rp * QSC) * C.ga[j][k], b = t2[e] * (rp * QSC) * C.gb[j][k]; o1[e] = a * C.c[j][k] - b * C.s[j][k]; o2[e] = b * C.c[j][k] + a * C.s[j][k]; }
;         qf[2][2 * f] = (int)cvt_pk4_fp8(o1[0], o1[1], o1[2], o1[3]); qf[2][2 * f + 1] = (int)cvt_pk4_fp8(o1[4], o1[5], o1[6], o1[7]);
;         qf[2][4 + 2 * f] = (int)cvt_pk4_fp8(o2[0], o2[1], o2[2], o2[3]); qf[2][5 + 2 * f] = (int)cvt_pk4_fp8(o2[4], o2[5], o2[6], o2[7]); }
	v_mov_b32_e32 v34, v28
	v_mov_b32_e32 v35, v24
	v_pk_mul_f32 v[32:33], v[34:35], v[32:33]
	v_mov_b32_e32 v34, v20
	v_mov_b32_e32 v35, v16
	v_pk_mul_f32 v[34:35], v[34:35], v[32:33]
	v_mov_b32_e32 v74, v79
	v_sub_f32_e32 v36, v35, v34
	v_mov_b32_e32 v34, v16
	v_mov_b32_e32 v35, v20
	v_pk_mul_f32 v[32:33], v[34:35], v[32:33]
	v_mov_b32_e32 v24, v29
	v_add_f32_e32 v34, v32, v33
	v_pk_mul_f32 v[32:33], v[74:75], v[96:97] op_sel_hi:[1,0]
	v_mov_b32_e32 v16, v21
	v_pk_mul_f32 v[24:25], v[24:25], v[32:33]
	v_mov_b32_e32 v20, v17
	v_pk_mul_f32 v[28:29], v[16:17], v[24:25]
	v_pk_mul_f32 v[16:17], v[20:21], v[24:25]
	v_mov_b32_e32 v20, v30
	v_add_f32_e32 v24, v16, v17
	v_mov_b32_e32 v16, v76
	v_mov_b32_e32 v17, v70
	v_pk_mul_f32 v[16:17], v[16:17], v[96:97] op_sel_hi:[1,0]
	v_mov_b32_e32 v21, v26
	v_pk_mul_f32 v[16:17], v[20:21], v[16:17]
	v_mov_b32_e32 v20, v22
	v_mov_b32_e32 v21, v18
	v_pk_mul_f32 v[20:21], v[20:21], v[16:17]
	v_mov_b32_e32 v70, v77
	v_sub_f32_e32 v25, v21, v20
	v_mov_b32_e32 v20, v18
	v_mov_b32_e32 v21, v22
	v_pk_mul_f32 v[16:17], v[20:21], v[16:17]
	v_sub_f32_e32 v28, v29, v28
	v_add_f32_e32 v29, v16, v17
	v_pk_mul_f32 v[16:17], v[70:71], v[96:97] op_sel_hi:[1,0]
	v_mov_b32_e32 v26, v31
	v_pk_mul_f32 v[16:17], v[26:27], v[16:17]
	v_mov_b32_e32 v18, v23
	v_mov_b32_e32 v22, v19
	v_pk_mul_f32 v[20:21], v[18:19], v[16:17]
	v_pk_mul_f32 v[16:17], v[22:23], v[16:17]
	v_sub_f32_e32 v20, v21, v20
	v_add_f32_e32 v21, v16, v17
	v_mov_b32_e32 v16, v72
	v_mov_b32_e32 v17, v66
	v_pk_mul_f32 v[16:17], v[16:17], v[96:97] op_sel_hi:[1,0]
	v_mov_b32_e32 v18, v12
	v_mov_b32_e32 v19, v8
	v_pk_mul_f32 v[16:17], v[18:19], v[16:17]
	v_mov_b32_e32 v18, v4
	v_mov_b32_e32 v19, v0
	v_pk_mul_f32 v[18:19], v[18:19], v[16:17]
	v_mov_b32_e32 v66, v73
	v_sub_f32_e32 v22, v19, v18
	v_mov_b32_e32 v18, v0
	v_mov_b32_e32 v19, v4
	v_pk_mul_f32 v[16:17], v[18:19], v[16:17]
	v_mov_b32_e32 v8, v13
	v_add_f32_e32 v18, v16, v17
	v_pk_mul_f32 v[16:17], v[66:67], v[96:97] op_sel_hi:[1,0]
	v_mov_b32_e32 v0, v5
	v_pk_mul_f32 v[8:9], v[8:9], v[16:17]
	v_mov_b32_e32 v4, v1
	v_pk_mul_f32 v[12:13], v[0:1], v[8:9]
	v_pk_mul_f32 v[0:1], v[4:5], v[8:9]
	v_mov_b32_e32 v4, v14
	v_add_f32_e32 v8, v0, v1
	v_mov_b32_e32 v0, v68
	v_mov_b32_e32 v1, v64
	v_pk_mul_f32 v[0:1], v[0:1], v[96:97] op_sel_hi:[1,0]
	v_mov_b32_e32 v5, v10
	v_pk_mul_f32 v[0:1], v[4:5], v[0:1]
	v_mov_b32_e32 v4, v6
	v_mov_b32_e32 v5, v2
	v_pk_mul_f32 v[4:5], v[4:5], v[0:1]
	v_cvt_pk_fp8_f32 v170, v162, v163 op_sel:[0,0,1]
	v_sub_f32_e32 v9, v5, v4
	v_mov_b32_e32 v4, v2
	v_mov_b32_e32 v5, v6
	v_sub_f32_e32 v12, v13, v12
	v_pk_mul_f32 v[0:1], v[4:5], v[0:1]
	v_mov_b32_e32 v64, v69
	v_cvt_pk_fp8_f32 v172, v142, v143
	v_cvt_pk_fp8_f32 v173, v140, v141
	v_cvt_pk_fp8_f32 v174, v134, v135
	v_cvt_pk_fp8_f32 v175, v132, v133
	v_cvt_pk_fp8_f32 v176, v126, v127
	v_cvt_pk_fp8_f32 v177, v124, v125
	v_cvt_pk_fp8_f32 v178, v118, v119
	v_cvt_pk_fp8_f32 v179, v116, v117
	v_cvt_pk_fp8_f32 v180, v110, v111
	v_cvt_pk_fp8_f32 v181, v108, v109
	v_cvt_pk_fp8_f32 v160, v94, v60
	v_cvt_pk_fp8_f32 v164, v97, v56
	v_add_f32_e32 v13, v0, v1
	v_pk_mul_f32 v[0:1], v[64:65], v[96:97] op_sel_hi:[1,0]
	v_mov_b32_e32 v10, v15
	v_cvt_pk_fp8_f32 v162, v36, v28
	v_cvt_pk_fp8_f32 v163, v22, v12
	v_cvt_pk_fp8_f32 v166, v34, v24
	v_cvt_pk_fp8_f32 v167, v18, v8
	v_pk_mul_f32 v[0:1], v[10:11], v[0:1]
	v_mov_b32_e32 v2, v7
	v_mov_b32_e32 v6, v3
	v_pk_mul_f32 v[4:5], v[2:3], v[0:1]
	v_pk_mul_f32 v[0:1], v[6:7], v[0:1]
	v_sub_f32_e32 v2, v5, v4
	v_add_f32_e32 v0, v0, v1
	v_cvt_pk_fp8_f32 v172, v138, v139 op_sel:[0,0,1]
	v_cvt_pk_fp8_f32 v173, v136, v137 op_sel:[0,0,1]
	v_cvt_pk_fp8_f32 v174, v130, v131 op_sel:[0,0,1]
	v_cvt_pk_fp8_f32 v175, v128, v129 op_sel:[0,0,1]
	v_cvt_pk_fp8_f32 v176, v122, v123 op_sel:[0,0,1]
	v_cvt_pk_fp8_f32 v177, v120, v121 op_sel:[0,0,1]
	v_cvt_pk_fp8_f32 v178, v114, v115 op_sel:[0,0,1]
	v_cvt_pk_fp8_f32 v179, v112, v113 op_sel:[0,0,1]
	v_cvt_pk_fp8_f32 v180, v106, v107 op_sel:[0,0,1]
	v_cvt_pk_fp8_f32 v181, v104, v105 op_sel:[0,0,1]
	v_cvt_pk_fp8_f32 v160, v57, v52 op_sel:[0,0,1]
	v_cvt_pk_fp8_f32 v164, v61, v53 op_sel:[0,0,1]
	v_cvt_pk_fp8_f32 v162, v25, v20 op_sel:[0,0,1]
	v_cvt_pk_fp8_f32 v163, v9, v2 op_sel:[0,0,1]
	v_cvt_pk_fp8_f32 v166, v29, v21 op_sel:[0,0,1]
	v_cvt_pk_fp8_f32 v167, v13, v0 op_sel:[0,0,1]
	s_mul_i32 s1, s41, 0x5000
	s_add_i32 s1, s1, 0
	v_bitop3_b32 v194, v194, 16, v195 bitop3:0x36
	v_add_u32_e32 v64, s1, v193
	v_add_u32_e32 v65, s1, v194
	ds_read_b128 v[16:19], v64
	ds_read_b128 v[20:23], v65
	ds_read_b128 v[48:51], v64 offset:2048
	ds_read_b128 v[52:55], v65 offset:2048
	v_mov_b64_e32 v[46:47], s[26:27]
	v_mov_b64_e32 v[44:45], s[24:25]
	v_mov_b64_e32 v[42:43], s[22:23]
	v_mov_b64_e32 v[40:41], s[20:21]
	v_mov_b64_e32 v[38:39], s[18:19]
	v_mov_b64_e32 v[36:37], s[16:17]
	v_mov_b64_e32 v[34:35], s[14:15]
	v_mov_b64_e32 v[32:33], s[12:13]
	s_cmp_gt_i32 s0, 62
	s_waitcnt lgkmcnt(2)
	v_mfma_f32_32x32x64_f8f6f4 v[0:15], v[16:23], v[168:175], v[32:47]
	s_waitcnt lgkmcnt(0)
	v_mfma_f32_32x32x64_f8f6f4 v[16:31], v[48:55], v[168:175], v[32:47]
	s_nop 14
	ds_read_b128 v[36:39], v65 offset:4096
	ds_read_b128 v[32:35], v64 offset:4096
	ds_read_b128 v[40:43], v64 offset:6144
	ds_read_b128 v[44:47], v65 offset:6144
	s_waitcnt lgkmcnt(2)
	v_mfma_f32_32x32x64_f8f6f4 v[0:15], v[32:39], v[176:183], v[0:15]
	s_waitcnt lgkmcnt(0)
	v_mfma_f32_32x32x64_f8f6f4 v[16:31], v[40:47], v[176:183], v[16:31]
	ds_read_b128 v[36:39], v65 offset:8192
	ds_read_b128 v[32:35], v64 offset:8192
	ds_read_b128 v[40:43], v64 offset:10240
	ds_read_b128 v[44:47], v65 offset:10240
	s_waitcnt lgkmcnt(2)
	v_mfma_f32_32x32x64_f8f6f4 v[0:15], v[32:39], v[160:167], v[0:15]
	s_waitcnt lgkmcnt(0)
	v_mfma_f32_32x32x64_f8f6f4 v[16:31], v[40:47], v[160:167], v[16:31]
	s_cbranch_scc1 .LBB0_515
; __device__ __forceinline__ void mask_tile(f32x16& p0, f32x16& p1, int dq, unsigned W) {
;     const float NEG = -__builtin_inff();
; #pragma unroll
;     for (int r = 0; r < 16; ++r) {
;         const int c = (r & 3) + 8 * (r >> 2);
;         if ((unsigned)(dq - c) >= W) p0[r] = NEG;
;         if ((unsigned)(dq - c - 32) >= W) p1[r] = NEG;
;     }
; }
	v_cmp_gt_u32_e32 vcc, 2.0, v197
	v_add_u32_e32 v32, 0xbfffffe0, v197
	s_nop 14
	v_cndmask_b32_e32 v0, v187, v0, vcc
	v_cmp_lt_u32_e32 vcc, s3, v32
	v_add_u32_e32 v32, 0xbfffffff, v197
	s_nop 0
	v_cndmask_b32_e32 v16, v187, v16, vcc
	v_cmp_lt_u32_e32 vcc, s3, v32
	v_add_u32_e32 v32, 0xbfffffdf, v197
	s_nop 0
	v_cndmask_b32_e32 v1, v187, v1, vcc
	v_cmp_lt_u32_e32 vcc, s3, v32
	v_add_u32_e32 v32, 0xbffffffe, v197
	s_nop 0
	v_cndmask_b32_e32 v17, v187, v17, vcc
	v_cmp_lt_u32_e32 vcc, s3, v32
	v_add_u32_e32 v32, 0xbfffffde, v197
	s_nop 0
	v_cndmask_b32_e32 v2, v187, v2, vcc
	v_cmp_lt_u32_e32 vcc, s3, v32
	v_add_u32_e32 v32, 0xbffffffd, v197
	s_nop 0
	v_cndmask_b32_e32 v18, v187, v18, vcc
	v_cmp_lt_u32_e32 vcc, s3, v32
	v_add_u32_e32 v32, 0xbfffffdd, v197
	s_nop 0
	v_cndmask_b32_e32 v3, v187, v3, vcc
	v_cmp_lt_u32_e32 vcc, s3, v32
	v_add_u32_e32 v32, 0xbffffff8, v197
	s_nop 0
	v_cndmask_b32_e32 v19, v187, v19, vcc
	v_cmp_lt_u32_e32 vcc, s3, v32
	v_add_u32_e32 v32, 0xbfffffd8, v197
	s_nop 0
	v_cndmask_b32_e32 v4, v187, v4, vcc
	v_cmp_lt_u32_e32 vcc, s3, v32
	v_add_u32_e32 v32, 0xbffffff7, v197
	s_nop 0
	v_cndmask_b32_e32 v20, v187, v20, vcc
	v_cmp_lt_u32_e32 vcc, s3, v32
	v_add_u32_e32 v32, 0xbfffffd7, v197
	s_nop 0
	v_cndmask_b32_e32 v5, v187, v5, vcc
	v_cmp_lt_u32_e32 vcc, s3, v32
	v_add_u32_e32 v32, 0xbffffff6, v197
	s_nop 0
	v_cndmask_b32_e32 v21, v187, v21, vcc
	v_cmp_lt_u32_e32 vcc, s3, v32
	v_add_u32_e32 v32, 0xbfffffd6, v197
	s_nop 0
	v_cndmask_b32_e32 v6, v187, v6, vcc
	v_cmp_lt_u32_e32 vcc, s3, v32
	v_add_u32_e32 v32, 0xbffffff5, v197
	s_nop 0
	v_cndmask_b32_e32 v22, v187, v22, vcc
	v_cmp_lt_u32_e32 vcc, s3, v32
	v_add_u32_e32 v32, 0xbfffffd5, v197
	s_nop 0
	v_cndmask_b32_e32 v7, v187, v7, vcc
	v_cmp_lt_u32_e32 vcc, s3, v32
	v_add_u32_e32 v32, 0xbffffff0, v197
	s_nop 0
	v_cndmask_b32_e32 v23, v187, v23, vcc
	v_cmp_lt_u32_e32 vcc, s3, v32
	v_add_u32_e32 v32, 0xbfffffd0, v197
	s_nop 0
	v_cndmask_b32_e32 v8, v187, v8, vcc
	v_cmp_lt_u32_e32 vcc, s3, v32
	v_add_u32_e32 v32, 0xbfffffef, v197
	s_nop 0
	v_cndmask_b32_e32 v24, v187, v24, vcc
	v_cmp_lt_u32_e32 vcc, s3, v32
	v_add_u32_e32 v32, 0xbfffffcf, v197
	s_nop 0
	v_cndmask_b32_e32 v9, v187, v9, vcc
	v_cmp_lt_u32_e32 vcc, s3, v32
	v_add_u32_e32 v32, 0xbfffffee, v197
	s_nop 0
	v_cndmask_b32_e32 v25, v187, v25, vcc
	v_cmp_lt_u32_e32 vcc, s3, v32
	v_add_u32_e32 v32, 0xbfffffce, v197
	s_nop 0
	v_cndmask_b32_e32 v10, v187, v10, vcc
	v_cmp_lt_u32_e32 vcc, s3, v32
	v_add_u32_e32 v32, 0xbfffffed, v197
	s_nop 0
	v_cndmask_b32_e32 v26, v187, v26, vcc
	v_cmp_lt_u32_e32 vcc, s3, v32
	v_add_u32_e32 v32, 0xbfffffcd, v197
	s_nop 0
	v_cndmask_b32_e32 v11, v187, v11, vcc
	v_cmp_lt_u32_e32 vcc, s3, v32
	v_add_u32_e32 v32, 0xbfffffe8, v197
	s_nop 0
	v_cndmask_b32_e32 v27, v187, v27, vcc
	v_cmp_lt_u32_e32 vcc, s3, v32
	v_add_u32_e32 v32, 0xbfffffc8, v197
	s_nop 0
	v_cndmask_b32_e32 v12, v187, v12, vcc
	v_cmp_lt_u32_e32 vcc, s3, v32
	v_add_u32_e32 v32, 0xbfffffe7, v197
	s_nop 0
	v_cndmask_b32_e32 v28, v187, v28, vcc
	v_cmp_lt_u32_e32 vcc, s3, v32
	v_add_u32_e32 v32, 0xbfffffc7, v197
	s_nop 0
	v_cndmask_b32_e32 v13, v187, v13, vcc
	v_cmp_lt_u32_e32 vcc, s3, v32
	v_add_u32_e32 v32, 0xbfffffe6, v197
	s_nop 0
	v_cndmask_b32_e32 v29, v187, v29, vcc
	v_cmp_lt_u32_e32 vcc, s3, v32
	v_add_u32_e32 v32, 0xbfffffc6, v197
	s_nop 0
	v_cndmask_b32_e32 v14, v187, v14, vcc
	v_cmp_lt_u32_e32 vcc, s3, v32
	v_add_u32_e32 v32, 0xbfffffe5, v197
	s_nop 0
	v_cndmask_b32_e32 v30, v187, v30, vcc
	v_cmp_lt_u32_e32 vcc, s3, v32
	v_add_u32_e32 v32, 0xbfffffc5, v197
	s_nop 0
	v_cndmask_b32_e32 v15, v187, v15, vcc
	v_cmp_lt_u32_e32 vcc, s3, v32
	s_nop 1
	v_cndmask_b32_e32 v31, v187, v31, vcc

; __device__ __forceinline__ unsigned cvt_pk4_fp8(float a, float b, float c, float d) { int w; asm("" : "=v"(w));     w = __builtin_amdgcn_cvt_pk_fp8_f32(a, b, w, false); w = __builtin_amdgcn_cvt_pk_fp8_f32(c, d, w, true); return (unsigned)w; }
; template <bool FIRST>
; __device__ __forceinline__ bool partialSM(f32x16& p0, f32x16& p1, float& M, f32x16& minit, float& alpha) {
;     float tmax = p0[0]; for (int r = 1; r < 16; ++r) tmax = fmaxf(tmax, p0[r]); for (int r = 0; r < 16; ++r) tmax = fmaxf(tmax, p1[r]);
;     { auto rr = __builtin_amdgcn_permlane32_swap(__float_as_uint(tmax), __float_as_uint(tmax), false, false);
;       tmax = fmaxf(__uint_as_float(rr[0]), __uint_as_float(rr[1])); }
;     const float d0 = tmax - PLOG2;
;     const bool moved = FIRST || !__all(d0 <= THR * 1.4426950408889634f);
;     if (__builtin_expect(moved, FIRST)) {
;         const float d = FIRST ? d0 : fmaxf(d0, 0.f);
;         alpha = __builtin_amdgcn_exp2f(-d); M += d;
;         for (int r = 0; r < 16; ++r) { p0[r] -= d; p1[r] -= d; }
;         const float mi = PLOG2 - M;
;         for (int r = 0; r < 16; ++r) minit[r] = mi;
;     } else alpha = 1.f;
;     for (int r = 0; r < 16; ++r) p0[r] = __builtin_amdgcn_exp2f(p0[r]);
;     return moved;
; }
; __device__ __forceinline__ void finishSM(f32x16& p0, f32x16& p1, i32x8& pa) {
;     for (int r = 0; r < 16; ++r) p1[r] = __builtin_amdgcn_exp2f(p1[r]);
; #pragma unroll
;     for (int v = 0; v < 4; ++v) { pa[v] = (int)cvt_pk4_fp8(p0[4 * v], p0[4 * v + 1], p0[4 * v + 2], p0[4 * v + 3]); pa[4 + v] = (int)cvt_pk4_fp8(p1[4 * v], p1[4 * v + 1], p1[4 * v + 2], p1[4 * v + 3]); }
; }
.LBB0_517:
	v_max_f32_e32 v32, v32, v32
	v_max_f32_e32 v33, v33, v33
	v_max_f32_e32 v32, v32, v33
	v_add_f32_e32 v195, -4.0, v32
	v_sub_f32_e32 v0, v0, v195
	v_sub_f32_e32 v1, v1, v195
	v_sub_f32_e32 v2, v2, v195
	v_sub_f32_e32 v3, v3, v195
	v_sub_f32_e32 v4, v4, v195
	v_sub_f32_e32 v5, v5, v195
	v_sub_f32_e32 v6, v6, v195
	v_sub_f32_e32 v7, v7, v195
	v_sub_f32_e32 v8, v8, v195
	v_sub_f32_e32 v9, v9, v195
	v_sub_f32_e32 v10, v10, v195
	v_sub_f32_e32 v11, v11, v195
	v_sub_f32_e32 v12, v12, v195
	v_sub_f32_e32 v13, v13, v195
	v_sub_f32_e32 v14, v14, v195
	v_sub_f32_e32 v15, v15, v195
	v_exp_f32_e32 v32, v0
	v_exp_f32_e32 v33, v1
	v_exp_f32_e32 v34, v2
	v_exp_f32_e32 v35, v3
	v_exp_f32_e32 v36, v4
	v_exp_f32_e32 v37, v5
	v_exp_f32_e32 v38, v6
	v_exp_f32_e32 v39, v7
	v_exp_f32_e32 v40, v8
	v_exp_f32_e32 v41, v9
	v_exp_f32_e32 v42, v10
	v_exp_f32_e32 v43, v11
	v_exp_f32_e32 v44, v12
	v_exp_f32_e32 v45, v13
	v_exp_f32_e32 v46, v14
	v_exp_f32_e32 v47, v15
	s_cmp_gt_i32 s41, 4
	s_cselect_b32 s1, -5, 1
	v_sub_f32_e32 v16, v16, v195
	v_sub_f32_e32 v17, v17, v195
	v_sub_f32_e32 v18, v18, v195
	v_sub_f32_e32 v19, v19, v195
	v_sub_f32_e32 v20, v20, v195
	v_sub_f32_e32 v21, v21, v195
	v_sub_f32_e32 v22, v22, v195
	v_sub_f32_e32 v23, v23, v195
	v_sub_f32_e32 v24, v24, v195
	v_sub_f32_e32 v25, v25, v195
	v_sub_f32_e32 v26, v26, v195
	v_sub_f32_e32 v27, v27, v195
	v_sub_f32_e32 v28, v28, v195
	v_sub_f32_e32 v29, v29, v195
	v_sub_f32_e32 v30, v30, v195
	v_sub_f32_e32 v31, v31, v195
	v_sub_f32_e32 v80, 4.0, v195
	s_add_i32 s1, s1, s41
	v_mov_b32_e32 v81, v80
	v_mov_b32_e32 v82, v80
	v_mov_b32_e32 v83, v80
	v_mov_b32_e32 v84, v80
	v_mov_b32_e32 v85, v80
	v_mov_b32_e32 v86, v80
	v_mov_b32_e32 v87, v80
	v_mov_b32_e32 v88, v80
	v_mov_b32_e32 v89, v80
	v_mov_b32_e32 v90, v80
	v_mov_b32_e32 v91, v80
	v_mov_b32_e32 v92, v80
	v_mov_b32_e32 v93, v80
	v_mov_b32_e32 v94, v80
	v_mov_b32_e32 v95, v80
	s_mul_i32 s92, s1, 0x5000
	s_add_i32 s6, s92, 0
	v_add_u32_e32 v48, s6, v193
	v_add_u32_e32 v49, s6, v194
	ds_read_b128 v[0:3], v48
	ds_read_b128 v[4:7], v49
	ds_read_b128 v[8:11], v48 offset:2048
	ds_read_b128 v[12:15], v49 offset:2048
	v_mov_b64_e32 v[110:111], v[94:95]
	v_mov_b64_e32 v[108:109], v[92:93]
	v_mov_b64_e32 v[106:107], v[90:91]
	v_mov_b64_e32 v[104:105], v[88:89]
	v_mov_b64_e32 v[102:103], v[86:87]
	v_mov_b64_e32 v[100:101], v[84:85]
	v_mov_b64_e32 v[98:99], v[82:83]
	v_mov_b64_e32 v[96:97], v[80:81]
	s_waitcnt lgkmcnt(2)
	v_mfma_f32_32x32x64_f8f6f4 v[112:127], v[0:7], v[168:175], v[80:95]
	s_nop 0
	v_cvt_pk_fp8_f32 v66, v32, v33
	v_cvt_pk_fp8_f32 v67, v36, v37
	v_cvt_pk_fp8_f32 v68, v40, v41
	v_cvt_pk_fp8_f32 v69, v44, v45
	v_cvt_pk_fp8_f32 v66, v34, v35 op_sel:[0,0,1]
	v_cvt_pk_fp8_f32 v67, v38, v39 op_sel:[0,0,1]
	s_waitcnt lgkmcnt(0)
	v_mfma_f32_32x32x64_f8f6f4 v[96:111], v[8:15], v[168:175], v[96:111]
	ds_read_b128 v[0:3], v48 offset:4096
	ds_read_b128 v[4:7], v49 offset:4096
	ds_read_b128 v[8:11], v48 offset:6144
	ds_read_b128 v[12:15], v49 offset:6144
	v_cvt_pk_fp8_f32 v68, v42, v43 op_sel:[0,0,1]
	v_cvt_pk_fp8_f32 v69, v46, v47 op_sel:[0,0,1]
	s_waitcnt lgkmcnt(2)
	v_mfma_f32_32x32x64_f8f6f4 v[112:127], v[0:7], v[176:183], v[112:127]
	s_waitcnt lgkmcnt(0)
	v_mfma_f32_32x32x64_f8f6f4 v[96:111], v[8:15], v[176:183], v[96:111]
	ds_read_b128 v[0:3], v48 offset:8192
	ds_read_b128 v[4:7], v49 offset:8192
	ds_read_b128 v[8:11], v48 offset:10240
	ds_read_b128 v[12:15], v49 offset:10240
	s_waitcnt lgkmcnt(2)
	v_mfma_f32_32x32x64_f8f6f4 v[112:127], v[0:7], v[160:167], v[112:127]
	v_exp_f32_e32 v0, v16
	v_exp_f32_e32 v1, v17
	v_exp_f32_e32 v4, v20
	v_exp_f32_e32 v5, v21
	v_exp_f32_e32 v2, v18
	v_exp_f32_e32 v3, v19
	v_exp_f32_e32 v6, v22
	v_exp_f32_e32 v7, v23
	v_cvt_pk_fp8_f32 v70, v0, v1
	v_cvt_pk_fp8_f32 v71, v4, v5
	v_cvt_pk_fp8_f32 v70, v2, v3 op_sel:[0,0,1]
	v_cvt_pk_fp8_f32 v71, v6, v7 op_sel:[0,0,1]
	s_waitcnt lgkmcnt(0)
	v_mfma_f32_32x32x64_f8f6f4 v[96:111], v[8:15], v[160:167], v[96:111]
	v_exp_f32_e32 v8, v24
	v_exp_f32_e32 v9, v25
	v_exp_f32_e32 v12, v28
	v_exp_f32_e32 v13, v29
	v_exp_f32_e32 v10, v26
	v_exp_f32_e32 v11, v27
	v_exp_f32_e32 v14, v30
	v_exp_f32_e32 v15, v31
	v_cvt_pk_fp8_f32 v72, v8, v9
	v_cvt_pk_fp8_f32 v73, v12, v13
	v_cvt_pk_fp8_f32 v72, v10, v11 op_sel:[0,0,1]
	v_cvt_pk_fp8_f32 v73, v14, v15 op_sel:[0,0,1]
	ds_read_b128 v[4:7], v65 offset:12288
	ds_read_b128 v[0:3], v64 offset:12288
	ds_read_b128 v[8:11], v64 offset:14336
	ds_read_b128 v[12:15], v65 offset:14336
	s_cmpk_gt_i32 s0, 0x7e
	s_waitcnt lgkmcnt(2)
	v_mfma_f32_32x32x64_f8f6f4 v[48:63], v[66:73], v[0:7], 0
	s_waitcnt lgkmcnt(0)
	v_mfma_f32_32x32x64_f8f6f4 v[32:47], v[66:73], v[8:15], 0
	ds_read_b128 v[4:7], v65 offset:16384
	ds_read_b128 v[0:3], v64 offset:16384
	ds_read_b128 v[8:11], v64 offset:18432
	ds_read_b128 v[12:15], v65 offset:18432
	s_waitcnt lgkmcnt(2)
	v_mfma_f32_32x32x64_f8f6f4 v[16:31], v[66:73], v[0:7], 0
	s_waitcnt lgkmcnt(0)
	v_mfma_f32_32x32x64_f8f6f4 v[0:15], v[66:73], v[8:15], 0
	v_mfma_f32_32x32x64_f8f6f4 v[64:79], v[66:73], v[152:159], 0
	s_cbranch_scc1 .LBB0_519
; __device__ __forceinline__ void mask_tile(f32x16& p0, f32x16& p1, int dq, unsigned W) {
;     const float NEG = -__builtin_inff();
; #pragma unroll
;     for (int r = 0; r < 16; ++r) {
;         const int c = (r & 3) + 8 * (r >> 2);
;         if ((unsigned)(dq - c) >= W) p0[r] = NEG;
;         if ((unsigned)(dq - c - 32) >= W) p1[r] = NEG;
;     }
; }
	v_add_u32_e32 v81, 0xbfffffc0, v197
	v_cmp_lt_u32_e32 vcc, s3, v81
	v_add_u32_e32 v81, 0xbfffffa0, v197
	s_nop 0
	v_cndmask_b32_e32 v112, v187, v112, vcc
	v_cmp_lt_u32_e32 vcc, s3, v81
	v_add_u32_e32 v81, 0xbfffffbf, v197
	s_nop 0
	v_cndmask_b32_e32 v96, v187, v96, vcc
	v_cmp_lt_u32_e32 vcc, s3, v81
	v_add_u32_e32 v81, 0xbfffff9f, v197
	s_nop 0
	v_cndmask_b32_e32 v113, v187, v113, vcc
	v_cmp_lt_u32_e32 vcc, s3, v81
	v_add_u32_e32 v81, 0xbfffffbe, v197
	s_nop 0
	v_cndmask_b32_e32 v97, v187, v97, vcc
	v_cmp_lt_u32_e32 vcc, s3, v81
	v_add_u32_e32 v81, 0xbfffff9e, v197
	s_nop 0
	v_cndmask_b32_e32 v114, v187, v114, vcc
	v_cmp_lt_u32_e32 vcc, s3, v81
	v_add_u32_e32 v81, 0xbfffffbd, v197
	s_nop 0
	v_cndmask_b32_e32 v98, v187, v98, vcc
	v_cmp_lt_u32_e32 vcc, s3, v81
	v_add_u32_e32 v81, 0xbfffff9d, v197
	s_nop 0
	v_cndmask_b32_e32 v115, v187, v115, vcc
	v_cmp_lt_u32_e32 vcc, s3, v81
	v_add_u32_e32 v81, 0xbfffffb8, v197
	s_nop 0
	v_cndmask_b32_e32 v99, v187, v99, vcc
	v_cmp_lt_u32_e32 vcc, s3, v81
	v_add_u32_e32 v81, 0xbfffff98, v197
	s_nop 0
	v_cndmask_b32_e32 v116, v187, v116, vcc
	v_cmp_lt_u32_e32 vcc, s3, v81
	v_add_u32_e32 v81, 0xbfffffb7, v197
	s_nop 0
	v_cndmask_b32_e32 v100, v187, v100, vcc
	v_cmp_lt_u32_e32 vcc, s3, v81
	v_add_u32_e32 v81, 0xbfffff97, v197
	s_nop 0
	v_cndmask_b32_e32 v117, v187, v117, vcc
	v_cmp_lt_u32_e32 vcc, s3, v81
	v_add_u32_e32 v81, 0xbfffffb6, v197
	s_nop 0
	v_cndmask_b32_e32 v101, v187, v101, vcc
	v_cmp_lt_u32_e32 vcc, s3, v81
	v_add_u32_e32 v81, 0xbfffff96, v197
	s_nop 0
	v_cndmask_b32_e32 v118, v187, v118, vcc
	v_cmp_lt_u32_e32 vcc, s3, v81
	v_add_u32_e32 v81, 0xbfffffb5, v197
	s_nop 0
	v_cndmask_b32_e32 v102, v187, v102, vcc
	v_cmp_lt_u32_e32 vcc, s3, v81
	v_add_u32_e32 v81, 0xbfffff95, v197
	s_nop 0
	v_cndmask_b32_e32 v119, v187, v119, vcc
	v_cmp_lt_u32_e32 vcc, s3, v81
	v_add_u32_e32 v81, 0xbfffffb0, v197
	s_nop 0
	v_cndmask_b32_e32 v103, v187, v103, vcc
	v_cmp_lt_u32_e32 vcc, s3, v81
	v_add_u32_e32 v81, 0xbfffff90, v197
	s_nop 0
	v_cndmask_b32_e32 v120, v187, v120, vcc
	v_cmp_lt_u32_e32 vcc, s3, v81
	v_add_u32_e32 v81, 0xbfffffaf, v197
	s_nop 0
	v_cndmask_b32_e32 v104, v187, v104, vcc
	v_cmp_lt_u32_e32 vcc, s3, v81
	v_add_u32_e32 v81, 0xbfffff8f, v197
	s_nop 0
	v_cndmask_b32_e32 v121, v187, v121, vcc
	v_cmp_lt_u32_e32 vcc, s3, v81
	v_add_u32_e32 v81, 0xbfffffae, v197
	s_nop 0
	v_cndmask_b32_e32 v105, v187, v105, vcc
	v_cmp_lt_u32_e32 vcc, s3, v81
	v_add_u32_e32 v81, 0xbfffff8e, v197
	s_nop 0
	v_cndmask_b32_e32 v122, v187, v122, vcc
	v_cmp_lt_u32_e32 vcc, s3, v81
	v_add_u32_e32 v81, 0xbfffffad, v197
	s_nop 0
	v_cndmask_b32_e32 v106, v187, v106, vcc
	v_cmp_lt_u32_e32 vcc, s3, v81
	v_add_u32_e32 v81, 0xbfffff8d, v197
	s_nop 0
	v_cndmask_b32_e32 v123, v187, v123, vcc
	v_cmp_lt_u32_e32 vcc, s3, v81
	v_add_u32_e32 v81, 0xbfffffa8, v197
	s_nop 0
	v_cndmask_b32_e32 v107, v187, v107, vcc
	v_cmp_lt_u32_e32 vcc, s3, v81
	v_add_u32_e32 v81, 0xbfffff88, v197
	s_nop 0
	v_cndmask_b32_e32 v124, v187, v124, vcc
	v_cmp_lt_u32_e32 vcc, s3, v81
	v_add_u32_e32 v81, 0xbfffffa7, v197
	s_nop 0
	v_cndmask_b32_e32 v108, v187, v108, vcc
	v_cmp_lt_u32_e32 vcc, s3, v81
	v_add_u32_e32 v81, 0xbfffff87, v197
	s_nop 0
	v_cndmask_b32_e32 v125, v187, v125, vcc
	v_cmp_lt_u32_e32 vcc, s3, v81
	v_add_u32_e32 v81, 0xbfffffa6, v197
	s_nop 0
	v_cndmask_b32_e32 v109, v187, v109, vcc
	v_cmp_lt_u32_e32 vcc, s3, v81
	v_add_u32_e32 v81, 0xbfffff86, v197
	s_nop 0
	v_cndmask_b32_e32 v126, v187, v126, vcc
	v_cmp_lt_u32_e32 vcc, s3, v81
	v_add_u32_e32 v81, 0xbfffffa5, v197
	s_nop 0
	v_cndmask_b32_e32 v110, v187, v110, vcc
	v_cmp_lt_u32_e32 vcc, s3, v81
	v_add_u32_e32 v81, 0xbfffff85, v197
	s_nop 0
	v_cndmask_b32_e32 v127, v187, v127, vcc
	v_cmp_lt_u32_e32 vcc, s3, v81
	s_nop 1
	v_cndmask_b32_e32 v111, v187, v111, vcc

; __device__ __forceinline__ void qkt(f32x16& p0, f32x16& p1, const char* stg, int ka, const i32x8* qf, const f32x16& minit) {
;     p0 = minit; p1 = minit;
; #pragma unroll
;     for (int s = 0; s < 3; ++s) { const char* a = stg + SOFF_K + s * 4096 + ka; const char* b = stg + SOFF_K + s * 4096 + (ka ^ 16);
;         const i32x4 a0 = *reinterpret_cast<const i32x4*>(a), a1 = *reinterpret_cast<const i32x4*>(b);
;         const i32x4 c0 = *reinterpret_cast<const i32x4*>(a + 2048), c1 = *reinterpret_cast<const i32x4*>(b + 2048);
;         p0 = __builtin_amdgcn_mfma_scale_f32_32x32x64_f8f6f4(__builtin_shufflevector(a0, a1, 0, 1, 2, 3, 4, 5, 6, 7), qf[s], p0, 0, 0, 0, 0, 0, 0);
;         p1 = __builtin_amdgcn_mfma_scale_f32_32x32x64_f8f6f4(__builtin_shufflevector(c0, c1, 0, 1, 2, 3, 4, 5, 6, 7), qf[s], p1, 0, 0, 0, 0, 0, 0); }
; }
; __device__ __forceinline__ void v_read(i32x8 (&vf)[4], const char* stg, int ka) {
; #pragma unroll
;     for (int d0 = 0; d0 < 4; ++d0) { const i32x4 a0 = *reinterpret_cast<const i32x4*>(stg + SOFF_V + d0 * 2048 + ka), a1 = *reinterpret_cast<const i32x4*>(stg + SOFF_V + d0 * 2048 + (ka ^ 16));
;         vf[d0] = __builtin_shufflevector(a0, a1, 0, 1, 2, 3, 4, 5, 6, 7); }
; }
; __device__ __forceinline__ void pv_mma(f32x16* o, f32x16& ol, const i32x8 (&vf)[4], const i32x8 ones, const i32x8 pa) {
; #pragma unroll
;     for (int d0 = 0; d0 < 4; ++d0) o[d0] = __builtin_amdgcn_mfma_scale_f32_32x32x64_f8f6f4(pa, vf[d0], o[d0], 0, 0, 0, 0, 0, 0);
;     ol = __builtin_amdgcn_mfma_scale_f32_32x32x64_f8f6f4(pa, ones, ol, 0, 0, 0, 0, 0, 0);
; }
.LBB0_532:
	s_cmp_gt_i32 s1, 4
	s_cselect_b32 s46, -5, 1
	s_add_i32 s46, s46, s1
	s_mulk_i32 s46, 0x5000
	s_add_i32 s46, s46, 0
	v_add_u32_e32 v199, s46, v193
	v_add_u32_e32 v200, s46, v194
	ds_read_b128 v[112:115], v199
	ds_read_b128 v[116:119], v200
	ds_read_b128 v[218:221], v199 offset:2048
	ds_read_b128 v[222:225], v200 offset:2048
	ds_read_b128 v[236:239], v199 offset:4096
	ds_read_b128 v[240:243], v200 offset:4096
	ds_read_b128 v[244:247], v199 offset:6144
	ds_read_b128 v[248:251], v200 offset:6144
	v_exp_f32_e32 v217, v96
	s_waitcnt lgkmcnt(6)
	v_mfma_f32_32x32x64_f8f6f4 v[128:143], v[112:119], v[168:175], v[80:95]
	v_exp_f32_e32 v97, v97
	v_exp_f32_e32 v98, v98
	v_exp_f32_e32 v99, v99
	v_exp_f32_e32 v102, v102
	v_exp_f32_e32 v104, v104
	v_exp_f32_e32 v105, v105
	v_exp_f32_e32 v108, v108
	v_exp_f32_e32 v109, v109
	v_exp_f32_e32 v106, v106
	v_exp_f32_e32 v107, v107
	v_exp_f32_e32 v110, v110
	v_exp_f32_e32 v111, v111
	s_waitcnt lgkmcnt(4)
	v_mfma_f32_32x32x64_f8f6f4 v[112:127], v[218:225], v[168:175], v[80:95]
	ds_read_b128 v[218:221], v199 offset:8192
	ds_read_b128 v[222:225], v200 offset:8192
	ds_read_b128 v[226:229], v199 offset:10240
	ds_read_b128 v[230:233], v200 offset:10240
	s_waitcnt lgkmcnt(6)
	v_mfma_f32_32x32x64_f8f6f4 v[128:143], v[236:243], v[176:183], v[128:143]
	s_waitcnt lgkmcnt(4)
	v_mfma_f32_32x32x64_f8f6f4 v[112:127], v[244:251], v[176:183], v[112:127]
	s_waitcnt lgkmcnt(2)
	v_mfma_f32_32x32x64_f8f6f4 v[128:143], v[218:225], v[160:167], v[128:143]
	v_exp_f32_e32 v218, v100
	v_exp_f32_e32 v219, v101
	v_exp_f32_e32 v220, v103
	s_nop 0
	v_cvt_pk_fp8_f32 v100, v217, v97
	v_cvt_pk_fp8_f32 v101, v218, v219
	v_cvt_pk_fp8_f32 v100, v98, v99 op_sel:[0,0,1]
	v_cvt_pk_fp8_f32 v101, v102, v220 op_sel:[0,0,1]
	s_waitcnt lgkmcnt(0)
	v_mfma_f32_32x32x64_f8f6f4 v[112:127], v[226:233], v[160:167], v[112:127]
	v_cvt_pk_fp8_f32 v96, v215, v216
	v_cvt_pk_fp8_f32 v97, v211, v212
	v_cvt_pk_fp8_f32 v98, v207, v208
	v_cvt_pk_fp8_f32 v102, v104, v105
	v_cvt_pk_fp8_f32 v99, v203, v204
	v_cvt_pk_fp8_f32 v103, v108, v109
	v_cvt_pk_fp8_f32 v96, v213, v214 op_sel:[0,0,1]
	v_cvt_pk_fp8_f32 v97, v209, v210 op_sel:[0,0,1]
	v_cvt_pk_fp8_f32 v98, v205, v206 op_sel:[0,0,1]
	v_cvt_pk_fp8_f32 v102, v106, v107 op_sel:[0,0,1]
	v_cvt_pk_fp8_f32 v99, v201, v202 op_sel:[0,0,1]
	v_cvt_pk_fp8_f32 v103, v110, v111 op_sel:[0,0,1]
	s_mul_i32 s46, s1, 0x5000
	s_add_i32 s46, s46, 0
	v_add_u32_e32 v202, s46, v194
	v_add_u32_e32 v201, s46, v193
	ds_read_b128 v[108:111], v202 offset:12288
	ds_read_b128 v[104:107], v201 offset:12288
	ds_read_b128 v[236:239], v201 offset:14336
	ds_read_b128 v[240:243], v202 offset:14336
	ds_read_b128 v[248:251], v202 offset:16384
	ds_read_b128 v[244:247], v201 offset:16384
	v_mfma_f32_32x32x64_f8f6f4 v[64:79], v[96:103], v[152:159], v[64:79]
	s_sub_i32 s46, s38, 64
	s_cmp_le_i32 s46, s0
	s_waitcnt lgkmcnt(4)
	v_mfma_f32_32x32x64_f8f6f4 v[48:63], v[96:103], v[104:111], v[48:63]
	ds_read_b128 v[104:107], v201 offset:18432
	ds_read_b128 v[108:111], v202 offset:18432
	s_waitcnt lgkmcnt(4)
	v_mfma_f32_32x32x64_f8f6f4 v[32:47], v[96:103], v[236:243], v[32:47]
	s_waitcnt lgkmcnt(2)
	v_mfma_f32_32x32x64_f8f6f4 v[16:31], v[96:103], v[244:251], v[16:31]
	s_waitcnt lgkmcnt(0)
	v_mfma_f32_32x32x64_f8f6f4 v[0:15], v[96:103], v[104:111], v[0:15]
	s_cbranch_scc1 .LBB0_534
	v_add_u32_e32 v96, 0x4000007b, v196
	v_cmp_gt_u32_e32 vcc, 2.0, v96
	v_add_u32_e32 v96, 0x5b, v196
	s_nop 0
	v_cndmask_b32_e32 v128, v187, v128, vcc
	v_cmp_lt_u32_e32 vcc, s3, v96
	v_add_u32_e32 v96, 0x7a, v196
	s_nop 0
	v_cndmask_b32_e32 v112, v187, v112, vcc
	v_cmp_lt_u32_e32 vcc, s3, v96
	v_add_u32_e32 v96, 0x5a, v196
	s_nop 0
	v_cndmask_b32_e32 v129, v187, v129, vcc
	v_cmp_lt_u32_e32 vcc, s3, v96
	v_add_u32_e32 v96, 0x79, v196
	s_nop 0
	v_cndmask_b32_e32 v113, v187, v113, vcc
	v_cmp_lt_u32_e32 vcc, s3, v96
	v_add_u32_e32 v96, 0x59, v196
	s_nop 0
	v_cndmask_b32_e32 v130, v187, v130, vcc
	v_cmp_lt_u32_e32 vcc, s3, v96
	v_add_u32_e32 v96, 0x78, v196
	s_nop 0
	v_cndmask_b32_e32 v114, v187, v114, vcc
	v_cmp_lt_u32_e32 vcc, s3, v96
	v_add_u32_e32 v96, 0x58, v196
	s_nop 0
	v_cndmask_b32_e32 v131, v187, v131, vcc
	v_cmp_lt_u32_e32 vcc, s3, v96
	v_add_u32_e32 v96, 0x73, v196
	s_nop 0
	v_cndmask_b32_e32 v115, v187, v115, vcc
	v_cmp_lt_u32_e32 vcc, s3, v96
	v_add_u32_e32 v96, 0x53, v196
	s_nop 0
	v_cndmask_b32_e32 v132, v187, v132, vcc
	v_cmp_lt_u32_e32 vcc, s3, v96
	v_add_u32_e32 v96, 0x72, v196
	s_nop 0
	v_cndmask_b32_e32 v116, v187, v116, vcc
	v_cmp_lt_u32_e32 vcc, s3, v96
	v_add_u32_e32 v96, 0x52, v196
	s_nop 0
	v_cndmask_b32_e32 v133, v187, v133, vcc
	v_cmp_lt_u32_e32 vcc, s3, v96
	v_add_u32_e32 v96, 0x71, v196
	s_nop 0
	v_cndmask_b32_e32 v117, v187, v117, vcc
	v_cmp_lt_u32_e32 vcc, s3, v96
	v_add_u32_e32 v96, 0x51, v196
	s_nop 0
	v_cndmask_b32_e32 v134, v187, v134, vcc
	v_cmp_lt_u32_e32 vcc, s3, v96
	v_add_u32_e32 v96, 0x70, v196
	s_nop 0
	v_cndmask_b32_e32 v118, v187, v118, vcc
	v_cmp_lt_u32_e32 vcc, s3, v96
	v_add_u32_e32 v96, 0x50, v196
	s_nop 0
	v_cndmask_b32_e32 v135, v187, v135, vcc
	v_cmp_lt_u32_e32 vcc, s3, v96
	v_add_u32_e32 v96, 0x6b, v196
	s_nop 0
	v_cndmask_b32_e32 v119, v187, v119, vcc
	v_cmp_lt_u32_e32 vcc, s3, v96
	v_add_u32_e32 v96, 0x4b, v196
	s_nop 0
	v_cndmask_b32_e32 v136, v187, v136, vcc
	v_cmp_lt_u32_e32 vcc, s3, v96
	v_add_u32_e32 v96, 0x6a, v196
	s_nop 0
	v_cndmask_b32_e32 v120, v187, v120, vcc
	v_cmp_lt_u32_e32 vcc, s3, v96
	v_add_u32_e32 v96, 0x4a, v196
	s_nop 0
	v_cndmask_b32_e32 v137, v187, v137, vcc
	v_cmp_lt_u32_e32 vcc, s3, v96
	v_add_u32_e32 v96, 0x69, v196
	s_nop 0
	v_cndmask_b32_e32 v121, v187, v121, vcc
	v_cmp_lt_u32_e32 vcc, s3, v96
	v_add_u32_e32 v96, 0x49, v196
	s_nop 0
	v_cndmask_b32_e32 v138, v187, v138, vcc
	v_cmp_lt_u32_e32 vcc, s3, v96
	v_add_u32_e32 v96, 0x68, v196
	s_nop 0
	v_cndmask_b32_e32 v122, v187, v122, vcc
	v_cmp_lt_u32_e32 vcc, s3, v96
	v_add_u32_e32 v96, 0x48, v196
	s_nop 0
	v_cndmask_b32_e32 v139, v187, v139, vcc
	v_cmp_lt_u32_e32 vcc, s3, v96
	v_add_u32_e32 v96, 0x63, v196
	s_nop 0
	v_cndmask_b32_e32 v123, v187, v123, vcc
	v_cmp_lt_u32_e32 vcc, s3, v96
	v_add_u32_e32 v96, 0x43, v196
	s_nop 0
	v_cndmask_b32_e32 v140, v187, v140, vcc
	v_cmp_lt_u32_e32 vcc, s3, v96
	v_add_u32_e32 v96, 0x62, v196
	s_nop 0
	v_cndmask_b32_e32 v124, v187, v124, vcc
	v_cmp_lt_u32_e32 vcc, s3, v96
	v_add_u32_e32 v96, 0x42, v196
	s_nop 0
	v_cndmask_b32_e32 v141, v187, v141, vcc
	v_cmp_lt_u32_e32 vcc, s3, v96
	v_add_u32_e32 v96, 0x61, v196
	s_nop 0
	v_cndmask_b32_e32 v125, v187, v125, vcc
	v_cmp_lt_u32_e32 vcc, s3, v96
	v_add_u32_e32 v96, 0x41, v196
	s_nop 0
	v_cndmask_b32_e32 v142, v187, v142, vcc
	v_cmp_lt_u32_e32 vcc, s3, v96
	v_add_u32_e32 v96, 0x60, v196
	s_nop 0
	v_cndmask_b32_e32 v126, v187, v126, vcc
	v_cmp_lt_u32_e32 vcc, s3, v96
	v_add_u32_e32 v96, 64, v196
	s_nop 0
	v_cndmask_b32_e32 v143, v187, v143, vcc
	v_cmp_lt_u32_e32 vcc, s3, v96
	s_nop 1
	v_cndmask_b32_e32 v127, v187, v127, vcc

; __device__ __forceinline__ void qkt(f32x16& p0, f32x16& p1, const char* stg, int ka, const i32x8* qf, const f32x16& minit) {
;     p0 = minit; p1 = minit;
; #pragma unroll
;     for (int s = 0; s < 3; ++s) { const char* a = stg + SOFF_K + s * 4096 + ka; const char* b = stg + SOFF_K + s * 4096 + (ka ^ 16);
;         const i32x4 a0 = *reinterpret_cast<const i32x4*>(a), a1 = *reinterpret_cast<const i32x4*>(b);
;         const i32x4 c0 = *reinterpret_cast<const i32x4*>(a + 2048), c1 = *reinterpret_cast<const i32x4*>(b + 2048);
;         p0 = __builtin_amdgcn_mfma_scale_f32_32x32x64_f8f6f4(__builtin_shufflevector(a0, a1, 0, 1, 2, 3, 4, 5, 6, 7), qf[s], p0, 0, 0, 0, 0, 0, 0);
;         p1 = __builtin_amdgcn_mfma_scale_f32_32x32x64_f8f6f4(__builtin_shufflevector(c0, c1, 0, 1, 2, 3, 4, 5, 6, 7), qf[s], p1, 0, 0, 0, 0, 0, 0); }
; }
; __device__ __forceinline__ void v_read(i32x8 (&vf)[4], const char* stg, int ka) {
; #pragma unroll
;     for (int d0 = 0; d0 < 4; ++d0) { const i32x4 a0 = *reinterpret_cast<const i32x4*>(stg + SOFF_V + d0 * 2048 + ka), a1 = *reinterpret_cast<const i32x4*>(stg + SOFF_V + d0 * 2048 + (ka ^ 16));
;         vf[d0] = __builtin_shufflevector(a0, a1, 0, 1, 2, 3, 4, 5, 6, 7); }
; }
; __device__ __forceinline__ void pv_mma(f32x16* o, f32x16& ol, const i32x8 (&vf)[4], const i32x8 ones, const i32x8 pa) {
; #pragma unroll
;     for (int d0 = 0; d0 < 4; ++d0) o[d0] = __builtin_amdgcn_mfma_scale_f32_32x32x64_f8f6f4(pa, vf[d0], o[d0], 0, 0, 0, 0, 0, 0);
;     ol = __builtin_amdgcn_mfma_scale_f32_32x32x64_f8f6f4(pa, ones, ol, 0, 0, 0, 0, 0, 0);
; }
.LBB0_539:
	s_cmp_gt_i32 s1, 3
	s_cselect_b32 s46, -4, 2
	s_add_i32 s1, s46, s1
	v_exp_f32_e32 v201, v128
	v_exp_f32_e32 v218, v129
	v_exp_f32_e32 v219, v130
	v_exp_f32_e32 v220, v131
	v_exp_f32_e32 v221, v132
	v_exp_f32_e32 v222, v133
	v_exp_f32_e32 v223, v134
	v_exp_f32_e32 v224, v135
	v_exp_f32_e32 v225, v136
	v_exp_f32_e32 v226, v137
	v_exp_f32_e32 v227, v138
	v_exp_f32_e32 v228, v139
	v_exp_f32_e32 v229, v140
	v_exp_f32_e32 v230, v141
	v_exp_f32_e32 v231, v142
	v_exp_f32_e32 v232, v143
	s_mul_i32 s92, s1, 0x5000
	s_add_i32 s46, s92, 0
	v_add_u32_e32 v233, s46, v193
	v_add_u32_e32 v234, s46, v194
	ds_read_b128 v[202:205], v233
	ds_read_b128 v[206:209], v234
	ds_read_b128 v[210:213], v233 offset:2048
	ds_read_b128 v[214:217], v234 offset:2048
	ds_read_b128 v[236:239], v233 offset:4096
	ds_read_b128 v[240:243], v234 offset:4096
	ds_read_b128 v[244:247], v233 offset:6144
	ds_read_b128 v[248:251], v234 offset:6144
	v_exp_f32_e32 v113, v113
	s_waitcnt lgkmcnt(6)
	v_mfma_f32_32x32x64_f8f6f4 v[128:143], v[202:209], v[168:175], v[96:111]
	v_exp_f32_e32 v114, v114
	v_exp_f32_e32 v115, v115
	v_exp_f32_e32 v118, v118
	v_exp_f32_e32 v120, v120
	v_exp_f32_e32 v121, v121
	v_exp_f32_e32 v124, v124
	v_exp_f32_e32 v125, v125
	v_exp_f32_e32 v122, v122
	v_exp_f32_e32 v123, v123
	v_exp_f32_e32 v126, v126
	v_exp_f32_e32 v127, v127
	s_waitcnt lgkmcnt(4)
	v_mfma_f32_32x32x64_f8f6f4 v[96:111], v[210:217], v[168:175], v[96:111]
	ds_read_b128 v[202:205], v233 offset:8192
	ds_read_b128 v[206:209], v234 offset:8192
	ds_read_b128 v[210:213], v233 offset:10240
	ds_read_b128 v[214:217], v234 offset:10240
	s_waitcnt lgkmcnt(6)
	v_mfma_f32_32x32x64_f8f6f4 v[128:143], v[236:243], v[176:183], v[128:143]
	s_waitcnt lgkmcnt(4)
	v_mfma_f32_32x32x64_f8f6f4 v[96:111], v[244:251], v[176:183], v[96:111]
	s_waitcnt lgkmcnt(2)
	v_mfma_f32_32x32x64_f8f6f4 v[128:143], v[202:209], v[160:167], v[128:143]
	v_exp_f32_e32 v202, v112
	v_exp_f32_e32 v203, v116
	v_exp_f32_e32 v204, v117
	v_exp_f32_e32 v205, v119
	s_nop 0
	v_cvt_pk_fp8_f32 v116, v202, v113
	v_cvt_pk_fp8_f32 v117, v203, v204
	v_cvt_pk_fp8_f32 v116, v114, v115 op_sel:[0,0,1]
	v_cvt_pk_fp8_f32 v117, v118, v205 op_sel:[0,0,1]
	s_waitcnt lgkmcnt(0)
	v_mfma_f32_32x32x64_f8f6f4 v[96:111], v[210:217], v[160:167], v[96:111]
	v_cvt_pk_fp8_f32 v112, v201, v218
	v_cvt_pk_fp8_f32 v113, v221, v222
	v_cvt_pk_fp8_f32 v114, v225, v226
	v_cvt_pk_fp8_f32 v118, v120, v121
	v_cvt_pk_fp8_f32 v115, v229, v230
	v_cvt_pk_fp8_f32 v119, v124, v125
	v_cvt_pk_fp8_f32 v112, v219, v220 op_sel:[0,0,1]
	v_cvt_pk_fp8_f32 v113, v223, v224 op_sel:[0,0,1]
	v_cvt_pk_fp8_f32 v114, v227, v228 op_sel:[0,0,1]
	v_cvt_pk_fp8_f32 v118, v122, v123 op_sel:[0,0,1]
	v_cvt_pk_fp8_f32 v115, v231, v232 op_sel:[0,0,1]
	v_cvt_pk_fp8_f32 v119, v126, v127 op_sel:[0,0,1]
	ds_read_b128 v[124:127], v200 offset:12288
	ds_read_b128 v[120:123], v199 offset:12288
	ds_read_b128 v[236:239], v199 offset:14336
	ds_read_b128 v[240:243], v200 offset:14336
	ds_read_b128 v[248:251], v200 offset:16384
	ds_read_b128 v[244:247], v199 offset:16384
	v_mfma_f32_32x32x64_f8f6f4 v[64:79], v[112:119], v[152:159], v[64:79]
	s_cmp_le_i32 s38, s0
	s_waitcnt lgkmcnt(4)
	v_mfma_f32_32x32x64_f8f6f4 v[48:63], v[112:119], v[120:127], v[48:63]
	ds_read_b128 v[120:123], v199 offset:18432
	ds_read_b128 v[124:127], v200 offset:18432
	s_waitcnt lgkmcnt(4)
	v_mfma_f32_32x32x64_f8f6f4 v[32:47], v[112:119], v[236:243], v[32:47]
	s_waitcnt lgkmcnt(2)
	v_mfma_f32_32x32x64_f8f6f4 v[16:31], v[112:119], v[244:251], v[16:31]
	s_waitcnt lgkmcnt(0)
	v_mfma_f32_32x32x64_f8f6f4 v[0:15], v[112:119], v[120:127], v[0:15]
	s_cbranch_scc1 .LBB0_541
; __device__ __forceinline__ void mask_tile(f32x16& p0, f32x16& p1, int dq, unsigned W) {
;     const float NEG = -__builtin_inff();
; #pragma unroll
;     for (int r = 0; r < 16; ++r) {
;         const int c = (r & 3) + 8 * (r >> 2);
;         if ((unsigned)(dq - c) >= W) p0[r] = NEG;
;         if ((unsigned)(dq - c - 32) >= W) p1[r] = NEG;
;     }
; }
	v_add_u32_e32 v112, 0x4000003b, v196
	v_cmp_gt_u32_e32 vcc, 2.0, v112
	v_add_u32_e32 v112, 27, v196
	s_nop 0
	v_cndmask_b32_e32 v128, v187, v128, vcc
	v_cmp_lt_u32_e32 vcc, s3, v112
	v_add_u32_e32 v112, 58, v196
	s_nop 0
	v_cndmask_b32_e32 v96, v187, v96, vcc
	v_cmp_lt_u32_e32 vcc, s3, v112
	v_add_u32_e32 v112, 26, v196
	s_nop 0
	v_cndmask_b32_e32 v129, v187, v129, vcc
	v_cmp_lt_u32_e32 vcc, s3, v112
	v_add_u32_e32 v112, 57, v196
	s_nop 0
	v_cndmask_b32_e32 v97, v187, v97, vcc
	v_cmp_lt_u32_e32 vcc, s3, v112
	v_add_u32_e32 v112, 25, v196
	s_nop 0
	v_cndmask_b32_e32 v130, v187, v130, vcc
	v_cmp_lt_u32_e32 vcc, s3, v112
	v_add_u32_e32 v112, 56, v196
	s_nop 0
	v_cndmask_b32_e32 v98, v187, v98, vcc
	v_cmp_lt_u32_e32 vcc, s3, v112
	v_add_u32_e32 v112, 24, v196
	s_nop 0
	v_cndmask_b32_e32 v131, v187, v131, vcc
	v_cmp_lt_u32_e32 vcc, s3, v112
	v_add_u32_e32 v112, 51, v196
	s_nop 0
	v_cndmask_b32_e32 v99, v187, v99, vcc
	v_cmp_lt_u32_e32 vcc, s3, v112
	v_add_u32_e32 v112, 19, v196
	s_nop 0
	v_cndmask_b32_e32 v132, v187, v132, vcc
	v_cmp_lt_u32_e32 vcc, s3, v112
	v_add_u32_e32 v112, 50, v196
	s_nop 0
	v_cndmask_b32_e32 v100, v187, v100, vcc
	v_cmp_lt_u32_e32 vcc, s3, v112
	v_add_u32_e32 v112, 18, v196
	s_nop 0
	v_cndmask_b32_e32 v133, v187, v133, vcc
	v_cmp_lt_u32_e32 vcc, s3, v112
	v_add_u32_e32 v112, 49, v196
	s_nop 0
	v_cndmask_b32_e32 v101, v187, v101, vcc
	v_cmp_lt_u32_e32 vcc, s3, v112
	v_add_u32_e32 v112, 17, v196
	s_nop 0
	v_cndmask_b32_e32 v134, v187, v134, vcc
	v_cmp_lt_u32_e32 vcc, s3, v112
	v_add_u32_e32 v112, 48, v196
	s_nop 0
	v_cndmask_b32_e32 v102, v187, v102, vcc
	v_cmp_lt_u32_e32 vcc, s3, v112
	v_add_u32_e32 v112, 16, v196
	s_nop 0
	v_cndmask_b32_e32 v135, v187, v135, vcc
	v_cmp_lt_u32_e32 vcc, s3, v112
	v_add_u32_e32 v112, 43, v196
	s_nop 0
	v_cndmask_b32_e32 v103, v187, v103, vcc
	v_cmp_lt_u32_e32 vcc, s3, v112
	v_add_u32_e32 v112, 11, v196
	s_nop 0
	v_cndmask_b32_e32 v136, v187, v136, vcc
	v_cmp_lt_u32_e32 vcc, s3, v112
	v_add_u32_e32 v112, 42, v196
	s_nop 0
	v_cndmask_b32_e32 v104, v187, v104, vcc
	v_cmp_lt_u32_e32 vcc, s3, v112
	v_add_u32_e32 v112, 10, v196
	s_nop 0
	v_cndmask_b32_e32 v137, v187, v137, vcc
	v_cmp_lt_u32_e32 vcc, s3, v112
	v_add_u32_e32 v112, 41, v196
	s_nop 0
	v_cndmask_b32_e32 v105, v187, v105, vcc
	v_cmp_lt_u32_e32 vcc, s3, v112
	v_add_u32_e32 v112, 9, v196
	s_nop 0
	v_cndmask_b32_e32 v138, v187, v138, vcc
	v_cmp_lt_u32_e32 vcc, s3, v112
	v_add_u32_e32 v112, 40, v196
	s_nop 0
	v_cndmask_b32_e32 v106, v187, v106, vcc
	v_cmp_lt_u32_e32 vcc, s3, v112
	v_add_u32_e32 v112, 8, v196
	s_nop 0
	v_cndmask_b32_e32 v139, v187, v139, vcc
	v_cmp_lt_u32_e32 vcc, s3, v112
	v_add_u32_e32 v112, 35, v196
	s_nop 0
	v_cndmask_b32_e32 v107, v187, v107, vcc
	v_cmp_lt_u32_e32 vcc, s3, v112
	v_add_u32_e32 v112, 3, v196
	s_nop 0
	v_cndmask_b32_e32 v140, v187, v140, vcc
	v_cmp_lt_u32_e32 vcc, s3, v112
	v_add_u32_e32 v112, 34, v196
	s_nop 0
	v_cndmask_b32_e32 v108, v187, v108, vcc
	v_cmp_lt_u32_e32 vcc, s3, v112
	v_add_u32_e32 v112, 2, v196
	s_nop 0
	v_cndmask_b32_e32 v141, v187, v141, vcc
	v_cmp_lt_u32_e32 vcc, s3, v112
	v_add_u32_e32 v112, 33, v196
	s_nop 0
	v_cndmask_b32_e32 v109, v187, v109, vcc
	v_cmp_lt_u32_e32 vcc, s3, v112
	v_add_u32_e32 v112, 1, v196
	s_nop 0
	v_cndmask_b32_e32 v142, v187, v142, vcc
	v_cmp_lt_u32_e32 vcc, s3, v112
	v_add_u32_e32 v112, 32, v196
	s_nop 0
	v_cndmask_b32_e32 v110, v187, v110, vcc
	v_cmp_lt_u32_e32 vcc, s3, v112
	s_nop 1
	v_cndmask_b32_e32 v143, v187, v143, vcc
	v_cmp_lt_u32_e32 vcc, s3, v196
	s_nop 1
	v_cndmask_b32_e32 v111, v187, v111, vcc

; __device__ __forceinline__ cgptr cuni(const void* p) { const unsigned long long v = (unsigned long long)p; const unsigned lo = __builtin_amdgcn_readfirstlane((unsigned)v), hi = __builtin_amdgcn_readfirstlane((unsigned)(v >> 32)); return (cgptr)(((unsigned long long)hi << 32) | lo); }
; __device__ __forceinline__ ConvItem conv_decode(int it, const float* wgu, const float* wd, unsigned char* WguT, unsigned char* WdT) {
;     constexpr int I_GU = NE * 16 * 128;
;     ConvItem c; int r = it, nbn, N; const float* src; unsigned char* dstp; bool gu;
;     if (r < I_GU) { const int e = r / (16 * 128); r -= e * (16 * 128); N = 4096; nbn = 128; src = wgu + (size_t)e * DM * 4096; dstp = WguT + (size_t)e * 4096 * DM; gu = true; }
;     else { r -= I_GU; const int e = r / (16 * 64); r -= e * (16 * 64); N = DM; nbn = 64; src = wd + (size_t)e * DFF * DM; dstp = WdT + (size_t)e * DM * DFF; gu = false; }
;     const int kb = r / nbn, nb = r - kb * nbn, n0 = nb * 32, k0 = kb * 128; int dst = n0;
;     if (gu) { const int j = n0 & 2047; dst = (j >> 7) * 256 + (j & 127) + ((n0 >= 2048) ? 128 : 0); }
;     c.src = cuni(src + (size_t)k0 * N + n0); c.dstp = cuni(dstp + (size_t)dst * DM + k0); c.N4 = (unsigned)N * 4u;
;     return c;
; }
.LBB0_557:
	v_cvt_f32_ubyte0_e32 v0, s12
	v_rcp_iflag_f32_e32 v0, v0
	s_sub_i32 s24, 0, s12
	s_abs_i32 s17, s9
	s_add_i32 s1, s3, s44
	v_mul_f32_e32 v0, 0x4f7ffffe, v0
	v_cvt_u32_f32_e32 v0, v0
	s_ashr_i32 s3, s9, 31
	v_readfirstlane_b32 s25, v0
	s_mul_i32 s24, s24, s25
	s_mul_hi_u32 s24, s25, s24
	s_add_i32 s25, s25, s24
	s_mul_hi_u32 s24, s17, s25
	s_mul_i32 s25, s24, s12
	s_sub_i32 s17, s17, s25
	s_add_i32 s26, s24, 1
	s_sub_i32 s25, s17, s12
	s_cmp_ge_u32 s17, s12
	s_cselect_b32 s24, s26, s24
	s_cselect_b32 s17, s25, s17
	s_add_i32 s25, s24, 1
	s_cmp_ge_u32 s17, s12
	s_cselect_b32 s17, s25, s24
	s_xor_b32 s17, s17, s3
	s_sub_i32 s3, s17, s3
	s_mul_i32 s12, s3, s12
	s_sub_i32 s12, s9, s12
	s_lshl_b32 s24, s12, 5
	s_lshl_b32 s9, s9, 6
	s_and_b32 s9, s9, 0xf00
	s_and_b32 s17, s24, 0x60
	s_or_b32 s9, s17, s9
	s_cmp_gt_i32 s12, 63
	s_cselect_b32 s12, 0x80, 0
	s_or_b32 s9, s9, s12
	s_and_b64 s[14:15], s[14:15], exec
	s_cselect_b32 s14, s9, s24
	s_lshl_b32 s3, s3, 7
	s_mul_hi_i32 s27, s3, s8
	s_mul_i32 s26, s3, s8
	s_ashr_i32 s9, s3, 31
	s_lshl_b64 s[26:27], s[26:27], 2
	s_add_u32 s12, s22, s26
	s_addc_u32 s15, s23, s27
	s_ashr_i32 s25, s24, 31
	s_lshl_b64 s[22:23], s[24:25], 2
	s_add_u32 s22, s12, s22
	s_addc_u32 s23, s15, s23
	s_ashr_i32 s15, s14, 31
	s_lshl_b64 s[14:15], s[14:15], 11
	s_add_u32 s12, s20, s14
	s_addc_u32 s15, s21, s15
	s_add_u32 s14, s12, s3
	s_addc_u32 s15, s15, s9
	s_lshl_b32 s3, s8, 5
	v_mul_lo_u32 v0, v130, s8
	s_add_u32 s20, s22, s3
	v_or_b32_e32 v56, v0, v131
	s_addc_u32 s21, s23, 0
	s_lshl_b32 s3, s8, 6
	global_load_dwordx4 v[4:7], v56, s[22:23] nt
	global_load_dwordx4 v[0:3], v56, s[20:21] nt
	s_add_u32 s20, s22, s3
	s_addc_u32 s21, s23, 0
	s_mul_i32 s3, s8, 0x60
	s_add_u32 s24, s22, s3
	s_addc_u32 s25, s23, 0
	s_lshl_b32 s3, s8, 7
	global_load_dwordx4 v[12:15], v56, s[20:21] nt
	global_load_dwordx4 v[8:11], v56, s[24:25] nt
	s_add_u32 s20, s22, s3
	s_addc_u32 s21, s23, 0
	s_mul_i32 s3, s8, 0xa0
	s_add_u32 s24, s22, s3
	s_addc_u32 s25, s23, 0
	s_mul_i32 s3, s8, 0xc0
	global_load_dwordx4 v[20:23], v56, s[20:21] nt
	global_load_dwordx4 v[16:19], v56, s[24:25] nt
	s_add_u32 s20, s22, s3
	s_addc_u32 s21, s23, 0
	s_mul_i32 s3, s8, 0xe0
	s_add_u32 s24, s22, s3
	s_addc_u32 s25, s23, 0
	s_lshl_b32 s3, s8, 8
	global_load_dwordx4 v[28:31], v56, s[20:21] nt
	global_load_dwordx4 v[24:27], v56, s[24:25] nt
	s_add_u32 s20, s22, s3
	s_addc_u32 s21, s23, 0
	s_mul_i32 s3, s8, 0x120
	s_add_u32 s24, s22, s3
	s_addc_u32 s25, s23, 0
	s_mul_i32 s3, s8, 0x140
	global_load_dwordx4 v[36:39], v56, s[20:21] nt
	global_load_dwordx4 v[32:35], v56, s[24:25] nt
	s_add_u32 s20, s22, s3
	s_addc_u32 s21, s23, 0
	s_mul_i32 s3, s8, 0x160
	s_add_u32 s24, s22, s3
	s_addc_u32 s25, s23, 0
	s_mul_i32 s3, s8, 0x180
	global_load_dwordx4 v[44:47], v56, s[20:21] nt
	global_load_dwordx4 v[40:43], v56, s[24:25] nt
	s_add_u32 s20, s22, s3
	s_addc_u32 s21, s23, 0
	s_mul_i32 s3, s8, 0x1a0
	s_add_u32 s24, s22, s3
	s_addc_u32 s25, s23, 0
	s_mul_i32 s3, s8, 0x1c0
	global_load_dwordx4 v[52:55], v56, s[20:21] nt
	global_load_dwordx4 v[48:51], v56, s[24:25] nt
	s_add_u32 s20, s22, s3
	s_addc_u32 s21, s23, 0
	s_mul_i32 s3, s8, 0x1e0
	s_add_u32 s8, s22, s3
	s_addc_u32 s9, s23, 0
	global_load_dwordx4 v[60:63], v56, s[20:21] nt
	s_nop 0
	global_load_dwordx4 v[56:59], v56, s[8:9] nt
	s_waitcnt vmcnt(35)
	v_pk_mul_f32 v[126:127], v[126:127], s[16:17] op_sel_hi:[1,0]
	v_pk_mul_f32 v[124:125], v[124:125], s[16:17] op_sel_hi:[1,0]
	s_waitcnt vmcnt(34)
	v_pk_mul_f32 v[118:119], v[118:119], s[16:17] op_sel_hi:[1,0]
	v_pk_mul_f32 v[116:117], v[116:117], s[16:17] op_sel_hi:[1,0]
	ds_write_b128 v132, v[124:127]
	ds_write_b128 v133, v[116:119]
	s_waitcnt vmcnt(33)
	v_pk_mul_f32 v[118:119], v[122:123], s[16:17] op_sel_hi:[1,0]
	v_pk_mul_f32 v[116:117], v[120:121], s[16:17] op_sel_hi:[1,0]
	s_waitcnt vmcnt(32)
	v_pk_mul_f32 v[110:111], v[110:111], s[16:17] op_sel_hi:[1,0]
	v_pk_mul_f32 v[108:109], v[108:109], s[16:17] op_sel_hi:[1,0]
	ds_write_b128 v134, v[116:119]
	ds_write_b128 v135, v[108:111]
	s_waitcnt vmcnt(31)
	v_pk_mul_f32 v[110:111], v[114:115], s[16:17] op_sel_hi:[1,0]
	v_pk_mul_f32 v[108:109], v[112:113], s[16:17] op_sel_hi:[1,0]
	s_waitcnt vmcnt(30)
	v_pk_mul_f32 v[102:103], v[102:103], s[16:17] op_sel_hi:[1,0]
	v_pk_mul_f32 v[100:101], v[100:101], s[16:17] op_sel_hi:[1,0]
	ds_write_b128 v136, v[108:111]
	ds_write_b128 v137, v[100:103]
	s_waitcnt vmcnt(29)
	v_pk_mul_f32 v[102:103], v[106:107], s[16:17] op_sel_hi:[1,0]
	v_pk_mul_f32 v[100:101], v[104:105], s[16:17] op_sel_hi:[1,0]
	s_waitcnt vmcnt(28)
	v_pk_mul_f32 v[94:95], v[94:95], s[16:17] op_sel_hi:[1,0]
	v_pk_mul_f32 v[92:93], v[92:93], s[16:17] op_sel_hi:[1,0]
	ds_write_b128 v138, v[100:103]
	ds_write_b128 v139, v[92:95]
	s_waitcnt vmcnt(27)
	v_pk_mul_f32 v[94:95], v[98:99], s[16:17] op_sel_hi:[1,0]
	v_pk_mul_f32 v[92:93], v[96:97], s[16:17] op_sel_hi:[1,0]
	s_waitcnt vmcnt(26)
	v_pk_mul_f32 v[86:87], v[86:87], s[16:17] op_sel_hi:[1,0]
	v_pk_mul_f32 v[84:85], v[84:85], s[16:17] op_sel_hi:[1,0]
	ds_write_b128 v140, v[92:95]
	ds_write_b128 v141, v[84:87]
	s_waitcnt vmcnt(25)
	v_pk_mul_f32 v[86:87], v[90:91], s[16:17] op_sel_hi:[1,0]
	v_pk_mul_f32 v[84:85], v[88:89], s[16:17] op_sel_hi:[1,0]
	s_waitcnt vmcnt(24)
	v_pk_mul_f32 v[78:79], v[78:79], s[16:17] op_sel_hi:[1,0]
	v_pk_mul_f32 v[76:77], v[76:77], s[16:17] op_sel_hi:[1,0]
	ds_write_b128 v142, v[84:87]
	ds_write_b128 v143, v[76:79]
	s_waitcnt vmcnt(23)
	v_pk_mul_f32 v[78:79], v[82:83], s[16:17] op_sel_hi:[1,0]
	v_pk_mul_f32 v[76:77], v[80:81], s[16:17] op_sel_hi:[1,0]
	s_waitcnt vmcnt(22)
	v_pk_mul_f32 v[70:71], v[70:71], s[16:17] op_sel_hi:[1,0]
	v_pk_mul_f32 v[68:69], v[68:69], s[16:17] op_sel_hi:[1,0]
	ds_write_b128 v144, v[76:79]
	ds_write_b128 v145, v[68:71]
	s_waitcnt vmcnt(21)
	v_pk_mul_f32 v[70:71], v[74:75], s[16:17] op_sel_hi:[1,0]
	v_pk_mul_f32 v[68:69], v[72:73], s[16:17] op_sel_hi:[1,0]
	s_waitcnt vmcnt(20)
	v_pk_mul_f32 v[66:67], v[66:67], s[16:17] op_sel_hi:[1,0]
	v_pk_mul_f32 v[64:65], v[64:65], s[16:17] op_sel_hi:[1,0]
	ds_write_b128 v146, v[68:71]
	ds_write_b128 v147, v[64:67]
	s_waitcnt lgkmcnt(0)
	ds_read2_b32 v[64:65], v148 offset1:32
	ds_read2_b32 v[72:73], v148 offset0:64 offset1:96
	ds_read2_b32 v[70:71], v148 offset0:128 offset1:160
	ds_read2_b32 v[74:75], v152 offset1:32
	s_waitcnt lgkmcnt(3)
	v_cvt_pk_fp8_f32 v68, v64, v65
	ds_read2_b32 v[64:65], v148 offset0:192 offset1:224
	ds_read2_b32 v[76:77], v152 offset0:64 offset1:96
	ds_read2_b32 v[78:79], v152 offset0:128 offset1:160
	s_waitcnt lgkmcnt(4)
	v_cvt_pk_fp8_f32 v69, v70, v71
	s_waitcnt lgkmcnt(3)
	v_cvt_pk_fp8_f32 v70, v74, v75
	ds_read2_b32 v[74:75], v152 offset0:192 offset1:224
	s_waitcnt lgkmcnt(1)
	v_cvt_pk_fp8_f32 v71, v78, v79
	v_cvt_pk_fp8_f32 v68, v72, v73 op_sel:[0,0,1]
	v_cvt_pk_fp8_f32 v69, v64, v65 op_sel:[0,0,1]
	v_cvt_pk_fp8_f32 v70, v76, v77 op_sel:[0,0,1]
	s_waitcnt lgkmcnt(0)
	v_cvt_pk_fp8_f32 v71, v74, v75 op_sel:[0,0,1]
	ds_read2_b32 v[72:73], v149 offset1:32
	v_lshl_add_u64 v[64:65], s[18:19], 0, v[128:129]
	ds_read2_b32 v[74:75], v153 offset1:32
	global_store_dwordx4 v[64:65], v[68:71], off nt
	ds_read2_b32 v[70:71], v149 offset0:128 offset1:160
	ds_read2_b32 v[64:65], v149 offset0:64 offset1:96
	s_waitcnt lgkmcnt(3)
	v_cvt_pk_fp8_f32 v68, v72, v73
	ds_read2_b32 v[72:73], v149 offset0:192 offset1:224
	ds_read2_b32 v[76:77], v153 offset0:64 offset1:96
	ds_read2_b32 v[78:79], v153 offset0:128 offset1:160
	s_waitcnt lgkmcnt(4)
	v_cvt_pk_fp8_f32 v69, v70, v71
	v_cvt_pk_fp8_f32 v70, v74, v75
	ds_read2_b32 v[74:75], v153 offset0:192 offset1:224
	s_waitcnt lgkmcnt(1)
	v_cvt_pk_fp8_f32 v71, v78, v79
	v_cvt_pk_fp8_f32 v68, v64, v65 op_sel:[0,0,1]
	v_cvt_pk_fp8_f32 v69, v72, v73 op_sel:[0,0,1]
	v_cvt_pk_fp8_f32 v70, v76, v77 op_sel:[0,0,1]
	s_waitcnt lgkmcnt(0)
	v_cvt_pk_fp8_f32 v71, v74, v75 op_sel:[0,0,1]
	s_add_u32 s8, s18, 0x4000
	ds_read2_b32 v[72:73], v150 offset1:32
	s_addc_u32 s9, s19, 0
	v_lshl_add_u64 v[64:65], s[8:9], 0, v[128:129]
	global_store_dwordx4 v[64:65], v[68:71], off nt
	ds_read2_b32 v[70:71], v150 offset0:128 offset1:160
	ds_read2_b32 v[74:75], v154 offset1:32
	ds_read2_b32 v[64:65], v150 offset0:64 offset1:96
	s_waitcnt lgkmcnt(3)
	v_cvt_pk_fp8_f32 v68, v72, v73
	ds_read2_b32 v[72:73], v150 offset0:192 offset1:224
	ds_read2_b32 v[76:77], v154 offset0:64 offset1:96
	ds_read2_b32 v[78:79], v154 offset0:128 offset1:160
	s_waitcnt lgkmcnt(5)
	v_cvt_pk_fp8_f32 v69, v70, v71
	s_waitcnt lgkmcnt(4)
	v_cvt_pk_fp8_f32 v70, v74, v75
	ds_read2_b32 v[74:75], v154 offset0:192 offset1:224
	s_waitcnt lgkmcnt(1)
	v_cvt_pk_fp8_f32 v71, v78, v79
	v_cvt_pk_fp8_f32 v68, v64, v65 op_sel:[0,0,1]
	v_cvt_pk_fp8_f32 v69, v72, v73 op_sel:[0,0,1]
	v_cvt_pk_fp8_f32 v70, v76, v77 op_sel:[0,0,1]
	s_waitcnt lgkmcnt(0)
	v_cvt_pk_fp8_f32 v71, v74, v75 op_sel:[0,0,1]
	s_add_u32 s8, s18, 0x8000
	s_addc_u32 s9, s19, 0
	v_lshl_add_u64 v[64:65], s[8:9], 0, v[128:129]
	ds_read2_b32 v[72:73], v151 offset1:32
	global_store_dwordx4 v[64:65], v[68:71], off nt
	ds_read2_b32 v[70:71], v151 offset0:128 offset1:160
	ds_read2_b32 v[74:75], v155 offset1:32
	ds_read2_b32 v[68:69], v151 offset0:64 offset1:96
	s_waitcnt lgkmcnt(3)
	v_cvt_pk_fp8_f32 v64, v72, v73
	ds_read2_b32 v[72:73], v151 offset0:192 offset1:224
	s_waitcnt lgkmcnt(3)
	v_cvt_pk_fp8_f32 v65, v70, v71
	ds_read2_b32 v[70:71], v155 offset0:128 offset1:160
	ds_read2_b32 v[76:77], v155 offset0:64 offset1:96
	s_waitcnt lgkmcnt(4)
	v_cvt_pk_fp8_f32 v66, v74, v75
	ds_read2_b32 v[74:75], v155 offset0:192 offset1:224
	s_waitcnt lgkmcnt(2)
	v_cvt_pk_fp8_f32 v67, v70, v71
	v_cvt_pk_fp8_f32 v64, v68, v69 op_sel:[0,0,1]
	v_cvt_pk_fp8_f32 v65, v72, v73 op_sel:[0,0,1]
	s_waitcnt lgkmcnt(1)
	v_cvt_pk_fp8_f32 v66, v76, v77 op_sel:[0,0,1]
	s_waitcnt lgkmcnt(0)
	v_cvt_pk_fp8_f32 v67, v74, v75 op_sel:[0,0,1]
	s_add_u32 s8, s18, 0xc000
	s_addc_u32 s9, s19, 0
	v_lshl_add_u64 v[68:69], s[8:9], 0, v[128:129]
	global_store_dwordx4 v[68:69], v[64:67], off nt
	s_waitcnt lgkmcnt(0)
	s_cmp_ge_i32 s1, s45
	s_cselect_b64 s[20:21], -1, 0

; __device__ __forceinline__ cgptr cuni(const void* p) { const unsigned long long v = (unsigned long long)p; const unsigned lo = __builtin_amdgcn_readfirstlane((unsigned)v), hi = __builtin_amdgcn_readfirstlane((unsigned)(v >> 32)); return (cgptr)(((unsigned long long)hi << 32) | lo); }
; __device__ __forceinline__ ConvItem conv_decode(int it, const float* wgu, const float* wd, unsigned char* WguT, unsigned char* WdT) {
;     constexpr int I_GU = NE * 16 * 128;
;     ConvItem c; int r = it, nbn, N; const float* src; unsigned char* dstp; bool gu;
;     if (r < I_GU) { const int e = r / (16 * 128); r -= e * (16 * 128); N = 4096; nbn = 128; src = wgu + (size_t)e * DM * 4096; dstp = WguT + (size_t)e * 4096 * DM; gu = true; }
;     else { r -= I_GU; const int e = r / (16 * 64); r -= e * (16 * 64); N = DM; nbn = 64; src = wd + (size_t)e * DFF * DM; dstp = WdT + (size_t)e * DM * DFF; gu = false; }
;     const int kb = r / nbn, nb = r - kb * nbn, n0 = nb * 32, k0 = kb * 128; int dst = n0;
;     if (gu) { const int j = n0 & 2047; dst = (j >> 7) * 256 + (j & 127) + ((n0 >= 2048) ? 128 : 0); }
;     c.src = cuni(src + (size_t)k0 * N + n0); c.dstp = cuni(dstp + (size_t)dst * DM + k0); c.N4 = (unsigned)N * 4u;
;     return c;
; }
.LBB0_564:
	s_waitcnt vmcnt(4)
	v_cvt_f32_ubyte0_e32 v64, s12
	v_rcp_iflag_f32_e32 v64, v64
	s_sub_i32 s27, 0, s12
	s_abs_i32 s26, s9
	s_ashr_i32 s17, s9, 31
	v_mul_f32_e32 v64, 0x4f7ffffe, v64
	v_cvt_u32_f32_e32 v64, v64
	v_add_u32_e32 v152, 0x400, v148
	v_add_u32_e32 v153, 0x400, v149
	v_add_u32_e32 v154, 0x400, v150
	v_readfirstlane_b32 s30, v64
	s_mul_i32 s27, s27, s30
	s_mul_hi_u32 s27, s30, s27
	s_add_i32 s30, s30, s27
	s_mul_hi_u32 s27, s26, s30
	s_mul_i32 s30, s27, s12
	s_sub_i32 s26, s26, s30
	s_add_i32 s31, s27, 1
	s_sub_i32 s30, s26, s12
	s_cmp_ge_u32 s26, s12
	s_cselect_b32 s27, s31, s27
	s_cselect_b32 s26, s30, s26
	s_add_i32 s30, s27, 1
	s_cmp_ge_u32 s26, s12
	s_cselect_b32 s26, s30, s27
	s_xor_b32 s26, s26, s17
	s_sub_i32 s17, s26, s17
	s_mul_i32 s12, s17, s12
	s_lshl_b32 s27, s9, 6
	s_sub_i32 s9, s9, s12
	s_lshl_b32 s26, s9, 5
	s_and_b32 s12, s27, 0xf00
	s_and_b32 s27, s26, 0x60
	s_or_b32 s12, s27, s12
	s_cmp_gt_i32 s9, 63
	s_cselect_b32 s9, 0x80, 0
	s_or_b32 s9, s12, s9
	s_and_b64 s[18:19], s[18:19], exec
	s_cselect_b32 s18, s9, s26
	s_lshl_b32 s9, s17, 7
	s_mul_hi_i32 s31, s9, s8
	s_mul_i32 s30, s9, s8
	s_ashr_i32 s12, s9, 31
	s_lshl_b64 s[30:31], s[30:31], 2
	s_add_u32 s17, s24, s30
	s_addc_u32 s19, s25, s31
	s_ashr_i32 s27, s26, 31
	s_lshl_b64 s[24:25], s[26:27], 2
	s_add_u32 s24, s17, s24
	s_addc_u32 s25, s19, s25
	s_ashr_i32 s19, s18, 31
	s_lshl_b64 s[18:19], s[18:19], 11
	s_add_u32 s17, s22, s18
	s_addc_u32 s19, s23, s19
	s_add_u32 s18, s17, s9
	s_addc_u32 s19, s19, s12
	s_lshl_b32 s9, s8, 5
	v_mul_lo_u32 v64, v130, s8
	s_add_u32 s22, s24, s9
	v_or_b32_e32 v64, v64, v131
	s_addc_u32 s23, s25, 0
	s_lshl_b32 s9, s8, 6
	global_load_dwordx4 v[124:127], v64, s[24:25] nt
	global_load_dwordx4 v[116:119], v64, s[22:23] nt
	s_add_u32 s22, s24, s9
	s_addc_u32 s23, s25, 0
	s_mul_i32 s9, s8, 0x60
	s_add_u32 s26, s24, s9
	s_addc_u32 s27, s25, 0
	s_lshl_b32 s9, s8, 7
	global_load_dwordx4 v[120:123], v64, s[22:23] nt
	global_load_dwordx4 v[108:111], v64, s[26:27] nt
	s_add_u32 s22, s24, s9
	s_addc_u32 s23, s25, 0
	s_mul_i32 s9, s8, 0xa0
	s_add_u32 s26, s24, s9
	s_addc_u32 s27, s25, 0
	s_mul_i32 s9, s8, 0xc0
	global_load_dwordx4 v[112:115], v64, s[22:23] nt
	global_load_dwordx4 v[100:103], v64, s[26:27] nt
	s_add_u32 s22, s24, s9
	s_addc_u32 s23, s25, 0
	s_mul_i32 s9, s8, 0xe0
	s_add_u32 s26, s24, s9
	s_addc_u32 s27, s25, 0
	s_lshl_b32 s9, s8, 8
	global_load_dwordx4 v[104:107], v64, s[22:23] nt
	global_load_dwordx4 v[92:95], v64, s[26:27] nt
	s_add_u32 s22, s24, s9
	s_addc_u32 s23, s25, 0
	s_mul_i32 s9, s8, 0x120
	s_add_u32 s26, s24, s9
	s_addc_u32 s27, s25, 0
	s_mul_i32 s9, s8, 0x140
	global_load_dwordx4 v[96:99], v64, s[22:23] nt
	global_load_dwordx4 v[84:87], v64, s[26:27] nt
	s_add_u32 s22, s24, s9
	s_addc_u32 s23, s25, 0
	s_mul_i32 s9, s8, 0x160
	s_add_u32 s26, s24, s9
	s_addc_u32 s27, s25, 0
	s_mul_i32 s9, s8, 0x180
	global_load_dwordx4 v[88:91], v64, s[22:23] nt
	global_load_dwordx4 v[76:79], v64, s[26:27] nt
	s_add_u32 s22, s24, s9
	s_addc_u32 s23, s25, 0
	s_mul_i32 s9, s8, 0x1a0
	s_add_u32 s26, s24, s9
	s_addc_u32 s27, s25, 0
	s_mul_i32 s9, s8, 0x1c0
	global_load_dwordx4 v[80:83], v64, s[22:23] nt
	global_load_dwordx4 v[68:71], v64, s[26:27] nt
	s_add_u32 s22, s24, s9
	s_addc_u32 s23, s25, 0
	s_mulk_i32 s8, 0x1e0
	s_add_u32 s8, s24, s8
	s_waitcnt vmcnt(29)
	v_pk_mul_f32 v[6:7], v[6:7], s[16:17] op_sel_hi:[1,0]
	v_pk_mul_f32 v[4:5], v[4:5], s[16:17] op_sel_hi:[1,0]
	s_waitcnt vmcnt(28)
	v_pk_mul_f32 v[2:3], v[2:3], s[16:17] op_sel_hi:[1,0]
	v_pk_mul_f32 v[0:1], v[0:1], s[16:17] op_sel_hi:[1,0]
	s_addc_u32 s9, s25, 0
	global_load_dwordx4 v[72:75], v64, s[22:23] nt
	s_nop 0
	global_load_dwordx4 v[64:67], v64, s[8:9] nt
	ds_write_b128 v132, v[4:7]
	ds_write_b128 v133, v[0:3]
	s_waitcnt vmcnt(29)
	v_pk_mul_f32 v[2:3], v[14:15], s[16:17] op_sel_hi:[1,0]
	v_pk_mul_f32 v[0:1], v[12:13], s[16:17] op_sel_hi:[1,0]
	ds_write_b128 v134, v[0:3]
	s_waitcnt vmcnt(28)
	v_pk_mul_f32 v[2:3], v[10:11], s[16:17] op_sel_hi:[1,0]
	v_pk_mul_f32 v[0:1], v[8:9], s[16:17] op_sel_hi:[1,0]
	ds_write_b128 v135, v[0:3]
	s_waitcnt vmcnt(27)
	v_pk_mul_f32 v[2:3], v[22:23], s[16:17] op_sel_hi:[1,0]
	v_pk_mul_f32 v[0:1], v[20:21], s[16:17] op_sel_hi:[1,0]
	ds_write_b128 v136, v[0:3]
	s_waitcnt vmcnt(26)
	v_pk_mul_f32 v[2:3], v[18:19], s[16:17] op_sel_hi:[1,0]
	v_pk_mul_f32 v[0:1], v[16:17], s[16:17] op_sel_hi:[1,0]
	ds_write_b128 v137, v[0:3]
	s_waitcnt vmcnt(25)
	v_pk_mul_f32 v[2:3], v[30:31], s[16:17] op_sel_hi:[1,0]
	v_pk_mul_f32 v[0:1], v[28:29], s[16:17] op_sel_hi:[1,0]
	ds_write_b128 v138, v[0:3]
	s_waitcnt vmcnt(24)
	v_pk_mul_f32 v[2:3], v[26:27], s[16:17] op_sel_hi:[1,0]
	v_pk_mul_f32 v[0:1], v[24:25], s[16:17] op_sel_hi:[1,0]
	ds_write_b128 v139, v[0:3]
	s_waitcnt vmcnt(23)
	v_pk_mul_f32 v[2:3], v[38:39], s[16:17] op_sel_hi:[1,0]
	v_pk_mul_f32 v[0:1], v[36:37], s[16:17] op_sel_hi:[1,0]
	ds_write_b128 v140, v[0:3]
	s_waitcnt vmcnt(22)
	v_pk_mul_f32 v[2:3], v[34:35], s[16:17] op_sel_hi:[1,0]
	v_pk_mul_f32 v[0:1], v[32:33], s[16:17] op_sel_hi:[1,0]
	ds_write_b128 v141, v[0:3]
	s_waitcnt vmcnt(21)
	v_pk_mul_f32 v[2:3], v[46:47], s[16:17] op_sel_hi:[1,0]
	v_pk_mul_f32 v[0:1], v[44:45], s[16:17] op_sel_hi:[1,0]
	ds_write_b128 v142, v[0:3]
	s_waitcnt vmcnt(20)
; #define CONV_LOAD(v, c) do { const unsigned lo_ = (unsigned)(lane >> 3) * (c).N4 + 16u * (unsigned)(lane & 7); _Pragma("unroll") for (int i = 0; i < 16; ++i) v[i] = __builtin_nontemporal_load((const GAS f32x4*)(cuni((const void*)((c).src + (size_t)(8 * i) * (c).N4)) + lo_)); } while (0)
; __device__ __forceinline__ void convert_expert_weights(const float* wgu, const float* wd, unsigned char* WguT, unsigned char* WdT, LAS float* scr, int gw, int NGW, int NIT, int lane) {
;     ...
;     for (;;) {
;         const bool hb = it + NGW < NIT; cb = conv_decode(hb ? it + NGW : it, wgu, wd, WguT, WdT); CONV_LOAD(vb, cb);
;         CONV_STORE(va, ca);
;         if (!hb) break;
;         it += NGW;
;         const bool ha = it + NGW < NIT; ca = conv_decode(ha ? it + NGW : it, wgu, wd, WguT, WdT); CONV_LOAD(va, ca);
;         CONV_STORE(vb, cb);
;         if (!ha) break;
;         it += NGW;
;     }
	v_pk_mul_f32 v[2:3], v[42:43], s[16:17] op_sel_hi:[1,0]
	v_pk_mul_f32 v[0:1], v[40:41], s[16:17] op_sel_hi:[1,0]
	ds_write_b128 v143, v[0:3]
	s_waitcnt vmcnt(19)
	v_pk_mul_f32 v[2:3], v[54:55], s[16:17] op_sel_hi:[1,0]
	v_pk_mul_f32 v[0:1], v[52:53], s[16:17] op_sel_hi:[1,0]
	ds_write_b128 v144, v[0:3]
	s_waitcnt vmcnt(18)
	v_pk_mul_f32 v[2:3], v[50:51], s[16:17] op_sel_hi:[1,0]
	v_pk_mul_f32 v[0:1], v[48:49], s[16:17] op_sel_hi:[1,0]
	ds_write_b128 v145, v[0:3]
	s_waitcnt vmcnt(17)
	v_pk_mul_f32 v[2:3], v[62:63], s[16:17] op_sel_hi:[1,0]
	v_pk_mul_f32 v[0:1], v[60:61], s[16:17] op_sel_hi:[1,0]
	ds_write_b128 v146, v[0:3]
	s_waitcnt vmcnt(16)
	v_pk_mul_f32 v[2:3], v[58:59], s[16:17] op_sel_hi:[1,0]
	v_pk_mul_f32 v[0:1], v[56:57], s[16:17] op_sel_hi:[1,0]
	ds_write_b128 v147, v[0:3]
	s_waitcnt lgkmcnt(0)
	ds_read2_b32 v[0:1], v148 offset1:32
	ds_read2_b32 v[8:9], v148 offset0:64 offset1:96
	s_add_u32 s8, s14, 0x4000
	s_waitcnt lgkmcnt(0)
	v_cvt_pk_fp8_f32 v4, v0, v1
	ds_read2_b32 v[0:1], v148 offset0:128 offset1:160
	ds_read2_b32 v[10:11], v148 offset0:192 offset1:224
	ds_read2_b32 v[12:13], v152 offset1:32
	s_waitcnt lgkmcnt(2)
	v_cvt_pk_fp8_f32 v5, v0, v1
	ds_read2_b32 v[0:1], v152 offset0:64 offset1:96
	ds_read2_b32 v[14:15], v152 offset0:128 offset1:160
	s_waitcnt lgkmcnt(2)
	v_cvt_pk_fp8_f32 v6, v12, v13
	ds_read2_b32 v[12:13], v152 offset0:192 offset1:224
	v_cvt_pk_fp8_f32 v4, v8, v9 op_sel:[0,0,1]
	s_waitcnt lgkmcnt(1)
	v_cvt_pk_fp8_f32 v7, v14, v15
	v_cvt_pk_fp8_f32 v5, v10, v11 op_sel:[0,0,1]
	v_cvt_pk_fp8_f32 v6, v0, v1 op_sel:[0,0,1]
	ds_read2_b32 v[0:1], v149 offset1:32
	s_waitcnt lgkmcnt(1)
	v_cvt_pk_fp8_f32 v7, v12, v13 op_sel:[0,0,1]
	v_lshl_add_u64 v[8:9], s[14:15], 0, v[128:129]
	s_addc_u32 s9, s15, 0
	v_add_u32_e32 v155, 0x400, v151
	global_store_dwordx4 v[8:9], v[4:7], off nt
	ds_read2_b32 v[8:9], v149 offset0:64 offset1:96
	s_waitcnt lgkmcnt(1)
	v_cvt_pk_fp8_f32 v4, v0, v1
	ds_read2_b32 v[0:1], v149 offset0:128 offset1:160
	ds_read2_b32 v[10:11], v149 offset0:192 offset1:224
	ds_read2_b32 v[12:13], v153 offset1:32
	s_waitcnt lgkmcnt(2)
	v_cvt_pk_fp8_f32 v5, v0, v1
	ds_read2_b32 v[0:1], v153 offset0:64 offset1:96
	ds_read2_b32 v[14:15], v153 offset0:128 offset1:160
	s_waitcnt lgkmcnt(2)
	v_cvt_pk_fp8_f32 v6, v12, v13
	ds_read2_b32 v[12:13], v153 offset0:192 offset1:224
	v_cvt_pk_fp8_f32 v4, v8, v9 op_sel:[0,0,1]
	s_waitcnt lgkmcnt(1)
	v_cvt_pk_fp8_f32 v7, v14, v15
	v_cvt_pk_fp8_f32 v5, v10, v11 op_sel:[0,0,1]
	v_cvt_pk_fp8_f32 v6, v0, v1 op_sel:[0,0,1]
	ds_read2_b32 v[0:1], v150 offset1:32
	s_waitcnt lgkmcnt(1)
	v_cvt_pk_fp8_f32 v7, v12, v13 op_sel:[0,0,1]
	v_lshl_add_u64 v[8:9], s[8:9], 0, v[128:129]
	s_add_u32 s8, s14, 0x8000
	s_addc_u32 s9, s15, 0
	global_store_dwordx4 v[8:9], v[4:7], off nt
	ds_read2_b32 v[8:9], v150 offset0:64 offset1:96
	s_nop 0
	s_waitcnt lgkmcnt(1)
	v_cvt_pk_fp8_f32 v4, v0, v1
	ds_read2_b32 v[0:1], v150 offset0:128 offset1:160
	ds_read2_b32 v[10:11], v150 offset0:192 offset1:224
	ds_read2_b32 v[12:13], v154 offset1:32
	s_waitcnt lgkmcnt(2)
	v_cvt_pk_fp8_f32 v5, v0, v1
	ds_read2_b32 v[0:1], v154 offset0:64 offset1:96
	ds_read2_b32 v[14:15], v154 offset0:128 offset1:160
	s_waitcnt lgkmcnt(2)
	v_cvt_pk_fp8_f32 v6, v12, v13
	ds_read2_b32 v[12:13], v154 offset0:192 offset1:224
	v_cvt_pk_fp8_f32 v4, v8, v9 op_sel:[0,0,1]
	s_waitcnt lgkmcnt(1)
	v_cvt_pk_fp8_f32 v7, v14, v15
	v_cvt_pk_fp8_f32 v5, v10, v11 op_sel:[0,0,1]
	v_cvt_pk_fp8_f32 v6, v0, v1 op_sel:[0,0,1]
	ds_read2_b32 v[8:9], v151 offset1:32
	s_waitcnt lgkmcnt(1)
	v_cvt_pk_fp8_f32 v7, v12, v13 op_sel:[0,0,1]
	v_lshl_add_u64 v[0:1], s[8:9], 0, v[128:129]
	s_add_u32 s8, s14, 0xc000
	s_addc_u32 s9, s15, 0
	global_store_dwordx4 v[0:1], v[4:7], off nt
	ds_read2_b32 v[4:5], v151 offset0:64 offset1:96
	s_waitcnt lgkmcnt(1)
	v_cvt_pk_fp8_f32 v0, v8, v9
	ds_read2_b32 v[6:7], v151 offset0:128 offset1:160
	ds_read2_b32 v[8:9], v151 offset0:192 offset1:224
	ds_read2_b32 v[10:11], v155 offset1:32
	s_waitcnt lgkmcnt(3)
	v_cvt_pk_fp8_f32 v0, v4, v5 op_sel:[0,0,1]
	s_waitcnt lgkmcnt(2)
	v_cvt_pk_fp8_f32 v1, v6, v7
	ds_read2_b32 v[6:7], v155 offset0:128 offset1:160
	ds_read2_b32 v[12:13], v155 offset0:64 offset1:96
	s_waitcnt lgkmcnt(2)
	v_cvt_pk_fp8_f32 v2, v10, v11
	ds_read2_b32 v[10:11], v155 offset0:192 offset1:224
	v_cvt_pk_fp8_f32 v1, v8, v9 op_sel:[0,0,1]
	s_waitcnt lgkmcnt(2)
	v_cvt_pk_fp8_f32 v3, v6, v7
	s_waitcnt lgkmcnt(1)
	v_cvt_pk_fp8_f32 v2, v12, v13 op_sel:[0,0,1]
	v_lshl_add_u64 v[4:5], s[8:9], 0, v[128:129]
	s_andn2_b64 vcc, exec, s[20:21]
	s_waitcnt lgkmcnt(0)
	v_cvt_pk_fp8_f32 v3, v10, v11 op_sel:[0,0,1]
	s_mov_b64 s[20:21], -1
	global_store_dwordx4 v[4:5], v[0:3], off nt
	s_waitcnt lgkmcnt(0)
	s_cbranch_vccnz .LBB0_558
	s_add_i32 s1, s0, s1
	s_cmp_lt_i32 s1, s45
	s_cselect_b32 s1, s1, s3
	s_cmp_lt_i32 s1, 0x10000
	s_cselect_b64 s[14:15], -1, 0
	s_cmp_gt_i32 s1, 0xffff
	s_mov_b64 s[24:25], -1
	s_cbranch_scc0 .LBB0_567
	s_add_i32 s8, s1, 0xffff0000
	s_lshr_b32 s12, s8, 10
	s_and_b32 s9, s1, 0x3ff
	s_lshl_b64 s[20:21], s[12:13], 22
	s_lshl_b64 s[22:23], s[12:13], 24
	s_add_u32 s22, s6, s22
	s_addc_u32 s23, s7, s23
	s_add_u32 s20, s77, s20
	v_readlane_b32 s8, v252, 33
	s_addc_u32 s21, s8, s21
	s_mov_b64 s[24:25], 0

; #define GAS __attribute__((address_space(1)))
; __device__ __forceinline__ unsigned cvt_pk_bf16(float lo, float hi) { unsigned r; asm volatile("v_cvt_pk_bf16_f32 %0, %1, %2" : "=v"(r) : "v"(lo), "v"(hi)); return r; }
; #define SBAR() __builtin_amdgcn_sched_barrier(0)
; __device__ __forceinline__ gptr uni(const GAS void* p) { const unsigned long long v = (unsigned long long)p; const unsigned lo = __builtin_amdgcn_readfirstlane((unsigned)v), hi = __builtin_amdgcn_readfirstlane((unsigned)(v >> 32)); return (gptr)(((unsigned long long)hi << 32) | lo); }
; #define QLOAD(ref) do { gptr qb_ = uni((const GAS void*)((ref).Q + (size_t)(wid * QBLK) * QS)); _Pragma("unroll") for (int d0 = 0; d0 < NQR; ++d0) S.qr[d0] = *reinterpret_cast<const GAS u32x2*>(qb_ + d0 * 16 + voff_q); } while (0)
; template <int AV>
; __device__ __forceinline__ void block(const BlockRef& cur, const BlockRef& nxt, char* lds, Seam& S, const int wid, const QNorm& QN) {
;     ...
;     SBAR(); QLOAD(nxt); v_read(vf, STGP(sc), ka); SBAR();
;     finishSM(pB0, pB1, pa); SBAR();
;     pv_mma(o, ol, vf, ones, pa);
;     S.g = INC6(sc, 1);
;     __builtin_amdgcn_s_setprio(0);
;     float rli[16];
; #pragma unroll
;     for (int r = 0; r < 16; ++r) rli[r] = __builtin_amdgcn_rcpf(ol[r]);
;     GAS char* Ow = (GAS char*)uni((const GAS void*)(cur.O + (size_t)(wid * QBLK) * OS));
;     const bool odd = (r32 & 1) != 0;
;     const unsigned voff_o = (unsigned)((4 * hi + (odd ? 1 : 0)) * OS + (r32 & ~1)) * 2u;
; #pragma unroll
;     for (int r = 0; r < 16; r += 2) { const int orow0 = (r & 3) + 8 * (r >> 2);
; #pragma unroll
;         for (int d0 = 0; d0 < 4; ++d0) { const float a = o[d0][r] * rli[r], b = o[d0][r + 1] * rli[r + 1];
;             const float send = odd ? a : b;
;             const float recv = __int_as_float(__builtin_amdgcn_mov_dpp(__float_as_int(send), 0xB1, 0xF, 0xF, true));
;             *(GAS unsigned*)(Ow + (size_t)orow0 * OS * 2 + d0 * 64 + voff_o) = cvt_pk_bf16(odd ? recv : a, odd ? b : recv); } }
.LBB0_575:
	s_add_u32 s6, s64, s95
	s_addc_u32 s7, s65, s11
	v_lshl_add_u64 v[80:81], s[6:7], 0, v[184:185]
	global_load_dwordx2 v[86:87], v[80:81], off
	global_load_dwordx2 v[84:85], v[80:81], off offset:16
	global_load_dwordx2 v[82:83], v[80:81], off offset:32
	s_nop 0
	global_load_dwordx2 v[80:81], v[80:81], off offset:48
	ds_read_b128 v[88:91], v202 offset:12288
	ds_read_b128 v[112:115], v202 offset:14336
	ds_read_b128 v[92:95], v201 offset:12288
	ds_read_b128 v[116:119], v201 offset:14336
	ds_read_b128 v[120:123], v202 offset:16384
	ds_read_b128 v[128:131], v202 offset:18432
	ds_read_b128 v[124:127], v201 offset:16384
	ds_read_b128 v[132:135], v201 offset:18432
	v_exp_f32_e32 v136, v96
	v_exp_f32_e32 v97, v97
	v_exp_f32_e32 v137, v100
	v_exp_f32_e32 v138, v101
	v_exp_f32_e32 v139, v103
	v_exp_f32_e32 v98, v98
	v_exp_f32_e32 v99, v99
	v_exp_f32_e32 v102, v102
	v_cvt_pk_fp8_f32 v100, v136, v97
	v_cvt_pk_fp8_f32 v101, v137, v138
	v_exp_f32_e32 v104, v104
	v_exp_f32_e32 v105, v105
	v_exp_f32_e32 v108, v108
	v_exp_f32_e32 v109, v109
	v_cvt_pk_fp8_f32 v100, v98, v99 op_sel:[0,0,1]
	v_cvt_pk_fp8_f32 v101, v102, v139 op_sel:[0,0,1]
	v_exp_f32_e32 v106, v106
	v_exp_f32_e32 v107, v107
	v_exp_f32_e32 v110, v110
	v_exp_f32_e32 v111, v111
	v_cvt_pk_fp8_f32 v96, v217, v218
	v_cvt_pk_fp8_f32 v97, v213, v214
	v_cvt_pk_fp8_f32 v98, v209, v210
	v_cvt_pk_fp8_f32 v102, v104, v105
	v_cvt_pk_fp8_f32 v99, v205, v206
	v_cvt_pk_fp8_f32 v103, v108, v109
	v_cvt_pk_fp8_f32 v96, v215, v216 op_sel:[0,0,1]
	v_cvt_pk_fp8_f32 v97, v211, v212 op_sel:[0,0,1]
	v_cvt_pk_fp8_f32 v98, v207, v208 op_sel:[0,0,1]
	v_cvt_pk_fp8_f32 v102, v106, v107 op_sel:[0,0,1]
	v_cvt_pk_fp8_f32 v99, v203, v204 op_sel:[0,0,1]
	v_cvt_pk_fp8_f32 v103, v110, v111 op_sel:[0,0,1]
	s_cmp_gt_i32 s0, 4
	s_cselect_b32 s1, -5, 1
	s_add_i32 s0, s1, s0
	s_waitcnt lgkmcnt(5)
	v_mfma_f32_32x32x64_f8f6f4 v[48:63], v[96:103], v[88:95], v[48:63]
	s_waitcnt lgkmcnt(4)
	v_mfma_f32_32x32x64_f8f6f4 v[0:15], v[96:103], v[112:119], v[0:15]
	s_waitcnt lgkmcnt(1)
	v_mfma_f32_32x32x64_f8f6f4 v[32:47], v[96:103], v[120:127], v[32:47]
	s_waitcnt lgkmcnt(0)
	v_mfma_f32_32x32x64_f8f6f4 v[16:31], v[96:103], v[128:135], v[16:31]
	v_mfma_f32_32x32x64_f8f6f4 v[64:79], v[96:103], v[152:159], v[64:79]
	s_setprio 0
	s_nop 15
	s_nop 2
	v_rcp_f32_e32 v88, v64
	v_rcp_f32_e32 v89, v65
	v_and_b32_e32 v90, 1, v188
	v_cmp_eq_u32_e32 vcc, 0, v90
	v_mul_f32_e32 v48, v48, v88
	v_mul_f32_e32 v49, v49, v89
	v_or_b32_e32 v64, v195, v90
	v_cndmask_b32_e32 v90, v48, v49, vcc
	v_lshlrev_b32_e32 v65, 1, v188
	s_add_u32 s6, s76, s60
	v_mov_b32_dpp v90, v90 quad_perm:[1,0,3,2] row_mask:0xf bank_mask:0xf bound_ctrl:1
	v_and_b32_e32 v65, 60, v65
	v_cndmask_b32_e32 v48, v90, v48, vcc
	s_addc_u32 s7, s77, s61
	v_lshl_or_b32 v184, v64, 12, v65
	v_cndmask_b32_e32 v49, v49, v90, vcc
	v_cvt_pk_bf16_f32 v48, v48, v49
	v_mul_f32_e32 v0, v0, v88
	v_mul_f32_e32 v1, v1, v89
	global_store_dword v184, v48, s[6:7]
	v_cndmask_b32_e32 v48, v0, v1, vcc
	v_rcp_f32_e32 v66, v66
	v_rcp_f32_e32 v67, v67
	v_mov_b32_dpp v48, v48 quad_perm:[1,0,3,2] row_mask:0xf bank_mask:0xf bound_ctrl:1
	v_cndmask_b32_e32 v0, v48, v0, vcc
	v_cndmask_b32_e32 v1, v1, v48, vcc
	v_cvt_pk_bf16_f32 v0, v0, v1
	global_store_dword v184, v0, s[6:7] offset:64
	v_mul_f32_e32 v0, v32, v88
	v_mul_f32_e32 v1, v33, v89
	v_cndmask_b32_e32 v32, v0, v1, vcc
	v_lshl_add_u64 v[64:65], s[6:7], 0, v[184:185]
	s_movk_i32 s1, 0x2000
	v_mov_b32_dpp v32, v32 quad_perm:[1,0,3,2] row_mask:0xf bank_mask:0xf bound_ctrl:1
	v_cndmask_b32_e32 v0, v32, v0, vcc
	v_cndmask_b32_e32 v1, v1, v32, vcc
	v_cvt_pk_bf16_f32 v0, v0, v1
	global_store_dword v184, v0, s[6:7] offset:128
	v_mul_f32_e32 v0, v16, v88
	v_mul_f32_e32 v1, v17, v89
	v_cndmask_b32_e32 v16, v0, v1, vcc
	v_mul_f32_e32 v2, v2, v66
	v_mul_f32_e32 v3, v3, v67
	v_mov_b32_dpp v16, v16 quad_perm:[1,0,3,2] row_mask:0xf bank_mask:0xf bound_ctrl:1
	v_cndmask_b32_e32 v0, v16, v0, vcc
	v_cndmask_b32_e32 v1, v1, v16, vcc
	v_cvt_pk_bf16_f32 v0, v0, v1
	global_store_dword v184, v0, s[6:7] offset:192
	v_mul_f32_e32 v0, v50, v66
	v_mul_f32_e32 v1, v51, v67
	v_cndmask_b32_e32 v16, v0, v1, vcc
	v_rcp_f32_e32 v68, v68
	v_rcp_f32_e32 v69, v69
	v_mov_b32_dpp v16, v16 quad_perm:[1,0,3,2] row_mask:0xf bank_mask:0xf bound_ctrl:1
	v_cndmask_b32_e32 v0, v16, v0, vcc
	v_cndmask_b32_e32 v1, v1, v16, vcc
	v_cvt_pk_bf16_f32 v16, v0, v1
	v_add_co_u32_e64 v0, s[6:7], s1, v64
	s_mov_b32 s1, 0x8000
	s_nop 0
	v_addc_co_u32_e64 v1, s[6:7], 0, v65, s[6:7]
	global_store_dword v[0:1], v16, off
	v_cndmask_b32_e32 v16, v2, v3, vcc
	v_rcp_f32_e32 v70, v70
	v_rcp_f32_e32 v71, v71
	v_mov_b32_dpp v16, v16 quad_perm:[1,0,3,2] row_mask:0xf bank_mask:0xf bound_ctrl:1
	v_cndmask_b32_e32 v2, v16, v2, vcc
	v_cndmask_b32_e32 v3, v3, v16, vcc
	v_cvt_pk_bf16_f32 v2, v2, v3
	global_store_dword v[0:1], v2, off offset:64
	v_mul_f32_e32 v2, v34, v66
	v_mul_f32_e32 v3, v35, v67
	v_cndmask_b32_e32 v16, v2, v3, vcc
	v_rcp_f32_e32 v72, v72
	v_rcp_f32_e32 v73, v73
	v_mov_b32_dpp v16, v16 quad_perm:[1,0,3,2] row_mask:0xf bank_mask:0xf bound_ctrl:1
	v_cndmask_b32_e32 v2, v16, v2, vcc
	v_cndmask_b32_e32 v3, v3, v16, vcc
	v_cvt_pk_bf16_f32 v2, v2, v3
	global_store_dword v[0:1], v2, off offset:128
	v_mul_f32_e32 v2, v18, v66
	v_mul_f32_e32 v3, v19, v67
	v_cndmask_b32_e32 v16, v2, v3, vcc
	v_rcp_f32_e32 v74, v74
	v_rcp_f32_e32 v75, v75
	v_mov_b32_dpp v16, v16 quad_perm:[1,0,3,2] row_mask:0xf bank_mask:0xf bound_ctrl:1
	v_cndmask_b32_e32 v2, v16, v2, vcc
	v_cndmask_b32_e32 v3, v3, v16, vcc
	v_cvt_pk_bf16_f32 v2, v2, v3
	global_store_dword v[0:1], v2, off offset:192
	v_mul_f32_e32 v0, v52, v68
	v_mul_f32_e32 v1, v53, v69
; #define GAS __attribute__((address_space(1)))
; __device__ __forceinline__ unsigned cvt_pk_bf16(float lo, float hi) { unsigned r; asm volatile("v_cvt_pk_bf16_f32 %0, %1, %2" : "=v"(r) : "v"(lo), "v"(hi)); return r; }
; __device__ __forceinline__ gptr uni(const GAS void* p) { const unsigned long long v = (unsigned long long)p; const unsigned lo = __builtin_amdgcn_readfirstlane((unsigned)v), hi = __builtin_amdgcn_readfirstlane((unsigned)(v >> 32)); return (gptr)(((unsigned long long)hi << 32) | lo); }
; template <int AV>
; __device__ __forceinline__ void block(const BlockRef& cur, const BlockRef& nxt, char* lds, Seam& S, const int wid, const QNorm& QN) {
;     ...
;     float rli[16];
; #pragma unroll
;     for (int r = 0; r < 16; ++r) rli[r] = __builtin_amdgcn_rcpf(ol[r]);
;     GAS char* Ow = (GAS char*)uni((const GAS void*)(cur.O + (size_t)(wid * QBLK) * OS));
;     const bool odd = (r32 & 1) != 0;
;     const unsigned voff_o = (unsigned)((4 * hi + (odd ? 1 : 0)) * OS + (r32 & ~1)) * 2u;
; #pragma unroll
;     for (int r = 0; r < 16; r += 2) { const int orow0 = (r & 3) + 8 * (r >> 2);
; #pragma unroll
;         for (int d0 = 0; d0 < 4; ++d0) { const float a = o[d0][r] * rli[r], b = o[d0][r + 1] * rli[r + 1];
;             const float send = odd ? a : b;
;             const float recv = __int_as_float(__builtin_amdgcn_mov_dpp(__float_as_int(send), 0xB1, 0xF, 0xF, true));
;             *(GAS unsigned*)(Ow + (size_t)orow0 * OS * 2 + d0 * 64 + voff_o) = cvt_pk_bf16(odd ? recv : a, odd ? b : recv); } }
	v_cndmask_b32_e32 v2, v0, v1, vcc
	v_mul_f32_e32 v3, v5, v69
	v_rcp_f32_e32 v76, v76
	v_mov_b32_dpp v2, v2 quad_perm:[1,0,3,2] row_mask:0xf bank_mask:0xf bound_ctrl:1
	v_cndmask_b32_e32 v0, v2, v0, vcc
	v_cndmask_b32_e32 v1, v1, v2, vcc
	v_cvt_pk_bf16_f32 v2, v0, v1
	v_add_co_u32_e64 v0, s[6:7], s1, v64
	s_mov_b32 s1, 0xa000
	s_nop 0
	v_addc_co_u32_e64 v1, s[6:7], 0, v65, s[6:7]
	global_store_dword v[0:1], v2, off
	v_mul_f32_e32 v2, v4, v68
	v_cndmask_b32_e32 v4, v2, v3, vcc
	v_rcp_f32_e32 v77, v77
	v_rcp_f32_e32 v78, v78
	v_mov_b32_dpp v4, v4 quad_perm:[1,0,3,2] row_mask:0xf bank_mask:0xf bound_ctrl:1
	v_cndmask_b32_e32 v2, v4, v2, vcc
	v_cndmask_b32_e32 v3, v3, v4, vcc
	v_cvt_pk_bf16_f32 v2, v2, v3
	global_store_dword v[0:1], v2, off offset:64
	v_mul_f32_e32 v2, v36, v68
	v_mul_f32_e32 v3, v37, v69
	v_cndmask_b32_e32 v4, v2, v3, vcc
	v_rcp_f32_e32 v79, v79
	s_mov_b32 s35, s41
	v_mov_b32_dpp v4, v4 quad_perm:[1,0,3,2] row_mask:0xf bank_mask:0xf bound_ctrl:1
	v_cndmask_b32_e32 v2, v4, v2, vcc
	v_cndmask_b32_e32 v3, v3, v4, vcc
	v_cvt_pk_bf16_f32 v2, v2, v3
	global_store_dword v[0:1], v2, off offset:128
	v_mul_f32_e32 v2, v20, v68
	v_mul_f32_e32 v3, v21, v69
	v_cndmask_b32_e32 v4, v2, v3, vcc
	s_mov_b64 s[76:77], s[68:69]
	s_mov_b64 s[82:83], s[74:75]
	v_mov_b32_dpp v4, v4 quad_perm:[1,0,3,2] row_mask:0xf bank_mask:0xf bound_ctrl:1
	v_cndmask_b32_e32 v2, v4, v2, vcc
	v_cndmask_b32_e32 v3, v3, v4, vcc
	v_cvt_pk_bf16_f32 v2, v2, v3
	global_store_dword v[0:1], v2, off offset:192
	v_mul_f32_e32 v0, v54, v70
	v_mul_f32_e32 v1, v55, v71
	v_cndmask_b32_e32 v2, v0, v1, vcc
	v_mul_f32_e32 v3, v7, v71
	s_mov_b64 s[80:81], s[72:73]
	v_mov_b32_dpp v2, v2 quad_perm:[1,0,3,2] row_mask:0xf bank_mask:0xf bound_ctrl:1
	v_cndmask_b32_e32 v0, v2, v0, vcc
	v_cndmask_b32_e32 v1, v1, v2, vcc
	v_cvt_pk_bf16_f32 v2, v0, v1
	v_add_co_u32_e64 v0, s[6:7], s1, v64
	s_mov_b32 s1, 0x10000
	s_nop 0
	v_addc_co_u32_e64 v1, s[6:7], 0, v65, s[6:7]
	global_store_dword v[0:1], v2, off
	v_mul_f32_e32 v2, v6, v70
	v_cndmask_b32_e32 v4, v2, v3, vcc
	s_mov_b64 s[78:79], s[70:71]
	v_readlane_b32 s84, v252, 28
	v_mov_b32_dpp v4, v4 quad_perm:[1,0,3,2] row_mask:0xf bank_mask:0xf bound_ctrl:1
	v_cndmask_b32_e32 v2, v4, v2, vcc
	v_cndmask_b32_e32 v3, v3, v4, vcc
	v_cvt_pk_bf16_f32 v2, v2, v3
	global_store_dword v[0:1], v2, off offset:64
	v_mul_f32_e32 v2, v38, v70
	v_mul_f32_e32 v3, v39, v71
	v_cndmask_b32_e32 v4, v2, v3, vcc
	s_nop 1
	v_mov_b32_dpp v4, v4 quad_perm:[1,0,3,2] row_mask:0xf bank_mask:0xf bound_ctrl:1
	v_cndmask_b32_e32 v2, v4, v2, vcc
	v_cndmask_b32_e32 v3, v3, v4, vcc
	v_cvt_pk_bf16_f32 v2, v2, v3
	global_store_dword v[0:1], v2, off offset:128
	v_mul_f32_e32 v2, v22, v70
	v_mul_f32_e32 v3, v23, v71
	v_cndmask_b32_e32 v4, v2, v3, vcc
	s_nop 1
	v_mov_b32_dpp v4, v4 quad_perm:[1,0,3,2] row_mask:0xf bank_mask:0xf bound_ctrl:1
	v_cndmask_b32_e32 v2, v4, v2, vcc
	v_cndmask_b32_e32 v3, v3, v4, vcc
	v_cvt_pk_bf16_f32 v2, v2, v3
	global_store_dword v[0:1], v2, off offset:192
	v_mul_f32_e32 v0, v56, v72
	v_mul_f32_e32 v1, v57, v73
	v_cndmask_b32_e32 v2, v0, v1, vcc
	v_mul_f32_e32 v3, v9, v73
	s_nop 0
	v_mov_b32_dpp v2, v2 quad_perm:[1,0,3,2] row_mask:0xf bank_mask:0xf bound_ctrl:1
	v_cndmask_b32_e32 v0, v2, v0, vcc
	v_cndmask_b32_e32 v1, v1, v2, vcc
	v_cvt_pk_bf16_f32 v2, v0, v1
	v_add_co_u32_e64 v0, s[6:7], s1, v64
	s_mov_b32 s1, 0x12000
	s_nop 0
	v_addc_co_u32_e64 v1, s[6:7], 0, v65, s[6:7]
	global_store_dword v[0:1], v2, off
	v_mul_f32_e32 v2, v8, v72
	v_cndmask_b32_e32 v4, v2, v3, vcc
	s_nop 1
	v_mov_b32_dpp v4, v4 quad_perm:[1,0,3,2] row_mask:0xf bank_mask:0xf bound_ctrl:1
	v_cndmask_b32_e32 v2, v4, v2, vcc
	v_cndmask_b32_e32 v3, v3, v4, vcc
	v_cvt_pk_bf16_f32 v2, v2, v3
	global_store_dword v[0:1], v2, off offset:64
	v_mul_f32_e32 v2, v40, v72
	v_mul_f32_e32 v3, v41, v73
	v_cndmask_b32_e32 v4, v2, v3, vcc
	s_nop 1
	v_mov_b32_dpp v4, v4 quad_perm:[1,0,3,2] row_mask:0xf bank_mask:0xf bound_ctrl:1
	v_cndmask_b32_e32 v2, v4, v2, vcc
	v_cndmask_b32_e32 v3, v3, v4, vcc
	v_cvt_pk_bf16_f32 v2, v2, v3
	global_store_dword v[0:1], v2, off offset:128
	v_mul_f32_e32 v2, v24, v72
	v_mul_f32_e32 v3, v25, v73
	v_cndmask_b32_e32 v4, v2, v3, vcc
	s_nop 1
	v_mov_b32_dpp v4, v4 quad_perm:[1,0,3,2] row_mask:0xf bank_mask:0xf bound_ctrl:1
	v_cndmask_b32_e32 v2, v4, v2, vcc
	v_cndmask_b32_e32 v3, v3, v4, vcc
	v_cvt_pk_bf16_f32 v2, v2, v3
; #define GAS __attribute__((address_space(1)))
; __device__ __forceinline__ unsigned cvt_pk_bf16(float lo, float hi) { unsigned r; asm volatile("v_cvt_pk_bf16_f32 %0, %1, %2" : "=v"(r) : "v"(lo), "v"(hi)); return r; }
; template <int AV>
; __device__ __forceinline__ void block(const BlockRef& cur, const BlockRef& nxt, char* lds, Seam& S, const int wid, const QNorm& QN) {
;     ...
; #pragma unroll
;     for (int r = 0; r < 16; r += 2) { const int orow0 = (r & 3) + 8 * (r >> 2);
; #pragma unroll
;         for (int d0 = 0; d0 < 4; ++d0) { const float a = o[d0][r] * rli[r], b = o[d0][r + 1] * rli[r + 1];
;             const float send = odd ? a : b;
;             const float recv = __int_as_float(__builtin_amdgcn_mov_dpp(__float_as_int(send), 0xB1, 0xF, 0xF, true));
;             *(GAS unsigned*)(Ow + (size_t)orow0 * OS * 2 + d0 * 64 + voff_o) = cvt_pk_bf16(odd ? recv : a, odd ? b : recv); } }
;     __syncthreads();
	global_store_dword v[0:1], v2, off offset:192
	v_mul_f32_e32 v0, v58, v74
	v_mul_f32_e32 v1, v59, v75
	v_cndmask_b32_e32 v2, v0, v1, vcc
	v_mul_f32_e32 v3, v11, v75
	s_nop 0
	v_mov_b32_dpp v2, v2 quad_perm:[1,0,3,2] row_mask:0xf bank_mask:0xf bound_ctrl:1
	v_cndmask_b32_e32 v0, v2, v0, vcc
	v_cndmask_b32_e32 v1, v1, v2, vcc
	v_cvt_pk_bf16_f32 v2, v0, v1
	v_add_co_u32_e64 v0, s[6:7], s1, v64
	s_mov_b32 s1, 0x18000
	s_nop 0
	v_addc_co_u32_e64 v1, s[6:7], 0, v65, s[6:7]
	global_store_dword v[0:1], v2, off
	v_mul_f32_e32 v2, v10, v74
	v_cndmask_b32_e32 v4, v2, v3, vcc
	s_nop 1
	v_mov_b32_dpp v4, v4 quad_perm:[1,0,3,2] row_mask:0xf bank_mask:0xf bound_ctrl:1
	v_cndmask_b32_e32 v2, v4, v2, vcc
	v_cndmask_b32_e32 v3, v3, v4, vcc
	v_cvt_pk_bf16_f32 v2, v2, v3
	global_store_dword v[0:1], v2, off offset:64
	v_mul_f32_e32 v2, v42, v74
	v_mul_f32_e32 v3, v43, v75
	v_cndmask_b32_e32 v4, v2, v3, vcc
	s_nop 1
	v_mov_b32_dpp v4, v4 quad_perm:[1,0,3,2] row_mask:0xf bank_mask:0xf bound_ctrl:1
	v_cndmask_b32_e32 v2, v4, v2, vcc
	v_cndmask_b32_e32 v3, v3, v4, vcc
	v_cvt_pk_bf16_f32 v2, v2, v3
	global_store_dword v[0:1], v2, off offset:128
	v_mul_f32_e32 v2, v26, v74
	v_mul_f32_e32 v3, v27, v75
	v_cndmask_b32_e32 v4, v2, v3, vcc
	s_nop 1
	v_mov_b32_dpp v4, v4 quad_perm:[1,0,3,2] row_mask:0xf bank_mask:0xf bound_ctrl:1
	v_cndmask_b32_e32 v2, v4, v2, vcc
	v_cndmask_b32_e32 v3, v3, v4, vcc
	v_cvt_pk_bf16_f32 v2, v2, v3
	global_store_dword v[0:1], v2, off offset:192
	v_mul_f32_e32 v0, v60, v76
	v_mul_f32_e32 v1, v61, v77
	v_cndmask_b32_e32 v2, v0, v1, vcc
	v_mul_f32_e32 v3, v13, v77
	s_nop 0
	v_mov_b32_dpp v2, v2 quad_perm:[1,0,3,2] row_mask:0xf bank_mask:0xf bound_ctrl:1
	v_cndmask_b32_e32 v0, v2, v0, vcc
	v_cndmask_b32_e32 v1, v1, v2, vcc
	v_cvt_pk_bf16_f32 v2, v0, v1
	v_add_co_u32_e64 v0, s[6:7], s1, v64
	s_mov_b32 s1, 0x1a000
	s_nop 0
	v_addc_co_u32_e64 v1, s[6:7], 0, v65, s[6:7]
	global_store_dword v[0:1], v2, off
	v_mul_f32_e32 v2, v12, v76
	v_cndmask_b32_e32 v4, v2, v3, vcc
	s_nop 1
	v_mov_b32_dpp v4, v4 quad_perm:[1,0,3,2] row_mask:0xf bank_mask:0xf bound_ctrl:1
	v_cndmask_b32_e32 v2, v4, v2, vcc
	v_cndmask_b32_e32 v3, v3, v4, vcc
	v_cvt_pk_bf16_f32 v2, v2, v3
	global_store_dword v[0:1], v2, off offset:64
	v_mul_f32_e32 v2, v44, v76
	v_mul_f32_e32 v3, v45, v77
	v_cndmask_b32_e32 v4, v2, v3, vcc
	s_nop 1
	v_mov_b32_dpp v4, v4 quad_perm:[1,0,3,2] row_mask:0xf bank_mask:0xf bound_ctrl:1
	v_cndmask_b32_e32 v2, v4, v2, vcc
	v_cndmask_b32_e32 v3, v3, v4, vcc
	v_cvt_pk_bf16_f32 v2, v2, v3
	global_store_dword v[0:1], v2, off offset:128
	v_mul_f32_e32 v2, v28, v76
	v_mul_f32_e32 v3, v29, v77
	v_cndmask_b32_e32 v4, v2, v3, vcc
	s_nop 1
	v_mov_b32_dpp v4, v4 quad_perm:[1,0,3,2] row_mask:0xf bank_mask:0xf bound_ctrl:1
	v_cndmask_b32_e32 v2, v4, v2, vcc
	v_cndmask_b32_e32 v3, v3, v4, vcc
	v_cvt_pk_bf16_f32 v2, v2, v3
	global_store_dword v[0:1], v2, off offset:192
	v_mul_f32_e32 v0, v62, v78
	v_mul_f32_e32 v1, v63, v79
	v_cndmask_b32_e32 v2, v0, v1, vcc
	v_mul_f32_e32 v3, v15, v79
	s_nop 0
	v_mov_b32_dpp v2, v2 quad_perm:[1,0,3,2] row_mask:0xf bank_mask:0xf bound_ctrl:1
	v_cndmask_b32_e32 v0, v2, v0, vcc
	v_cndmask_b32_e32 v1, v1, v2, vcc
	v_cvt_pk_bf16_f32 v2, v0, v1
	v_add_co_u32_e64 v0, s[6:7], s1, v64
	s_mov_b32 s1, s54
	s_nop 0
	v_addc_co_u32_e64 v1, s[6:7], 0, v65, s[6:7]
	global_store_dword v[0:1], v2, off
	v_mul_f32_e32 v2, v14, v78
	v_cndmask_b32_e32 v4, v2, v3, vcc
	s_mov_b64 s[6:7], s[64:65]
	s_nop 0
	v_mov_b32_dpp v4, v4 quad_perm:[1,0,3,2] row_mask:0xf bank_mask:0xf bound_ctrl:1
	v_cndmask_b32_e32 v2, v4, v2, vcc
	v_cndmask_b32_e32 v3, v3, v4, vcc
	v_cvt_pk_bf16_f32 v2, v2, v3
	global_store_dword v[0:1], v2, off offset:64
	v_mul_f32_e32 v2, v46, v78
	v_mul_f32_e32 v3, v47, v79
	v_cndmask_b32_e32 v4, v2, v3, vcc
	s_nop 1
	v_mov_b32_dpp v4, v4 quad_perm:[1,0,3,2] row_mask:0xf bank_mask:0xf bound_ctrl:1
	v_cndmask_b32_e32 v2, v4, v2, vcc
	v_cndmask_b32_e32 v3, v3, v4, vcc
	v_cvt_pk_bf16_f32 v2, v2, v3
	global_store_dword v[0:1], v2, off offset:128
	v_mul_f32_e32 v2, v30, v78
	v_mul_f32_e32 v3, v31, v79
	v_cndmask_b32_e32 v4, v2, v3, vcc
	s_nop 1
	v_mov_b32_dpp v4, v4 quad_perm:[1,0,3,2] row_mask:0xf bank_mask:0xf bound_ctrl:1
	v_cndmask_b32_e32 v2, v4, v2, vcc
	v_cndmask_b32_e32 v3, v3, v4, vcc
	s_andn2_b64 vcc, exec, s[66:67]
	v_cvt_pk_bf16_f32 v2, v2, v3
	global_store_dword v[0:1], v2, off offset:192
	s_barrier
	s_cbranch_vccz .LBB0_613

; __device__ __forceinline__ void qnorm_rope(const u32x2 (&q)[12], const QCoef& C, i32x8 (&qf)[3]) {
;     float sn = 0.f, sp = 0.f, v[8];
; #pragma unroll
;     for (int f = 0; f < 8; ++f) { unpk8(q[f], v);
; #pragma unroll
;         for (int e = 0; e < 8; ++e) sn += v[e] * v[e]; }
; #pragma unroll
;     for (int f = 8; f < 12; ++f) { unpk8(q[f], v);
; #pragma unroll
;         for (int e = 0; e < 8; ++e) sp += v[e] * v[e]; }
;     { auto rr = __builtin_amdgcn_permlane32_swap(__float_as_uint(sn), __float_as_uint(sn), false, false); sn = __uint_as_float(rr[0]) + __uint_as_float(rr[1]); }
.LBB0_582:
	s_waitcnt vmcnt(27)
	v_cvt_pk_f32_fp8_e32 v[174:175], v86
	v_cvt_pk_f32_fp8_sdwa v[168:169], v86 src0_sel:WORD_1
	v_lshlrev_b32_e32 v89, 2, v188
	v_cvt_pk_f32_fp8_e32 v[172:173], v87
	v_mul_f32_e32 v86, v175, v175
	v_and_b32_e32 v88, 32, v188
	v_and_b32_e32 v90, 48, v89
	v_lshlrev_b32_e32 v194, 6, v198
	v_cvt_pk_f32_fp8_sdwa v[166:167], v87 src0_sel:WORD_1
	v_pk_fma_f32 v[86:87], v[174:175], v[174:175], v[86:87] op_sel_hi:[1,1,0]
	v_bitop3_b32 v193, v89, v88, 48 bitop3:0x6c
	v_bitop3_b32 v192, v90, v194, v88 bitop3:0xde
	v_pk_fma_f32 v[86:87], v[168:169], v[168:169], v[86:87]
	v_mul_f32_e32 v88, v169, v169
	v_pk_add_f32 v[86:87], v[88:89], v[86:87] op_sel_hi:[0,1]
	v_pk_fma_f32 v[86:87], v[172:173], v[172:173], v[86:87]
	v_mul_f32_e32 v88, v173, v173
	s_waitcnt vmcnt(26)
	v_cvt_pk_f32_fp8_e32 v[170:171], v84
	v_pk_add_f32 v[86:87], v[88:89], v[86:87] op_sel_hi:[0,1]
	v_pk_fma_f32 v[86:87], v[166:167], v[166:167], v[86:87]
	v_mul_f32_e32 v88, v167, v167
	v_cvt_pk_f32_fp8_sdwa v[162:163], v84 src0_sel:WORD_1
	v_pk_add_f32 v[86:87], v[88:89], v[86:87] op_sel_hi:[0,1]
	v_cvt_pk_f32_fp8_e32 v[164:165], v85
	v_cvt_pk_f32_fp8_sdwa v[160:161], v85 src0_sel:WORD_1
	v_pk_fma_f32 v[84:85], v[170:171], v[170:171], v[86:87]
	v_mul_f32_e32 v86, v171, v171
	v_pk_add_f32 v[84:85], v[86:87], v[84:85] op_sel_hi:[0,1]
	v_pk_fma_f32 v[84:85], v[162:163], v[162:163], v[84:85]
	v_mul_f32_e32 v86, v163, v163
	v_pk_add_f32 v[84:85], v[86:87], v[84:85] op_sel_hi:[0,1]
	v_pk_fma_f32 v[84:85], v[164:165], v[164:165], v[84:85]
	v_mul_f32_e32 v86, v165, v165
	s_waitcnt vmcnt(25)
	v_cvt_pk_f32_fp8_e32 v[142:143], v82
	v_pk_add_f32 v[84:85], v[86:87], v[84:85] op_sel_hi:[0,1]
	v_pk_fma_f32 v[84:85], v[160:161], v[160:161], v[84:85]
	v_mul_f32_e32 v86, v161, v161
	v_cvt_pk_f32_fp8_sdwa v[138:139], v82 src0_sel:WORD_1
	v_pk_add_f32 v[84:85], v[86:87], v[84:85] op_sel_hi:[0,1]
	v_cvt_pk_f32_fp8_e32 v[140:141], v83
	v_cvt_pk_f32_fp8_sdwa v[136:137], v83 src0_sel:WORD_1
	v_pk_fma_f32 v[82:83], v[142:143], v[142:143], v[84:85]
	v_mul_f32_e32 v84, v143, v143
	v_pk_add_f32 v[82:83], v[84:85], v[82:83] op_sel_hi:[0,1]
	v_pk_fma_f32 v[82:83], v[138:139], v[138:139], v[82:83]
	v_mul_f32_e32 v84, v139, v139
	v_pk_add_f32 v[82:83], v[84:85], v[82:83] op_sel_hi:[0,1]
	v_pk_fma_f32 v[82:83], v[140:141], v[140:141], v[82:83]
	v_mul_f32_e32 v84, v141, v141
	s_waitcnt vmcnt(24)
	v_cvt_pk_f32_fp8_e32 v[134:135], v80
	v_pk_add_f32 v[82:83], v[84:85], v[82:83] op_sel_hi:[0,1]
	v_pk_fma_f32 v[82:83], v[136:137], v[136:137], v[82:83]
	v_mul_f32_e32 v84, v137, v137
	v_cvt_pk_f32_fp8_sdwa v[130:131], v80 src0_sel:WORD_1
	v_pk_add_f32 v[82:83], v[84:85], v[82:83] op_sel_hi:[0,1]
	v_cvt_pk_f32_fp8_e32 v[132:133], v81
	v_cvt_pk_f32_fp8_sdwa v[128:129], v81 src0_sel:WORD_1
	v_pk_fma_f32 v[80:81], v[134:135], v[134:135], v[82:83]
	v_mul_f32_e32 v82, v135, v135
	v_pk_add_f32 v[80:81], v[82:83], v[80:81] op_sel_hi:[0,1]
	v_pk_fma_f32 v[80:81], v[130:131], v[130:131], v[80:81]
	v_mul_f32_e32 v82, v131, v131
	v_pk_add_f32 v[80:81], v[82:83], v[80:81] op_sel_hi:[0,1]
	v_pk_fma_f32 v[80:81], v[132:133], v[132:133], v[80:81]
	v_mul_f32_e32 v82, v133, v133
	s_waitcnt vmcnt(23)
	v_cvt_pk_f32_fp8_e32 v[126:127], v78
	v_pk_add_f32 v[80:81], v[82:83], v[80:81] op_sel_hi:[0,1]
	v_pk_fma_f32 v[80:81], v[128:129], v[128:129], v[80:81]
	v_mul_f32_e32 v82, v129, v129
	v_cvt_pk_f32_fp8_sdwa v[122:123], v78 src0_sel:WORD_1
	v_pk_add_f32 v[80:81], v[82:83], v[80:81] op_sel_hi:[0,1]
	v_cvt_pk_f32_fp8_e32 v[124:125], v79
	v_cvt_pk_f32_fp8_sdwa v[120:121], v79 src0_sel:WORD_1
	v_pk_fma_f32 v[78:79], v[126:127], v[126:127], v[80:81]
	v_mul_f32_e32 v80, v127, v127
	v_pk_add_f32 v[78:79], v[80:81], v[78:79] op_sel_hi:[0,1]
	v_pk_fma_f32 v[78:79], v[122:123], v[122:123], v[78:79]
	v_mul_f32_e32 v80, v123, v123
	v_pk_add_f32 v[78:79], v[80:81], v[78:79] op_sel_hi:[0,1]
	v_pk_fma_f32 v[78:79], v[124:125], v[124:125], v[78:79]
	v_mul_f32_e32 v80, v125, v125
	s_waitcnt vmcnt(22)
	v_cvt_pk_f32_fp8_e32 v[118:119], v76
	v_pk_add_f32 v[78:79], v[80:81], v[78:79] op_sel_hi:[0,1]
	v_pk_fma_f32 v[78:79], v[120:121], v[120:121], v[78:79]
	v_mul_f32_e32 v80, v121, v121
	v_cvt_pk_f32_fp8_sdwa v[114:115], v76 src0_sel:WORD_1
	v_pk_add_f32 v[78:79], v[80:81], v[78:79] op_sel_hi:[0,1]
	v_cvt_pk_f32_fp8_e32 v[116:117], v77
	v_cvt_pk_f32_fp8_sdwa v[112:113], v77 src0_sel:WORD_1
	v_pk_fma_f32 v[76:77], v[118:119], v[118:119], v[78:79]
	v_mul_f32_e32 v78, v119, v119
	v_pk_add_f32 v[76:77], v[78:79], v[76:77] op_sel_hi:[0,1]
	v_pk_fma_f32 v[76:77], v[114:115], v[114:115], v[76:77]
	v_mul_f32_e32 v78, v115, v115
	v_pk_add_f32 v[76:77], v[78:79], v[76:77] op_sel_hi:[0,1]
	v_pk_fma_f32 v[76:77], v[116:117], v[116:117], v[76:77]
	v_mul_f32_e32 v78, v117, v117
	s_waitcnt vmcnt(21)
	v_cvt_pk_f32_fp8_e32 v[110:111], v74
	v_pk_add_f32 v[76:77], v[78:79], v[76:77] op_sel_hi:[0,1]
	v_pk_fma_f32 v[76:77], v[112:113], v[112:113], v[76:77]
	v_mul_f32_e32 v78, v113, v113
	v_cvt_pk_f32_fp8_sdwa v[106:107], v74 src0_sel:WORD_1
	s_waitcnt vmcnt(19)
; __device__ __forceinline__ unsigned cvt_pk4_fp8(float a, float b, float c, float d) { int w; asm("" : "=v"(w));     w = __builtin_amdgcn_cvt_pk_fp8_f32(a, b, w, false); w = __builtin_amdgcn_cvt_pk_fp8_f32(c, d, w, true); return (unsigned)w; }
; __device__ __forceinline__ void qnorm_rope(const u32x2 (&q)[12], const QCoef& C, i32x8 (&qf)[3]) {
;     ...
;     for (int f = 0; f < 8; ++f) { unpk8(q[f], v);
; #pragma unroll
;         for (int e = 0; e < 8; ++e) sn += v[e] * v[e]; }
; #pragma unroll
;     for (int f = 8; f < 12; ++f) { unpk8(q[f], v);
; #pragma unroll
;         for (int e = 0; e < 8; ++e) sp += v[e] * v[e]; }
;     { auto rr = __builtin_amdgcn_permlane32_swap(__float_as_uint(sn), __float_as_uint(sn), false, false); sn = __uint_as_float(rr[0]) + __uint_as_float(rr[1]); }
;     { auto rr = __builtin_amdgcn_permlane32_swap(__float_as_uint(sp), __float_as_uint(sp), false, false); sp = __uint_as_float(rr[0]) + __uint_as_float(rr[1]); }
;     const float rn = rsqrtf(sn * (1.f / 128.f) + RMS_EPS), rp = rsqrtf(sp * (1.f / 64.f) + RMS_EPS);
; #pragma unroll
;     for (int f = 0; f < 8; ++f) { unpk8(q[f], v);
; #pragma unroll
;         for (int e = 0; e < 8; ++e) v[e] *= rn * QSC;
;         qf[f >> 2][2 * (f & 3)] = (int)cvt_pk4_fp8(v[0], v[1], v[2], v[3]); qf[f >> 2][2 * (f & 3) + 1] = (int)cvt_pk4_fp8(v[4], v[5], v[6], v[7]); }
	v_cvt_pk_f32_fp8_e32 v[90:91], v66
	v_pk_add_f32 v[76:77], v[78:79], v[76:77] op_sel_hi:[0,1]
	v_cvt_pk_f32_fp8_e32 v[108:109], v75
	v_cvt_pk_f32_fp8_sdwa v[104:105], v75 src0_sel:WORD_1
	v_pk_fma_f32 v[74:75], v[110:111], v[110:111], v[76:77]
	v_mul_f32_e32 v76, v111, v111
	v_cvt_pk_f32_fp8_sdwa v[86:87], v66 src0_sel:WORD_1
	v_pk_add_f32 v[74:75], v[76:77], v[74:75] op_sel_hi:[0,1]
	v_pk_fma_f32 v[74:75], v[106:107], v[106:107], v[74:75]
	v_mul_f32_e32 v76, v107, v107
	v_cvt_pk_f32_fp8_e32 v[82:83], v67
	v_mul_f32_e32 v66, v91, v91
	v_pk_add_f32 v[74:75], v[76:77], v[74:75] op_sel_hi:[0,1]
	v_cvt_pk_f32_fp8_sdwa v[80:81], v67 src0_sel:WORD_1
	v_pk_fma_f32 v[66:67], v[90:91], v[90:91], v[66:67] op_sel_hi:[1,1,0]
	v_pk_fma_f32 v[74:75], v[108:109], v[108:109], v[74:75]
	v_mul_f32_e32 v76, v109, v109
	v_cvt_pk_f32_fp8_e32 v[102:103], v70
	v_cvt_pk_f32_fp8_sdwa v[98:99], v70 src0_sel:WORD_1
	v_pk_fma_f32 v[66:67], v[86:87], v[86:87], v[66:67]
	v_mul_f32_e32 v70, v87, v87
	v_pk_add_f32 v[74:75], v[76:77], v[74:75] op_sel_hi:[0,1]
	v_pk_add_f32 v[66:67], v[70:71], v[66:67] op_sel_hi:[0,1]
	v_pk_fma_f32 v[74:75], v[104:105], v[104:105], v[74:75]
	v_mul_f32_e32 v76, v105, v105
	v_pk_fma_f32 v[66:67], v[82:83], v[82:83], v[66:67]
	v_mul_f32_e32 v70, v83, v83
	v_pk_add_f32 v[176:177], v[76:77], v[74:75] op_sel_hi:[0,1]
	v_pk_add_f32 v[66:67], v[70:71], v[66:67] op_sel_hi:[0,1]
	s_waitcnt vmcnt(18)
	v_cvt_pk_f32_fp8_e32 v[74:75], v64
	v_pk_fma_f32 v[66:67], v[80:81], v[80:81], v[66:67]
	v_mul_f32_e32 v70, v81, v81
	v_cvt_pk_f32_fp8_e32 v[100:101], v71
	v_cvt_pk_f32_fp8_sdwa v[96:97], v71 src0_sel:WORD_1
	v_pk_add_f32 v[76:77], v[70:71], v[66:67] op_sel_hi:[0,1]
	v_cvt_pk_f32_fp8_sdwa v[70:71], v64 src0_sel:WORD_1
	v_cvt_pk_f32_fp8_e32 v[66:67], v65
	v_pk_fma_f32 v[76:77], v[74:75], v[74:75], v[76:77]
	v_mul_f32_e32 v78, v75, v75
	v_pk_add_f32 v[76:77], v[78:79], v[76:77] op_sel_hi:[0,1]
	v_cvt_pk_f32_fp8_sdwa v[64:65], v65 src0_sel:WORD_1
	v_pk_fma_f32 v[76:77], v[70:71], v[70:71], v[76:77]
	v_mul_f32_e32 v78, v71, v71
	v_pk_add_f32 v[76:77], v[78:79], v[76:77] op_sel_hi:[0,1]
	v_pk_fma_f32 v[76:77], v[66:67], v[66:67], v[76:77]
	v_mul_f32_e32 v78, v67, v67
	s_waitcnt vmcnt(17)
	v_cvt_pk_f32_fp8_e32 v[94:95], v72
	v_pk_add_f32 v[76:77], v[78:79], v[76:77] op_sel_hi:[0,1]
	v_pk_fma_f32 v[76:77], v[64:65], v[64:65], v[76:77]
	v_mul_f32_e32 v78, v65, v65
	v_cvt_pk_f32_fp8_sdwa v[92:93], v72 src0_sel:WORD_1
	v_pk_add_f32 v[76:77], v[78:79], v[76:77] op_sel_hi:[0,1]
	v_cvt_pk_f32_fp8_e32 v[88:89], v73
	v_cvt_pk_f32_fp8_sdwa v[84:85], v73 src0_sel:WORD_1
	v_pk_fma_f32 v[72:73], v[94:95], v[94:95], v[76:77]
	v_mul_f32_e32 v76, v95, v95
	v_pk_add_f32 v[72:73], v[76:77], v[72:73] op_sel_hi:[0,1]
	v_pk_fma_f32 v[72:73], v[92:93], v[92:93], v[72:73]
	v_mul_f32_e32 v76, v93, v93
	v_pk_add_f32 v[72:73], v[76:77], v[72:73] op_sel_hi:[0,1]
	v_pk_fma_f32 v[72:73], v[88:89], v[88:89], v[72:73]
	v_mul_f32_e32 v76, v89, v89
	v_pk_add_f32 v[72:73], v[76:77], v[72:73] op_sel_hi:[0,1]
	s_waitcnt vmcnt(16)
	v_cvt_pk_f32_fp8_e32 v[78:79], v68
	v_pk_fma_f32 v[72:73], v[84:85], v[84:85], v[72:73]
	v_mul_f32_e32 v76, v85, v85
	v_pk_add_f32 v[178:179], v[76:77], v[72:73] op_sel_hi:[0,1]
	v_cvt_pk_f32_fp8_sdwa v[76:77], v68 src0_sel:WORD_1
	v_cvt_pk_f32_fp8_e32 v[72:73], v69
	v_pk_fma_f32 v[178:179], v[78:79], v[78:79], v[178:179]
	v_mul_f32_e32 v180, v79, v79
	v_pk_add_f32 v[178:179], v[180:181], v[178:179] op_sel_hi:[0,1]
	v_cvt_pk_f32_fp8_sdwa v[68:69], v69 src0_sel:WORD_1
	v_pk_fma_f32 v[178:179], v[76:77], v[76:77], v[178:179]
	v_mul_f32_e32 v180, v77, v77
	v_pk_add_f32 v[178:179], v[180:181], v[178:179] op_sel_hi:[0,1]
	v_pk_fma_f32 v[178:179], v[72:73], v[72:73], v[178:179]
	v_mul_f32_e32 v180, v73, v73
	v_pk_add_f32 v[178:179], v[180:181], v[178:179] op_sel_hi:[0,1]
	v_pk_fma_f32 v[178:179], v[68:69], v[68:69], v[178:179]
	v_mul_f32_e32 v180, v69, v69
	v_pk_add_f32 v[178:179], v[180:181], v[178:179] op_sel_hi:[0,1]
	v_pk_fma_f32 v[176:177], v[102:103], v[102:103], v[176:177]
	v_mul_f32_e32 v180, v103, v103
	v_pk_add_f32 v[176:177], v[180:181], v[176:177] op_sel_hi:[0,1]
	v_pk_fma_f32 v[176:177], v[98:99], v[98:99], v[176:177]
	v_mul_f32_e32 v180, v99, v99
	v_pk_add_f32 v[176:177], v[180:181], v[176:177] op_sel_hi:[0,1]
	v_pk_fma_f32 v[176:177], v[100:101], v[100:101], v[176:177]
	v_mul_f32_e32 v180, v101, v101
	v_pk_add_f32 v[176:177], v[180:181], v[176:177] op_sel_hi:[0,1]
	v_pk_fma_f32 v[176:177], v[96:97], v[96:97], v[176:177]
	v_mul_f32_e32 v180, v97, v97
	v_pk_add_f32 v[176:177], v[180:181], v[176:177] op_sel_hi:[0,1]
	v_mov_b32_e32 v181, v176
	s_nop 1
	v_permlane32_swap_b32_e32 v176, v181
	v_mov_b32_e32 v180, v178
	s_nop 1
	v_permlane32_swap_b32_e32 v178, v180
	v_mov_b32_e32 v179, v176
	s_mov_b32 s6, 0x3c800000
	v_pk_add_f32 v[176:177], v[178:179], v[180:181]
	s_brev_b32 s7, 60
	v_pk_fma_f32 v[176:177], v[176:177], s[6:7], v[186:187] op_sel_hi:[1,1,0]
	s_nop 0
	v_mul_f32_e32 v178, 0x4b800000, v177
	v_cmp_gt_f32_e64 s[6:7], s30, v177
	v_cmp_gt_f32_e32 vcc, s30, v176
	s_nop 0
	v_cndmask_b32_e64 v177, v177, v178, s[6:7]
	v_rsq_f32_e32 v177, v177
	s_nop 0
	v_mul_f32_e32 v178, 0x45800000, v177
	v_cndmask_b32_e64 v177, v177, v178, s[6:7]
	v_mul_f32_e32 v178, 0x4b800000, v176
	v_cndmask_b32_e32 v176, v176, v178, vcc
	v_mul_f32_e32 v182, 0x3e800000, v177
	v_rsq_f32_e32 v196, v176
	v_mul_f32_e32 v174, v174, v182
	v_mul_f32_e32 v175, v175, v182
	v_mul_f32_e32 v176, v168, v182
	v_mul_f32_e32 v177, v167, v182
	v_mul_f32_e32 v169, v169, v182
	v_cvt_pk_fp8_f32 v168, v174, v175
	v_mul_f32_e32 v172, v172, v182
	v_mul_f32_e32 v173, v173, v182
	v_mul_f32_e32 v166, v166, v182
; __device__ __forceinline__ unsigned cvt_pk4_fp8(float a, float b, float c, float d) { int w; asm("" : "=v"(w));     w = __builtin_amdgcn_cvt_pk_fp8_f32(a, b, w, false); w = __builtin_amdgcn_cvt_pk_fp8_f32(c, d, w, true); return (unsigned)w; }
; __device__ __forceinline__ void qnorm_rope(const u32x2 (&q)[12], const QCoef& C, i32x8 (&qf)[3]) {
;     ...
;     const float rn = rsqrtf(sn * (1.f / 128.f) + RMS_EPS), rp = rsqrtf(sp * (1.f / 64.f) + RMS_EPS);
; #pragma unroll
;     for (int f = 0; f < 8; ++f) { unpk8(q[f], v);
; #pragma unroll
;         for (int e = 0; e < 8; ++e) v[e] *= rn * QSC;
;         qf[f >> 2][2 * (f & 3)] = (int)cvt_pk4_fp8(v[0], v[1], v[2], v[3]); qf[f >> 2][2 * (f & 3) + 1] = (int)cvt_pk4_fp8(v[4], v[5], v[6], v[7]); }
; #pragma unroll
;     for (int f = 0; f < 2; ++f) {
;         float t1[8], t2[8], o1[8], o2[8]; unpk8(q[8 + f], t1); unpk8(q[10 + f], t2);
; #pragma unroll
;         for (int e = 0; e < 8; ++e) { const int j = 2 * f + (e >> 2), k = e & 3; const float a = t1[e] * (rp * QSC) * C.ga[j][k], b = t2[e] * (rp * QSC) * C.gb[j][k]; o1[e] = a * C.c[j][k] - b * C.s[j][k]; o2[e] = b * C.c[j][k] + a * C.s[j][k]; }
;         qf[2][2 * f] = (int)cvt_pk4_fp8(o1[0], o1[1], o1[2], o1[3]); qf[2][2 * f + 1] = (int)cvt_pk4_fp8(o1[4], o1[5], o1[6], o1[7]);
;         qf[2][4 + 2 * f] = (int)cvt_pk4_fp8(o2[0], o2[1], o2[2], o2[3]); qf[2][5 + 2 * f] = (int)cvt_pk4_fp8(o2[4], o2[5], o2[6], o2[7]); }
	v_cvt_pk_fp8_f32 v168, v176, v169 op_sel:[0,0,1]
	v_cvt_pk_fp8_f32 v169, v172, v173
	v_mul_f32_e32 v100, v100, v182
	v_mul_f32_e32 v101, v101, v182
	v_cvt_pk_fp8_f32 v169, v166, v177 op_sel:[0,0,1]
	v_mul_f32_e32 v166, v170, v182
	v_mul_f32_e32 v171, v171, v182
	v_mul_f32_e32 v162, v162, v182
	v_mul_f32_e32 v163, v163, v182
	v_mul_f32_e32 v164, v164, v182
	v_mul_f32_e32 v165, v165, v182
	v_mul_f32_e32 v160, v160, v182
	v_mul_f32_e32 v161, v161, v182
	v_mul_f32_e32 v142, v142, v182
	v_mul_f32_e32 v143, v143, v182
	v_mul_f32_e32 v138, v138, v182
	v_mul_f32_e32 v139, v139, v182
	v_mul_f32_e32 v140, v140, v182
	v_mul_f32_e32 v141, v141, v182
	v_mul_f32_e32 v136, v136, v182
	v_mul_f32_e32 v137, v137, v182
	v_mul_f32_e32 v134, v134, v182
	v_mul_f32_e32 v135, v135, v182
	v_mul_f32_e32 v130, v130, v182
	v_mul_f32_e32 v131, v131, v182
	v_mul_f32_e32 v132, v132, v182
	v_mul_f32_e32 v133, v133, v182
	v_mul_f32_e32 v128, v128, v182
	v_mul_f32_e32 v129, v129, v182
	v_mul_f32_e32 v126, v126, v182
	v_mul_f32_e32 v127, v127, v182
	v_mul_f32_e32 v122, v122, v182
	v_mul_f32_e32 v123, v123, v182
	v_mul_f32_e32 v124, v124, v182
	v_mul_f32_e32 v125, v125, v182
	v_mul_f32_e32 v120, v120, v182
	v_mul_f32_e32 v121, v121, v182
	v_mul_f32_e32 v118, v118, v182
	v_mul_f32_e32 v119, v119, v182
	v_mul_f32_e32 v114, v114, v182
	v_mul_f32_e32 v115, v115, v182
	v_mul_f32_e32 v116, v116, v182
	v_mul_f32_e32 v117, v117, v182
	v_mul_f32_e32 v112, v112, v182
	v_mul_f32_e32 v113, v113, v182
	v_mul_f32_e32 v110, v110, v182
	v_mul_f32_e32 v111, v111, v182
	v_mul_f32_e32 v106, v106, v182
	v_mul_f32_e32 v107, v107, v182
	v_mul_f32_e32 v108, v108, v182
	v_mul_f32_e32 v109, v109, v182
	v_mul_f32_e32 v104, v104, v182
	v_mul_f32_e32 v105, v105, v182
	v_mul_f32_e32 v102, v102, v182
	v_mul_f32_e32 v103, v103, v182
	v_mul_f32_e32 v98, v98, v182
	v_mul_f32_e32 v99, v99, v182
	v_mul_f32_e32 v96, v96, v182
	v_mul_f32_e32 v97, v97, v182
	v_cvt_pk_fp8_f32 v183, v100, v101
	v_cvt_pk_fp8_f32 v182, v102, v103
	v_mul_f32_e32 v197, 0x45800000, v196
	s_waitcnt vmcnt(8)
	v_mov_b32_e32 v100, v60
	v_cvt_pk_fp8_f32 v183, v96, v97 op_sel:[0,0,1]
	v_cndmask_b32_e32 v96, v196, v197, vcc
	v_cvt_pk_fp8_f32 v182, v98, v99 op_sel:[0,0,1]
	v_mul_f32_e32 v96, 0x3e800000, v96
	v_mov_b32_e32 v98, v94
	v_mov_b32_e32 v99, v90
	v_pk_mul_f32 v[98:99], v[98:99], v[96:97] op_sel_hi:[1,0]
	v_mov_b32_e32 v101, v56
	v_pk_mul_f32 v[98:99], v[100:101], v[98:99]
	v_mov_b32_e32 v100, v52
	v_mov_b32_e32 v101, v48
	v_pk_mul_f32 v[100:101], v[100:101], v[98:99]
	v_mov_b32_e32 v90, v95
	v_sub_f32_e32 v94, v101, v100
	v_mov_b32_e32 v100, v48
	v_mov_b32_e32 v101, v52
	v_pk_mul_f32 v[98:99], v[100:101], v[98:99]
	v_mov_b32_e32 v56, v61
	v_add_f32_e32 v97, v98, v99
	v_pk_mul_f32 v[90:91], v[90:91], v[96:97] op_sel_hi:[1,0]
	v_mov_b32_e32 v48, v53
	v_pk_mul_f32 v[56:57], v[56:57], v[90:91]
	v_mov_b32_e32 v52, v49
	v_pk_mul_f32 v[60:61], v[48:49], v[56:57]
	v_pk_mul_f32 v[48:49], v[52:53], v[56:57]
	v_mov_b32_e32 v52, v62
	v_add_f32_e32 v56, v48, v49
	v_mov_b32_e32 v48, v92
	v_mov_b32_e32 v49, v86
	v_pk_mul_f32 v[48:49], v[48:49], v[96:97] op_sel_hi:[1,0]
	v_mov_b32_e32 v53, v58
	v_pk_mul_f32 v[48:49], v[52:53], v[48:49]
	v_mov_b32_e32 v52, v54
	v_mov_b32_e32 v53, v50
	v_pk_mul_f32 v[52:53], v[52:53], v[48:49]
	v_mov_b32_e32 v86, v93
	v_sub_f32_e32 v57, v53, v52
	v_mov_b32_e32 v52, v50
	v_mov_b32_e32 v53, v54
	v_pk_mul_f32 v[48:49], v[52:53], v[48:49]
	v_sub_f32_e32 v60, v61, v60
	v_add_f32_e32 v61, v48, v49
	v_pk_mul_f32 v[48:49], v[86:87], v[96:97] op_sel_hi:[1,0]
	v_mov_b32_e32 v58, v63
	v_pk_mul_f32 v[48:49], v[58:59], v[48:49]
	v_mov_b32_e32 v50, v55
	v_mov_b32_e32 v54, v51
	v_pk_mul_f32 v[52:53], v[50:51], v[48:49]
	v_pk_mul_f32 v[48:49], v[54:55], v[48:49]
	v_sub_f32_e32 v52, v53, v52
	v_add_f32_e32 v53, v48, v49
	v_mov_b32_e32 v48, v88
	v_mov_b32_e32 v49, v82
	v_pk_mul_f32 v[48:49], v[48:49], v[96:97] op_sel_hi:[1,0]
	v_mov_b32_e32 v50, v44
	v_mov_b32_e32 v51, v40
	v_pk_mul_f32 v[48:49], v[50:51], v[48:49]
	v_mov_b32_e32 v50, v36
	v_mov_b32_e32 v51, v32
	v_pk_mul_f32 v[50:51], v[50:51], v[48:49]
	v_mov_b32_e32 v82, v89
	v_sub_f32_e32 v54, v51, v50
	v_mov_b32_e32 v50, v32
	v_mov_b32_e32 v51, v36
	v_pk_mul_f32 v[48:49], v[50:51], v[48:49]
	v_mov_b32_e32 v40, v45
	v_add_f32_e32 v50, v48, v49
	v_pk_mul_f32 v[48:49], v[82:83], v[96:97] op_sel_hi:[1,0]
	v_mov_b32_e32 v32, v37
	v_pk_mul_f32 v[40:41], v[40:41], v[48:49]
	v_mov_b32_e32 v36, v33
	v_pk_mul_f32 v[44:45], v[32:33], v[40:41]
	v_pk_mul_f32 v[32:33], v[36:37], v[40:41]
	v_add_f32_e32 v40, v32, v33
	v_mov_b32_e32 v32, v84
	v_mov_b32_e32 v33, v80
	v_cvt_pk_fp8_f32 v170, v166, v171
	v_pk_mul_f32 v[32:33], v[32:33], v[96:97] op_sel_hi:[1,0]
	v_mov_b32_e32 v36, v46
	v_mov_b32_e32 v37, v42
	v_cvt_pk_fp8_f32 v171, v164, v165
	v_pk_mul_f32 v[32:33], v[36:37], v[32:33]
	v_mov_b32_e32 v36, v38
	v_mov_b32_e32 v37, v34
	v_pk_mul_f32 v[36:37], v[36:37], v[32:33]
	v_mov_b32_e32 v80, v85
	v_sub_f32_e32 v41, v37, v36
	v_mov_b32_e32 v36, v34
	v_mov_b32_e32 v37, v38
	v_pk_mul_f32 v[32:33], v[36:37], v[32:33]
	v_cvt_pk_fp8_f32 v171, v160, v161 op_sel:[0,0,1]
	v_sub_f32_e32 v44, v45, v44
	v_add_f32_e32 v45, v32, v33
	v_pk_mul_f32 v[32:33], v[80:81], v[96:97] op_sel_hi:[1,0]
	v_mov_b32_e32 v42, v47
	v_cvt_pk_fp8_f32 v165, v50, v40
	v_pk_mul_f32 v[32:33], v[42:43], v[32:33]
	v_mov_b32_e32 v34, v39
	v_mov_b32_e32 v38, v35
	v_cvt_pk_fp8_f32 v161, v54, v44
	v_pk_mul_f32 v[36:37], v[34:35], v[32:33]
	v_pk_mul_f32 v[32:33], v[38:39], v[32:33]
	v_sub_f32_e32 v34, v37, v36
	v_add_f32_e32 v32, v32, v33
	v_cvt_pk_fp8_f32 v165, v45, v32 op_sel:[0,0,1]
	v_mov_b32_e32 v32, v78
	v_mov_b32_e32 v33, v74
	v_cvt_pk_fp8_f32 v161, v41, v34 op_sel:[0,0,1]
	v_pk_mul_f32 v[32:33], v[32:33], v[96:97] op_sel_hi:[1,0]
	s_waitcnt vmcnt(0)
; __device__ __forceinline__ unsigned cvt_pk4_fp8(float a, float b, float c, float d) { int w; asm("" : "=v"(w));     w = __builtin_amdgcn_cvt_pk_fp8_f32(a, b, w, false); w = __builtin_amdgcn_cvt_pk_fp8_f32(c, d, w, true); return (unsigned)w; }
; __device__ __forceinline__ void qkt(f32x16& p0, f32x16& p1, const char* stg, int ka, const i32x8* qf, const f32x16& minit) {
;     p0 = minit; p1 = minit;
; #pragma unroll
;     for (int s = 0; s < 3; ++s) { const char* a = stg + SOFF_K + s * 4096 + ka; const char* b = stg + SOFF_K + s * 4096 + (ka ^ 16);
;         const i32x4 a0 = *reinterpret_cast<const i32x4*>(a), a1 = *reinterpret_cast<const i32x4*>(b);
;         const i32x4 c0 = *reinterpret_cast<const i32x4*>(a + 2048), c1 = *reinterpret_cast<const i32x4*>(b + 2048);
;         p0 = __builtin_amdgcn_mfma_scale_f32_32x32x64_f8f6f4(__builtin_shufflevector(a0, a1, 0, 1, 2, 3, 4, 5, 6, 7), qf[s], p0, 0, 0, 0, 0, 0, 0);
;         p1 = __builtin_amdgcn_mfma_scale_f32_32x32x64_f8f6f4(__builtin_shufflevector(c0, c1, 0, 1, 2, 3, 4, 5, 6, 7), qf[s], p1, 0, 0, 0, 0, 0, 0); }
; }
; __device__ __forceinline__ void qnorm_rope(const u32x2 (&q)[12], const QCoef& C, i32x8 (&qf)[3]) {
;     ...
;     for (int f = 0; f < 2; ++f) {
;         float t1[8], t2[8], o1[8], o2[8]; unpk8(q[8 + f], t1); unpk8(q[10 + f], t2);
; #pragma unroll
;         for (int e = 0; e < 8; ++e) { const int j = 2 * f + (e >> 2), k = e & 3; const float a = t1[e] * (rp * QSC) * C.ga[j][k], b = t2[e] * (rp * QSC) * C.gb[j][k]; o1[e] = a * C.c[j][k] - b * C.s[j][k]; o2[e] = b * C.c[j][k] + a * C.s[j][k]; }
;         qf[2][2 * f] = (int)cvt_pk4_fp8(o1[0], o1[1], o1[2], o1[3]); qf[2][2 * f + 1] = (int)cvt_pk4_fp8(o1[4], o1[5], o1[6], o1[7]);
;         qf[2][4 + 2 * f] = (int)cvt_pk4_fp8(o2[0], o2[1], o2[2], o2[3]); qf[2][5 + 2 * f] = (int)cvt_pk4_fp8(o2[4], o2[5], o2[6], o2[7]); }
	v_mov_b32_e32 v34, v28
	v_mov_b32_e32 v35, v24
	v_pk_mul_f32 v[32:33], v[34:35], v[32:33]
	v_mov_b32_e32 v34, v20
	v_mov_b32_e32 v35, v16
	v_pk_mul_f32 v[34:35], v[34:35], v[32:33]
	v_mov_b32_e32 v74, v79
	v_sub_f32_e32 v36, v35, v34
	v_mov_b32_e32 v34, v16
	v_mov_b32_e32 v35, v20
	v_pk_mul_f32 v[32:33], v[34:35], v[32:33]
	v_mov_b32_e32 v24, v29
	v_add_f32_e32 v34, v32, v33
	v_pk_mul_f32 v[32:33], v[74:75], v[96:97] op_sel_hi:[1,0]
	v_mov_b32_e32 v16, v21
	v_pk_mul_f32 v[24:25], v[24:25], v[32:33]
	v_mov_b32_e32 v20, v17
	v_pk_mul_f32 v[28:29], v[16:17], v[24:25]
	v_pk_mul_f32 v[16:17], v[20:21], v[24:25]
	v_mov_b32_e32 v20, v30
	v_add_f32_e32 v24, v16, v17
	v_mov_b32_e32 v16, v76
	v_mov_b32_e32 v17, v70
	v_pk_mul_f32 v[16:17], v[16:17], v[96:97] op_sel_hi:[1,0]
	v_mov_b32_e32 v21, v26
	v_pk_mul_f32 v[16:17], v[20:21], v[16:17]
	v_mov_b32_e32 v20, v22
	v_mov_b32_e32 v21, v18
	v_pk_mul_f32 v[20:21], v[20:21], v[16:17]
	v_mov_b32_e32 v70, v77
	v_sub_f32_e32 v25, v21, v20
	v_mov_b32_e32 v20, v18
	v_mov_b32_e32 v21, v22
	v_pk_mul_f32 v[16:17], v[20:21], v[16:17]
	v_sub_f32_e32 v28, v29, v28
	v_add_f32_e32 v29, v16, v17
	v_pk_mul_f32 v[16:17], v[70:71], v[96:97] op_sel_hi:[1,0]
	v_mov_b32_e32 v26, v31
	v_pk_mul_f32 v[16:17], v[26:27], v[16:17]
	v_mov_b32_e32 v18, v23
	v_mov_b32_e32 v22, v19
	v_pk_mul_f32 v[20:21], v[18:19], v[16:17]
	v_pk_mul_f32 v[16:17], v[22:23], v[16:17]
	v_sub_f32_e32 v20, v21, v20
	v_add_f32_e32 v21, v16, v17
	v_mov_b32_e32 v16, v72
	v_mov_b32_e32 v17, v66
	v_pk_mul_f32 v[16:17], v[16:17], v[96:97] op_sel_hi:[1,0]
	v_mov_b32_e32 v18, v12
	v_mov_b32_e32 v19, v8
	v_pk_mul_f32 v[16:17], v[18:19], v[16:17]
	v_mov_b32_e32 v18, v4
	v_mov_b32_e32 v19, v0
	v_pk_mul_f32 v[18:19], v[18:19], v[16:17]
	v_mov_b32_e32 v66, v73
	v_sub_f32_e32 v22, v19, v18
	v_mov_b32_e32 v18, v0
	v_mov_b32_e32 v19, v4
	v_pk_mul_f32 v[16:17], v[18:19], v[16:17]
	v_mov_b32_e32 v8, v13
	v_add_f32_e32 v18, v16, v17
	v_pk_mul_f32 v[16:17], v[66:67], v[96:97] op_sel_hi:[1,0]
	v_mov_b32_e32 v0, v5
	v_pk_mul_f32 v[8:9], v[8:9], v[16:17]
	v_mov_b32_e32 v4, v1
	v_pk_mul_f32 v[12:13], v[0:1], v[8:9]
	v_pk_mul_f32 v[0:1], v[4:5], v[8:9]
	v_mov_b32_e32 v4, v14
	v_add_f32_e32 v8, v0, v1
	v_mov_b32_e32 v0, v68
	v_mov_b32_e32 v1, v64
	v_pk_mul_f32 v[0:1], v[0:1], v[96:97] op_sel_hi:[1,0]
	v_mov_b32_e32 v5, v10
	v_pk_mul_f32 v[0:1], v[4:5], v[0:1]
	v_mov_b32_e32 v4, v6
	v_mov_b32_e32 v5, v2
	v_pk_mul_f32 v[4:5], v[4:5], v[0:1]
	v_cvt_pk_fp8_f32 v170, v162, v163 op_sel:[0,0,1]
	v_sub_f32_e32 v9, v5, v4
	v_mov_b32_e32 v4, v2
	v_mov_b32_e32 v5, v6
	v_sub_f32_e32 v12, v13, v12
	v_pk_mul_f32 v[0:1], v[4:5], v[0:1]
	v_mov_b32_e32 v64, v69
	v_cvt_pk_fp8_f32 v172, v142, v143
	v_cvt_pk_fp8_f32 v173, v140, v141
	v_cvt_pk_fp8_f32 v174, v134, v135
	v_cvt_pk_fp8_f32 v175, v132, v133
	v_cvt_pk_fp8_f32 v176, v126, v127
	v_cvt_pk_fp8_f32 v177, v124, v125
	v_cvt_pk_fp8_f32 v178, v118, v119
	v_cvt_pk_fp8_f32 v179, v116, v117
	v_cvt_pk_fp8_f32 v180, v110, v111
	v_cvt_pk_fp8_f32 v181, v108, v109
	v_cvt_pk_fp8_f32 v160, v94, v60
	v_cvt_pk_fp8_f32 v164, v97, v56
	v_add_f32_e32 v13, v0, v1
	v_pk_mul_f32 v[0:1], v[64:65], v[96:97] op_sel_hi:[1,0]
	v_mov_b32_e32 v10, v15
	v_cvt_pk_fp8_f32 v162, v36, v28
	v_cvt_pk_fp8_f32 v163, v22, v12
	v_cvt_pk_fp8_f32 v166, v34, v24
	v_cvt_pk_fp8_f32 v167, v18, v8
	v_pk_mul_f32 v[0:1], v[10:11], v[0:1]
	v_mov_b32_e32 v2, v7
	v_mov_b32_e32 v6, v3
	v_pk_mul_f32 v[4:5], v[2:3], v[0:1]
	v_pk_mul_f32 v[0:1], v[6:7], v[0:1]
	v_sub_f32_e32 v2, v5, v4
	v_add_f32_e32 v0, v0, v1
	v_cvt_pk_fp8_f32 v172, v138, v139 op_sel:[0,0,1]
	v_cvt_pk_fp8_f32 v173, v136, v137 op_sel:[0,0,1]
	v_cvt_pk_fp8_f32 v174, v130, v131 op_sel:[0,0,1]
	v_cvt_pk_fp8_f32 v175, v128, v129 op_sel:[0,0,1]
	v_cvt_pk_fp8_f32 v176, v122, v123 op_sel:[0,0,1]
	v_cvt_pk_fp8_f32 v177, v120, v121 op_sel:[0,0,1]
	v_cvt_pk_fp8_f32 v178, v114, v115 op_sel:[0,0,1]
	v_cvt_pk_fp8_f32 v179, v112, v113 op_sel:[0,0,1]
	v_cvt_pk_fp8_f32 v180, v106, v107 op_sel:[0,0,1]
	v_cvt_pk_fp8_f32 v181, v104, v105 op_sel:[0,0,1]
	v_cvt_pk_fp8_f32 v160, v57, v52 op_sel:[0,0,1]
	v_cvt_pk_fp8_f32 v164, v61, v53 op_sel:[0,0,1]
	v_cvt_pk_fp8_f32 v162, v25, v20 op_sel:[0,0,1]
	v_cvt_pk_fp8_f32 v163, v9, v2 op_sel:[0,0,1]
	v_cvt_pk_fp8_f32 v166, v29, v21 op_sel:[0,0,1]
	v_cvt_pk_fp8_f32 v167, v13, v0 op_sel:[0,0,1]
	s_mul_i32 s6, s0, 0x5000
	s_add_i32 s6, s6, 0
	v_bitop3_b32 v193, v193, 16, v194 bitop3:0x36
	v_add_u32_e32 v48, s6, v192
	v_add_u32_e32 v49, s6, v193
	ds_read_b128 v[16:19], v48
	ds_read_b128 v[20:23], v49
	v_mov_b64_e32 v[46:47], s[26:27]
	v_mov_b64_e32 v[44:45], s[24:25]
	v_mov_b64_e32 v[42:43], s[22:23]
	v_mov_b64_e32 v[40:41], s[20:21]
	v_mov_b64_e32 v[38:39], s[18:19]
	v_mov_b64_e32 v[36:37], s[16:17]
	v_mov_b64_e32 v[34:35], s[14:15]
	v_mov_b64_e32 v[32:33], s[12:13]
	ds_read_b128 v[50:53], v48 offset:2048
	ds_read_b128 v[54:57], v49 offset:2048
	s_waitcnt lgkmcnt(2)
	v_mfma_f32_32x32x64_f8f6f4 v[0:15], v[16:23], v[168:175], v[32:47]
	s_and_b64 vcc, exec, s[4:5]
	s_waitcnt lgkmcnt(0)
	v_mfma_f32_32x32x64_f8f6f4 v[16:31], v[50:57], v[168:175], v[32:47]
	s_nop 14
	ds_read_b128 v[36:39], v49 offset:4096
	ds_read_b128 v[32:35], v48 offset:4096
	ds_read_b128 v[40:43], v48 offset:6144
	ds_read_b128 v[44:47], v49 offset:6144
	s_waitcnt lgkmcnt(2)
	v_mfma_f32_32x32x64_f8f6f4 v[0:15], v[32:39], v[176:183], v[0:15]
	s_waitcnt lgkmcnt(0)
	v_mfma_f32_32x32x64_f8f6f4 v[16:31], v[40:47], v[176:183], v[16:31]
	ds_read_b128 v[36:39], v49 offset:8192
	ds_read_b128 v[32:35], v48 offset:8192
	ds_read_b128 v[40:43], v48 offset:10240
	ds_read_b128 v[44:47], v49 offset:10240
	s_waitcnt lgkmcnt(2)
	v_mfma_f32_32x32x64_f8f6f4 v[0:15], v[32:39], v[160:167], v[0:15]
	s_waitcnt lgkmcnt(0)
	v_mfma_f32_32x32x64_f8f6f4 v[16:31], v[40:47], v[160:167], v[16:31]
	s_nop 15
	s_nop 1
	v_max_f32_e32 v32, v1, v1
	v_max_f32_e32 v33, v0, v0
	v_max_f32_e32 v32, v33, v32
	v_max3_f32 v32, v32, v2, v3
	v_max3_f32 v32, v32, v4, v5
	v_max3_f32 v32, v32, v6, v7
	v_max3_f32 v32, v32, v8, v9
	v_max3_f32 v32, v32, v10, v11
	v_max3_f32 v32, v32, v12, v13
	v_max3_f32 v32, v32, v14, v15
	v_max3_f32 v32, v32, v16, v17
	v_max3_f32 v32, v32, v18, v19
	v_max3_f32 v32, v32, v20, v21
	v_max3_f32 v32, v32, v22, v23
	v_max3_f32 v32, v32, v24, v25
	v_max3_f32 v32, v32, v26, v27
	v_max3_f32 v32, v32, v28, v29
	v_max3_f32 v32, v32, v30, v31
	v_mov_b32_e32 v33, v32
	s_nop 1
	v_permlane32_swap_b32_e32 v32, v33
	s_cbranch_vccnz .LBB0_584
	s_setprio 1
; template <bool FIRST>
; __device__ __forceinline__ bool partialSM(f32x16& p0, f32x16& p1, float& M, f32x16& minit, float& alpha) {
;     float tmax = p0[0]; for (int r = 1; r < 16; ++r) tmax = fmaxf(tmax, p0[r]); for (int r = 0; r < 16; ++r) tmax = fmaxf(tmax, p1[r]);
;     { auto rr = __builtin_amdgcn_permlane32_swap(__float_as_uint(tmax), __float_as_uint(tmax), false, false);
;       tmax = fmaxf(__uint_as_float(rr[0]), __uint_as_float(rr[1])); }
;     const float d0 = tmax - PLOG2;
;     const bool moved = FIRST || !__all(d0 <= THR * 1.4426950408889634f);
;     if (__builtin_expect(moved, FIRST)) {
;         const float d = FIRST ? d0 : fmaxf(d0, 0.f);
;         alpha = __builtin_amdgcn_exp2f(-d); M += d;
;         for (int r = 0; r < 16; ++r) { p0[r] -= d; p1[r] -= d; }
;         const float mi = PLOG2 - M;
;         for (int r = 0; r < 16; ++r) minit[r] = mi;
;     } else alpha = 1.f;
;     for (int r = 0; r < 16; ++r) p0[r] = __builtin_amdgcn_exp2f(p0[r]);
;     return moved;
; }
; __device__ __forceinline__ void finishSM(f32x16& p0, f32x16& p1, i32x8& pa) {
;     for (int r = 0; r < 16; ++r) p1[r] = __builtin_amdgcn_exp2f(p1[r]);
; #pragma unroll
;     for (int v = 0; v < 4; ++v) { pa[v] = (int)cvt_pk4_fp8(p0[4 * v], p0[4 * v + 1], p0[4 * v + 2], p0[4 * v + 3]); pa[4 + v] = (int)cvt_pk4_fp8(p1[4 * v], p1[4 * v + 1], p1[4 * v + 2], p1[4 * v + 3]); }
; }
; __device__ __forceinline__ void qkt(f32x16& p0, f32x16& p1, const char* stg, int ka, const i32x8* qf, const f32x16& minit) {
;     p0 = minit; p1 = minit;
; #pragma unroll
;     for (int s = 0; s < 3; ++s) { const char* a = stg + SOFF_K + s * 4096 + ka; const char* b = stg + SOFF_K + s * 4096 + (ka ^ 16);
;         const i32x4 a0 = *reinterpret_cast<const i32x4*>(a), a1 = *reinterpret_cast<const i32x4*>(b);
;         const i32x4 c0 = *reinterpret_cast<const i32x4*>(a + 2048), c1 = *reinterpret_cast<const i32x4*>(b + 2048);
;         p0 = __builtin_amdgcn_mfma_scale_f32_32x32x64_f8f6f4(__builtin_shufflevector(a0, a1, 0, 1, 2, 3, 4, 5, 6, 7), qf[s], p0, 0, 0, 0, 0, 0, 0);
;         p1 = __builtin_amdgcn_mfma_scale_f32_32x32x64_f8f6f4(__builtin_shufflevector(c0, c1, 0, 1, 2, 3, 4, 5, 6, 7), qf[s], p1, 0, 0, 0, 0, 0, 0); }
; }
; __device__ __forceinline__ void v_read(i32x8 (&vf)[4], const char* stg, int ka) {
; #pragma unroll
.LBB0_584:
	v_max_f32_e32 v32, v32, v32
	v_max_f32_e32 v33, v33, v33
	v_max_f32_e32 v32, v32, v33
	v_add_f32_e32 v194, -4.0, v32
	v_sub_f32_e32 v0, v0, v194
	v_sub_f32_e32 v1, v1, v194
	v_sub_f32_e32 v2, v2, v194
	v_sub_f32_e32 v3, v3, v194
	v_sub_f32_e32 v4, v4, v194
	v_sub_f32_e32 v5, v5, v194
	v_sub_f32_e32 v6, v6, v194
	v_sub_f32_e32 v7, v7, v194
	v_sub_f32_e32 v8, v8, v194
	v_sub_f32_e32 v9, v9, v194
	v_sub_f32_e32 v10, v10, v194
	v_sub_f32_e32 v11, v11, v194
	v_sub_f32_e32 v12, v12, v194
	v_sub_f32_e32 v13, v13, v194
	v_sub_f32_e32 v14, v14, v194
	v_sub_f32_e32 v15, v15, v194
	v_exp_f32_e32 v32, v0
	v_exp_f32_e32 v33, v1
	v_exp_f32_e32 v34, v2
	v_exp_f32_e32 v35, v3
	v_exp_f32_e32 v36, v4
	v_exp_f32_e32 v37, v5
	v_exp_f32_e32 v38, v6
	v_exp_f32_e32 v39, v7
	v_exp_f32_e32 v40, v8
	v_exp_f32_e32 v41, v9
	v_exp_f32_e32 v42, v10
	v_exp_f32_e32 v43, v11
	v_exp_f32_e32 v44, v12
	v_exp_f32_e32 v45, v13
	v_exp_f32_e32 v46, v14
	v_exp_f32_e32 v47, v15
	s_cmp_gt_i32 s0, 4
	v_sub_f32_e32 v80, 4.0, v194
	s_cselect_b32 s6, -5, 1
	v_sub_f32_e32 v16, v16, v194
	v_sub_f32_e32 v17, v17, v194
	v_sub_f32_e32 v18, v18, v194
	v_sub_f32_e32 v19, v19, v194
	v_sub_f32_e32 v20, v20, v194
	v_sub_f32_e32 v21, v21, v194
	v_sub_f32_e32 v22, v22, v194
	v_sub_f32_e32 v23, v23, v194
	v_sub_f32_e32 v24, v24, v194
	v_sub_f32_e32 v25, v25, v194
	v_sub_f32_e32 v26, v26, v194
	v_sub_f32_e32 v27, v27, v194
	v_sub_f32_e32 v28, v28, v194
	v_sub_f32_e32 v29, v29, v194
	v_sub_f32_e32 v30, v30, v194
	v_sub_f32_e32 v31, v31, v194
	v_mov_b32_e32 v81, v80
	v_mov_b32_e32 v82, v80
	s_add_i32 s0, s6, s0
	v_mov_b32_e32 v83, v80
	v_mov_b32_e32 v84, v80
	v_mov_b32_e32 v85, v80
	v_mov_b32_e32 v86, v80
	v_mov_b32_e32 v87, v80
	v_mov_b32_e32 v88, v80
	v_mov_b32_e32 v89, v80
	v_mov_b32_e32 v90, v80
	v_mov_b32_e32 v91, v80
	v_mov_b32_e32 v92, v80
	v_mov_b32_e32 v93, v80
	v_mov_b32_e32 v94, v80
	v_mov_b32_e32 v95, v80
	s_mul_i32 s6, s0, 0x5000
	s_add_i32 s6, s6, 0
	v_add_u32_e32 v50, s6, v192
	v_add_u32_e32 v51, s6, v193
	ds_read_b128 v[0:3], v50
	ds_read_b128 v[4:7], v51
	ds_read_b128 v[8:11], v50 offset:2048
	ds_read_b128 v[12:15], v51 offset:2048
	v_mov_b64_e32 v[110:111], v[94:95]
	v_mov_b64_e32 v[108:109], v[92:93]
	v_mov_b64_e32 v[106:107], v[90:91]
	v_mov_b64_e32 v[104:105], v[88:89]
	v_mov_b64_e32 v[102:103], v[86:87]
	v_mov_b64_e32 v[100:101], v[84:85]
	v_mov_b64_e32 v[98:99], v[82:83]
	v_mov_b64_e32 v[96:97], v[80:81]
	s_waitcnt lgkmcnt(2)
	v_mfma_f32_32x32x64_f8f6f4 v[112:127], v[0:7], v[168:175], v[80:95]
	s_nop 0
	v_cvt_pk_fp8_f32 v64, v32, v33
	v_cvt_pk_fp8_f32 v65, v36, v37
	v_cvt_pk_fp8_f32 v66, v40, v41
	v_cvt_pk_fp8_f32 v67, v44, v45
	v_cvt_pk_fp8_f32 v64, v34, v35 op_sel:[0,0,1]
	v_cvt_pk_fp8_f32 v65, v38, v39 op_sel:[0,0,1]
	s_waitcnt lgkmcnt(0)
	v_mfma_f32_32x32x64_f8f6f4 v[96:111], v[8:15], v[168:175], v[96:111]
	ds_read_b128 v[0:3], v50 offset:4096
	ds_read_b128 v[4:7], v51 offset:4096
	ds_read_b128 v[8:11], v50 offset:6144
	ds_read_b128 v[12:15], v51 offset:6144
	v_cvt_pk_fp8_f32 v66, v42, v43 op_sel:[0,0,1]
	v_cvt_pk_fp8_f32 v67, v46, v47 op_sel:[0,0,1]
	s_waitcnt lgkmcnt(2)
	v_mfma_f32_32x32x64_f8f6f4 v[112:127], v[0:7], v[176:183], v[112:127]
	s_waitcnt lgkmcnt(0)
	v_mfma_f32_32x32x64_f8f6f4 v[96:111], v[8:15], v[176:183], v[96:111]
	ds_read_b128 v[0:3], v50 offset:8192
	ds_read_b128 v[4:7], v51 offset:8192
	ds_read_b128 v[8:11], v50 offset:10240
	ds_read_b128 v[12:15], v51 offset:10240
	s_waitcnt lgkmcnt(2)
	v_mfma_f32_32x32x64_f8f6f4 v[112:127], v[0:7], v[160:167], v[112:127]
	v_exp_f32_e32 v0, v16
	v_exp_f32_e32 v1, v17
	v_exp_f32_e32 v4, v20
	v_exp_f32_e32 v5, v21
	v_exp_f32_e32 v2, v18
	v_exp_f32_e32 v3, v19
	v_exp_f32_e32 v6, v22
	v_exp_f32_e32 v7, v23
	v_cvt_pk_fp8_f32 v68, v0, v1
	v_cvt_pk_fp8_f32 v69, v4, v5
	v_cvt_pk_fp8_f32 v68, v2, v3 op_sel:[0,0,1]
	v_cvt_pk_fp8_f32 v69, v6, v7 op_sel:[0,0,1]
	s_waitcnt lgkmcnt(0)
	v_mfma_f32_32x32x64_f8f6f4 v[96:111], v[8:15], v[160:167], v[96:111]
	v_exp_f32_e32 v8, v24
	v_exp_f32_e32 v9, v25
	v_exp_f32_e32 v12, v28
	v_exp_f32_e32 v13, v29
	v_exp_f32_e32 v10, v26
	v_exp_f32_e32 v11, v27
	v_exp_f32_e32 v14, v30
	v_exp_f32_e32 v15, v31
	v_cvt_pk_fp8_f32 v70, v8, v9
	v_cvt_pk_fp8_f32 v71, v12, v13
	v_cvt_pk_fp8_f32 v70, v10, v11 op_sel:[0,0,1]
	v_cvt_pk_fp8_f32 v71, v14, v15 op_sel:[0,0,1]
	v_max_f32_e32 v81, v113, v113
	v_max_f32_e32 v82, v112, v112
	v_max_f32_e32 v81, v82, v81
	v_max3_f32 v81, v81, v114, v115
	v_max3_f32 v81, v81, v116, v117
	ds_read_b128 v[0:3], v48 offset:12288
	ds_read_b128 v[4:7], v49 offset:12288
	ds_read_b128 v[8:11], v48 offset:14336
	ds_read_b128 v[12:15], v49 offset:14336
	ds_read_b128 v[16:19], v48 offset:16384
	ds_read_b128 v[20:23], v49 offset:16384
	ds_read_b128 v[24:27], v48 offset:18432
	ds_read_b128 v[28:31], v49 offset:18432
	v_max3_f32 v81, v81, v118, v119
	v_max3_f32 v81, v81, v120, v121
	v_max3_f32 v81, v81, v122, v123
	v_max3_f32 v81, v81, v124, v125
	v_max3_f32 v81, v81, v126, v127
	s_waitcnt lgkmcnt(6)
	v_mfma_f32_32x32x64_f8f6f4 v[48:63], v[64:71], v[0:7], 0
	v_max3_f32 v81, v81, v96, v97
	v_max3_f32 v81, v81, v98, v99
	v_max3_f32 v81, v81, v100, v101
	v_max3_f32 v81, v81, v102, v103
	v_max3_f32 v81, v81, v104, v105
	v_max3_f32 v81, v81, v106, v107
	v_max3_f32 v81, v81, v108, v109
	v_max3_f32 v81, v81, v110, v111
	v_mov_b32_e32 v82, v81
	s_nop 1
	v_permlane32_swap_b32_e32 v81, v82
	v_max_f32_e32 v82, v82, v82
	v_max_f32_e32 v81, v81, v81
	v_max_f32_e32 v81, v81, v82
	v_add_f32_e32 v82, -4.0, v81
	s_waitcnt lgkmcnt(4)
	v_mfma_f32_32x32x64_f8f6f4 v[0:15], v[64:71], v[8:15], 0
	v_cmp_ge_f32_e32 vcc, s31, v82
	s_cmp_lg_u64 vcc, exec
	s_cselect_b64 s[6:7], -1, 0
	s_cmp_eq_u64 vcc, exec
	v_mov_b32_e32 v81, 1.0
	s_waitcnt lgkmcnt(2)
	v_mfma_f32_32x32x64_f8f6f4 v[32:47], v[64:71], v[16:23], 0
	s_waitcnt lgkmcnt(0)
	v_mfma_f32_32x32x64_f8f6f4 v[16:31], v[64:71], v[24:31], 0
	v_mfma_f32_32x32x64_f8f6f4 v[64:79], v[64:71], v[152:159], 0
	s_cbranch_scc0 .LBB0_612
	v_lshlrev_b32_e32 v195, 2, v195
	s_andn2_b64 vcc, exec, s[6:7]
	v_cmp_gt_u32_e64 s[6:7], 32, v188
	s_cbranch_vccnz .LBB0_589

; __device__ __forceinline__ void mask_tile(f32x16& p0, f32x16& p1, int dq, unsigned W) {
;     const float NEG = -__builtin_inff();
; #pragma unroll
;     for (int r = 0; r < 16; ++r) {
;         const int c = (r & 3) + 8 * (r >> 2);
;         if ((unsigned)(dq - c) >= W) p0[r] = NEG;
;         if ((unsigned)(dq - c - 32) >= W) p1[r] = NEG;
;     }
; }
; __device__ __forceinline__ void qkt(f32x16& p0, f32x16& p1, const char* stg, int ka, const i32x8* qf, const f32x16& minit) {
;     p0 = minit; p1 = minit;
; #pragma unroll
;     for (int s = 0; s < 3; ++s) { const char* a = stg + SOFF_K + s * 4096 + ka; const char* b = stg + SOFF_K + s * 4096 + (ka ^ 16);
;         const i32x4 a0 = *reinterpret_cast<const i32x4*>(a), a1 = *reinterpret_cast<const i32x4*>(b);
;         const i32x4 c0 = *reinterpret_cast<const i32x4*>(a + 2048), c1 = *reinterpret_cast<const i32x4*>(b + 2048);
;         p0 = __builtin_amdgcn_mfma_scale_f32_32x32x64_f8f6f4(__builtin_shufflevector(a0, a1, 0, 1, 2, 3, 4, 5, 6, 7), qf[s], p0, 0, 0, 0, 0, 0, 0);
;         p1 = __builtin_amdgcn_mfma_scale_f32_32x32x64_f8f6f4(__builtin_shufflevector(c0, c1, 0, 1, 2, 3, 4, 5, 6, 7), qf[s], p1, 0, 0, 0, 0, 0, 0); }
; }
; __device__ __forceinline__ void v_read(i32x8 (&vf)[4], const char* stg, int ka) {
; #pragma unroll
;     for (int d0 = 0; d0 < 4; ++d0) { const i32x4 a0 = *reinterpret_cast<const i32x4*>(stg + SOFF_V + d0 * 2048 + ka), a1 = *reinterpret_cast<const i32x4*>(stg + SOFF_V + d0 * 2048 + (ka ^ 16));
;         vf[d0] = __builtin_shufflevector(a0, a1, 0, 1, 2, 3, 4, 5, 6, 7); }
; }
; __device__ __forceinline__ void pv_mma(f32x16* o, f32x16& ol, const i32x8 (&vf)[4], const i32x8 ones, const i32x8 pa) {
; #pragma unroll
;     for (int d0 = 0; d0 < 4; ++d0) o[d0] = __builtin_amdgcn_mfma_scale_f32_32x32x64_f8f6f4(pa, vf[d0], o[d0], 0, 0, 0, 0, 0, 0);
;     ol = __builtin_amdgcn_mfma_scale_f32_32x32x64_f8f6f4(pa, ones, ol, 0, 0, 0, 0, 0, 0);
; }
.LBB0_594:
	s_cmp_gt_i32 s0, 4
	s_cselect_b32 s46, -5, 1
	s_add_i32 s46, s46, s0
	s_mulk_i32 s46, 0x5000
	s_add_i32 s46, s46, 0
	v_add_u32_e32 v199, s46, v192
	v_add_u32_e32 v200, s46, v193
	ds_read_b128 v[112:115], v199
	ds_read_b128 v[116:119], v200
	ds_read_b128 v[220:223], v199 offset:2048
	ds_read_b128 v[224:227], v200 offset:2048
	ds_read_b128 v[236:239], v199 offset:4096
	ds_read_b128 v[240:243], v200 offset:4096
	ds_read_b128 v[244:247], v199 offset:6144
	ds_read_b128 v[248:251], v200 offset:6144
	v_exp_f32_e32 v201, v96
	s_waitcnt lgkmcnt(6)
	v_mfma_f32_32x32x64_f8f6f4 v[128:143], v[112:119], v[168:175], v[80:95]
	v_exp_f32_e32 v97, v97
	v_exp_f32_e32 v202, v100
	v_exp_f32_e32 v219, v101
	v_exp_f32_e32 v98, v98
	v_exp_f32_e32 v99, v99
	v_exp_f32_e32 v102, v102
	v_exp_f32_e32 v104, v104
	v_exp_f32_e32 v105, v105
	v_exp_f32_e32 v108, v108
	v_exp_f32_e32 v109, v109
	v_exp_f32_e32 v106, v106
	v_exp_f32_e32 v107, v107
	v_exp_f32_e32 v110, v110
	v_exp_f32_e32 v111, v111
	s_waitcnt lgkmcnt(4)
	v_mfma_f32_32x32x64_f8f6f4 v[112:127], v[220:227], v[168:175], v[80:95]
	ds_read_b128 v[220:223], v199 offset:8192
	ds_read_b128 v[224:227], v200 offset:8192
	ds_read_b128 v[228:231], v199 offset:10240
	ds_read_b128 v[232:235], v200 offset:10240
	s_waitcnt lgkmcnt(6)
	v_mfma_f32_32x32x64_f8f6f4 v[128:143], v[236:243], v[176:183], v[128:143]
	s_waitcnt lgkmcnt(4)
	v_mfma_f32_32x32x64_f8f6f4 v[112:127], v[244:251], v[176:183], v[112:127]
	s_waitcnt lgkmcnt(2)
	v_mfma_f32_32x32x64_f8f6f4 v[128:143], v[220:227], v[160:167], v[128:143]
	v_exp_f32_e32 v220, v103
	s_nop 0
	v_cvt_pk_fp8_f32 v100, v201, v97
	v_cvt_pk_fp8_f32 v101, v202, v219
	v_cvt_pk_fp8_f32 v100, v98, v99 op_sel:[0,0,1]
	v_cvt_pk_fp8_f32 v101, v102, v220 op_sel:[0,0,1]
	v_cvt_pk_fp8_f32 v96, v217, v218
	s_waitcnt lgkmcnt(0)
	v_mfma_f32_32x32x64_f8f6f4 v[112:127], v[228:235], v[160:167], v[112:127]
	v_cvt_pk_fp8_f32 v97, v213, v214
	v_cvt_pk_fp8_f32 v98, v209, v210
	v_cvt_pk_fp8_f32 v102, v104, v105
	v_cvt_pk_fp8_f32 v99, v205, v206
	v_cvt_pk_fp8_f32 v103, v108, v109
	v_cvt_pk_fp8_f32 v96, v215, v216 op_sel:[0,0,1]
	v_cvt_pk_fp8_f32 v97, v211, v212 op_sel:[0,0,1]
	v_cvt_pk_fp8_f32 v98, v207, v208 op_sel:[0,0,1]
	v_cvt_pk_fp8_f32 v102, v106, v107 op_sel:[0,0,1]
	v_cvt_pk_fp8_f32 v99, v203, v204 op_sel:[0,0,1]
	v_cvt_pk_fp8_f32 v103, v110, v111 op_sel:[0,0,1]
	s_mul_i32 s46, s0, 0x5000
	s_add_i32 s46, s46, 0
	v_add_u32_e32 v202, s46, v193
	v_add_u32_e32 v201, s46, v192
	ds_read_b128 v[108:111], v202 offset:12288
	ds_read_b128 v[104:107], v201 offset:12288
	ds_read_b128 v[236:239], v201 offset:14336
	ds_read_b128 v[240:243], v202 offset:14336
	ds_read_b128 v[248:251], v202 offset:16384
	ds_read_b128 v[244:247], v201 offset:16384
	v_mfma_f32_32x32x64_f8f6f4 v[64:79], v[96:103], v[152:159], v[64:79]
	s_sub_i32 s46, s1, 64
	s_cmp_le_u32 s46, s39
	s_waitcnt lgkmcnt(4)
	v_mfma_f32_32x32x64_f8f6f4 v[48:63], v[96:103], v[104:111], v[48:63]
	ds_read_b128 v[104:107], v201 offset:18432
	ds_read_b128 v[108:111], v202 offset:18432
	s_waitcnt lgkmcnt(4)
	v_mfma_f32_32x32x64_f8f6f4 v[0:15], v[96:103], v[236:243], v[0:15]
	s_waitcnt lgkmcnt(2)
	v_mfma_f32_32x32x64_f8f6f4 v[32:47], v[96:103], v[244:251], v[32:47]
	s_waitcnt lgkmcnt(0)
	v_mfma_f32_32x32x64_f8f6f4 v[16:31], v[96:103], v[104:111], v[16:31]
	s_cbranch_scc1 .LBB0_596
	v_add_u32_e32 v96, 0x4000007b, v198
	v_cmp_gt_u32_e32 vcc, 2.0, v96
	v_add_u32_e32 v96, 0x5b, v198
	s_nop 0
	v_cndmask_b32_e32 v128, v187, v128, vcc
	v_cmp_lt_u32_e32 vcc, s37, v96
	v_add_u32_e32 v96, 0x7a, v198
	s_nop 0
	v_cndmask_b32_e32 v112, v187, v112, vcc
	v_cmp_lt_u32_e32 vcc, s37, v96
	v_add_u32_e32 v96, 0x5a, v198
	s_nop 0
	v_cndmask_b32_e32 v129, v187, v129, vcc
	v_cmp_lt_u32_e32 vcc, s37, v96
	v_add_u32_e32 v96, 0x79, v198
	s_nop 0
	v_cndmask_b32_e32 v113, v187, v113, vcc
	v_cmp_lt_u32_e32 vcc, s37, v96
	v_add_u32_e32 v96, 0x59, v198
	s_nop 0
	v_cndmask_b32_e32 v130, v187, v130, vcc
	v_cmp_lt_u32_e32 vcc, s37, v96
	v_add_u32_e32 v96, 0x78, v198
	s_nop 0
	v_cndmask_b32_e32 v114, v187, v114, vcc
	v_cmp_lt_u32_e32 vcc, s37, v96
	v_add_u32_e32 v96, 0x58, v198
	s_nop 0
	v_cndmask_b32_e32 v131, v187, v131, vcc
	v_cmp_lt_u32_e32 vcc, s37, v96
	v_add_u32_e32 v96, 0x73, v198
	s_nop 0
	v_cndmask_b32_e32 v115, v187, v115, vcc
	v_cmp_lt_u32_e32 vcc, s37, v96
	v_add_u32_e32 v96, 0x53, v198
	s_nop 0
	v_cndmask_b32_e32 v132, v187, v132, vcc
	v_cmp_lt_u32_e32 vcc, s37, v96
	v_add_u32_e32 v96, 0x72, v198
	s_nop 0
	v_cndmask_b32_e32 v116, v187, v116, vcc
	v_cmp_lt_u32_e32 vcc, s37, v96
	v_add_u32_e32 v96, 0x52, v198
	s_nop 0
	v_cndmask_b32_e32 v133, v187, v133, vcc
	v_cmp_lt_u32_e32 vcc, s37, v96
	v_add_u32_e32 v96, 0x71, v198
	s_nop 0
	v_cndmask_b32_e32 v117, v187, v117, vcc
	v_cmp_lt_u32_e32 vcc, s37, v96
	v_add_u32_e32 v96, 0x51, v198
	s_nop 0
	v_cndmask_b32_e32 v134, v187, v134, vcc
	v_cmp_lt_u32_e32 vcc, s37, v96
	v_add_u32_e32 v96, 0x70, v198
	s_nop 0
	v_cndmask_b32_e32 v118, v187, v118, vcc
	v_cmp_lt_u32_e32 vcc, s37, v96
	v_add_u32_e32 v96, 0x50, v198
	s_nop 0
	v_cndmask_b32_e32 v135, v187, v135, vcc
	v_cmp_lt_u32_e32 vcc, s37, v96
	v_add_u32_e32 v96, 0x6b, v198
	s_nop 0
	v_cndmask_b32_e32 v119, v187, v119, vcc
	v_cmp_lt_u32_e32 vcc, s37, v96
	v_add_u32_e32 v96, 0x4b, v198
	s_nop 0
	v_cndmask_b32_e32 v136, v187, v136, vcc
	v_cmp_lt_u32_e32 vcc, s37, v96
	v_add_u32_e32 v96, 0x6a, v198
	s_nop 0
	v_cndmask_b32_e32 v120, v187, v120, vcc
	v_cmp_lt_u32_e32 vcc, s37, v96
	v_add_u32_e32 v96, 0x4a, v198
	s_nop 0
	v_cndmask_b32_e32 v137, v187, v137, vcc
	v_cmp_lt_u32_e32 vcc, s37, v96
	v_add_u32_e32 v96, 0x69, v198
	s_nop 0
	v_cndmask_b32_e32 v121, v187, v121, vcc
	v_cmp_lt_u32_e32 vcc, s37, v96
	v_add_u32_e32 v96, 0x49, v198
	s_nop 0
	v_cndmask_b32_e32 v138, v187, v138, vcc
	v_cmp_lt_u32_e32 vcc, s37, v96
	v_add_u32_e32 v96, 0x68, v198
	s_nop 0
	v_cndmask_b32_e32 v122, v187, v122, vcc
	v_cmp_lt_u32_e32 vcc, s37, v96
	v_add_u32_e32 v96, 0x48, v198
	s_nop 0
	v_cndmask_b32_e32 v139, v187, v139, vcc
	v_cmp_lt_u32_e32 vcc, s37, v96
	v_add_u32_e32 v96, 0x63, v198
	s_nop 0
	v_cndmask_b32_e32 v123, v187, v123, vcc
	v_cmp_lt_u32_e32 vcc, s37, v96
	v_add_u32_e32 v96, 0x43, v198
	s_nop 0
	v_cndmask_b32_e32 v140, v187, v140, vcc
	v_cmp_lt_u32_e32 vcc, s37, v96
	v_add_u32_e32 v96, 0x62, v198
	s_nop 0
	v_cndmask_b32_e32 v124, v187, v124, vcc
	v_cmp_lt_u32_e32 vcc, s37, v96
	v_add_u32_e32 v96, 0x42, v198
	s_nop 0
	v_cndmask_b32_e32 v141, v187, v141, vcc
	v_cmp_lt_u32_e32 vcc, s37, v96
	v_add_u32_e32 v96, 0x61, v198
	s_nop 0
	v_cndmask_b32_e32 v125, v187, v125, vcc
	v_cmp_lt_u32_e32 vcc, s37, v96
	v_add_u32_e32 v96, 0x41, v198
	s_nop 0
	v_cndmask_b32_e32 v142, v187, v142, vcc
	v_cmp_lt_u32_e32 vcc, s37, v96
	v_add_u32_e32 v96, 0x60, v198
	s_nop 0
	v_cndmask_b32_e32 v126, v187, v126, vcc
	v_cmp_lt_u32_e32 vcc, s37, v96
	v_add_u32_e32 v96, 64, v198
	s_nop 0
	v_cndmask_b32_e32 v143, v187, v143, vcc
	v_cmp_lt_u32_e32 vcc, s37, v96
	s_nop 1
	v_cndmask_b32_e32 v127, v187, v127, vcc

; template <bool FIRST>
; __device__ __forceinline__ bool partialSM(f32x16& p0, f32x16& p1, float& M, f32x16& minit, float& alpha) {
;     ...
;     for (int r = 0; r < 16; ++r) p0[r] = __builtin_amdgcn_exp2f(p0[r]);
;     return moved;
; }
; __device__ __forceinline__ void finishSM(f32x16& p0, f32x16& p1, i32x8& pa) {
;     for (int r = 0; r < 16; ++r) p1[r] = __builtin_amdgcn_exp2f(p1[r]);
; #pragma unroll
;     for (int v = 0; v < 4; ++v) { pa[v] = (int)cvt_pk4_fp8(p0[4 * v], p0[4 * v + 1], p0[4 * v + 2], p0[4 * v + 3]); pa[4 + v] = (int)cvt_pk4_fp8(p1[4 * v], p1[4 * v + 1], p1[4 * v + 2], p1[4 * v + 3]); }
; }
; __device__ __forceinline__ void qkt(f32x16& p0, f32x16& p1, const char* stg, int ka, const i32x8* qf, const f32x16& minit) {
;     p0 = minit; p1 = minit;
; #pragma unroll
;     for (int s = 0; s < 3; ++s) { const char* a = stg + SOFF_K + s * 4096 + ka; const char* b = stg + SOFF_K + s * 4096 + (ka ^ 16);
;         const i32x4 a0 = *reinterpret_cast<const i32x4*>(a), a1 = *reinterpret_cast<const i32x4*>(b);
;         const i32x4 c0 = *reinterpret_cast<const i32x4*>(a + 2048), c1 = *reinterpret_cast<const i32x4*>(b + 2048);
;         p0 = __builtin_amdgcn_mfma_scale_f32_32x32x64_f8f6f4(__builtin_shufflevector(a0, a1, 0, 1, 2, 3, 4, 5, 6, 7), qf[s], p0, 0, 0, 0, 0, 0, 0);
;         p1 = __builtin_amdgcn_mfma_scale_f32_32x32x64_f8f6f4(__builtin_shufflevector(c0, c1, 0, 1, 2, 3, 4, 5, 6, 7), qf[s], p1, 0, 0, 0, 0, 0, 0); }
; }
; __device__ __forceinline__ void v_read(i32x8 (&vf)[4], const char* stg, int ka) {
; #pragma unroll
;     for (int d0 = 0; d0 < 4; ++d0) { const i32x4 a0 = *reinterpret_cast<const i32x4*>(stg + SOFF_V + d0 * 2048 + ka), a1 = *reinterpret_cast<const i32x4*>(stg + SOFF_V + d0 * 2048 + (ka ^ 16));
;         vf[d0] = __builtin_shufflevector(a0, a1, 0, 1, 2, 3, 4, 5, 6, 7); }
; }
; __device__ __forceinline__ void pv_mma(f32x16* o, f32x16& ol, const i32x8 (&vf)[4], const i32x8 ones, const i32x8 pa) {
; #pragma unroll
;     for (int d0 = 0; d0 < 4; ++d0) o[d0] = __builtin_amdgcn_mfma_scale_f32_32x32x64_f8f6f4(pa, vf[d0], o[d0], 0, 0, 0, 0, 0, 0);
;     ol = __builtin_amdgcn_mfma_scale_f32_32x32x64_f8f6f4(pa, ones, ol, 0, 0, 0, 0, 0, 0);
; }
.LBB0_601:
	s_cmp_gt_i32 s0, 3
	s_cselect_b32 s46, -4, 2
	s_add_i32 s0, s46, s0
	v_exp_f32_e32 v203, v128
	v_exp_f32_e32 v220, v129
	v_exp_f32_e32 v221, v130
	v_exp_f32_e32 v222, v131
	v_exp_f32_e32 v223, v132
	v_exp_f32_e32 v224, v133
	v_exp_f32_e32 v225, v134
	v_exp_f32_e32 v226, v135
	v_exp_f32_e32 v227, v136
	v_exp_f32_e32 v228, v137
	v_exp_f32_e32 v229, v138
	v_exp_f32_e32 v230, v139
	v_exp_f32_e32 v231, v140
	v_exp_f32_e32 v232, v141
	v_exp_f32_e32 v233, v142
	v_exp_f32_e32 v234, v143
	s_mul_i32 s46, s0, 0x5000
	s_add_i32 s46, s46, 0
	v_add_u32_e32 v202, s46, v192
	v_add_u32_e32 v201, s46, v193
	ds_read_b128 v[204:207], v202
	ds_read_b128 v[208:211], v201
	ds_read_b128 v[212:215], v202 offset:2048
	ds_read_b128 v[216:219], v201 offset:2048
	ds_read_b128 v[236:239], v202 offset:4096
	ds_read_b128 v[240:243], v201 offset:4096
	ds_read_b128 v[244:247], v202 offset:6144
	ds_read_b128 v[248:251], v201 offset:6144
	v_exp_f32_e32 v113, v113
	s_waitcnt lgkmcnt(6)
	v_mfma_f32_32x32x64_f8f6f4 v[128:143], v[204:211], v[168:175], v[96:111]
	v_exp_f32_e32 v114, v114
	v_exp_f32_e32 v115, v115
	v_exp_f32_e32 v118, v118
	v_exp_f32_e32 v120, v120
	v_exp_f32_e32 v121, v121
	v_exp_f32_e32 v124, v124
	v_exp_f32_e32 v125, v125
	v_exp_f32_e32 v122, v122
	v_exp_f32_e32 v123, v123
	v_exp_f32_e32 v126, v126
	v_exp_f32_e32 v127, v127
	s_waitcnt lgkmcnt(4)
	v_mfma_f32_32x32x64_f8f6f4 v[96:111], v[212:219], v[168:175], v[96:111]
	ds_read_b128 v[204:207], v202 offset:8192
	ds_read_b128 v[208:211], v201 offset:8192
	ds_read_b128 v[212:215], v202 offset:10240
	ds_read_b128 v[216:219], v201 offset:10240
	s_waitcnt lgkmcnt(6)
	v_mfma_f32_32x32x64_f8f6f4 v[128:143], v[236:243], v[176:183], v[128:143]
	s_waitcnt lgkmcnt(4)
	v_mfma_f32_32x32x64_f8f6f4 v[96:111], v[244:251], v[176:183], v[96:111]
	s_waitcnt lgkmcnt(2)
	v_mfma_f32_32x32x64_f8f6f4 v[128:143], v[204:211], v[160:167], v[128:143]
	v_exp_f32_e32 v204, v112
	v_exp_f32_e32 v205, v116
	v_exp_f32_e32 v206, v117
	v_exp_f32_e32 v207, v119
	s_nop 0
	v_cvt_pk_fp8_f32 v116, v204, v113
	v_cvt_pk_fp8_f32 v117, v205, v206
	v_cvt_pk_fp8_f32 v116, v114, v115 op_sel:[0,0,1]
	v_cvt_pk_fp8_f32 v117, v118, v207 op_sel:[0,0,1]
	s_waitcnt lgkmcnt(0)
	v_mfma_f32_32x32x64_f8f6f4 v[96:111], v[212:219], v[160:167], v[96:111]
	v_cvt_pk_fp8_f32 v112, v203, v220
	v_cvt_pk_fp8_f32 v113, v223, v224
	v_cvt_pk_fp8_f32 v114, v227, v228
	v_cvt_pk_fp8_f32 v118, v120, v121
	v_cvt_pk_fp8_f32 v115, v231, v232
	v_cvt_pk_fp8_f32 v119, v124, v125
	v_cvt_pk_fp8_f32 v112, v221, v222 op_sel:[0,0,1]
	v_cvt_pk_fp8_f32 v113, v225, v226 op_sel:[0,0,1]
	v_cvt_pk_fp8_f32 v114, v229, v230 op_sel:[0,0,1]
	v_cvt_pk_fp8_f32 v118, v122, v123 op_sel:[0,0,1]
	v_cvt_pk_fp8_f32 v115, v233, v234 op_sel:[0,0,1]
	v_cvt_pk_fp8_f32 v119, v126, v127 op_sel:[0,0,1]
	ds_read_b128 v[124:127], v200 offset:12288
	ds_read_b128 v[120:123], v199 offset:12288
	ds_read_b128 v[236:239], v199 offset:14336
	ds_read_b128 v[240:243], v200 offset:14336
	ds_read_b128 v[248:251], v200 offset:16384
	ds_read_b128 v[244:247], v199 offset:16384
	v_mfma_f32_32x32x64_f8f6f4 v[64:79], v[112:119], v[152:159], v[64:79]
	s_cmp_le_u32 s1, s39
	s_waitcnt lgkmcnt(4)
	v_mfma_f32_32x32x64_f8f6f4 v[48:63], v[112:119], v[120:127], v[48:63]
	ds_read_b128 v[120:123], v199 offset:18432
	ds_read_b128 v[124:127], v200 offset:18432
	s_waitcnt lgkmcnt(4)
	v_mfma_f32_32x32x64_f8f6f4 v[0:15], v[112:119], v[236:243], v[0:15]
	s_waitcnt lgkmcnt(2)
	v_mfma_f32_32x32x64_f8f6f4 v[32:47], v[112:119], v[244:251], v[32:47]
	s_waitcnt lgkmcnt(0)
	v_mfma_f32_32x32x64_f8f6f4 v[16:31], v[112:119], v[120:127], v[16:31]
	s_cbranch_scc1 .LBB0_603
; __device__ __forceinline__ void mask_tile(f32x16& p0, f32x16& p1, int dq, unsigned W) {
;     const float NEG = -__builtin_inff();
; #pragma unroll
;     for (int r = 0; r < 16; ++r) {
;         const int c = (r & 3) + 8 * (r >> 2);
;         if ((unsigned)(dq - c) >= W) p0[r] = NEG;
;         if ((unsigned)(dq - c - 32) >= W) p1[r] = NEG;
;     }
; }
	v_add_u32_e32 v112, 0x4000003b, v198
	v_cmp_gt_u32_e32 vcc, 2.0, v112
	v_add_u32_e32 v112, 27, v198
	s_nop 0
	v_cndmask_b32_e32 v128, v187, v128, vcc
	v_cmp_lt_u32_e32 vcc, s37, v112
	v_add_u32_e32 v112, 58, v198
	s_nop 0
	v_cndmask_b32_e32 v96, v187, v96, vcc
	v_cmp_lt_u32_e32 vcc, s37, v112
	v_add_u32_e32 v112, 26, v198
	s_nop 0
	v_cndmask_b32_e32 v129, v187, v129, vcc
	v_cmp_lt_u32_e32 vcc, s37, v112
	v_add_u32_e32 v112, 57, v198
	s_nop 0
	v_cndmask_b32_e32 v97, v187, v97, vcc
	v_cmp_lt_u32_e32 vcc, s37, v112
	v_add_u32_e32 v112, 25, v198
	s_nop 0
	v_cndmask_b32_e32 v130, v187, v130, vcc
	v_cmp_lt_u32_e32 vcc, s37, v112
	v_add_u32_e32 v112, 56, v198
	s_nop 0
	v_cndmask_b32_e32 v98, v187, v98, vcc
	v_cmp_lt_u32_e32 vcc, s37, v112
	v_add_u32_e32 v112, 24, v198
	s_nop 0
	v_cndmask_b32_e32 v131, v187, v131, vcc
	v_cmp_lt_u32_e32 vcc, s37, v112
	v_add_u32_e32 v112, 51, v198
	s_nop 0
	v_cndmask_b32_e32 v99, v187, v99, vcc
	v_cmp_lt_u32_e32 vcc, s37, v112
	v_add_u32_e32 v112, 19, v198
	s_nop 0
	v_cndmask_b32_e32 v132, v187, v132, vcc
	v_cmp_lt_u32_e32 vcc, s37, v112
	v_add_u32_e32 v112, 50, v198
	s_nop 0
	v_cndmask_b32_e32 v100, v187, v100, vcc
	v_cmp_lt_u32_e32 vcc, s37, v112
	v_add_u32_e32 v112, 18, v198
	s_nop 0
	v_cndmask_b32_e32 v133, v187, v133, vcc
	v_cmp_lt_u32_e32 vcc, s37, v112
	v_add_u32_e32 v112, 49, v198
	s_nop 0
	v_cndmask_b32_e32 v101, v187, v101, vcc
	v_cmp_lt_u32_e32 vcc, s37, v112
	v_add_u32_e32 v112, 17, v198
	s_nop 0
	v_cndmask_b32_e32 v134, v187, v134, vcc
	v_cmp_lt_u32_e32 vcc, s37, v112
	v_add_u32_e32 v112, 48, v198
	s_nop 0
	v_cndmask_b32_e32 v102, v187, v102, vcc
	v_cmp_lt_u32_e32 vcc, s37, v112
	v_add_u32_e32 v112, 16, v198
	s_nop 0
	v_cndmask_b32_e32 v135, v187, v135, vcc
	v_cmp_lt_u32_e32 vcc, s37, v112
	v_add_u32_e32 v112, 43, v198
	s_nop 0
	v_cndmask_b32_e32 v103, v187, v103, vcc
	v_cmp_lt_u32_e32 vcc, s37, v112
	v_add_u32_e32 v112, 11, v198
	s_nop 0
	v_cndmask_b32_e32 v136, v187, v136, vcc
	v_cmp_lt_u32_e32 vcc, s37, v112
	v_add_u32_e32 v112, 42, v198
	s_nop 0
	v_cndmask_b32_e32 v104, v187, v104, vcc
	v_cmp_lt_u32_e32 vcc, s37, v112
	v_add_u32_e32 v112, 10, v198
	s_nop 0
	v_cndmask_b32_e32 v137, v187, v137, vcc
	v_cmp_lt_u32_e32 vcc, s37, v112
	v_add_u32_e32 v112, 41, v198
	s_nop 0
	v_cndmask_b32_e32 v105, v187, v105, vcc
	v_cmp_lt_u32_e32 vcc, s37, v112
	v_add_u32_e32 v112, 9, v198
	s_nop 0
	v_cndmask_b32_e32 v138, v187, v138, vcc
	v_cmp_lt_u32_e32 vcc, s37, v112
	v_add_u32_e32 v112, 40, v198
	s_nop 0
	v_cndmask_b32_e32 v106, v187, v106, vcc
	v_cmp_lt_u32_e32 vcc, s37, v112
	v_add_u32_e32 v112, 8, v198
	s_nop 0
	v_cndmask_b32_e32 v139, v187, v139, vcc
	v_cmp_lt_u32_e32 vcc, s37, v112
	v_add_u32_e32 v112, 35, v198
	s_nop 0
	v_cndmask_b32_e32 v107, v187, v107, vcc
	v_cmp_lt_u32_e32 vcc, s37, v112
	v_add_u32_e32 v112, 3, v198
	s_nop 0
	v_cndmask_b32_e32 v140, v187, v140, vcc
	v_cmp_lt_u32_e32 vcc, s37, v112
	v_add_u32_e32 v112, 34, v198
	s_nop 0
	v_cndmask_b32_e32 v108, v187, v108, vcc
	v_cmp_lt_u32_e32 vcc, s37, v112
	v_add_u32_e32 v112, 2, v198
	s_nop 0
	v_cndmask_b32_e32 v141, v187, v141, vcc
	v_cmp_lt_u32_e32 vcc, s37, v112
	v_add_u32_e32 v112, 33, v198
	s_nop 0
	v_cndmask_b32_e32 v109, v187, v109, vcc
	v_cmp_lt_u32_e32 vcc, s37, v112
	v_add_u32_e32 v112, 1, v198
	s_nop 0
	v_cndmask_b32_e32 v142, v187, v142, vcc
	v_cmp_lt_u32_e32 vcc, s37, v112
	v_add_u32_e32 v112, 32, v198
	s_nop 0
	v_cndmask_b32_e32 v110, v187, v110, vcc
	v_cmp_lt_u32_e32 vcc, s37, v112
	s_nop 1
	v_cndmask_b32_e32 v143, v187, v143, vcc
	v_cmp_lt_u32_e32 vcc, s37, v198
	s_nop 1
	v_cndmask_b32_e32 v111, v187, v111, vcc

; __device__ __forceinline__ void mask_tile(f32x16& p0, f32x16& p1, int dq, unsigned W) {
;     const float NEG = -__builtin_inff();
; #pragma unroll
;     for (int r = 0; r < 16; ++r) {
;         const int c = (r & 3) + 8 * (r >> 2);
;         if ((unsigned)(dq - c) >= W) p0[r] = NEG;
;         if ((unsigned)(dq - c - 32) >= W) p1[r] = NEG;
;     }
; }
; __device__ __forceinline__ void qkt(f32x16& p0, f32x16& p1, const char* stg, int ka, const i32x8* qf, const f32x16& minit) {
;     p0 = minit; p1 = minit;
; #pragma unroll
;     for (int s = 0; s < 3; ++s) { const char* a = stg + SOFF_K + s * 4096 + ka; const char* b = stg + SOFF_K + s * 4096 + (ka ^ 16);
;         const i32x4 a0 = *reinterpret_cast<const i32x4*>(a), a1 = *reinterpret_cast<const i32x4*>(b);
;         const i32x4 c0 = *reinterpret_cast<const i32x4*>(a + 2048), c1 = *reinterpret_cast<const i32x4*>(b + 2048);
;         p0 = __builtin_amdgcn_mfma_scale_f32_32x32x64_f8f6f4(__builtin_shufflevector(a0, a1, 0, 1, 2, 3, 4, 5, 6, 7), qf[s], p0, 0, 0, 0, 0, 0, 0);
;         p1 = __builtin_amdgcn_mfma_scale_f32_32x32x64_f8f6f4(__builtin_shufflevector(c0, c1, 0, 1, 2, 3, 4, 5, 6, 7), qf[s], p1, 0, 0, 0, 0, 0, 0); }
; }
; __device__ __forceinline__ void v_read(i32x8 (&vf)[4], const char* stg, int ka) {
; #pragma unroll
;     for (int d0 = 0; d0 < 4; ++d0) { const i32x4 a0 = *reinterpret_cast<const i32x4*>(stg + SOFF_V + d0 * 2048 + ka), a1 = *reinterpret_cast<const i32x4*>(stg + SOFF_V + d0 * 2048 + (ka ^ 16));
;         vf[d0] = __builtin_shufflevector(a0, a1, 0, 1, 2, 3, 4, 5, 6, 7); }
; }
; __device__ __forceinline__ void pv_mma(f32x16* o, f32x16& ol, const i32x8 (&vf)[4], const i32x8 ones, const i32x8 pa) {
; #pragma unroll
;     for (int d0 = 0; d0 < 4; ++d0) o[d0] = __builtin_amdgcn_mfma_scale_f32_32x32x64_f8f6f4(pa, vf[d0], o[d0], 0, 0, 0, 0, 0, 0);
;     ol = __builtin_amdgcn_mfma_scale_f32_32x32x64_f8f6f4(pa, ones, ol, 0, 0, 0, 0, 0, 0);
; }
.LBB0_667:
	s_cmp_gt_i32 s1, 4
	s_cselect_b32 s46, -5, 1
	s_add_i32 s46, s46, s1
	s_mulk_i32 s46, 0x5000
	s_add_i32 s46, s46, 0
	v_add_u32_e32 v199, s46, v193
	v_add_u32_e32 v200, s46, v194
	ds_read_b128 v[112:115], v199
	ds_read_b128 v[116:119], v200
	ds_read_b128 v[218:221], v199 offset:2048
	ds_read_b128 v[222:225], v200 offset:2048
	ds_read_b128 v[236:239], v199 offset:4096
	ds_read_b128 v[240:243], v200 offset:4096
	ds_read_b128 v[244:247], v199 offset:6144
	ds_read_b128 v[248:251], v200 offset:6144
	v_exp_f32_e32 v217, v96
	s_waitcnt lgkmcnt(6)
	v_mfma_f32_32x32x64_f8f6f4 v[128:143], v[112:119], v[168:175], v[80:95]
	v_exp_f32_e32 v97, v97
	v_exp_f32_e32 v98, v98
	v_exp_f32_e32 v99, v99
	v_exp_f32_e32 v102, v102
	v_exp_f32_e32 v104, v104
	v_exp_f32_e32 v105, v105
	v_exp_f32_e32 v108, v108
	v_exp_f32_e32 v109, v109
	v_exp_f32_e32 v106, v106
	v_exp_f32_e32 v107, v107
	v_exp_f32_e32 v110, v110
	v_exp_f32_e32 v111, v111
	s_waitcnt lgkmcnt(4)
	v_mfma_f32_32x32x64_f8f6f4 v[112:127], v[218:225], v[168:175], v[80:95]
	ds_read_b128 v[218:221], v199 offset:8192
	ds_read_b128 v[222:225], v200 offset:8192
	ds_read_b128 v[226:229], v199 offset:10240
	ds_read_b128 v[230:233], v200 offset:10240
	s_waitcnt lgkmcnt(6)
	v_mfma_f32_32x32x64_f8f6f4 v[128:143], v[236:243], v[176:183], v[128:143]
	s_waitcnt lgkmcnt(4)
	v_mfma_f32_32x32x64_f8f6f4 v[112:127], v[244:251], v[176:183], v[112:127]
	s_waitcnt lgkmcnt(2)
	v_mfma_f32_32x32x64_f8f6f4 v[128:143], v[218:225], v[160:167], v[128:143]
	v_exp_f32_e32 v218, v100
	v_exp_f32_e32 v219, v101
	v_exp_f32_e32 v220, v103
	s_nop 0
	v_cvt_pk_fp8_f32 v100, v217, v97
	v_cvt_pk_fp8_f32 v101, v218, v219
	v_cvt_pk_fp8_f32 v100, v98, v99 op_sel:[0,0,1]
	v_cvt_pk_fp8_f32 v101, v102, v220 op_sel:[0,0,1]
	s_waitcnt lgkmcnt(0)
	v_mfma_f32_32x32x64_f8f6f4 v[112:127], v[226:233], v[160:167], v[112:127]
	v_cvt_pk_fp8_f32 v96, v215, v216
	v_cvt_pk_fp8_f32 v97, v211, v212
	v_cvt_pk_fp8_f32 v98, v207, v208
	v_cvt_pk_fp8_f32 v102, v104, v105
	v_cvt_pk_fp8_f32 v99, v203, v204
	v_cvt_pk_fp8_f32 v103, v108, v109
	v_cvt_pk_fp8_f32 v96, v213, v214 op_sel:[0,0,1]
	v_cvt_pk_fp8_f32 v97, v209, v210 op_sel:[0,0,1]
	v_cvt_pk_fp8_f32 v98, v205, v206 op_sel:[0,0,1]
	v_cvt_pk_fp8_f32 v102, v106, v107 op_sel:[0,0,1]
	v_cvt_pk_fp8_f32 v99, v201, v202 op_sel:[0,0,1]
	v_cvt_pk_fp8_f32 v103, v110, v111 op_sel:[0,0,1]
	s_mul_i32 s46, s1, 0x5000
	s_add_i32 s46, s46, 0
	v_add_u32_e32 v202, s46, v194
	v_add_u32_e32 v201, s46, v193
	ds_read_b128 v[108:111], v202 offset:12288
	ds_read_b128 v[104:107], v201 offset:12288
	ds_read_b128 v[236:239], v201 offset:14336
	ds_read_b128 v[240:243], v202 offset:14336
	ds_read_b128 v[248:251], v202 offset:16384
	ds_read_b128 v[244:247], v201 offset:16384
	v_mfma_f32_32x32x64_f8f6f4 v[64:79], v[96:103], v[152:159], v[64:79]
	s_sub_i32 s46, s39, 64
	s_cmp_le_i32 s46, s0
	s_waitcnt lgkmcnt(4)
	v_mfma_f32_32x32x64_f8f6f4 v[48:63], v[96:103], v[104:111], v[48:63]
	ds_read_b128 v[104:107], v201 offset:18432
	ds_read_b128 v[108:111], v202 offset:18432
	s_waitcnt lgkmcnt(4)
	v_mfma_f32_32x32x64_f8f6f4 v[32:47], v[96:103], v[236:243], v[32:47]
	s_waitcnt lgkmcnt(2)
	v_mfma_f32_32x32x64_f8f6f4 v[16:31], v[96:103], v[244:251], v[16:31]
	s_waitcnt lgkmcnt(0)
	v_mfma_f32_32x32x64_f8f6f4 v[0:15], v[96:103], v[104:111], v[0:15]
	s_cbranch_scc1 .LBB0_669
	v_add_u32_e32 v96, 0x4000007b, v196
	v_cmp_gt_u32_e32 vcc, 2.0, v96
	v_add_u32_e32 v96, 0x5b, v196
	s_nop 0
	v_cndmask_b32_e32 v128, v187, v128, vcc
	v_cmp_lt_u32_e32 vcc, s3, v96
	v_add_u32_e32 v96, 0x7a, v196
	s_nop 0
	v_cndmask_b32_e32 v112, v187, v112, vcc
	v_cmp_lt_u32_e32 vcc, s3, v96
	v_add_u32_e32 v96, 0x5a, v196
	s_nop 0
	v_cndmask_b32_e32 v129, v187, v129, vcc
	v_cmp_lt_u32_e32 vcc, s3, v96
	v_add_u32_e32 v96, 0x79, v196
	s_nop 0
	v_cndmask_b32_e32 v113, v187, v113, vcc
	v_cmp_lt_u32_e32 vcc, s3, v96
	v_add_u32_e32 v96, 0x59, v196
	s_nop 0
	v_cndmask_b32_e32 v130, v187, v130, vcc
	v_cmp_lt_u32_e32 vcc, s3, v96
	v_add_u32_e32 v96, 0x78, v196
	s_nop 0
	v_cndmask_b32_e32 v114, v187, v114, vcc
	v_cmp_lt_u32_e32 vcc, s3, v96
	v_add_u32_e32 v96, 0x58, v196
	s_nop 0
	v_cndmask_b32_e32 v131, v187, v131, vcc
	v_cmp_lt_u32_e32 vcc, s3, v96
	v_add_u32_e32 v96, 0x73, v196
	s_nop 0
	v_cndmask_b32_e32 v115, v187, v115, vcc
	v_cmp_lt_u32_e32 vcc, s3, v96
	v_add_u32_e32 v96, 0x53, v196
	s_nop 0
	v_cndmask_b32_e32 v132, v187, v132, vcc
	v_cmp_lt_u32_e32 vcc, s3, v96
	v_add_u32_e32 v96, 0x72, v196
	s_nop 0
	v_cndmask_b32_e32 v116, v187, v116, vcc
	v_cmp_lt_u32_e32 vcc, s3, v96
	v_add_u32_e32 v96, 0x52, v196
	s_nop 0
	v_cndmask_b32_e32 v133, v187, v133, vcc
	v_cmp_lt_u32_e32 vcc, s3, v96
	v_add_u32_e32 v96, 0x71, v196
	s_nop 0
	v_cndmask_b32_e32 v117, v187, v117, vcc
	v_cmp_lt_u32_e32 vcc, s3, v96
	v_add_u32_e32 v96, 0x51, v196
	s_nop 0
	v_cndmask_b32_e32 v134, v187, v134, vcc
	v_cmp_lt_u32_e32 vcc, s3, v96
	v_add_u32_e32 v96, 0x70, v196
	s_nop 0
	v_cndmask_b32_e32 v118, v187, v118, vcc
	v_cmp_lt_u32_e32 vcc, s3, v96
	v_add_u32_e32 v96, 0x50, v196
	s_nop 0
	v_cndmask_b32_e32 v135, v187, v135, vcc
	v_cmp_lt_u32_e32 vcc, s3, v96
	v_add_u32_e32 v96, 0x6b, v196
	s_nop 0
	v_cndmask_b32_e32 v119, v187, v119, vcc
	v_cmp_lt_u32_e32 vcc, s3, v96
	v_add_u32_e32 v96, 0x4b, v196
	s_nop 0
	v_cndmask_b32_e32 v136, v187, v136, vcc
	v_cmp_lt_u32_e32 vcc, s3, v96
	v_add_u32_e32 v96, 0x6a, v196
	s_nop 0
	v_cndmask_b32_e32 v120, v187, v120, vcc
	v_cmp_lt_u32_e32 vcc, s3, v96
	v_add_u32_e32 v96, 0x4a, v196
	s_nop 0
	v_cndmask_b32_e32 v137, v187, v137, vcc
	v_cmp_lt_u32_e32 vcc, s3, v96
	v_add_u32_e32 v96, 0x69, v196
	s_nop 0
	v_cndmask_b32_e32 v121, v187, v121, vcc
	v_cmp_lt_u32_e32 vcc, s3, v96
	v_add_u32_e32 v96, 0x49, v196
	s_nop 0
	v_cndmask_b32_e32 v138, v187, v138, vcc
	v_cmp_lt_u32_e32 vcc, s3, v96
	v_add_u32_e32 v96, 0x68, v196
	s_nop 0
	v_cndmask_b32_e32 v122, v187, v122, vcc
	v_cmp_lt_u32_e32 vcc, s3, v96
	v_add_u32_e32 v96, 0x48, v196
	s_nop 0
	v_cndmask_b32_e32 v139, v187, v139, vcc
	v_cmp_lt_u32_e32 vcc, s3, v96
	v_add_u32_e32 v96, 0x63, v196
	s_nop 0
	v_cndmask_b32_e32 v123, v187, v123, vcc
	v_cmp_lt_u32_e32 vcc, s3, v96
	v_add_u32_e32 v96, 0x43, v196
	s_nop 0
	v_cndmask_b32_e32 v140, v187, v140, vcc
	v_cmp_lt_u32_e32 vcc, s3, v96
	v_add_u32_e32 v96, 0x62, v196
	s_nop 0
	v_cndmask_b32_e32 v124, v187, v124, vcc
	v_cmp_lt_u32_e32 vcc, s3, v96
	v_add_u32_e32 v96, 0x42, v196
	s_nop 0
	v_cndmask_b32_e32 v141, v187, v141, vcc
	v_cmp_lt_u32_e32 vcc, s3, v96
	v_add_u32_e32 v96, 0x61, v196
	s_nop 0
	v_cndmask_b32_e32 v125, v187, v125, vcc
	v_cmp_lt_u32_e32 vcc, s3, v96
	v_add_u32_e32 v96, 0x41, v196
	s_nop 0
	v_cndmask_b32_e32 v142, v187, v142, vcc
	v_cmp_lt_u32_e32 vcc, s3, v96
	v_add_u32_e32 v96, 0x60, v196
	s_nop 0
	v_cndmask_b32_e32 v126, v187, v126, vcc
	v_cmp_lt_u32_e32 vcc, s3, v96
	v_add_u32_e32 v96, 64, v196
	s_nop 0
	v_cndmask_b32_e32 v143, v187, v143, vcc
	v_cmp_lt_u32_e32 vcc, s3, v96
	s_nop 1
	v_cndmask_b32_e32 v127, v187, v127, vcc

; template <bool FIRST>
; __device__ __forceinline__ bool partialSM(f32x16& p0, f32x16& p1, float& M, f32x16& minit, float& alpha) {
;     ...
;     for (int r = 0; r < 16; ++r) p0[r] = __builtin_amdgcn_exp2f(p0[r]);
;     return moved;
; }
; __device__ __forceinline__ void finishSM(f32x16& p0, f32x16& p1, i32x8& pa) {
;     for (int r = 0; r < 16; ++r) p1[r] = __builtin_amdgcn_exp2f(p1[r]);
; #pragma unroll
;     for (int v = 0; v < 4; ++v) { pa[v] = (int)cvt_pk4_fp8(p0[4 * v], p0[4 * v + 1], p0[4 * v + 2], p0[4 * v + 3]); pa[4 + v] = (int)cvt_pk4_fp8(p1[4 * v], p1[4 * v + 1], p1[4 * v + 2], p1[4 * v + 3]); }
; }
; __device__ __forceinline__ void qkt(f32x16& p0, f32x16& p1, const char* stg, int ka, const i32x8* qf, const f32x16& minit) {
;     p0 = minit; p1 = minit;
; #pragma unroll
;     for (int s = 0; s < 3; ++s) { const char* a = stg + SOFF_K + s * 4096 + ka; const char* b = stg + SOFF_K + s * 4096 + (ka ^ 16);
;         const i32x4 a0 = *reinterpret_cast<const i32x4*>(a), a1 = *reinterpret_cast<const i32x4*>(b);
;         const i32x4 c0 = *reinterpret_cast<const i32x4*>(a + 2048), c1 = *reinterpret_cast<const i32x4*>(b + 2048);
;         p0 = __builtin_amdgcn_mfma_scale_f32_32x32x64_f8f6f4(__builtin_shufflevector(a0, a1, 0, 1, 2, 3, 4, 5, 6, 7), qf[s], p0, 0, 0, 0, 0, 0, 0);
;         p1 = __builtin_amdgcn_mfma_scale_f32_32x32x64_f8f6f4(__builtin_shufflevector(c0, c1, 0, 1, 2, 3, 4, 5, 6, 7), qf[s], p1, 0, 0, 0, 0, 0, 0); }
; }
; __device__ __forceinline__ void v_read(i32x8 (&vf)[4], const char* stg, int ka) {
; #pragma unroll
;     for (int d0 = 0; d0 < 4; ++d0) { const i32x4 a0 = *reinterpret_cast<const i32x4*>(stg + SOFF_V + d0 * 2048 + ka), a1 = *reinterpret_cast<const i32x4*>(stg + SOFF_V + d0 * 2048 + (ka ^ 16));
;         vf[d0] = __builtin_shufflevector(a0, a1, 0, 1, 2, 3, 4, 5, 6, 7); }
; }
; __device__ __forceinline__ void pv_mma(f32x16* o, f32x16& ol, const i32x8 (&vf)[4], const i32x8 ones, const i32x8 pa) {
; #pragma unroll
;     for (int d0 = 0; d0 < 4; ++d0) o[d0] = __builtin_amdgcn_mfma_scale_f32_32x32x64_f8f6f4(pa, vf[d0], o[d0], 0, 0, 0, 0, 0, 0);
;     ol = __builtin_amdgcn_mfma_scale_f32_32x32x64_f8f6f4(pa, ones, ol, 0, 0, 0, 0, 0, 0);
; }
.LBB0_674:
	s_cmp_gt_i32 s1, 3
	s_cselect_b32 s46, -4, 2
	s_add_i32 s1, s46, s1
	v_exp_f32_e32 v201, v128
	v_exp_f32_e32 v218, v129
	v_exp_f32_e32 v219, v130
	v_exp_f32_e32 v220, v131
	v_exp_f32_e32 v221, v132
	v_exp_f32_e32 v222, v133
	v_exp_f32_e32 v223, v134
	v_exp_f32_e32 v224, v135
	v_exp_f32_e32 v225, v136
	v_exp_f32_e32 v226, v137
	v_exp_f32_e32 v227, v138
	v_exp_f32_e32 v228, v139
	v_exp_f32_e32 v229, v140
	v_exp_f32_e32 v230, v141
	v_exp_f32_e32 v231, v142
	v_exp_f32_e32 v232, v143
	s_mul_i32 s92, s1, 0x5000
	s_add_i32 s46, s92, 0
	v_add_u32_e32 v233, s46, v193
	v_add_u32_e32 v234, s46, v194
	ds_read_b128 v[202:205], v233
	ds_read_b128 v[206:209], v234
	ds_read_b128 v[210:213], v233 offset:2048
	ds_read_b128 v[214:217], v234 offset:2048
	ds_read_b128 v[236:239], v233 offset:4096
	ds_read_b128 v[240:243], v234 offset:4096
	ds_read_b128 v[244:247], v233 offset:6144
	ds_read_b128 v[248:251], v234 offset:6144
	v_exp_f32_e32 v113, v113
	s_waitcnt lgkmcnt(6)
	v_mfma_f32_32x32x64_f8f6f4 v[128:143], v[202:209], v[168:175], v[96:111]
	v_exp_f32_e32 v114, v114
	v_exp_f32_e32 v115, v115
	v_exp_f32_e32 v118, v118
	v_exp_f32_e32 v120, v120
	v_exp_f32_e32 v121, v121
	v_exp_f32_e32 v124, v124
	v_exp_f32_e32 v125, v125
	v_exp_f32_e32 v122, v122
	v_exp_f32_e32 v123, v123
	v_exp_f32_e32 v126, v126
	v_exp_f32_e32 v127, v127
	s_waitcnt lgkmcnt(4)
	v_mfma_f32_32x32x64_f8f6f4 v[96:111], v[210:217], v[168:175], v[96:111]
	ds_read_b128 v[202:205], v233 offset:8192
	ds_read_b128 v[206:209], v234 offset:8192
	ds_read_b128 v[210:213], v233 offset:10240
	ds_read_b128 v[214:217], v234 offset:10240
	s_waitcnt lgkmcnt(6)
	v_mfma_f32_32x32x64_f8f6f4 v[128:143], v[236:243], v[176:183], v[128:143]
	s_waitcnt lgkmcnt(4)
	v_mfma_f32_32x32x64_f8f6f4 v[96:111], v[244:251], v[176:183], v[96:111]
	s_waitcnt lgkmcnt(2)
	v_mfma_f32_32x32x64_f8f6f4 v[128:143], v[202:209], v[160:167], v[128:143]
	v_exp_f32_e32 v202, v112
	v_exp_f32_e32 v203, v116
	v_exp_f32_e32 v204, v117
	v_exp_f32_e32 v205, v119
	s_nop 0
	v_cvt_pk_fp8_f32 v116, v202, v113
	v_cvt_pk_fp8_f32 v117, v203, v204
	v_cvt_pk_fp8_f32 v116, v114, v115 op_sel:[0,0,1]
	v_cvt_pk_fp8_f32 v117, v118, v205 op_sel:[0,0,1]
	s_waitcnt lgkmcnt(0)
	v_mfma_f32_32x32x64_f8f6f4 v[96:111], v[210:217], v[160:167], v[96:111]
	v_cvt_pk_fp8_f32 v112, v201, v218
	v_cvt_pk_fp8_f32 v113, v221, v222
	v_cvt_pk_fp8_f32 v114, v225, v226
	v_cvt_pk_fp8_f32 v118, v120, v121
	v_cvt_pk_fp8_f32 v115, v229, v230
	v_cvt_pk_fp8_f32 v119, v124, v125
	v_cvt_pk_fp8_f32 v112, v219, v220 op_sel:[0,0,1]
	v_cvt_pk_fp8_f32 v113, v223, v224 op_sel:[0,0,1]
	v_cvt_pk_fp8_f32 v114, v227, v228 op_sel:[0,0,1]
	v_cvt_pk_fp8_f32 v118, v122, v123 op_sel:[0,0,1]
	v_cvt_pk_fp8_f32 v115, v231, v232 op_sel:[0,0,1]
	v_cvt_pk_fp8_f32 v119, v126, v127 op_sel:[0,0,1]
	ds_read_b128 v[124:127], v200 offset:12288
	ds_read_b128 v[120:123], v199 offset:12288
	ds_read_b128 v[236:239], v199 offset:14336
	ds_read_b128 v[240:243], v200 offset:14336
	ds_read_b128 v[248:251], v200 offset:16384
	ds_read_b128 v[244:247], v199 offset:16384
	v_mfma_f32_32x32x64_f8f6f4 v[64:79], v[112:119], v[152:159], v[64:79]
	s_cmp_le_i32 s39, s0
	s_waitcnt lgkmcnt(4)
	v_mfma_f32_32x32x64_f8f6f4 v[48:63], v[112:119], v[120:127], v[48:63]
	ds_read_b128 v[120:123], v199 offset:18432
	ds_read_b128 v[124:127], v200 offset:18432
	s_waitcnt lgkmcnt(4)
	v_mfma_f32_32x32x64_f8f6f4 v[32:47], v[112:119], v[236:243], v[32:47]
	s_waitcnt lgkmcnt(2)
	v_mfma_f32_32x32x64_f8f6f4 v[16:31], v[112:119], v[244:251], v[16:31]
	s_waitcnt lgkmcnt(0)
	v_mfma_f32_32x32x64_f8f6f4 v[0:15], v[112:119], v[120:127], v[0:15]
	s_cbranch_scc1 .LBB0_676
; __device__ __forceinline__ void mask_tile(f32x16& p0, f32x16& p1, int dq, unsigned W) {
;     const float NEG = -__builtin_inff();
; #pragma unroll
;     for (int r = 0; r < 16; ++r) {
;         const int c = (r & 3) + 8 * (r >> 2);
;         if ((unsigned)(dq - c) >= W) p0[r] = NEG;
;         if ((unsigned)(dq - c - 32) >= W) p1[r] = NEG;
;     }
; }
	v_add_u32_e32 v112, 0x4000003b, v196
	v_cmp_gt_u32_e32 vcc, 2.0, v112
	v_add_u32_e32 v112, 27, v196
	s_nop 0
	v_cndmask_b32_e32 v128, v187, v128, vcc
	v_cmp_lt_u32_e32 vcc, s3, v112
	v_add_u32_e32 v112, 58, v196
	s_nop 0
	v_cndmask_b32_e32 v96, v187, v96, vcc
	v_cmp_lt_u32_e32 vcc, s3, v112
	v_add_u32_e32 v112, 26, v196
	s_nop 0
	v_cndmask_b32_e32 v129, v187, v129, vcc
	v_cmp_lt_u32_e32 vcc, s3, v112
	v_add_u32_e32 v112, 57, v196
	s_nop 0
	v_cndmask_b32_e32 v97, v187, v97, vcc
	v_cmp_lt_u32_e32 vcc, s3, v112
	v_add_u32_e32 v112, 25, v196
	s_nop 0
	v_cndmask_b32_e32 v130, v187, v130, vcc
	v_cmp_lt_u32_e32 vcc, s3, v112
	v_add_u32_e32 v112, 56, v196
	s_nop 0
	v_cndmask_b32_e32 v98, v187, v98, vcc
	v_cmp_lt_u32_e32 vcc, s3, v112
	v_add_u32_e32 v112, 24, v196
	s_nop 0
	v_cndmask_b32_e32 v131, v187, v131, vcc
	v_cmp_lt_u32_e32 vcc, s3, v112
	v_add_u32_e32 v112, 51, v196
	s_nop 0
	v_cndmask_b32_e32 v99, v187, v99, vcc
	v_cmp_lt_u32_e32 vcc, s3, v112
	v_add_u32_e32 v112, 19, v196
	s_nop 0
	v_cndmask_b32_e32 v132, v187, v132, vcc
	v_cmp_lt_u32_e32 vcc, s3, v112
	v_add_u32_e32 v112, 50, v196
	s_nop 0
	v_cndmask_b32_e32 v100, v187, v100, vcc
	v_cmp_lt_u32_e32 vcc, s3, v112
	v_add_u32_e32 v112, 18, v196
	s_nop 0
	v_cndmask_b32_e32 v133, v187, v133, vcc
	v_cmp_lt_u32_e32 vcc, s3, v112
	v_add_u32_e32 v112, 49, v196
	s_nop 0
	v_cndmask_b32_e32 v101, v187, v101, vcc
	v_cmp_lt_u32_e32 vcc, s3, v112
	v_add_u32_e32 v112, 17, v196
	s_nop 0
	v_cndmask_b32_e32 v134, v187, v134, vcc
	v_cmp_lt_u32_e32 vcc, s3, v112
	v_add_u32_e32 v112, 48, v196
	s_nop 0
	v_cndmask_b32_e32 v102, v187, v102, vcc
	v_cmp_lt_u32_e32 vcc, s3, v112
	v_add_u32_e32 v112, 16, v196
	s_nop 0
	v_cndmask_b32_e32 v135, v187, v135, vcc
	v_cmp_lt_u32_e32 vcc, s3, v112
	v_add_u32_e32 v112, 43, v196
	s_nop 0
	v_cndmask_b32_e32 v103, v187, v103, vcc
	v_cmp_lt_u32_e32 vcc, s3, v112
	v_add_u32_e32 v112, 11, v196
	s_nop 0
	v_cndmask_b32_e32 v136, v187, v136, vcc
	v_cmp_lt_u32_e32 vcc, s3, v112
	v_add_u32_e32 v112, 42, v196
	s_nop 0
	v_cndmask_b32_e32 v104, v187, v104, vcc
	v_cmp_lt_u32_e32 vcc, s3, v112
	v_add_u32_e32 v112, 10, v196
	s_nop 0
	v_cndmask_b32_e32 v137, v187, v137, vcc
	v_cmp_lt_u32_e32 vcc, s3, v112
	v_add_u32_e32 v112, 41, v196
	s_nop 0
	v_cndmask_b32_e32 v105, v187, v105, vcc
	v_cmp_lt_u32_e32 vcc, s3, v112
	v_add_u32_e32 v112, 9, v196
	s_nop 0
	v_cndmask_b32_e32 v138, v187, v138, vcc
	v_cmp_lt_u32_e32 vcc, s3, v112
	v_add_u32_e32 v112, 40, v196
	s_nop 0
	v_cndmask_b32_e32 v106, v187, v106, vcc
	v_cmp_lt_u32_e32 vcc, s3, v112
	v_add_u32_e32 v112, 8, v196
	s_nop 0
	v_cndmask_b32_e32 v139, v187, v139, vcc
	v_cmp_lt_u32_e32 vcc, s3, v112
	v_add_u32_e32 v112, 35, v196
	s_nop 0
	v_cndmask_b32_e32 v107, v187, v107, vcc
	v_cmp_lt_u32_e32 vcc, s3, v112
	v_add_u32_e32 v112, 3, v196
	s_nop 0
	v_cndmask_b32_e32 v140, v187, v140, vcc
	v_cmp_lt_u32_e32 vcc, s3, v112
	v_add_u32_e32 v112, 34, v196
	s_nop 0
	v_cndmask_b32_e32 v108, v187, v108, vcc
	v_cmp_lt_u32_e32 vcc, s3, v112
	v_add_u32_e32 v112, 2, v196
	s_nop 0
	v_cndmask_b32_e32 v141, v187, v141, vcc
	v_cmp_lt_u32_e32 vcc, s3, v112
	v_add_u32_e32 v112, 33, v196
	s_nop 0
	v_cndmask_b32_e32 v109, v187, v109, vcc
	v_cmp_lt_u32_e32 vcc, s3, v112
	v_add_u32_e32 v112, 1, v196
	s_nop 0
	v_cndmask_b32_e32 v142, v187, v142, vcc
	v_cmp_lt_u32_e32 vcc, s3, v112
	v_add_u32_e32 v112, 32, v196
	s_nop 0
	v_cndmask_b32_e32 v110, v187, v110, vcc
	v_cmp_lt_u32_e32 vcc, s3, v112
	s_nop 1
	v_cndmask_b32_e32 v143, v187, v143, vcc
	v_cmp_lt_u32_e32 vcc, s3, v196
	s_nop 1
	v_cndmask_b32_e32 v111, v187, v111, vcc

; #define GAS __attribute__((address_space(1)))
; __device__ __forceinline__ unsigned cvt_pk_bf16(float lo, float hi) { unsigned r; asm volatile("v_cvt_pk_bf16_f32 %0, %1, %2" : "=v"(r) : "v"(lo), "v"(hi)); return r; }
; #define SBAR() __builtin_amdgcn_sched_barrier(0)
; __device__ __forceinline__ gptr uni(const GAS void* p) { const unsigned long long v = (unsigned long long)p; const unsigned lo = __builtin_amdgcn_readfirstlane((unsigned)v), hi = __builtin_amdgcn_readfirstlane((unsigned)(v >> 32)); return (gptr)(((unsigned long long)hi << 32) | lo); }
; #define QLOAD(ref) do { gptr qb_ = uni((const GAS void*)((ref).Q + (size_t)(wid * QBLK) * QS)); _Pragma("unroll") for (int d0 = 0; d0 < NQR; ++d0) S.qr[d0] = *reinterpret_cast<const GAS u32x2*>(qb_ + d0 * 16 + voff_q); } while (0)
; template <int AV>
; __device__ __forceinline__ void block(const BlockRef& cur, const BlockRef& nxt, char* lds, Seam& S, const int wid, const QNorm& QN) {
;     ...
;     SBAR(); QLOAD(nxt); v_read(vf, STGP(sc), ka); SBAR();
;     finishSM(pB0, pB1, pa); SBAR();
;     pv_mma(o, ol, vf, ones, pa);
;     S.g = INC6(sc, 1);
;     __builtin_amdgcn_s_setprio(0);
;     float rli[16];
; #pragma unroll
;     for (int r = 0; r < 16; ++r) rli[r] = __builtin_amdgcn_rcpf(ol[r]);
;     GAS char* Ow = (GAS char*)uni((const GAS void*)(cur.O + (size_t)(wid * QBLK) * OS));
;     const bool odd = (r32 & 1) != 0;
;     const unsigned voff_o = (unsigned)((4 * hi + (odd ? 1 : 0)) * OS + (r32 & ~1)) * 2u;
; #pragma unroll
;     for (int r = 0; r < 16; r += 2) { const int orow0 = (r & 3) + 8 * (r >> 2);
; #pragma unroll
;         for (int d0 = 0; d0 < 4; ++d0) { const float a = o[d0][r] * rli[r], b = o[d0][r + 1] * rli[r + 1];
;             const float send = odd ? a : b;
;             const float recv = __int_as_float(__builtin_amdgcn_mov_dpp(__float_as_int(send), 0xB1, 0xF, 0xF, true));
;             *(GAS unsigned*)(Ow + (size_t)orow0 * OS * 2 + d0 * 64 + voff_o) = cvt_pk_bf16(odd ? recv : a, odd ? b : recv); } }
.LBB0_710:
	s_add_u32 s6, s64, s95
	s_addc_u32 s7, s65, s11
	v_lshl_add_u64 v[80:81], s[6:7], 0, v[184:185]
	global_load_dwordx2 v[86:87], v[80:81], off
	global_load_dwordx2 v[84:85], v[80:81], off offset:16
	global_load_dwordx2 v[82:83], v[80:81], off offset:32
	s_nop 0
	global_load_dwordx2 v[80:81], v[80:81], off offset:48
	ds_read_b128 v[88:91], v202 offset:12288
	ds_read_b128 v[112:115], v202 offset:14336
	ds_read_b128 v[92:95], v201 offset:12288
	ds_read_b128 v[116:119], v201 offset:14336
	ds_read_b128 v[120:123], v202 offset:16384
	ds_read_b128 v[128:131], v202 offset:18432
	ds_read_b128 v[124:127], v201 offset:16384
	ds_read_b128 v[132:135], v201 offset:18432
	v_exp_f32_e32 v136, v96
	v_exp_f32_e32 v97, v97
	v_exp_f32_e32 v137, v100
	v_exp_f32_e32 v138, v101
	v_exp_f32_e32 v139, v103
	v_exp_f32_e32 v98, v98
	v_exp_f32_e32 v99, v99
	v_exp_f32_e32 v102, v102
	v_cvt_pk_fp8_f32 v100, v136, v97
	v_cvt_pk_fp8_f32 v101, v137, v138
	v_exp_f32_e32 v104, v104
	v_exp_f32_e32 v105, v105
	v_exp_f32_e32 v108, v108
	v_exp_f32_e32 v109, v109
	v_cvt_pk_fp8_f32 v100, v98, v99 op_sel:[0,0,1]
	v_cvt_pk_fp8_f32 v101, v102, v139 op_sel:[0,0,1]
	v_exp_f32_e32 v106, v106
	v_exp_f32_e32 v107, v107
	v_exp_f32_e32 v110, v110
	v_exp_f32_e32 v111, v111
	v_cvt_pk_fp8_f32 v96, v217, v218
	v_cvt_pk_fp8_f32 v97, v213, v214
	v_cvt_pk_fp8_f32 v98, v209, v210
	v_cvt_pk_fp8_f32 v102, v104, v105
	v_cvt_pk_fp8_f32 v99, v205, v206
	v_cvt_pk_fp8_f32 v103, v108, v109
	v_cvt_pk_fp8_f32 v96, v215, v216 op_sel:[0,0,1]
	v_cvt_pk_fp8_f32 v97, v211, v212 op_sel:[0,0,1]
	v_cvt_pk_fp8_f32 v98, v207, v208 op_sel:[0,0,1]
	v_cvt_pk_fp8_f32 v102, v106, v107 op_sel:[0,0,1]
	v_cvt_pk_fp8_f32 v99, v203, v204 op_sel:[0,0,1]
	v_cvt_pk_fp8_f32 v103, v110, v111 op_sel:[0,0,1]
	s_cmp_gt_i32 s0, 4
	s_cselect_b32 s1, -5, 1
	s_add_i32 s0, s1, s0
	s_waitcnt lgkmcnt(5)
	v_mfma_f32_32x32x64_f8f6f4 v[48:63], v[96:103], v[88:95], v[48:63]
	s_waitcnt lgkmcnt(4)
	v_mfma_f32_32x32x64_f8f6f4 v[0:15], v[96:103], v[112:119], v[0:15]
	s_waitcnt lgkmcnt(1)
	v_mfma_f32_32x32x64_f8f6f4 v[32:47], v[96:103], v[120:127], v[32:47]
	s_waitcnt lgkmcnt(0)
	v_mfma_f32_32x32x64_f8f6f4 v[16:31], v[96:103], v[128:135], v[16:31]
	v_mfma_f32_32x32x64_f8f6f4 v[64:79], v[96:103], v[152:159], v[64:79]
	s_setprio 0
	s_nop 15
	s_nop 2
	v_rcp_f32_e32 v88, v64
	v_rcp_f32_e32 v89, v65
	v_and_b32_e32 v90, 1, v188
	v_cmp_eq_u32_e32 vcc, 0, v90
	v_mul_f32_e32 v48, v48, v88
	v_mul_f32_e32 v49, v49, v89
	v_or_b32_e32 v64, v195, v90
	v_cndmask_b32_e32 v90, v48, v49, vcc
	v_lshlrev_b32_e32 v65, 1, v188
	s_add_u32 s6, s76, s60
	v_mov_b32_dpp v90, v90 quad_perm:[1,0,3,2] row_mask:0xf bank_mask:0xf bound_ctrl:1
	v_and_b32_e32 v65, 60, v65
	v_cndmask_b32_e32 v48, v90, v48, vcc
	s_addc_u32 s7, s77, s61
	v_lshl_or_b32 v184, v64, 12, v65
	v_cndmask_b32_e32 v49, v49, v90, vcc
	v_cvt_pk_bf16_f32 v48, v48, v49
	v_mul_f32_e32 v0, v0, v88
	v_mul_f32_e32 v1, v1, v89
	global_store_dword v184, v48, s[6:7]
	v_cndmask_b32_e32 v48, v0, v1, vcc
	v_rcp_f32_e32 v66, v66
	v_rcp_f32_e32 v67, v67
	v_mov_b32_dpp v48, v48 quad_perm:[1,0,3,2] row_mask:0xf bank_mask:0xf bound_ctrl:1
	v_cndmask_b32_e32 v0, v48, v0, vcc
	v_cndmask_b32_e32 v1, v1, v48, vcc
	v_cvt_pk_bf16_f32 v0, v0, v1
	global_store_dword v184, v0, s[6:7] offset:64
	v_mul_f32_e32 v0, v32, v88
	v_mul_f32_e32 v1, v33, v89
	v_cndmask_b32_e32 v32, v0, v1, vcc
	v_lshl_add_u64 v[64:65], s[6:7], 0, v[184:185]
	s_movk_i32 s1, 0x2000
	v_mov_b32_dpp v32, v32 quad_perm:[1,0,3,2] row_mask:0xf bank_mask:0xf bound_ctrl:1
	v_cndmask_b32_e32 v0, v32, v0, vcc
	v_cndmask_b32_e32 v1, v1, v32, vcc
	v_cvt_pk_bf16_f32 v0, v0, v1
	global_store_dword v184, v0, s[6:7] offset:128
	v_mul_f32_e32 v0, v16, v88
	v_mul_f32_e32 v1, v17, v89
	v_cndmask_b32_e32 v16, v0, v1, vcc
	v_mul_f32_e32 v2, v2, v66
	v_mul_f32_e32 v3, v3, v67
	v_mov_b32_dpp v16, v16 quad_perm:[1,0,3,2] row_mask:0xf bank_mask:0xf bound_ctrl:1
	v_cndmask_b32_e32 v0, v16, v0, vcc
	v_cndmask_b32_e32 v1, v1, v16, vcc
	v_cvt_pk_bf16_f32 v0, v0, v1
	global_store_dword v184, v0, s[6:7] offset:192
	v_mul_f32_e32 v0, v50, v66
	v_mul_f32_e32 v1, v51, v67
	v_cndmask_b32_e32 v16, v0, v1, vcc
	v_rcp_f32_e32 v68, v68
	v_rcp_f32_e32 v69, v69
	v_mov_b32_dpp v16, v16 quad_perm:[1,0,3,2] row_mask:0xf bank_mask:0xf bound_ctrl:1
	v_cndmask_b32_e32 v0, v16, v0, vcc
	v_cndmask_b32_e32 v1, v1, v16, vcc
	v_cvt_pk_bf16_f32 v16, v0, v1
	v_add_co_u32_e64 v0, s[6:7], s1, v64
	s_mov_b32 s1, 0x8000
	s_nop 0
	v_addc_co_u32_e64 v1, s[6:7], 0, v65, s[6:7]
	global_store_dword v[0:1], v16, off
	v_cndmask_b32_e32 v16, v2, v3, vcc
	v_rcp_f32_e32 v70, v70
	v_rcp_f32_e32 v71, v71
	v_mov_b32_dpp v16, v16 quad_perm:[1,0,3,2] row_mask:0xf bank_mask:0xf bound_ctrl:1
	v_cndmask_b32_e32 v2, v16, v2, vcc
	v_cndmask_b32_e32 v3, v3, v16, vcc
	v_cvt_pk_bf16_f32 v2, v2, v3
	global_store_dword v[0:1], v2, off offset:64
	v_mul_f32_e32 v2, v34, v66
	v_mul_f32_e32 v3, v35, v67
	v_cndmask_b32_e32 v16, v2, v3, vcc
	v_rcp_f32_e32 v72, v72
	v_rcp_f32_e32 v73, v73
	v_mov_b32_dpp v16, v16 quad_perm:[1,0,3,2] row_mask:0xf bank_mask:0xf bound_ctrl:1
	v_cndmask_b32_e32 v2, v16, v2, vcc
	v_cndmask_b32_e32 v3, v3, v16, vcc
	v_cvt_pk_bf16_f32 v2, v2, v3
	global_store_dword v[0:1], v2, off offset:128
	v_mul_f32_e32 v2, v18, v66
	v_mul_f32_e32 v3, v19, v67
	v_cndmask_b32_e32 v16, v2, v3, vcc
	v_rcp_f32_e32 v74, v74
	v_rcp_f32_e32 v75, v75
	v_mov_b32_dpp v16, v16 quad_perm:[1,0,3,2] row_mask:0xf bank_mask:0xf bound_ctrl:1
	v_cndmask_b32_e32 v2, v16, v2, vcc
	v_cndmask_b32_e32 v3, v3, v16, vcc
	v_cvt_pk_bf16_f32 v2, v2, v3
	global_store_dword v[0:1], v2, off offset:192
	v_mul_f32_e32 v0, v52, v68
	v_mul_f32_e32 v1, v53, v69
; #define GAS __attribute__((address_space(1)))
; __device__ __forceinline__ unsigned cvt_pk_bf16(float lo, float hi) { unsigned r; asm volatile("v_cvt_pk_bf16_f32 %0, %1, %2" : "=v"(r) : "v"(lo), "v"(hi)); return r; }
; __device__ __forceinline__ gptr uni(const GAS void* p) { const unsigned long long v = (unsigned long long)p; const unsigned lo = __builtin_amdgcn_readfirstlane((unsigned)v), hi = __builtin_amdgcn_readfirstlane((unsigned)(v >> 32)); return (gptr)(((unsigned long long)hi << 32) | lo); }
; template <int AV>
; __device__ __forceinline__ void block(const BlockRef& cur, const BlockRef& nxt, char* lds, Seam& S, const int wid, const QNorm& QN) {
;     ...
;     float rli[16];
; #pragma unroll
;     for (int r = 0; r < 16; ++r) rli[r] = __builtin_amdgcn_rcpf(ol[r]);
;     GAS char* Ow = (GAS char*)uni((const GAS void*)(cur.O + (size_t)(wid * QBLK) * OS));
;     const bool odd = (r32 & 1) != 0;
;     const unsigned voff_o = (unsigned)((4 * hi + (odd ? 1 : 0)) * OS + (r32 & ~1)) * 2u;
; #pragma unroll
;     for (int r = 0; r < 16; r += 2) { const int orow0 = (r & 3) + 8 * (r >> 2);
; #pragma unroll
;         for (int d0 = 0; d0 < 4; ++d0) { const float a = o[d0][r] * rli[r], b = o[d0][r + 1] * rli[r + 1];
;             const float send = odd ? a : b;
;             const float recv = __int_as_float(__builtin_amdgcn_mov_dpp(__float_as_int(send), 0xB1, 0xF, 0xF, true));
;             *(GAS unsigned*)(Ow + (size_t)orow0 * OS * 2 + d0 * 64 + voff_o) = cvt_pk_bf16(odd ? recv : a, odd ? b : recv); } }
	v_cndmask_b32_e32 v2, v0, v1, vcc
	v_mul_f32_e32 v3, v5, v69
	v_rcp_f32_e32 v76, v76
	v_mov_b32_dpp v2, v2 quad_perm:[1,0,3,2] row_mask:0xf bank_mask:0xf bound_ctrl:1
	v_cndmask_b32_e32 v0, v2, v0, vcc
	v_cndmask_b32_e32 v1, v1, v2, vcc
	v_cvt_pk_bf16_f32 v2, v0, v1
	v_add_co_u32_e64 v0, s[6:7], s1, v64
	s_mov_b32 s1, 0xa000
	s_nop 0
	v_addc_co_u32_e64 v1, s[6:7], 0, v65, s[6:7]
	global_store_dword v[0:1], v2, off
	v_mul_f32_e32 v2, v4, v68
	v_cndmask_b32_e32 v4, v2, v3, vcc
	v_rcp_f32_e32 v77, v77
	v_rcp_f32_e32 v78, v78
	v_mov_b32_dpp v4, v4 quad_perm:[1,0,3,2] row_mask:0xf bank_mask:0xf bound_ctrl:1
	v_cndmask_b32_e32 v2, v4, v2, vcc
	v_cndmask_b32_e32 v3, v3, v4, vcc
	v_cvt_pk_bf16_f32 v2, v2, v3
	global_store_dword v[0:1], v2, off offset:64
	v_mul_f32_e32 v2, v36, v68
	v_mul_f32_e32 v3, v37, v69
	v_cndmask_b32_e32 v4, v2, v3, vcc
	v_rcp_f32_e32 v79, v79
	s_mov_b32 s35, s54
	v_mov_b32_dpp v4, v4 quad_perm:[1,0,3,2] row_mask:0xf bank_mask:0xf bound_ctrl:1
	v_cndmask_b32_e32 v2, v4, v2, vcc
	v_cndmask_b32_e32 v3, v3, v4, vcc
	v_cvt_pk_bf16_f32 v2, v2, v3
	global_store_dword v[0:1], v2, off offset:128
	v_mul_f32_e32 v2, v20, v68
	v_mul_f32_e32 v3, v21, v69
	v_cndmask_b32_e32 v4, v2, v3, vcc
	s_mov_b64 s[76:77], s[68:69]
	s_mov_b64 s[82:83], s[74:75]
	v_mov_b32_dpp v4, v4 quad_perm:[1,0,3,2] row_mask:0xf bank_mask:0xf bound_ctrl:1
	v_cndmask_b32_e32 v2, v4, v2, vcc
	v_cndmask_b32_e32 v3, v3, v4, vcc
	v_cvt_pk_bf16_f32 v2, v2, v3
	global_store_dword v[0:1], v2, off offset:192
	v_mul_f32_e32 v0, v54, v70
	v_mul_f32_e32 v1, v55, v71
	v_cndmask_b32_e32 v2, v0, v1, vcc
	v_mul_f32_e32 v3, v7, v71
	s_mov_b64 s[80:81], s[72:73]
	v_mov_b32_dpp v2, v2 quad_perm:[1,0,3,2] row_mask:0xf bank_mask:0xf bound_ctrl:1
	v_cndmask_b32_e32 v0, v2, v0, vcc
	v_cndmask_b32_e32 v1, v1, v2, vcc
	v_cvt_pk_bf16_f32 v2, v0, v1
	v_add_co_u32_e64 v0, s[6:7], s1, v64
	s_mov_b32 s1, 0x10000
	s_nop 0
	v_addc_co_u32_e64 v1, s[6:7], 0, v65, s[6:7]
	global_store_dword v[0:1], v2, off
	v_mul_f32_e32 v2, v6, v70
	v_cndmask_b32_e32 v4, v2, v3, vcc
	s_mov_b64 s[78:79], s[70:71]
	v_readlane_b32 s84, v252, 28
	v_mov_b32_dpp v4, v4 quad_perm:[1,0,3,2] row_mask:0xf bank_mask:0xf bound_ctrl:1
	v_cndmask_b32_e32 v2, v4, v2, vcc
	v_cndmask_b32_e32 v3, v3, v4, vcc
	v_cvt_pk_bf16_f32 v2, v2, v3
	global_store_dword v[0:1], v2, off offset:64
	v_mul_f32_e32 v2, v38, v70
	v_mul_f32_e32 v3, v39, v71
	v_cndmask_b32_e32 v4, v2, v3, vcc
	s_nop 1
	v_mov_b32_dpp v4, v4 quad_perm:[1,0,3,2] row_mask:0xf bank_mask:0xf bound_ctrl:1
	v_cndmask_b32_e32 v2, v4, v2, vcc
	v_cndmask_b32_e32 v3, v3, v4, vcc
	v_cvt_pk_bf16_f32 v2, v2, v3
	global_store_dword v[0:1], v2, off offset:128
	v_mul_f32_e32 v2, v22, v70
	v_mul_f32_e32 v3, v23, v71
	v_cndmask_b32_e32 v4, v2, v3, vcc
	s_nop 1
	v_mov_b32_dpp v4, v4 quad_perm:[1,0,3,2] row_mask:0xf bank_mask:0xf bound_ctrl:1
	v_cndmask_b32_e32 v2, v4, v2, vcc
	v_cndmask_b32_e32 v3, v3, v4, vcc
	v_cvt_pk_bf16_f32 v2, v2, v3
	global_store_dword v[0:1], v2, off offset:192
	v_mul_f32_e32 v0, v56, v72
	v_mul_f32_e32 v1, v57, v73
	v_cndmask_b32_e32 v2, v0, v1, vcc
	v_mul_f32_e32 v3, v9, v73
	s_nop 0
	v_mov_b32_dpp v2, v2 quad_perm:[1,0,3,2] row_mask:0xf bank_mask:0xf bound_ctrl:1
	v_cndmask_b32_e32 v0, v2, v0, vcc
	v_cndmask_b32_e32 v1, v1, v2, vcc
	v_cvt_pk_bf16_f32 v2, v0, v1
	v_add_co_u32_e64 v0, s[6:7], s1, v64
	s_mov_b32 s1, 0x12000
	s_nop 0
	v_addc_co_u32_e64 v1, s[6:7], 0, v65, s[6:7]
	global_store_dword v[0:1], v2, off
	v_mul_f32_e32 v2, v8, v72
	v_cndmask_b32_e32 v4, v2, v3, vcc
	s_nop 1
	v_mov_b32_dpp v4, v4 quad_perm:[1,0,3,2] row_mask:0xf bank_mask:0xf bound_ctrl:1
	v_cndmask_b32_e32 v2, v4, v2, vcc
	v_cndmask_b32_e32 v3, v3, v4, vcc
	v_cvt_pk_bf16_f32 v2, v2, v3
	global_store_dword v[0:1], v2, off offset:64
	v_mul_f32_e32 v2, v40, v72
	v_mul_f32_e32 v3, v41, v73
	v_cndmask_b32_e32 v4, v2, v3, vcc
	s_nop 1
	v_mov_b32_dpp v4, v4 quad_perm:[1,0,3,2] row_mask:0xf bank_mask:0xf bound_ctrl:1
	v_cndmask_b32_e32 v2, v4, v2, vcc
	v_cndmask_b32_e32 v3, v3, v4, vcc
	v_cvt_pk_bf16_f32 v2, v2, v3
	global_store_dword v[0:1], v2, off offset:128
	v_mul_f32_e32 v2, v24, v72
	v_mul_f32_e32 v3, v25, v73
	v_cndmask_b32_e32 v4, v2, v3, vcc
	s_nop 1
	v_mov_b32_dpp v4, v4 quad_perm:[1,0,3,2] row_mask:0xf bank_mask:0xf bound_ctrl:1
	v_cndmask_b32_e32 v2, v4, v2, vcc
	v_cndmask_b32_e32 v3, v3, v4, vcc
	v_cvt_pk_bf16_f32 v2, v2, v3
; #define GAS __attribute__((address_space(1)))
; __device__ __forceinline__ unsigned cvt_pk_bf16(float lo, float hi) { unsigned r; asm volatile("v_cvt_pk_bf16_f32 %0, %1, %2" : "=v"(r) : "v"(lo), "v"(hi)); return r; }
; template <int AV>
; __device__ __forceinline__ void block(const BlockRef& cur, const BlockRef& nxt, char* lds, Seam& S, const int wid, const QNorm& QN) {
;     ...
; #pragma unroll
;     for (int r = 0; r < 16; r += 2) { const int orow0 = (r & 3) + 8 * (r >> 2);
; #pragma unroll
;         for (int d0 = 0; d0 < 4; ++d0) { const float a = o[d0][r] * rli[r], b = o[d0][r + 1] * rli[r + 1];
;             const float send = odd ? a : b;
;             const float recv = __int_as_float(__builtin_amdgcn_mov_dpp(__float_as_int(send), 0xB1, 0xF, 0xF, true));
;             *(GAS unsigned*)(Ow + (size_t)orow0 * OS * 2 + d0 * 64 + voff_o) = cvt_pk_bf16(odd ? recv : a, odd ? b : recv); } }
;     __syncthreads();
	global_store_dword v[0:1], v2, off offset:192
	v_mul_f32_e32 v0, v58, v74
	v_mul_f32_e32 v1, v59, v75
	v_cndmask_b32_e32 v2, v0, v1, vcc
	v_mul_f32_e32 v3, v11, v75
	s_nop 0
	v_mov_b32_dpp v2, v2 quad_perm:[1,0,3,2] row_mask:0xf bank_mask:0xf bound_ctrl:1
	v_cndmask_b32_e32 v0, v2, v0, vcc
	v_cndmask_b32_e32 v1, v1, v2, vcc
	v_cvt_pk_bf16_f32 v2, v0, v1
	v_add_co_u32_e64 v0, s[6:7], s1, v64
	s_mov_b32 s1, 0x18000
	s_nop 0
	v_addc_co_u32_e64 v1, s[6:7], 0, v65, s[6:7]
	global_store_dword v[0:1], v2, off
	v_mul_f32_e32 v2, v10, v74
	v_cndmask_b32_e32 v4, v2, v3, vcc
	s_nop 1
	v_mov_b32_dpp v4, v4 quad_perm:[1,0,3,2] row_mask:0xf bank_mask:0xf bound_ctrl:1
	v_cndmask_b32_e32 v2, v4, v2, vcc
	v_cndmask_b32_e32 v3, v3, v4, vcc
	v_cvt_pk_bf16_f32 v2, v2, v3
	global_store_dword v[0:1], v2, off offset:64
	v_mul_f32_e32 v2, v42, v74
	v_mul_f32_e32 v3, v43, v75
	v_cndmask_b32_e32 v4, v2, v3, vcc
	s_nop 1
	v_mov_b32_dpp v4, v4 quad_perm:[1,0,3,2] row_mask:0xf bank_mask:0xf bound_ctrl:1
	v_cndmask_b32_e32 v2, v4, v2, vcc
	v_cndmask_b32_e32 v3, v3, v4, vcc
	v_cvt_pk_bf16_f32 v2, v2, v3
	global_store_dword v[0:1], v2, off offset:128
	v_mul_f32_e32 v2, v26, v74
	v_mul_f32_e32 v3, v27, v75
	v_cndmask_b32_e32 v4, v2, v3, vcc
	s_nop 1
	v_mov_b32_dpp v4, v4 quad_perm:[1,0,3,2] row_mask:0xf bank_mask:0xf bound_ctrl:1
	v_cndmask_b32_e32 v2, v4, v2, vcc
	v_cndmask_b32_e32 v3, v3, v4, vcc
	v_cvt_pk_bf16_f32 v2, v2, v3
	global_store_dword v[0:1], v2, off offset:192
	v_mul_f32_e32 v0, v60, v76
	v_mul_f32_e32 v1, v61, v77
	v_cndmask_b32_e32 v2, v0, v1, vcc
	v_mul_f32_e32 v3, v13, v77
	s_nop 0
	v_mov_b32_dpp v2, v2 quad_perm:[1,0,3,2] row_mask:0xf bank_mask:0xf bound_ctrl:1
	v_cndmask_b32_e32 v0, v2, v0, vcc
	v_cndmask_b32_e32 v1, v1, v2, vcc
	v_cvt_pk_bf16_f32 v2, v0, v1
	v_add_co_u32_e64 v0, s[6:7], s1, v64
	s_mov_b32 s1, 0x1a000
	s_nop 0
	v_addc_co_u32_e64 v1, s[6:7], 0, v65, s[6:7]
	global_store_dword v[0:1], v2, off
	v_mul_f32_e32 v2, v12, v76
	v_cndmask_b32_e32 v4, v2, v3, vcc
	s_nop 1
	v_mov_b32_dpp v4, v4 quad_perm:[1,0,3,2] row_mask:0xf bank_mask:0xf bound_ctrl:1
	v_cndmask_b32_e32 v2, v4, v2, vcc
	v_cndmask_b32_e32 v3, v3, v4, vcc
	v_cvt_pk_bf16_f32 v2, v2, v3
	global_store_dword v[0:1], v2, off offset:64
	v_mul_f32_e32 v2, v44, v76
	v_mul_f32_e32 v3, v45, v77
	v_cndmask_b32_e32 v4, v2, v3, vcc
	s_nop 1
	v_mov_b32_dpp v4, v4 quad_perm:[1,0,3,2] row_mask:0xf bank_mask:0xf bound_ctrl:1
	v_cndmask_b32_e32 v2, v4, v2, vcc
	v_cndmask_b32_e32 v3, v3, v4, vcc
	v_cvt_pk_bf16_f32 v2, v2, v3
	global_store_dword v[0:1], v2, off offset:128
	v_mul_f32_e32 v2, v28, v76
	v_mul_f32_e32 v3, v29, v77
	v_cndmask_b32_e32 v4, v2, v3, vcc
	s_nop 1
	v_mov_b32_dpp v4, v4 quad_perm:[1,0,3,2] row_mask:0xf bank_mask:0xf bound_ctrl:1
	v_cndmask_b32_e32 v2, v4, v2, vcc
	v_cndmask_b32_e32 v3, v3, v4, vcc
	v_cvt_pk_bf16_f32 v2, v2, v3
	global_store_dword v[0:1], v2, off offset:192
	v_mul_f32_e32 v0, v62, v78
	v_mul_f32_e32 v1, v63, v79
	v_cndmask_b32_e32 v2, v0, v1, vcc
	v_mul_f32_e32 v3, v15, v79
	s_nop 0
	v_mov_b32_dpp v2, v2 quad_perm:[1,0,3,2] row_mask:0xf bank_mask:0xf bound_ctrl:1
	v_cndmask_b32_e32 v0, v2, v0, vcc
	v_cndmask_b32_e32 v1, v1, v2, vcc
	v_cvt_pk_bf16_f32 v2, v0, v1
	v_add_co_u32_e64 v0, s[6:7], s1, v64
	s_mov_b32 s1, s55
	s_nop 0
	v_addc_co_u32_e64 v1, s[6:7], 0, v65, s[6:7]
	global_store_dword v[0:1], v2, off
	v_mul_f32_e32 v2, v14, v78
	v_cndmask_b32_e32 v4, v2, v3, vcc
	s_mov_b64 s[6:7], s[64:65]
	s_nop 0
	v_mov_b32_dpp v4, v4 quad_perm:[1,0,3,2] row_mask:0xf bank_mask:0xf bound_ctrl:1
	v_cndmask_b32_e32 v2, v4, v2, vcc
	v_cndmask_b32_e32 v3, v3, v4, vcc
	v_cvt_pk_bf16_f32 v2, v2, v3
	global_store_dword v[0:1], v2, off offset:64
	v_mul_f32_e32 v2, v46, v78
	v_mul_f32_e32 v3, v47, v79
	v_cndmask_b32_e32 v4, v2, v3, vcc
	s_nop 1
	v_mov_b32_dpp v4, v4 quad_perm:[1,0,3,2] row_mask:0xf bank_mask:0xf bound_ctrl:1
	v_cndmask_b32_e32 v2, v4, v2, vcc
	v_cndmask_b32_e32 v3, v3, v4, vcc
	v_cvt_pk_bf16_f32 v2, v2, v3
	global_store_dword v[0:1], v2, off offset:128
	v_mul_f32_e32 v2, v30, v78
	v_mul_f32_e32 v3, v31, v79
	v_cndmask_b32_e32 v4, v2, v3, vcc
	s_nop 1
	v_mov_b32_dpp v4, v4 quad_perm:[1,0,3,2] row_mask:0xf bank_mask:0xf bound_ctrl:1
	v_cndmask_b32_e32 v2, v4, v2, vcc
	v_cndmask_b32_e32 v3, v3, v4, vcc
	s_andn2_b64 vcc, exec, s[66:67]
	v_cvt_pk_bf16_f32 v2, v2, v3
	global_store_dword v[0:1], v2, off offset:192
	s_barrier
	s_cbranch_vccz .LBB0_748

; __device__ __forceinline__ void mask_tile(f32x16& p0, f32x16& p1, int dq, unsigned W) {
;     const float NEG = -__builtin_inff();
; #pragma unroll
;     for (int r = 0; r < 16; ++r) {
;         const int c = (r & 3) + 8 * (r >> 2);
;         if ((unsigned)(dq - c) >= W) p0[r] = NEG;
;         if ((unsigned)(dq - c - 32) >= W) p1[r] = NEG;
;     }
; }
; __device__ __forceinline__ void qkt(f32x16& p0, f32x16& p1, const char* stg, int ka, const i32x8* qf, const f32x16& minit) {
;     p0 = minit; p1 = minit;
; #pragma unroll
;     for (int s = 0; s < 3; ++s) { const char* a = stg + SOFF_K + s * 4096 + ka; const char* b = stg + SOFF_K + s * 4096 + (ka ^ 16);
;         const i32x4 a0 = *reinterpret_cast<const i32x4*>(a), a1 = *reinterpret_cast<const i32x4*>(b);
;         const i32x4 c0 = *reinterpret_cast<const i32x4*>(a + 2048), c1 = *reinterpret_cast<const i32x4*>(b + 2048);
;         p0 = __builtin_amdgcn_mfma_scale_f32_32x32x64_f8f6f4(__builtin_shufflevector(a0, a1, 0, 1, 2, 3, 4, 5, 6, 7), qf[s], p0, 0, 0, 0, 0, 0, 0);
;         p1 = __builtin_amdgcn_mfma_scale_f32_32x32x64_f8f6f4(__builtin_shufflevector(c0, c1, 0, 1, 2, 3, 4, 5, 6, 7), qf[s], p1, 0, 0, 0, 0, 0, 0); }
; }
; __device__ __forceinline__ void v_read(i32x8 (&vf)[4], const char* stg, int ka) {
; #pragma unroll
;     for (int d0 = 0; d0 < 4; ++d0) { const i32x4 a0 = *reinterpret_cast<const i32x4*>(stg + SOFF_V + d0 * 2048 + ka), a1 = *reinterpret_cast<const i32x4*>(stg + SOFF_V + d0 * 2048 + (ka ^ 16));
;         vf[d0] = __builtin_shufflevector(a0, a1, 0, 1, 2, 3, 4, 5, 6, 7); }
; }
; __device__ __forceinline__ void pv_mma(f32x16* o, f32x16& ol, const i32x8 (&vf)[4], const i32x8 ones, const i32x8 pa) {
; #pragma unroll
;     for (int d0 = 0; d0 < 4; ++d0) o[d0] = __builtin_amdgcn_mfma_scale_f32_32x32x64_f8f6f4(pa, vf[d0], o[d0], 0, 0, 0, 0, 0, 0);
;     ol = __builtin_amdgcn_mfma_scale_f32_32x32x64_f8f6f4(pa, ones, ol, 0, 0, 0, 0, 0, 0);
; }
.LBB0_729:
	s_cmp_gt_i32 s0, 4
	s_cselect_b32 s36, -5, 1
	s_add_i32 s36, s36, s0
	s_mulk_i32 s36, 0x5000
	s_add_i32 s36, s36, 0
	v_add_u32_e32 v199, s36, v192
	v_add_u32_e32 v200, s36, v193
	ds_read_b128 v[112:115], v199
	ds_read_b128 v[116:119], v200
	ds_read_b128 v[220:223], v199 offset:2048
	ds_read_b128 v[224:227], v200 offset:2048
	ds_read_b128 v[236:239], v199 offset:4096
	ds_read_b128 v[240:243], v200 offset:4096
	ds_read_b128 v[244:247], v199 offset:6144
	ds_read_b128 v[248:251], v200 offset:6144
	v_exp_f32_e32 v201, v96
	s_waitcnt lgkmcnt(6)
	v_mfma_f32_32x32x64_f8f6f4 v[128:143], v[112:119], v[168:175], v[80:95]
	v_exp_f32_e32 v97, v97
	v_exp_f32_e32 v202, v100
	v_exp_f32_e32 v219, v101
	v_exp_f32_e32 v98, v98
	v_exp_f32_e32 v99, v99
	v_exp_f32_e32 v102, v102
	v_exp_f32_e32 v104, v104
	v_exp_f32_e32 v105, v105
	v_exp_f32_e32 v108, v108
	v_exp_f32_e32 v109, v109
	v_exp_f32_e32 v106, v106
	v_exp_f32_e32 v107, v107
	v_exp_f32_e32 v110, v110
	v_exp_f32_e32 v111, v111
	s_waitcnt lgkmcnt(4)
	v_mfma_f32_32x32x64_f8f6f4 v[112:127], v[220:227], v[168:175], v[80:95]
	ds_read_b128 v[220:223], v199 offset:8192
	ds_read_b128 v[224:227], v200 offset:8192
	ds_read_b128 v[228:231], v199 offset:10240
	ds_read_b128 v[232:235], v200 offset:10240
	s_waitcnt lgkmcnt(6)
	v_mfma_f32_32x32x64_f8f6f4 v[128:143], v[236:243], v[176:183], v[128:143]
	s_waitcnt lgkmcnt(4)
	v_mfma_f32_32x32x64_f8f6f4 v[112:127], v[244:251], v[176:183], v[112:127]
	s_waitcnt lgkmcnt(2)
	v_mfma_f32_32x32x64_f8f6f4 v[128:143], v[220:227], v[160:167], v[128:143]
	v_exp_f32_e32 v220, v103
	s_nop 0
	v_cvt_pk_fp8_f32 v100, v201, v97
	v_cvt_pk_fp8_f32 v101, v202, v219
	v_cvt_pk_fp8_f32 v100, v98, v99 op_sel:[0,0,1]
	v_cvt_pk_fp8_f32 v101, v102, v220 op_sel:[0,0,1]
	v_cvt_pk_fp8_f32 v96, v217, v218
	s_waitcnt lgkmcnt(0)
	v_mfma_f32_32x32x64_f8f6f4 v[112:127], v[228:235], v[160:167], v[112:127]
	v_cvt_pk_fp8_f32 v97, v213, v214
	v_cvt_pk_fp8_f32 v98, v209, v210
	v_cvt_pk_fp8_f32 v102, v104, v105
	v_cvt_pk_fp8_f32 v99, v205, v206
	v_cvt_pk_fp8_f32 v103, v108, v109
	v_cvt_pk_fp8_f32 v96, v215, v216 op_sel:[0,0,1]
	v_cvt_pk_fp8_f32 v97, v211, v212 op_sel:[0,0,1]
	v_cvt_pk_fp8_f32 v98, v207, v208 op_sel:[0,0,1]
	v_cvt_pk_fp8_f32 v102, v106, v107 op_sel:[0,0,1]
	v_cvt_pk_fp8_f32 v99, v203, v204 op_sel:[0,0,1]
	v_cvt_pk_fp8_f32 v103, v110, v111 op_sel:[0,0,1]
	s_mul_i32 s36, s0, 0x5000
	s_add_i32 s36, s36, 0
	v_add_u32_e32 v202, s36, v193
	v_add_u32_e32 v201, s36, v192
	ds_read_b128 v[108:111], v202 offset:12288
	ds_read_b128 v[104:107], v201 offset:12288
	ds_read_b128 v[236:239], v201 offset:14336
	ds_read_b128 v[240:243], v202 offset:14336
	ds_read_b128 v[248:251], v202 offset:16384
	ds_read_b128 v[244:247], v201 offset:16384
	v_mfma_f32_32x32x64_f8f6f4 v[64:79], v[96:103], v[152:159], v[64:79]
	s_sub_i32 s36, s1, 64
	s_cmp_le_u32 s36, s39
	s_waitcnt lgkmcnt(4)
	v_mfma_f32_32x32x64_f8f6f4 v[48:63], v[96:103], v[104:111], v[48:63]
	ds_read_b128 v[104:107], v201 offset:18432
	ds_read_b128 v[108:111], v202 offset:18432
	s_waitcnt lgkmcnt(4)
	v_mfma_f32_32x32x64_f8f6f4 v[0:15], v[96:103], v[236:243], v[0:15]
	s_waitcnt lgkmcnt(2)
	v_mfma_f32_32x32x64_f8f6f4 v[32:47], v[96:103], v[244:251], v[32:47]
	s_waitcnt lgkmcnt(0)
	v_mfma_f32_32x32x64_f8f6f4 v[16:31], v[96:103], v[104:111], v[16:31]
	s_cbranch_scc1 .LBB0_731
	v_add_u32_e32 v96, 0x4000007b, v198
	v_cmp_gt_u32_e32 vcc, 2.0, v96
	v_add_u32_e32 v96, 0x5b, v198
	s_nop 0
	v_cndmask_b32_e32 v128, v187, v128, vcc
	v_cmp_lt_u32_e32 vcc, s41, v96
	v_add_u32_e32 v96, 0x7a, v198
	s_nop 0
	v_cndmask_b32_e32 v112, v187, v112, vcc
	v_cmp_lt_u32_e32 vcc, s41, v96
	v_add_u32_e32 v96, 0x5a, v198
	s_nop 0
	v_cndmask_b32_e32 v129, v187, v129, vcc
	v_cmp_lt_u32_e32 vcc, s41, v96
	v_add_u32_e32 v96, 0x79, v198
	s_nop 0
	v_cndmask_b32_e32 v113, v187, v113, vcc
	v_cmp_lt_u32_e32 vcc, s41, v96
	v_add_u32_e32 v96, 0x59, v198
	s_nop 0
	v_cndmask_b32_e32 v130, v187, v130, vcc
	v_cmp_lt_u32_e32 vcc, s41, v96
	v_add_u32_e32 v96, 0x78, v198
	s_nop 0
	v_cndmask_b32_e32 v114, v187, v114, vcc
	v_cmp_lt_u32_e32 vcc, s41, v96
	v_add_u32_e32 v96, 0x58, v198
	s_nop 0
	v_cndmask_b32_e32 v131, v187, v131, vcc
	v_cmp_lt_u32_e32 vcc, s41, v96
	v_add_u32_e32 v96, 0x73, v198
	s_nop 0
	v_cndmask_b32_e32 v115, v187, v115, vcc
	v_cmp_lt_u32_e32 vcc, s41, v96
	v_add_u32_e32 v96, 0x53, v198
	s_nop 0
	v_cndmask_b32_e32 v132, v187, v132, vcc
	v_cmp_lt_u32_e32 vcc, s41, v96
	v_add_u32_e32 v96, 0x72, v198
	s_nop 0
	v_cndmask_b32_e32 v116, v187, v116, vcc
	v_cmp_lt_u32_e32 vcc, s41, v96
	v_add_u32_e32 v96, 0x52, v198
	s_nop 0
	v_cndmask_b32_e32 v133, v187, v133, vcc
	v_cmp_lt_u32_e32 vcc, s41, v96
	v_add_u32_e32 v96, 0x71, v198
	s_nop 0
	v_cndmask_b32_e32 v117, v187, v117, vcc
	v_cmp_lt_u32_e32 vcc, s41, v96
	v_add_u32_e32 v96, 0x51, v198
	s_nop 0
	v_cndmask_b32_e32 v134, v187, v134, vcc
	v_cmp_lt_u32_e32 vcc, s41, v96
	v_add_u32_e32 v96, 0x70, v198
	s_nop 0
	v_cndmask_b32_e32 v118, v187, v118, vcc
	v_cmp_lt_u32_e32 vcc, s41, v96
	v_add_u32_e32 v96, 0x50, v198
	s_nop 0
	v_cndmask_b32_e32 v135, v187, v135, vcc
	v_cmp_lt_u32_e32 vcc, s41, v96
	v_add_u32_e32 v96, 0x6b, v198
	s_nop 0
	v_cndmask_b32_e32 v119, v187, v119, vcc
	v_cmp_lt_u32_e32 vcc, s41, v96
	v_add_u32_e32 v96, 0x4b, v198
	s_nop 0
	v_cndmask_b32_e32 v136, v187, v136, vcc
	v_cmp_lt_u32_e32 vcc, s41, v96
	v_add_u32_e32 v96, 0x6a, v198
	s_nop 0
	v_cndmask_b32_e32 v120, v187, v120, vcc
	v_cmp_lt_u32_e32 vcc, s41, v96
	v_add_u32_e32 v96, 0x4a, v198
	s_nop 0
	v_cndmask_b32_e32 v137, v187, v137, vcc
	v_cmp_lt_u32_e32 vcc, s41, v96
	v_add_u32_e32 v96, 0x69, v198
	s_nop 0
	v_cndmask_b32_e32 v121, v187, v121, vcc
	v_cmp_lt_u32_e32 vcc, s41, v96
	v_add_u32_e32 v96, 0x49, v198
	s_nop 0
	v_cndmask_b32_e32 v138, v187, v138, vcc
	v_cmp_lt_u32_e32 vcc, s41, v96
	v_add_u32_e32 v96, 0x68, v198
	s_nop 0
	v_cndmask_b32_e32 v122, v187, v122, vcc
	v_cmp_lt_u32_e32 vcc, s41, v96
	v_add_u32_e32 v96, 0x48, v198
	s_nop 0
	v_cndmask_b32_e32 v139, v187, v139, vcc
	v_cmp_lt_u32_e32 vcc, s41, v96
	v_add_u32_e32 v96, 0x63, v198
	s_nop 0
	v_cndmask_b32_e32 v123, v187, v123, vcc
	v_cmp_lt_u32_e32 vcc, s41, v96
	v_add_u32_e32 v96, 0x43, v198
	s_nop 0
	v_cndmask_b32_e32 v140, v187, v140, vcc
	v_cmp_lt_u32_e32 vcc, s41, v96
	v_add_u32_e32 v96, 0x62, v198
	s_nop 0
	v_cndmask_b32_e32 v124, v187, v124, vcc
	v_cmp_lt_u32_e32 vcc, s41, v96
	v_add_u32_e32 v96, 0x42, v198
	s_nop 0
	v_cndmask_b32_e32 v141, v187, v141, vcc
	v_cmp_lt_u32_e32 vcc, s41, v96
	v_add_u32_e32 v96, 0x61, v198
	s_nop 0
	v_cndmask_b32_e32 v125, v187, v125, vcc
	v_cmp_lt_u32_e32 vcc, s41, v96
	v_add_u32_e32 v96, 0x41, v198
	s_nop 0
	v_cndmask_b32_e32 v142, v187, v142, vcc
	v_cmp_lt_u32_e32 vcc, s41, v96
	v_add_u32_e32 v96, 0x60, v198
	s_nop 0
	v_cndmask_b32_e32 v126, v187, v126, vcc
	v_cmp_lt_u32_e32 vcc, s41, v96
	v_add_u32_e32 v96, 64, v198
	s_nop 0
	v_cndmask_b32_e32 v143, v187, v143, vcc
	v_cmp_lt_u32_e32 vcc, s41, v96
	s_nop 1
	v_cndmask_b32_e32 v127, v187, v127, vcc

; template <bool FIRST>
; __device__ __forceinline__ bool partialSM(f32x16& p0, f32x16& p1, float& M, f32x16& minit, float& alpha) {
;     ...
;     for (int r = 0; r < 16; ++r) p0[r] = __builtin_amdgcn_exp2f(p0[r]);
;     return moved;
; }
; __device__ __forceinline__ void finishSM(f32x16& p0, f32x16& p1, i32x8& pa) {
;     for (int r = 0; r < 16; ++r) p1[r] = __builtin_amdgcn_exp2f(p1[r]);
; #pragma unroll
;     for (int v = 0; v < 4; ++v) { pa[v] = (int)cvt_pk4_fp8(p0[4 * v], p0[4 * v + 1], p0[4 * v + 2], p0[4 * v + 3]); pa[4 + v] = (int)cvt_pk4_fp8(p1[4 * v], p1[4 * v + 1], p1[4 * v + 2], p1[4 * v + 3]); }
; }
; __device__ __forceinline__ void qkt(f32x16& p0, f32x16& p1, const char* stg, int ka, const i32x8* qf, const f32x16& minit) {
;     p0 = minit; p1 = minit;
; #pragma unroll
;     for (int s = 0; s < 3; ++s) { const char* a = stg + SOFF_K + s * 4096 + ka; const char* b = stg + SOFF_K + s * 4096 + (ka ^ 16);
;         const i32x4 a0 = *reinterpret_cast<const i32x4*>(a), a1 = *reinterpret_cast<const i32x4*>(b);
;         const i32x4 c0 = *reinterpret_cast<const i32x4*>(a + 2048), c1 = *reinterpret_cast<const i32x4*>(b + 2048);
;         p0 = __builtin_amdgcn_mfma_scale_f32_32x32x64_f8f6f4(__builtin_shufflevector(a0, a1, 0, 1, 2, 3, 4, 5, 6, 7), qf[s], p0, 0, 0, 0, 0, 0, 0);
;         p1 = __builtin_amdgcn_mfma_scale_f32_32x32x64_f8f6f4(__builtin_shufflevector(c0, c1, 0, 1, 2, 3, 4, 5, 6, 7), qf[s], p1, 0, 0, 0, 0, 0, 0); }
; }
; __device__ __forceinline__ void v_read(i32x8 (&vf)[4], const char* stg, int ka) {
; #pragma unroll
;     for (int d0 = 0; d0 < 4; ++d0) { const i32x4 a0 = *reinterpret_cast<const i32x4*>(stg + SOFF_V + d0 * 2048 + ka), a1 = *reinterpret_cast<const i32x4*>(stg + SOFF_V + d0 * 2048 + (ka ^ 16));
;         vf[d0] = __builtin_shufflevector(a0, a1, 0, 1, 2, 3, 4, 5, 6, 7); }
; }
; __device__ __forceinline__ void pv_mma(f32x16* o, f32x16& ol, const i32x8 (&vf)[4], const i32x8 ones, const i32x8 pa) {
; #pragma unroll
;     for (int d0 = 0; d0 < 4; ++d0) o[d0] = __builtin_amdgcn_mfma_scale_f32_32x32x64_f8f6f4(pa, vf[d0], o[d0], 0, 0, 0, 0, 0, 0);
;     ol = __builtin_amdgcn_mfma_scale_f32_32x32x64_f8f6f4(pa, ones, ol, 0, 0, 0, 0, 0, 0);
; }
.LBB0_736:
	s_cmp_gt_i32 s0, 3
	s_cselect_b32 s36, -4, 2
	s_add_i32 s0, s36, s0
	v_exp_f32_e32 v203, v128
	v_exp_f32_e32 v220, v129
	v_exp_f32_e32 v221, v130
	v_exp_f32_e32 v222, v131
	v_exp_f32_e32 v223, v132
	v_exp_f32_e32 v224, v133
	v_exp_f32_e32 v225, v134
	v_exp_f32_e32 v226, v135
	v_exp_f32_e32 v227, v136
	v_exp_f32_e32 v228, v137
	v_exp_f32_e32 v229, v138
	v_exp_f32_e32 v230, v139
	v_exp_f32_e32 v231, v140
	v_exp_f32_e32 v232, v141
	v_exp_f32_e32 v233, v142
	v_exp_f32_e32 v234, v143
	s_mul_i32 s36, s0, 0x5000
	s_add_i32 s36, s36, 0
	v_add_u32_e32 v202, s36, v192
	v_add_u32_e32 v201, s36, v193
	ds_read_b128 v[204:207], v202
	ds_read_b128 v[208:211], v201
	ds_read_b128 v[212:215], v202 offset:2048
	ds_read_b128 v[216:219], v201 offset:2048
	ds_read_b128 v[236:239], v202 offset:4096
	ds_read_b128 v[240:243], v201 offset:4096
	ds_read_b128 v[244:247], v202 offset:6144
	ds_read_b128 v[248:251], v201 offset:6144
	v_exp_f32_e32 v113, v113
	s_waitcnt lgkmcnt(6)
	v_mfma_f32_32x32x64_f8f6f4 v[128:143], v[204:211], v[168:175], v[96:111]
	v_exp_f32_e32 v114, v114
	v_exp_f32_e32 v115, v115
	v_exp_f32_e32 v118, v118
	v_exp_f32_e32 v120, v120
	v_exp_f32_e32 v121, v121
	v_exp_f32_e32 v124, v124
	v_exp_f32_e32 v125, v125
	v_exp_f32_e32 v122, v122
	v_exp_f32_e32 v123, v123
	v_exp_f32_e32 v126, v126
	v_exp_f32_e32 v127, v127
	s_waitcnt lgkmcnt(4)
	v_mfma_f32_32x32x64_f8f6f4 v[96:111], v[212:219], v[168:175], v[96:111]
	ds_read_b128 v[204:207], v202 offset:8192
	ds_read_b128 v[208:211], v201 offset:8192
	ds_read_b128 v[212:215], v202 offset:10240
	ds_read_b128 v[216:219], v201 offset:10240
	s_waitcnt lgkmcnt(6)
	v_mfma_f32_32x32x64_f8f6f4 v[128:143], v[236:243], v[176:183], v[128:143]
	s_waitcnt lgkmcnt(4)
	v_mfma_f32_32x32x64_f8f6f4 v[96:111], v[244:251], v[176:183], v[96:111]
	s_waitcnt lgkmcnt(2)
	v_mfma_f32_32x32x64_f8f6f4 v[128:143], v[204:211], v[160:167], v[128:143]
	v_exp_f32_e32 v204, v112
	v_exp_f32_e32 v205, v116
	v_exp_f32_e32 v206, v117
	v_exp_f32_e32 v207, v119
	s_nop 0
	v_cvt_pk_fp8_f32 v116, v204, v113
	v_cvt_pk_fp8_f32 v117, v205, v206
	v_cvt_pk_fp8_f32 v116, v114, v115 op_sel:[0,0,1]
	v_cvt_pk_fp8_f32 v117, v118, v207 op_sel:[0,0,1]
	s_waitcnt lgkmcnt(0)
	v_mfma_f32_32x32x64_f8f6f4 v[96:111], v[212:219], v[160:167], v[96:111]
	v_cvt_pk_fp8_f32 v112, v203, v220
	v_cvt_pk_fp8_f32 v113, v223, v224
	v_cvt_pk_fp8_f32 v114, v227, v228
	v_cvt_pk_fp8_f32 v118, v120, v121
	v_cvt_pk_fp8_f32 v115, v231, v232
	v_cvt_pk_fp8_f32 v119, v124, v125
	v_cvt_pk_fp8_f32 v112, v221, v222 op_sel:[0,0,1]
	v_cvt_pk_fp8_f32 v113, v225, v226 op_sel:[0,0,1]
	v_cvt_pk_fp8_f32 v114, v229, v230 op_sel:[0,0,1]
	v_cvt_pk_fp8_f32 v118, v122, v123 op_sel:[0,0,1]
	v_cvt_pk_fp8_f32 v115, v233, v234 op_sel:[0,0,1]
	v_cvt_pk_fp8_f32 v119, v126, v127 op_sel:[0,0,1]
	ds_read_b128 v[124:127], v200 offset:12288
	ds_read_b128 v[120:123], v199 offset:12288
	ds_read_b128 v[236:239], v199 offset:14336
	ds_read_b128 v[240:243], v200 offset:14336
	ds_read_b128 v[248:251], v200 offset:16384
	ds_read_b128 v[244:247], v199 offset:16384
	v_mfma_f32_32x32x64_f8f6f4 v[64:79], v[112:119], v[152:159], v[64:79]
	s_cmp_le_u32 s1, s39
	s_waitcnt lgkmcnt(4)
	v_mfma_f32_32x32x64_f8f6f4 v[48:63], v[112:119], v[120:127], v[48:63]
	ds_read_b128 v[120:123], v199 offset:18432
	ds_read_b128 v[124:127], v200 offset:18432
	s_waitcnt lgkmcnt(4)
	v_mfma_f32_32x32x64_f8f6f4 v[0:15], v[112:119], v[236:243], v[0:15]
	s_waitcnt lgkmcnt(2)
	v_mfma_f32_32x32x64_f8f6f4 v[32:47], v[112:119], v[244:251], v[32:47]
	s_waitcnt lgkmcnt(0)
	v_mfma_f32_32x32x64_f8f6f4 v[16:31], v[112:119], v[120:127], v[16:31]
	s_cbranch_scc1 .LBB0_738
; __device__ __forceinline__ void mask_tile(f32x16& p0, f32x16& p1, int dq, unsigned W) {
;     const float NEG = -__builtin_inff();
; #pragma unroll
;     for (int r = 0; r < 16; ++r) {
;         const int c = (r & 3) + 8 * (r >> 2);
;         if ((unsigned)(dq - c) >= W) p0[r] = NEG;
;         if ((unsigned)(dq - c - 32) >= W) p1[r] = NEG;
;     }
; }
	v_add_u32_e32 v112, 0x4000003b, v198
	v_cmp_gt_u32_e32 vcc, 2.0, v112
	v_add_u32_e32 v112, 27, v198
	s_nop 0
	v_cndmask_b32_e32 v128, v187, v128, vcc
	v_cmp_lt_u32_e32 vcc, s41, v112
	v_add_u32_e32 v112, 58, v198
	s_nop 0
	v_cndmask_b32_e32 v96, v187, v96, vcc
	v_cmp_lt_u32_e32 vcc, s41, v112
	v_add_u32_e32 v112, 26, v198
	s_nop 0
	v_cndmask_b32_e32 v129, v187, v129, vcc
	v_cmp_lt_u32_e32 vcc, s41, v112
	v_add_u32_e32 v112, 57, v198
	s_nop 0
	v_cndmask_b32_e32 v97, v187, v97, vcc
	v_cmp_lt_u32_e32 vcc, s41, v112
	v_add_u32_e32 v112, 25, v198
	s_nop 0
	v_cndmask_b32_e32 v130, v187, v130, vcc
	v_cmp_lt_u32_e32 vcc, s41, v112
	v_add_u32_e32 v112, 56, v198
	s_nop 0
	v_cndmask_b32_e32 v98, v187, v98, vcc
	v_cmp_lt_u32_e32 vcc, s41, v112
	v_add_u32_e32 v112, 24, v198
	s_nop 0
	v_cndmask_b32_e32 v131, v187, v131, vcc
	v_cmp_lt_u32_e32 vcc, s41, v112
	v_add_u32_e32 v112, 51, v198
	s_nop 0
	v_cndmask_b32_e32 v99, v187, v99, vcc
	v_cmp_lt_u32_e32 vcc, s41, v112
	v_add_u32_e32 v112, 19, v198
	s_nop 0
	v_cndmask_b32_e32 v132, v187, v132, vcc
	v_cmp_lt_u32_e32 vcc, s41, v112
	v_add_u32_e32 v112, 50, v198
	s_nop 0
	v_cndmask_b32_e32 v100, v187, v100, vcc
	v_cmp_lt_u32_e32 vcc, s41, v112
	v_add_u32_e32 v112, 18, v198
	s_nop 0
	v_cndmask_b32_e32 v133, v187, v133, vcc
	v_cmp_lt_u32_e32 vcc, s41, v112
	v_add_u32_e32 v112, 49, v198
	s_nop 0
	v_cndmask_b32_e32 v101, v187, v101, vcc
	v_cmp_lt_u32_e32 vcc, s41, v112
	v_add_u32_e32 v112, 17, v198
	s_nop 0
	v_cndmask_b32_e32 v134, v187, v134, vcc
	v_cmp_lt_u32_e32 vcc, s41, v112
	v_add_u32_e32 v112, 48, v198
	s_nop 0
	v_cndmask_b32_e32 v102, v187, v102, vcc
	v_cmp_lt_u32_e32 vcc, s41, v112
	v_add_u32_e32 v112, 16, v198
	s_nop 0
	v_cndmask_b32_e32 v135, v187, v135, vcc
	v_cmp_lt_u32_e32 vcc, s41, v112
	v_add_u32_e32 v112, 43, v198
	s_nop 0
	v_cndmask_b32_e32 v103, v187, v103, vcc
	v_cmp_lt_u32_e32 vcc, s41, v112
	v_add_u32_e32 v112, 11, v198
	s_nop 0
	v_cndmask_b32_e32 v136, v187, v136, vcc
	v_cmp_lt_u32_e32 vcc, s41, v112
	v_add_u32_e32 v112, 42, v198
	s_nop 0
	v_cndmask_b32_e32 v104, v187, v104, vcc
	v_cmp_lt_u32_e32 vcc, s41, v112
	v_add_u32_e32 v112, 10, v198
	s_nop 0
	v_cndmask_b32_e32 v137, v187, v137, vcc
	v_cmp_lt_u32_e32 vcc, s41, v112
	v_add_u32_e32 v112, 41, v198
	s_nop 0
	v_cndmask_b32_e32 v105, v187, v105, vcc
	v_cmp_lt_u32_e32 vcc, s41, v112
	v_add_u32_e32 v112, 9, v198
	s_nop 0
	v_cndmask_b32_e32 v138, v187, v138, vcc
	v_cmp_lt_u32_e32 vcc, s41, v112
	v_add_u32_e32 v112, 40, v198
	s_nop 0
	v_cndmask_b32_e32 v106, v187, v106, vcc
	v_cmp_lt_u32_e32 vcc, s41, v112
	v_add_u32_e32 v112, 8, v198
	s_nop 0
	v_cndmask_b32_e32 v139, v187, v139, vcc
	v_cmp_lt_u32_e32 vcc, s41, v112
	v_add_u32_e32 v112, 35, v198
	s_nop 0
	v_cndmask_b32_e32 v107, v187, v107, vcc
	v_cmp_lt_u32_e32 vcc, s41, v112
	v_add_u32_e32 v112, 3, v198
	s_nop 0
	v_cndmask_b32_e32 v140, v187, v140, vcc
	v_cmp_lt_u32_e32 vcc, s41, v112
	v_add_u32_e32 v112, 34, v198
	s_nop 0
	v_cndmask_b32_e32 v108, v187, v108, vcc
	v_cmp_lt_u32_e32 vcc, s41, v112
	v_add_u32_e32 v112, 2, v198
	s_nop 0
	v_cndmask_b32_e32 v141, v187, v141, vcc
	v_cmp_lt_u32_e32 vcc, s41, v112
	v_add_u32_e32 v112, 33, v198
	s_nop 0
	v_cndmask_b32_e32 v109, v187, v109, vcc
	v_cmp_lt_u32_e32 vcc, s41, v112
	v_add_u32_e32 v112, 1, v198
	s_nop 0
	v_cndmask_b32_e32 v142, v187, v142, vcc
	v_cmp_lt_u32_e32 vcc, s41, v112
	v_add_u32_e32 v112, 32, v198
	s_nop 0
	v_cndmask_b32_e32 v110, v187, v110, vcc
	v_cmp_lt_u32_e32 vcc, s41, v112
	s_nop 1
	v_cndmask_b32_e32 v143, v187, v143, vcc
	v_cmp_lt_u32_e32 vcc, s41, v198
	s_nop 1
	v_cndmask_b32_e32 v111, v187, v111, vcc

; __device__ __forceinline__ cgptr cuni(const void* p) { const unsigned long long v = (unsigned long long)p; const unsigned lo = __builtin_amdgcn_readfirstlane((unsigned)v), hi = __builtin_amdgcn_readfirstlane((unsigned)(v >> 32)); return (cgptr)(((unsigned long long)hi << 32) | lo); }
; #define CONV_LOAD(v, c) do { const unsigned lo_ = (unsigned)(lane >> 3) * (c).N4 + 16u * (unsigned)(lane & 7); _Pragma("unroll") for (int i = 0; i < 16; ++i) v[i] = __builtin_nontemporal_load((const GAS f32x4*)(cuni((const void*)((c).src + (size_t)(8 * i) * (c).N4)) + lo_)); } while (0)
; __device__ __forceinline__ ConvItem conv_decode(int it, const float* wgu, const float* wd, unsigned char* WguT, unsigned char* WdT) {
;     constexpr int I_GU = NE * 16 * 128;
;     ConvItem c; int r = it, nbn, N; const float* src; unsigned char* dstp; bool gu;
;     if (r < I_GU) { const int e = r / (16 * 128); r -= e * (16 * 128); N = 4096; nbn = 128; src = wgu + (size_t)e * DM * 4096; dstp = WguT + (size_t)e * 4096 * DM; gu = true; }
;     else { r -= I_GU; const int e = r / (16 * 64); r -= e * (16 * 64); N = DM; nbn = 64; src = wd + (size_t)e * DFF * DM; dstp = WdT + (size_t)e * DM * DFF; gu = false; }
;     const int kb = r / nbn, nb = r - kb * nbn, n0 = nb * 32, k0 = kb * 128; int dst = n0;
;     if (gu) { const int j = n0 & 2047; dst = (j >> 7) * 256 + (j & 127) + ((n0 >= 2048) ? 128 : 0); }
;     c.src = cuni(src + (size_t)k0 * N + n0); c.dstp = cuni(dstp + (size_t)dst * DM + k0); c.N4 = (unsigned)N * 4u;
;     return c;
; }
; __device__ __forceinline__ void convert_expert_weights(const float* wgu, const float* wd, unsigned char* WguT, unsigned char* WdT, LAS float* scr, int gw, int NGW, int NIT, int lane) {
;     ...
;         const bool hb = it + NGW < NIT; cb = conv_decode(hb ? it + NGW : it, wgu, wd, WguT, WdT); CONV_LOAD(vb, cb);
;         CONV_STORE(va, ca);
.LBB0_757:
	v_cvt_f32_ubyte0_e32 v0, s9
	v_rcp_iflag_f32_e32 v0, v0
	s_sub_i32 s11, 0, s9
	s_abs_i32 s10, s8
	s_add_i32 s38, s1, s44
	v_mul_f32_e32 v0, 0x4f7ffffe, v0
	v_cvt_u32_f32_e32 v0, v0
	s_ashr_i32 s1, s8, 31
	v_readfirstlane_b32 s12, v0
	s_mul_i32 s11, s11, s12
	s_mul_hi_u32 s11, s12, s11
	s_add_i32 s12, s12, s11
	s_mul_hi_u32 s11, s10, s12
	s_mul_i32 s12, s11, s9
	s_sub_i32 s10, s10, s12
	s_add_i32 s17, s11, 1
	s_sub_i32 s12, s10, s9
	s_cmp_ge_u32 s10, s9
	s_cselect_b32 s11, s17, s11
	s_cselect_b32 s10, s12, s10
	s_add_i32 s12, s11, 1
	s_cmp_ge_u32 s10, s9
	s_cselect_b32 s10, s12, s11
	s_xor_b32 s10, s10, s1
	s_sub_i32 s1, s10, s1
	s_mul_i32 s9, s1, s9
	s_sub_i32 s9, s8, s9
	s_lshl_b32 s10, s9, 5
	s_lshl_b32 s8, s8, 6
	s_and_b32 s8, s8, 0xf00
	s_and_b32 s11, s10, 0x60
	s_or_b32 s8, s11, s8
	s_cmp_gt_i32 s9, 63
	s_cselect_b32 s9, 0x80, 0
	s_or_b32 s11, s8, s9
	s_and_b64 s[8:9], s[14:15], exec
	s_cselect_b32 s8, s11, s10
	s_lshl_b32 s1, s1, 7
	s_mul_hi_i32 s15, s1, s3
	s_mul_i32 s14, s1, s3
	s_ashr_i32 s12, s1, 31
	s_lshl_b64 s[14:15], s[14:15], 2
	s_add_u32 s9, s22, s14
	s_addc_u32 s14, s23, s15
	s_ashr_i32 s11, s10, 31
	s_lshl_b64 s[10:11], s[10:11], 2
	s_add_u32 s22, s9, s10
	s_addc_u32 s23, s14, s11
	s_ashr_i32 s9, s8, 31
	s_lshl_b64 s[8:9], s[8:9], 11
	s_add_u32 s8, s20, s8
	s_addc_u32 s9, s21, s9
	s_add_u32 s14, s8, s1
	s_addc_u32 s15, s9, s12
	s_lshl_b32 s1, s3, 5
	v_mul_lo_u32 v0, v130, s3
	s_add_u32 s8, s22, s1
	v_or_b32_e32 v56, v0, v131
	s_addc_u32 s9, s23, 0
	s_lshl_b32 s1, s3, 6
	global_load_dwordx4 v[4:7], v56, s[22:23] nt
	global_load_dwordx4 v[0:3], v56, s[8:9] nt
	s_add_u32 s8, s22, s1
	s_addc_u32 s9, s23, 0
	s_mul_i32 s1, s3, 0x60
	s_add_u32 s10, s22, s1
	s_addc_u32 s11, s23, 0
	s_lshl_b32 s1, s3, 7
	global_load_dwordx4 v[12:15], v56, s[8:9] nt
	global_load_dwordx4 v[8:11], v56, s[10:11] nt
	s_add_u32 s8, s22, s1
	s_addc_u32 s9, s23, 0
	s_mul_i32 s1, s3, 0xa0
	s_add_u32 s10, s22, s1
	s_addc_u32 s11, s23, 0
	s_mul_i32 s1, s3, 0xc0
	global_load_dwordx4 v[20:23], v56, s[8:9] nt
	global_load_dwordx4 v[16:19], v56, s[10:11] nt
	s_add_u32 s8, s22, s1
	s_addc_u32 s9, s23, 0
	s_mul_i32 s1, s3, 0xe0
	s_add_u32 s10, s22, s1
	s_addc_u32 s11, s23, 0
	s_lshl_b32 s1, s3, 8
	global_load_dwordx4 v[28:31], v56, s[8:9] nt
	global_load_dwordx4 v[24:27], v56, s[10:11] nt
	s_add_u32 s8, s22, s1
	s_addc_u32 s9, s23, 0
	s_mul_i32 s1, s3, 0x120
	s_add_u32 s10, s22, s1
	s_addc_u32 s11, s23, 0
	s_mul_i32 s1, s3, 0x140
	global_load_dwordx4 v[36:39], v56, s[8:9] nt
	global_load_dwordx4 v[32:35], v56, s[10:11] nt
	s_add_u32 s8, s22, s1
	s_addc_u32 s9, s23, 0
	s_mul_i32 s1, s3, 0x160
	s_add_u32 s10, s22, s1
	s_addc_u32 s11, s23, 0
	s_mul_i32 s1, s3, 0x180
	global_load_dwordx4 v[44:47], v56, s[8:9] nt
	global_load_dwordx4 v[40:43], v56, s[10:11] nt
	s_add_u32 s8, s22, s1
	s_addc_u32 s9, s23, 0
	s_mul_i32 s1, s3, 0x1a0
	s_add_u32 s10, s22, s1
	s_addc_u32 s11, s23, 0
	s_mul_i32 s1, s3, 0x1c0
	global_load_dwordx4 v[52:55], v56, s[8:9] nt
	global_load_dwordx4 v[48:51], v56, s[10:11] nt
	s_add_u32 s8, s22, s1
	s_addc_u32 s9, s23, 0
	s_mul_i32 s1, s3, 0x1e0
	s_add_u32 s10, s22, s1
	s_addc_u32 s11, s23, 0
	global_load_dwordx4 v[60:63], v56, s[8:9] nt
	s_nop 0
	global_load_dwordx4 v[56:59], v56, s[10:11] nt
	s_waitcnt vmcnt(35)
	v_pk_mul_f32 v[126:127], v[126:127], s[16:17] op_sel_hi:[1,0]
	v_pk_mul_f32 v[124:125], v[124:125], s[16:17] op_sel_hi:[1,0]
	s_waitcnt vmcnt(34)
	v_pk_mul_f32 v[118:119], v[118:119], s[16:17] op_sel_hi:[1,0]
	v_pk_mul_f32 v[116:117], v[116:117], s[16:17] op_sel_hi:[1,0]
	ds_write_b128 v132, v[124:127]
	ds_write_b128 v133, v[116:119]
	s_waitcnt vmcnt(33)
	v_pk_mul_f32 v[118:119], v[122:123], s[16:17] op_sel_hi:[1,0]
	v_pk_mul_f32 v[116:117], v[120:121], s[16:17] op_sel_hi:[1,0]
	s_waitcnt vmcnt(32)
	v_pk_mul_f32 v[110:111], v[110:111], s[16:17] op_sel_hi:[1,0]
	v_pk_mul_f32 v[108:109], v[108:109], s[16:17] op_sel_hi:[1,0]
	ds_write_b128 v134, v[116:119]
	ds_write_b128 v135, v[108:111]
	s_waitcnt vmcnt(31)
	v_pk_mul_f32 v[110:111], v[114:115], s[16:17] op_sel_hi:[1,0]
	v_pk_mul_f32 v[108:109], v[112:113], s[16:17] op_sel_hi:[1,0]
	s_waitcnt vmcnt(30)
	v_pk_mul_f32 v[102:103], v[102:103], s[16:17] op_sel_hi:[1,0]
	v_pk_mul_f32 v[100:101], v[100:101], s[16:17] op_sel_hi:[1,0]
	ds_write_b128 v136, v[108:111]
	ds_write_b128 v137, v[100:103]
	s_waitcnt vmcnt(29)
	v_pk_mul_f32 v[102:103], v[106:107], s[16:17] op_sel_hi:[1,0]
	v_pk_mul_f32 v[100:101], v[104:105], s[16:17] op_sel_hi:[1,0]
	s_waitcnt vmcnt(28)
	v_pk_mul_f32 v[94:95], v[94:95], s[16:17] op_sel_hi:[1,0]
	v_pk_mul_f32 v[92:93], v[92:93], s[16:17] op_sel_hi:[1,0]
	ds_write_b128 v138, v[100:103]
	ds_write_b128 v139, v[92:95]
	s_waitcnt vmcnt(27)
	v_pk_mul_f32 v[94:95], v[98:99], s[16:17] op_sel_hi:[1,0]
	v_pk_mul_f32 v[92:93], v[96:97], s[16:17] op_sel_hi:[1,0]
	s_waitcnt vmcnt(26)
	v_pk_mul_f32 v[86:87], v[86:87], s[16:17] op_sel_hi:[1,0]
	v_pk_mul_f32 v[84:85], v[84:85], s[16:17] op_sel_hi:[1,0]
	ds_write_b128 v140, v[92:95]
	ds_write_b128 v141, v[84:87]
	s_waitcnt vmcnt(25)
	v_pk_mul_f32 v[86:87], v[90:91], s[16:17] op_sel_hi:[1,0]
	v_pk_mul_f32 v[84:85], v[88:89], s[16:17] op_sel_hi:[1,0]
	s_waitcnt vmcnt(24)
	v_pk_mul_f32 v[78:79], v[78:79], s[16:17] op_sel_hi:[1,0]
	v_pk_mul_f32 v[76:77], v[76:77], s[16:17] op_sel_hi:[1,0]
	ds_write_b128 v142, v[84:87]
	ds_write_b128 v143, v[76:79]
	s_waitcnt vmcnt(23)
	v_pk_mul_f32 v[78:79], v[82:83], s[16:17] op_sel_hi:[1,0]
	v_pk_mul_f32 v[76:77], v[80:81], s[16:17] op_sel_hi:[1,0]
	s_waitcnt vmcnt(22)
	v_pk_mul_f32 v[70:71], v[70:71], s[16:17] op_sel_hi:[1,0]
	v_pk_mul_f32 v[68:69], v[68:69], s[16:17] op_sel_hi:[1,0]
	ds_write_b128 v144, v[76:79]
	ds_write_b128 v145, v[68:71]
	s_waitcnt vmcnt(21)
	v_pk_mul_f32 v[70:71], v[74:75], s[16:17] op_sel_hi:[1,0]
	v_pk_mul_f32 v[68:69], v[72:73], s[16:17] op_sel_hi:[1,0]
	s_waitcnt vmcnt(20)
	v_pk_mul_f32 v[66:67], v[66:67], s[16:17] op_sel_hi:[1,0]
	v_pk_mul_f32 v[64:65], v[64:65], s[16:17] op_sel_hi:[1,0]
	ds_write_b128 v146, v[68:71]
	ds_write_b128 v147, v[64:67]
	s_waitcnt lgkmcnt(0)
	ds_read2_b32 v[64:65], v148 offset1:32
	ds_read2_b32 v[72:73], v148 offset0:64 offset1:96
	ds_read2_b32 v[70:71], v148 offset0:128 offset1:160
	ds_read2_b32 v[74:75], v152 offset1:32
	s_waitcnt lgkmcnt(3)
	v_cvt_pk_fp8_f32 v68, v64, v65
	ds_read2_b32 v[64:65], v148 offset0:192 offset1:224
	ds_read2_b32 v[76:77], v152 offset0:64 offset1:96
	ds_read2_b32 v[78:79], v152 offset0:128 offset1:160
	s_waitcnt lgkmcnt(4)
	v_cvt_pk_fp8_f32 v69, v70, v71
	s_waitcnt lgkmcnt(3)
	v_cvt_pk_fp8_f32 v70, v74, v75
	ds_read2_b32 v[74:75], v152 offset0:192 offset1:224
	s_waitcnt lgkmcnt(1)
	v_cvt_pk_fp8_f32 v71, v78, v79
	v_cvt_pk_fp8_f32 v68, v72, v73 op_sel:[0,0,1]
	v_cvt_pk_fp8_f32 v69, v64, v65 op_sel:[0,0,1]
	v_cvt_pk_fp8_f32 v70, v76, v77 op_sel:[0,0,1]
	s_waitcnt lgkmcnt(0)
	v_cvt_pk_fp8_f32 v71, v74, v75 op_sel:[0,0,1]
	ds_read2_b32 v[72:73], v149 offset1:32
	v_lshl_add_u64 v[64:65], s[18:19], 0, v[128:129]
	ds_read2_b32 v[74:75], v153 offset1:32
	global_store_dwordx4 v[64:65], v[68:71], off nt
	ds_read2_b32 v[70:71], v149 offset0:128 offset1:160
	ds_read2_b32 v[64:65], v149 offset0:64 offset1:96
	s_waitcnt lgkmcnt(3)
	v_cvt_pk_fp8_f32 v68, v72, v73
	ds_read2_b32 v[72:73], v149 offset0:192 offset1:224
	ds_read2_b32 v[76:77], v153 offset0:64 offset1:96
	ds_read2_b32 v[78:79], v153 offset0:128 offset1:160
	s_waitcnt lgkmcnt(4)
	v_cvt_pk_fp8_f32 v69, v70, v71
	v_cvt_pk_fp8_f32 v70, v74, v75
	ds_read2_b32 v[74:75], v153 offset0:192 offset1:224
	s_waitcnt lgkmcnt(1)
	v_cvt_pk_fp8_f32 v71, v78, v79
	v_cvt_pk_fp8_f32 v68, v64, v65 op_sel:[0,0,1]
	v_cvt_pk_fp8_f32 v69, v72, v73 op_sel:[0,0,1]
	v_cvt_pk_fp8_f32 v70, v76, v77 op_sel:[0,0,1]
	s_waitcnt lgkmcnt(0)
	v_cvt_pk_fp8_f32 v71, v74, v75 op_sel:[0,0,1]
	s_add_u32 s8, s18, 0x4000
	ds_read2_b32 v[72:73], v150 offset1:32
	s_addc_u32 s9, s19, 0
	v_lshl_add_u64 v[64:65], s[8:9], 0, v[128:129]
	global_store_dwordx4 v[64:65], v[68:71], off nt
	ds_read2_b32 v[70:71], v150 offset0:128 offset1:160
	ds_read2_b32 v[74:75], v154 offset1:32
	ds_read2_b32 v[64:65], v150 offset0:64 offset1:96
	s_waitcnt lgkmcnt(3)
	v_cvt_pk_fp8_f32 v68, v72, v73
	ds_read2_b32 v[72:73], v150 offset0:192 offset1:224
	ds_read2_b32 v[76:77], v154 offset0:64 offset1:96
	ds_read2_b32 v[78:79], v154 offset0:128 offset1:160
	s_waitcnt lgkmcnt(5)
	v_cvt_pk_fp8_f32 v69, v70, v71
	s_waitcnt lgkmcnt(4)
	v_cvt_pk_fp8_f32 v70, v74, v75
	ds_read2_b32 v[74:75], v154 offset0:192 offset1:224
	s_waitcnt lgkmcnt(1)
	v_cvt_pk_fp8_f32 v71, v78, v79
	v_cvt_pk_fp8_f32 v68, v64, v65 op_sel:[0,0,1]
	v_cvt_pk_fp8_f32 v69, v72, v73 op_sel:[0,0,1]
	v_cvt_pk_fp8_f32 v70, v76, v77 op_sel:[0,0,1]
	s_waitcnt lgkmcnt(0)
	v_cvt_pk_fp8_f32 v71, v74, v75 op_sel:[0,0,1]
	s_add_u32 s8, s18, 0x8000
	s_addc_u32 s9, s19, 0
	v_lshl_add_u64 v[64:65], s[8:9], 0, v[128:129]
	ds_read2_b32 v[72:73], v151 offset1:32
	global_store_dwordx4 v[64:65], v[68:71], off nt
	ds_read2_b32 v[70:71], v151 offset0:128 offset1:160
	ds_read2_b32 v[74:75], v155 offset1:32
	ds_read2_b32 v[68:69], v151 offset0:64 offset1:96
	s_waitcnt lgkmcnt(3)
	v_cvt_pk_fp8_f32 v64, v72, v73
	ds_read2_b32 v[72:73], v151 offset0:192 offset1:224
	s_waitcnt lgkmcnt(3)
	v_cvt_pk_fp8_f32 v65, v70, v71
	ds_read2_b32 v[70:71], v155 offset0:128 offset1:160
	ds_read2_b32 v[76:77], v155 offset0:64 offset1:96
	s_waitcnt lgkmcnt(4)
	v_cvt_pk_fp8_f32 v66, v74, v75
	ds_read2_b32 v[74:75], v155 offset0:192 offset1:224
	s_waitcnt lgkmcnt(2)
	v_cvt_pk_fp8_f32 v67, v70, v71
	v_cvt_pk_fp8_f32 v64, v68, v69 op_sel:[0,0,1]
	v_cvt_pk_fp8_f32 v65, v72, v73 op_sel:[0,0,1]
	s_waitcnt lgkmcnt(1)
	v_cvt_pk_fp8_f32 v66, v76, v77 op_sel:[0,0,1]
	s_waitcnt lgkmcnt(0)
	v_cvt_pk_fp8_f32 v67, v74, v75 op_sel:[0,0,1]
	s_add_u32 s8, s18, 0xc000
	s_addc_u32 s9, s19, 0
	v_lshl_add_u64 v[68:69], s[8:9], 0, v[128:129]
	global_store_dwordx4 v[68:69], v[64:67], off nt
	s_waitcnt lgkmcnt(0)
	s_cmp_ge_i32 s38, s45
	s_cselect_b64 s[20:21], -1, 0

; __device__ __forceinline__ cgptr cuni(const void* p) { const unsigned long long v = (unsigned long long)p; const unsigned lo = __builtin_amdgcn_readfirstlane((unsigned)v), hi = __builtin_amdgcn_readfirstlane((unsigned)(v >> 32)); return (cgptr)(((unsigned long long)hi << 32) | lo); }
; #define CONV_LOAD(v, c) do { const unsigned lo_ = (unsigned)(lane >> 3) * (c).N4 + 16u * (unsigned)(lane & 7); _Pragma("unroll") for (int i = 0; i < 16; ++i) v[i] = __builtin_nontemporal_load((const GAS f32x4*)(cuni((const void*)((c).src + (size_t)(8 * i) * (c).N4)) + lo_)); } while (0)
; __device__ __forceinline__ ConvItem conv_decode(int it, const float* wgu, const float* wd, unsigned char* WguT, unsigned char* WdT) {
;     constexpr int I_GU = NE * 16 * 128;
;     ConvItem c; int r = it, nbn, N; const float* src; unsigned char* dstp; bool gu;
;     if (r < I_GU) { const int e = r / (16 * 128); r -= e * (16 * 128); N = 4096; nbn = 128; src = wgu + (size_t)e * DM * 4096; dstp = WguT + (size_t)e * 4096 * DM; gu = true; }
;     else { r -= I_GU; const int e = r / (16 * 64); r -= e * (16 * 64); N = DM; nbn = 64; src = wd + (size_t)e * DFF * DM; dstp = WdT + (size_t)e * DM * DFF; gu = false; }
;     const int kb = r / nbn, nb = r - kb * nbn, n0 = nb * 32, k0 = kb * 128; int dst = n0;
;     if (gu) { const int j = n0 & 2047; dst = (j >> 7) * 256 + (j & 127) + ((n0 >= 2048) ? 128 : 0); }
;     c.src = cuni(src + (size_t)k0 * N + n0); c.dstp = cuni(dstp + (size_t)dst * DM + k0); c.N4 = (unsigned)N * 4u;
;     return c;
; }
; __device__ __forceinline__ void convert_expert_weights(const float* wgu, const float* wd, unsigned char* WguT, unsigned char* WdT, LAS float* scr, int gw, int NGW, int NIT, int lane) {
;     ...
;         const bool ha = it + NGW < NIT; ca = conv_decode(ha ? it + NGW : it, wgu, wd, WguT, WdT); CONV_LOAD(va, ca);
;         CONV_STORE(vb, cb);
.LBB0_764:
	s_waitcnt vmcnt(4)
	v_cvt_f32_ubyte0_e32 v64, s9
	v_rcp_iflag_f32_e32 v64, v64
	s_sub_i32 s12, 0, s9
	s_abs_i32 s11, s8
	s_ashr_i32 s10, s8, 31
	v_mul_f32_e32 v64, 0x4f7ffffe, v64
	v_cvt_u32_f32_e32 v64, v64
	v_add_u32_e32 v152, 0x400, v148
	v_add_u32_e32 v153, 0x400, v149
	v_add_u32_e32 v154, 0x400, v150
	v_readfirstlane_b32 s17, v64
	s_mul_i32 s12, s12, s17
	s_mul_hi_u32 s12, s17, s12
	s_add_i32 s17, s17, s12
	s_mul_hi_u32 s12, s11, s17
	s_mul_i32 s17, s12, s9
	s_sub_i32 s11, s11, s17
	s_add_i32 s26, s12, 1
	s_sub_i32 s17, s11, s9
	s_cmp_ge_u32 s11, s9
	s_cselect_b32 s12, s26, s12
	s_cselect_b32 s11, s17, s11
	s_add_i32 s17, s12, 1
	s_cmp_ge_u32 s11, s9
	s_cselect_b32 s11, s17, s12
	s_xor_b32 s11, s11, s10
	s_sub_i32 s17, s11, s10
	s_mul_i32 s9, s17, s9
	s_sub_i32 s9, s8, s9
	s_lshl_b32 s12, s8, 6
	s_lshl_b32 s8, s9, 5
	s_and_b32 s10, s12, 0xf00
	s_and_b32 s11, s8, 0x60
	s_or_b32 s10, s11, s10
	s_cmp_gt_i32 s9, 63
	s_cselect_b32 s9, 0x80, 0
	s_or_b32 s9, s10, s9
	s_and_b64 s[10:11], s[18:19], exec
	s_cselect_b32 s10, s9, s8
	s_lshl_b32 s12, s17, 7
	s_mul_hi_i32 s19, s12, s3
	s_mul_i32 s18, s12, s3
	s_ashr_i32 s17, s12, 31
	s_lshl_b64 s[18:19], s[18:19], 2
	s_add_u32 s11, s24, s18
	s_addc_u32 s18, s25, s19
	s_ashr_i32 s9, s8, 31
	s_lshl_b64 s[8:9], s[8:9], 2
	s_add_u32 s24, s11, s8
	s_addc_u32 s25, s18, s9
	s_ashr_i32 s11, s10, 31
	s_lshl_b64 s[8:9], s[10:11], 11
	s_add_u32 s8, s22, s8
	s_addc_u32 s9, s23, s9
	s_add_u32 s18, s8, s12
	s_addc_u32 s19, s9, s17
	v_mul_lo_u32 v64, v130, s3
	s_lshl_b32 s8, s3, 5
	v_or_b32_e32 v64, v64, v131
	s_add_u32 s8, s24, s8
	s_addc_u32 s9, s25, 0
	global_load_dwordx4 v[124:127], v64, s[24:25] nt
	global_load_dwordx4 v[116:119], v64, s[8:9] nt
	s_lshl_b32 s8, s3, 6
	s_add_u32 s8, s24, s8
	s_addc_u32 s9, s25, 0
	s_mul_i32 s10, s3, 0x60
	s_add_u32 s10, s24, s10
	s_addc_u32 s11, s25, 0
	global_load_dwordx4 v[120:123], v64, s[8:9] nt
	global_load_dwordx4 v[108:111], v64, s[10:11] nt
	s_lshl_b32 s8, s3, 7
	s_add_u32 s8, s24, s8
	s_addc_u32 s9, s25, 0
	s_mul_i32 s10, s3, 0xa0
	s_add_u32 s10, s24, s10
	s_addc_u32 s11, s25, 0
	global_load_dwordx4 v[112:115], v64, s[8:9] nt
	global_load_dwordx4 v[100:103], v64, s[10:11] nt
	s_mul_i32 s8, s3, 0xc0
	s_add_u32 s8, s24, s8
	s_addc_u32 s9, s25, 0
	s_mul_i32 s10, s3, 0xe0
	s_add_u32 s10, s24, s10
	s_addc_u32 s11, s25, 0
	global_load_dwordx4 v[104:107], v64, s[8:9] nt
	global_load_dwordx4 v[92:95], v64, s[10:11] nt
	s_lshl_b32 s8, s3, 8
	s_add_u32 s8, s24, s8
	s_addc_u32 s9, s25, 0
	s_mul_i32 s10, s3, 0x120
	s_add_u32 s10, s24, s10
	s_addc_u32 s11, s25, 0
	global_load_dwordx4 v[96:99], v64, s[8:9] nt
	global_load_dwordx4 v[84:87], v64, s[10:11] nt
	s_mul_i32 s8, s3, 0x140
	s_add_u32 s8, s24, s8
	s_addc_u32 s9, s25, 0
	s_mul_i32 s10, s3, 0x160
	s_add_u32 s10, s24, s10
	s_addc_u32 s11, s25, 0
	global_load_dwordx4 v[88:91], v64, s[8:9] nt
	global_load_dwordx4 v[76:79], v64, s[10:11] nt
	s_mul_i32 s8, s3, 0x180
	s_add_u32 s8, s24, s8
	s_addc_u32 s9, s25, 0
	s_mul_i32 s10, s3, 0x1a0
	s_add_u32 s10, s24, s10
	s_addc_u32 s11, s25, 0
	global_load_dwordx4 v[80:83], v64, s[8:9] nt
	global_load_dwordx4 v[68:71], v64, s[10:11] nt
	s_mul_i32 s8, s3, 0x1c0
	s_add_u32 s8, s24, s8
	s_addc_u32 s9, s25, 0
	s_mulk_i32 s3, 0x1e0
	s_add_u32 s10, s24, s3
	s_waitcnt vmcnt(29)
	v_pk_mul_f32 v[6:7], v[6:7], s[16:17] op_sel_hi:[1,0]
	v_pk_mul_f32 v[4:5], v[4:5], s[16:17] op_sel_hi:[1,0]
	s_waitcnt vmcnt(28)
	v_pk_mul_f32 v[2:3], v[2:3], s[16:17] op_sel_hi:[1,0]
	v_pk_mul_f32 v[0:1], v[0:1], s[16:17] op_sel_hi:[1,0]
	s_addc_u32 s11, s25, 0
	global_load_dwordx4 v[72:75], v64, s[8:9] nt
	s_nop 0
	global_load_dwordx4 v[64:67], v64, s[10:11] nt
	ds_write_b128 v132, v[4:7]
	ds_write_b128 v133, v[0:3]
	s_waitcnt vmcnt(29)
	v_pk_mul_f32 v[2:3], v[14:15], s[16:17] op_sel_hi:[1,0]
	v_pk_mul_f32 v[0:1], v[12:13], s[16:17] op_sel_hi:[1,0]
	ds_write_b128 v134, v[0:3]
	s_waitcnt vmcnt(28)
	v_pk_mul_f32 v[2:3], v[10:11], s[16:17] op_sel_hi:[1,0]
	v_pk_mul_f32 v[0:1], v[8:9], s[16:17] op_sel_hi:[1,0]
	ds_write_b128 v135, v[0:3]
	s_waitcnt vmcnt(27)
	v_pk_mul_f32 v[2:3], v[22:23], s[16:17] op_sel_hi:[1,0]
	v_pk_mul_f32 v[0:1], v[20:21], s[16:17] op_sel_hi:[1,0]
	ds_write_b128 v136, v[0:3]
	s_waitcnt vmcnt(26)
	v_pk_mul_f32 v[2:3], v[18:19], s[16:17] op_sel_hi:[1,0]
	v_pk_mul_f32 v[0:1], v[16:17], s[16:17] op_sel_hi:[1,0]
	ds_write_b128 v137, v[0:3]
	s_waitcnt vmcnt(25)
	v_pk_mul_f32 v[2:3], v[30:31], s[16:17] op_sel_hi:[1,0]
	v_pk_mul_f32 v[0:1], v[28:29], s[16:17] op_sel_hi:[1,0]
	ds_write_b128 v138, v[0:3]
	s_waitcnt vmcnt(24)
	v_pk_mul_f32 v[2:3], v[26:27], s[16:17] op_sel_hi:[1,0]
	v_pk_mul_f32 v[0:1], v[24:25], s[16:17] op_sel_hi:[1,0]
	ds_write_b128 v139, v[0:3]
	s_waitcnt vmcnt(23)
	v_pk_mul_f32 v[2:3], v[38:39], s[16:17] op_sel_hi:[1,0]
	v_pk_mul_f32 v[0:1], v[36:37], s[16:17] op_sel_hi:[1,0]
	ds_write_b128 v140, v[0:3]
	s_waitcnt vmcnt(22)
	v_pk_mul_f32 v[2:3], v[34:35], s[16:17] op_sel_hi:[1,0]
	v_pk_mul_f32 v[0:1], v[32:33], s[16:17] op_sel_hi:[1,0]
	ds_write_b128 v141, v[0:3]
	s_waitcnt vmcnt(21)
	v_pk_mul_f32 v[2:3], v[46:47], s[16:17] op_sel_hi:[1,0]
	v_pk_mul_f32 v[0:1], v[44:45], s[16:17] op_sel_hi:[1,0]
	ds_write_b128 v142, v[0:3]
	s_waitcnt vmcnt(20)
; #define CONV_LOAD(v, c) do { const unsigned lo_ = (unsigned)(lane >> 3) * (c).N4 + 16u * (unsigned)(lane & 7); _Pragma("unroll") for (int i = 0; i < 16; ++i) v[i] = __builtin_nontemporal_load((const GAS f32x4*)(cuni((const void*)((c).src + (size_t)(8 * i) * (c).N4)) + lo_)); } while (0)
; __device__ __forceinline__ void convert_expert_weights(const float* wgu, const float* wd, unsigned char* WguT, unsigned char* WdT, LAS float* scr, int gw, int NGW, int NIT, int lane) {
;     ...
;         if (!hb) break;
;         it += NGW;
;         const bool ha = it + NGW < NIT; ca = conv_decode(ha ? it + NGW : it, wgu, wd, WguT, WdT); CONV_LOAD(va, ca);
	v_pk_mul_f32 v[2:3], v[42:43], s[16:17] op_sel_hi:[1,0]
	v_pk_mul_f32 v[0:1], v[40:41], s[16:17] op_sel_hi:[1,0]
	ds_write_b128 v143, v[0:3]
	s_waitcnt vmcnt(19)
	v_pk_mul_f32 v[2:3], v[54:55], s[16:17] op_sel_hi:[1,0]
	v_pk_mul_f32 v[0:1], v[52:53], s[16:17] op_sel_hi:[1,0]
	ds_write_b128 v144, v[0:3]
	s_waitcnt vmcnt(18)
	v_pk_mul_f32 v[2:3], v[50:51], s[16:17] op_sel_hi:[1,0]
	v_pk_mul_f32 v[0:1], v[48:49], s[16:17] op_sel_hi:[1,0]
	ds_write_b128 v145, v[0:3]
	s_waitcnt vmcnt(17)
	v_pk_mul_f32 v[2:3], v[62:63], s[16:17] op_sel_hi:[1,0]
	v_pk_mul_f32 v[0:1], v[60:61], s[16:17] op_sel_hi:[1,0]
	ds_write_b128 v146, v[0:3]
	s_waitcnt vmcnt(16)
	v_pk_mul_f32 v[2:3], v[58:59], s[16:17] op_sel_hi:[1,0]
	v_pk_mul_f32 v[0:1], v[56:57], s[16:17] op_sel_hi:[1,0]
	ds_write_b128 v147, v[0:3]
	s_waitcnt lgkmcnt(0)
	ds_read2_b32 v[0:1], v148 offset1:32
	ds_read2_b32 v[8:9], v148 offset0:64 offset1:96
	s_add_u32 s8, s14, 0x4000
	s_waitcnt lgkmcnt(0)
	v_cvt_pk_fp8_f32 v4, v0, v1
	ds_read2_b32 v[0:1], v148 offset0:128 offset1:160
	ds_read2_b32 v[10:11], v148 offset0:192 offset1:224
	ds_read2_b32 v[12:13], v152 offset1:32
	s_waitcnt lgkmcnt(2)
	v_cvt_pk_fp8_f32 v5, v0, v1
	ds_read2_b32 v[0:1], v152 offset0:64 offset1:96
	ds_read2_b32 v[14:15], v152 offset0:128 offset1:160
	s_waitcnt lgkmcnt(2)
	v_cvt_pk_fp8_f32 v6, v12, v13
	ds_read2_b32 v[12:13], v152 offset0:192 offset1:224
	v_cvt_pk_fp8_f32 v4, v8, v9 op_sel:[0,0,1]
	s_waitcnt lgkmcnt(1)
	v_cvt_pk_fp8_f32 v7, v14, v15
	v_cvt_pk_fp8_f32 v5, v10, v11 op_sel:[0,0,1]
	v_cvt_pk_fp8_f32 v6, v0, v1 op_sel:[0,0,1]
	ds_read2_b32 v[0:1], v149 offset1:32
	s_waitcnt lgkmcnt(1)
	v_cvt_pk_fp8_f32 v7, v12, v13 op_sel:[0,0,1]
	v_lshl_add_u64 v[8:9], s[14:15], 0, v[128:129]
	s_addc_u32 s9, s15, 0
	v_add_u32_e32 v155, 0x400, v151
	global_store_dwordx4 v[8:9], v[4:7], off nt
	ds_read2_b32 v[8:9], v149 offset0:64 offset1:96
	s_waitcnt lgkmcnt(1)
	v_cvt_pk_fp8_f32 v4, v0, v1
	ds_read2_b32 v[0:1], v149 offset0:128 offset1:160
	ds_read2_b32 v[10:11], v149 offset0:192 offset1:224
	ds_read2_b32 v[12:13], v153 offset1:32
	s_waitcnt lgkmcnt(2)
	v_cvt_pk_fp8_f32 v5, v0, v1
	ds_read2_b32 v[0:1], v153 offset0:64 offset1:96
	ds_read2_b32 v[14:15], v153 offset0:128 offset1:160
	s_waitcnt lgkmcnt(2)
	v_cvt_pk_fp8_f32 v6, v12, v13
	ds_read2_b32 v[12:13], v153 offset0:192 offset1:224
	v_cvt_pk_fp8_f32 v4, v8, v9 op_sel:[0,0,1]
	s_waitcnt lgkmcnt(1)
	v_cvt_pk_fp8_f32 v7, v14, v15
	v_cvt_pk_fp8_f32 v5, v10, v11 op_sel:[0,0,1]
	v_cvt_pk_fp8_f32 v6, v0, v1 op_sel:[0,0,1]
	ds_read2_b32 v[0:1], v150 offset1:32
	s_waitcnt lgkmcnt(1)
	v_cvt_pk_fp8_f32 v7, v12, v13 op_sel:[0,0,1]
	v_lshl_add_u64 v[8:9], s[8:9], 0, v[128:129]
	s_add_u32 s8, s14, 0x8000
	s_addc_u32 s9, s15, 0
	global_store_dwordx4 v[8:9], v[4:7], off nt
	ds_read2_b32 v[8:9], v150 offset0:64 offset1:96
	s_nop 0
	s_waitcnt lgkmcnt(1)
	v_cvt_pk_fp8_f32 v4, v0, v1
	ds_read2_b32 v[0:1], v150 offset0:128 offset1:160
	ds_read2_b32 v[10:11], v150 offset0:192 offset1:224
	ds_read2_b32 v[12:13], v154 offset1:32
	s_waitcnt lgkmcnt(2)
	v_cvt_pk_fp8_f32 v5, v0, v1
	ds_read2_b32 v[0:1], v154 offset0:64 offset1:96
	ds_read2_b32 v[14:15], v154 offset0:128 offset1:160
	s_waitcnt lgkmcnt(2)
	v_cvt_pk_fp8_f32 v6, v12, v13
	ds_read2_b32 v[12:13], v154 offset0:192 offset1:224
	v_cvt_pk_fp8_f32 v4, v8, v9 op_sel:[0,0,1]
	s_waitcnt lgkmcnt(1)
	v_cvt_pk_fp8_f32 v7, v14, v15
	v_cvt_pk_fp8_f32 v5, v10, v11 op_sel:[0,0,1]
	v_cvt_pk_fp8_f32 v6, v0, v1 op_sel:[0,0,1]
	ds_read2_b32 v[8:9], v151 offset1:32
	s_waitcnt lgkmcnt(1)
	v_cvt_pk_fp8_f32 v7, v12, v13 op_sel:[0,0,1]
	v_lshl_add_u64 v[0:1], s[8:9], 0, v[128:129]
	s_add_u32 s8, s14, 0xc000
	s_addc_u32 s9, s15, 0
	global_store_dwordx4 v[0:1], v[4:7], off nt
	ds_read2_b32 v[4:5], v151 offset0:64 offset1:96
	s_waitcnt lgkmcnt(1)
	v_cvt_pk_fp8_f32 v0, v8, v9
	ds_read2_b32 v[6:7], v151 offset0:128 offset1:160
	ds_read2_b32 v[8:9], v151 offset0:192 offset1:224
	ds_read2_b32 v[10:11], v155 offset1:32
	s_waitcnt lgkmcnt(3)
	v_cvt_pk_fp8_f32 v0, v4, v5 op_sel:[0,0,1]
	s_waitcnt lgkmcnt(2)
	v_cvt_pk_fp8_f32 v1, v6, v7
	ds_read2_b32 v[6:7], v155 offset0:128 offset1:160
	ds_read2_b32 v[12:13], v155 offset0:64 offset1:96
	s_waitcnt lgkmcnt(2)
	v_cvt_pk_fp8_f32 v2, v10, v11
	ds_read2_b32 v[10:11], v155 offset0:192 offset1:224
	v_cvt_pk_fp8_f32 v1, v8, v9 op_sel:[0,0,1]
	s_waitcnt lgkmcnt(2)
	v_cvt_pk_fp8_f32 v3, v6, v7
	s_waitcnt lgkmcnt(1)
	v_cvt_pk_fp8_f32 v2, v12, v13 op_sel:[0,0,1]
	v_lshl_add_u64 v[4:5], s[8:9], 0, v[128:129]
	s_andn2_b64 vcc, exec, s[20:21]
	s_waitcnt lgkmcnt(0)
	v_cvt_pk_fp8_f32 v3, v10, v11 op_sel:[0,0,1]
	s_mov_b64 s[20:21], -1
	global_store_dwordx4 v[4:5], v[0:3], off nt
	s_waitcnt lgkmcnt(0)
	s_cbranch_vccnz .LBB0_758
	s_add_i32 s3, s0, s38
	s_cmp_lt_i32 s3, s45
	s_cselect_b32 s3, s3, s1
	s_cmp_lt_i32 s3, 0x10000
	s_cselect_b64 s[14:15], -1, 0
	s_cmp_gt_i32 s3, 0xffff
	s_mov_b64 s[24:25], -1
	s_cbranch_scc0 .LBB0_767
	s_add_i32 s8, s3, 0xffff0000
	s_lshr_b32 s12, s8, 10
	s_and_b32 s8, s3, 0x3ff
	s_lshl_b64 s[10:11], s[12:13], 22
	s_lshl_b64 s[20:21], s[12:13], 24
	s_add_u32 s22, s6, s20
	s_addc_u32 s23, s7, s21
	s_add_u32 s20, s77, s10
	v_readlane_b32 s9, v252, 33
	s_addc_u32 s21, s9, s11
	s_mov_b64 s[24:25], 0

; __device__ __forceinline__ unsigned cvt_pk_bf16(float lo, float hi) { unsigned r; asm volatile("v_cvt_pk_bf16_f32 %0, %1, %2" : "=v"(r) : "v"(lo), "v"(hi)); return r; }
; __device__ __forceinline__ unsigned cvt_pk4_fp8(float a, float b, float c, float d) { int w; asm("" : "=v"(w));     w = __builtin_amdgcn_cvt_pk_fp8_f32(a, b, w, false); w = __builtin_amdgcn_cvt_pk_fp8_f32(c, d, w, true); return (unsigned)w; }
;     __device__ __forceinline__ void operator()(const f32x4 (&acc)[2][2][4][2], const Unit& u, int wr, int wc, int fr, int fq) const {
;         const int row0 = u.pm * BM + wr * 64 + fr, col0 = u.pn * BM + wc * 32 + 8 * fq;
;         f32x4 gv[2][2];
; #pragma unroll
;         for (int bj = 0; bj < 2; ++bj)
; #pragma unroll
;             for (int n = 0; n < 2; ++n) gv[bj][n] = *(const f32x4*)(g + col0 + bj * HALF + 4 * n);
; #pragma unroll
;         for (int ai = 0; ai < 2; ++ai)
; #pragma unroll
;             for (int m = 0; m < 4; ++m) { const size_t off = (size_t)(row0 + ai * HALF + m * 16) * DM + col0;
; #pragma unroll
;                 for (int bj = 0; bj < 2; ++bj) { const f32x4 v0 = *(const f32x4*)(base + off + bj * HALF) + acc[ai][bj][m][0], v1 = *(const f32x4*)(base + off + bj * HALF + 4) + acc[ai][bj][m][1];
;                     { u32x4 xw; xw.x = cvt_pk_bf16(v0[0], v0[1]); xw.y = cvt_pk_bf16(v0[2], v0[3]); xw.z = cvt_pk_bf16(v1[0], v1[1]); xw.w = cvt_pk_bf16(v1[2], v1[3]); *(u32x4*)(C + off + bj * HALF) = xw; }
;                     const f32x4 h0 = v0 * gv[bj][0], h1 = v1 * gv[bj][1];
;                     u32x2 w; w.x = cvt_pk4_fp8(h0[0], h0[1], h0[2], h0[3]); w.y = cvt_pk4_fp8(h1[0], h1[1], h1[2], h1[3]);
;                     *(u32x2*)(H2 + off + bj * HALF) = w; } }
;     }
.LBB0_921:
	s_lshl_b32 s36, s52, 8
	v_mbcnt_lo_u32_b32 v96, -1, 0
	v_mbcnt_hi_u32_b32 v96, -1, v96
	s_add_i32 s36, s36, s34
	s_lshl_b32 s35, s35, 8
	v_ashrrev_i32_e32 v97, 1, v96
	s_or_b32 s35, s35, s84
	v_and_b32_e32 v97, -8, v97
	v_and_or_b32 v144, v96, 15, s36
	v_add_u32_e32 v148, s35, v97
	v_ashrrev_i32_e32 v145, 31, v144
	v_ashrrev_i32_e32 v149, 31, v148
	v_lshlrev_b64 v[96:97], 11, v[144:145]
	v_lshl_add_u64 v[146:147], v[96:97], 0, v[148:149]
	v_lshl_add_u64 v[168:169], v[146:147], 2, s[6:7]
	global_load_dwordx4 v[160:163], v[168:169], off
	global_load_dwordx4 v[164:167], v[168:169], off offset:16
	v_lshl_add_u64 v[100:101], v[148:149], 2, s[12:13]
	global_load_dwordx4 v[116:119], v[100:101], off
	global_load_dwordx4 v[112:115], v[100:101], off offset:16
	global_load_dwordx4 v[96:99], v[100:101], off offset:528
	s_nop 0
	global_load_dwordx4 v[100:103], v[100:101], off offset:512
	v_lshlrev_b32_e32 v232, 2, v146
	global_load_dwordx4 v[176:179], v232, s[6:7] offset:512
	global_load_dwordx4 v[180:183], v232, s[6:7] offset:528
	v_add_u32_e32 v233, 0x20000, v232
	global_load_dwordx4 v[184:187], v233, s[6:7]
	global_load_dwordx4 v[188:191], v233, s[6:7] offset:16
	v_add_u32_e32 v233, 0x20000, v232
	global_load_dwordx4 v[192:195], v233, s[6:7] offset:512
	global_load_dwordx4 v[196:199], v233, s[6:7] offset:528
	v_add_u32_e32 v233, 0x40000, v232
	global_load_dwordx4 v[200:203], v233, s[6:7]
	global_load_dwordx4 v[204:207], v233, s[6:7] offset:16
	v_add_u32_e32 v233, 0x40000, v232
	global_load_dwordx4 v[208:211], v233, s[6:7] offset:512
	global_load_dwordx4 v[212:215], v233, s[6:7] offset:528
	v_add_u32_e32 v233, 0x60000, v232
	global_load_dwordx4 v[216:219], v233, s[6:7]
	global_load_dwordx4 v[220:223], v233, s[6:7] offset:16
	v_add_u32_e32 v233, 0x60000, v232
	global_load_dwordx4 v[224:227], v233, s[6:7] offset:512
	global_load_dwordx4 v[228:231], v233, s[6:7] offset:528
	v_lshl_add_u64 v[172:173], v[146:147], 1, s[14:15]
	v_lshl_add_u64 v[174:175], s[10:11], 0, v[146:147]
	s_andn2_b64 vcc, exec, s[50:51]
	s_mov_b64 s[50:51], -1
	s_waitcnt vmcnt(19)
	v_pk_add_f32 v[140:141], v[140:141], v[160:161]
	s_waitcnt vmcnt(18)
	v_pk_add_f32 v[160:161], v[138:139], v[166:167]
	v_pk_add_f32 v[138:139], v[136:137], v[164:165]
	v_pk_add_f32 v[142:143], v[142:143], v[162:163]
	v_cvt_pk_bf16_f32 v136, v140, v141
	s_waitcnt vmcnt(17)
	v_pk_mul_f32 v[140:141], v[116:117], v[140:141]
	s_waitcnt vmcnt(16)
	v_pk_mul_f32 v[162:163], v[112:113], v[138:139]
	v_cvt_pk_fp8_f32 v170, v140, v141
	v_cvt_pk_fp8_f32 v171, v162, v163
	v_cvt_pk_bf16_f32 v137, v142, v143
	v_pk_mul_f32 v[140:141], v[118:119], v[142:143]
	v_pk_mul_f32 v[142:143], v[114:115], v[160:161]
	v_cvt_pk_fp8_f32 v170, v140, v141 op_sel:[0,0,1]
	v_cvt_pk_fp8_f32 v171, v142, v143 op_sel:[0,0,1]
	v_cvt_pk_bf16_f32 v138, v138, v139
	v_cvt_pk_bf16_f32 v139, v160, v161
	global_store_dwordx4 v[172:173], v[136:139], off
	global_store_dwordx2 v[174:175], v[170:171], off
	v_or_b32_e32 v162, 16, v144
	v_ashrrev_i32_e32 v163, 31, v162
	v_lshlrev_b64 v[162:163], 11, v[162:163]
	v_lshl_add_u64 v[162:163], v[162:163], 0, v[148:149]
	v_lshl_add_u64 v[164:165], v[162:163], 2, s[6:7]
	s_waitcnt vmcnt(14)
	v_pk_add_f32 v[132:133], v[132:133], v[176:177]
	v_pk_add_f32 v[136:137], v[130:131], v[182:183]
	v_pk_add_f32 v[130:131], v[128:129], v[180:181]
	v_pk_add_f32 v[134:135], v[134:135], v[178:179]
	v_add_u32_e32 v233, 0x100000, v232
	global_load_dwordx4 v[176:179], v233, s[6:7]
	global_load_dwordx4 v[180:183], v233, s[6:7] offset:16
	v_cvt_pk_bf16_f32 v128, v132, v133
	v_pk_mul_f32 v[132:133], v[100:101], v[132:133]
	v_pk_mul_f32 v[138:139], v[96:97], v[130:131]
	v_cvt_pk_fp8_f32 v160, v132, v133
	v_cvt_pk_fp8_f32 v161, v138, v139
	v_cvt_pk_bf16_f32 v129, v134, v135
	v_pk_mul_f32 v[132:133], v[102:103], v[134:135]
	v_pk_mul_f32 v[134:135], v[98:99], v[136:137]
	v_cvt_pk_fp8_f32 v160, v132, v133 op_sel:[0,0,1]
	v_cvt_pk_fp8_f32 v161, v134, v135 op_sel:[0,0,1]
	v_cvt_pk_bf16_f32 v130, v130, v131
	v_cvt_pk_bf16_f32 v131, v136, v137
	global_store_dwordx4 v[172:173], v[128:131], off offset:256
	global_store_dwordx2 v[174:175], v[160:161], off offset:128
	v_lshl_add_u64 v[138:139], v[162:163], 1, s[14:15]
	v_lshl_add_u64 v[140:141], s[10:11], 0, v[162:163]
	s_waitcnt vmcnt(16)
	v_pk_add_f32 v[124:125], v[124:125], v[184:185]
	v_pk_add_f32 v[128:129], v[122:123], v[190:191]
	v_pk_add_f32 v[122:123], v[120:121], v[188:189]
	v_pk_add_f32 v[126:127], v[126:127], v[186:187]
	v_add_u32_e32 v233, 0x100000, v232
	global_load_dwordx4 v[184:187], v233, s[6:7] offset:512
	global_load_dwordx4 v[188:191], v233, s[6:7] offset:528
	v_cvt_pk_bf16_f32 v120, v124, v125
	v_pk_mul_f32 v[124:125], v[116:117], v[124:125]
	v_pk_mul_f32 v[130:131], v[112:113], v[122:123]
	v_cvt_pk_fp8_f32 v136, v124, v125
	v_cvt_pk_fp8_f32 v137, v130, v131
	v_cvt_pk_bf16_f32 v121, v126, v127
	v_pk_mul_f32 v[124:125], v[118:119], v[126:127]
	v_pk_mul_f32 v[126:127], v[114:115], v[128:129]
	v_cvt_pk_fp8_f32 v136, v124, v125 op_sel:[0,0,1]
	v_cvt_pk_fp8_f32 v137, v126, v127 op_sel:[0,0,1]
	v_cvt_pk_bf16_f32 v122, v122, v123
	v_cvt_pk_bf16_f32 v123, v128, v129
	global_store_dwordx4 v[138:139], v[120:123], off
	global_store_dwordx2 v[140:141], v[136:137], off
	v_or_b32_e32 v130, 32, v144
	v_ashrrev_i32_e32 v131, 31, v130
	v_lshlrev_b64 v[130:131], 11, v[130:131]
	v_lshl_add_u64 v[130:131], v[130:131], 0, v[148:149]
	v_lshl_add_u64 v[132:133], v[130:131], 2, s[6:7]
	s_waitcnt vmcnt(18)
; __device__ __forceinline__ unsigned cvt_pk_bf16(float lo, float hi) { unsigned r; asm volatile("v_cvt_pk_bf16_f32 %0, %1, %2" : "=v"(r) : "v"(lo), "v"(hi)); return r; }
; __device__ __forceinline__ unsigned cvt_pk4_fp8(float a, float b, float c, float d) { int w; asm("" : "=v"(w));     w = __builtin_amdgcn_cvt_pk_fp8_f32(a, b, w, false); w = __builtin_amdgcn_cvt_pk_fp8_f32(c, d, w, true); return (unsigned)w; }
;     __device__ __forceinline__ void operator()(const f32x4 (&acc)[2][2][4][2], const Unit& u, int wr, int wc, int fr, int fq) const {
;         const int row0 = u.pm * BM + wr * 64 + fr, col0 = u.pn * BM + wc * 32 + 8 * fq;
;         f32x4 gv[2][2];
; #pragma unroll
;         for (int bj = 0; bj < 2; ++bj)
; #pragma unroll
;             for (int n = 0; n < 2; ++n) gv[bj][n] = *(const f32x4*)(g + col0 + bj * HALF + 4 * n);
; #pragma unroll
;         for (int ai = 0; ai < 2; ++ai)
; #pragma unroll
;             for (int m = 0; m < 4; ++m) { const size_t off = (size_t)(row0 + ai * HALF + m * 16) * DM + col0;
; #pragma unroll
;                 for (int bj = 0; bj < 2; ++bj) { const f32x4 v0 = *(const f32x4*)(base + off + bj * HALF) + acc[ai][bj][m][0], v1 = *(const f32x4*)(base + off + bj * HALF + 4) + acc[ai][bj][m][1];
;                     { u32x4 xw; xw.x = cvt_pk_bf16(v0[0], v0[1]); xw.y = cvt_pk_bf16(v0[2], v0[3]); xw.z = cvt_pk_bf16(v1[0], v1[1]); xw.w = cvt_pk_bf16(v1[2], v1[3]); *(u32x4*)(C + off + bj * HALF) = xw; }
;                     const f32x4 h0 = v0 * gv[bj][0], h1 = v1 * gv[bj][1];
;                     u32x2 w; w.x = cvt_pk4_fp8(h0[0], h0[1], h0[2], h0[3]); w.y = cvt_pk4_fp8(h1[0], h1[1], h1[2], h1[3]);
;                     *(u32x2*)(H2 + off + bj * HALF) = w; } }
;     }
	v_pk_add_f32 v[108:109], v[108:109], v[192:193]
	v_pk_add_f32 v[120:121], v[106:107], v[198:199]
	v_pk_add_f32 v[106:107], v[104:105], v[196:197]
	v_pk_add_f32 v[110:111], v[110:111], v[194:195]
	v_add_u32_e32 v233, 0x120000, v232
	global_load_dwordx4 v[192:195], v233, s[6:7]
	global_load_dwordx4 v[196:199], v233, s[6:7] offset:16
	v_cvt_pk_bf16_f32 v104, v108, v109
	v_pk_mul_f32 v[108:109], v[100:101], v[108:109]
	v_pk_mul_f32 v[122:123], v[96:97], v[106:107]
	v_cvt_pk_fp8_f32 v128, v108, v109
	v_cvt_pk_fp8_f32 v129, v122, v123
	v_cvt_pk_bf16_f32 v105, v110, v111
	v_pk_mul_f32 v[108:109], v[102:103], v[110:111]
	v_pk_mul_f32 v[110:111], v[98:99], v[120:121]
	v_cvt_pk_fp8_f32 v128, v108, v109 op_sel:[0,0,1]
	v_cvt_pk_fp8_f32 v129, v110, v111 op_sel:[0,0,1]
	v_cvt_pk_bf16_f32 v106, v106, v107
	v_cvt_pk_bf16_f32 v107, v120, v121
	global_store_dwordx4 v[138:139], v[104:107], off offset:256
	global_store_dwordx2 v[140:141], v[128:129], off offset:128
	v_lshl_add_u64 v[122:123], v[130:131], 1, s[14:15]
	v_lshl_add_u64 v[124:125], s[10:11], 0, v[130:131]
	s_waitcnt vmcnt(20)
	v_pk_add_f32 v[92:93], v[92:93], v[200:201]
	v_pk_add_f32 v[104:105], v[90:91], v[206:207]
	v_pk_add_f32 v[90:91], v[88:89], v[204:205]
	v_pk_add_f32 v[94:95], v[94:95], v[202:203]
	v_add_u32_e32 v233, 0x120000, v232
	global_load_dwordx4 v[200:203], v233, s[6:7] offset:512
	global_load_dwordx4 v[204:207], v233, s[6:7] offset:528
	v_cvt_pk_bf16_f32 v88, v92, v93
	v_pk_mul_f32 v[92:93], v[116:117], v[92:93]
	v_pk_mul_f32 v[106:107], v[112:113], v[90:91]
	v_cvt_pk_fp8_f32 v120, v92, v93
	v_cvt_pk_fp8_f32 v121, v106, v107
	v_cvt_pk_bf16_f32 v89, v94, v95
	v_pk_mul_f32 v[92:93], v[118:119], v[94:95]
	v_pk_mul_f32 v[94:95], v[114:115], v[104:105]
	v_cvt_pk_fp8_f32 v120, v92, v93 op_sel:[0,0,1]
	v_cvt_pk_fp8_f32 v121, v94, v95 op_sel:[0,0,1]
	v_cvt_pk_bf16_f32 v90, v90, v91
	v_cvt_pk_bf16_f32 v91, v104, v105
	global_store_dwordx4 v[122:123], v[88:91], off
	global_store_dwordx2 v[124:125], v[120:121], off
	v_or_b32_e32 v106, 48, v144
	v_ashrrev_i32_e32 v107, 31, v106
	v_lshlrev_b64 v[106:107], 11, v[106:107]
	v_lshl_add_u64 v[106:107], v[106:107], 0, v[148:149]
	v_lshl_add_u64 v[108:109], v[106:107], 2, s[6:7]
	s_waitcnt vmcnt(22)
	v_pk_add_f32 v[84:85], v[84:85], v[208:209]
	v_pk_add_f32 v[88:89], v[82:83], v[214:215]
	v_pk_add_f32 v[82:83], v[80:81], v[212:213]
	v_pk_add_f32 v[86:87], v[86:87], v[210:211]
	v_add_u32_e32 v233, 0x140000, v232
	global_load_dwordx4 v[208:211], v233, s[6:7]
	global_load_dwordx4 v[212:215], v233, s[6:7] offset:16
	v_cvt_pk_bf16_f32 v80, v84, v85
	v_pk_mul_f32 v[84:85], v[100:101], v[84:85]
	v_pk_mul_f32 v[90:91], v[96:97], v[82:83]
	v_cvt_pk_fp8_f32 v104, v84, v85
	v_cvt_pk_fp8_f32 v105, v90, v91
	v_cvt_pk_bf16_f32 v81, v86, v87
	v_pk_mul_f32 v[84:85], v[102:103], v[86:87]
	v_pk_mul_f32 v[86:87], v[98:99], v[88:89]
	v_cvt_pk_fp8_f32 v104, v84, v85 op_sel:[0,0,1]
	v_cvt_pk_fp8_f32 v105, v86, v87 op_sel:[0,0,1]
	v_cvt_pk_bf16_f32 v82, v82, v83
	v_cvt_pk_bf16_f32 v83, v88, v89
	global_store_dwordx4 v[122:123], v[80:83], off offset:256
	global_store_dwordx2 v[124:125], v[104:105], off offset:128
	v_lshl_add_u64 v[90:91], v[106:107], 1, s[14:15]
	v_lshl_add_u64 v[92:93], s[10:11], 0, v[106:107]
	s_waitcnt vmcnt(24)
	v_pk_add_f32 v[76:77], v[76:77], v[216:217]
	v_pk_add_f32 v[80:81], v[74:75], v[222:223]
	v_pk_add_f32 v[74:75], v[72:73], v[220:221]
	v_pk_add_f32 v[78:79], v[78:79], v[218:219]
	v_add_u32_e32 v233, 0x140000, v232
	global_load_dwordx4 v[216:219], v233, s[6:7] offset:512
	global_load_dwordx4 v[220:223], v233, s[6:7] offset:528
	v_cvt_pk_bf16_f32 v72, v76, v77
	v_pk_mul_f32 v[76:77], v[116:117], v[76:77]
	v_pk_mul_f32 v[82:83], v[112:113], v[74:75]
	v_cvt_pk_fp8_f32 v88, v76, v77
	v_cvt_pk_fp8_f32 v89, v82, v83
	v_cvt_pk_bf16_f32 v73, v78, v79
	v_pk_mul_f32 v[76:77], v[118:119], v[78:79]
	v_pk_mul_f32 v[78:79], v[114:115], v[80:81]
	v_cvt_pk_fp8_f32 v88, v76, v77 op_sel:[0,0,1]
	v_cvt_pk_fp8_f32 v89, v78, v79 op_sel:[0,0,1]
	v_cvt_pk_bf16_f32 v74, v74, v75
	v_cvt_pk_bf16_f32 v75, v80, v81
	global_store_dwordx4 v[90:91], v[72:75], off
	global_store_dwordx2 v[92:93], v[88:89], off
	v_lshl_add_u64 v[82:83], v[146:147], 0, s[20:21]
	v_lshl_add_u64 v[84:85], v[82:83], 2, s[6:7]
	s_waitcnt vmcnt(26)
	v_pk_add_f32 v[68:69], v[68:69], v[224:225]
	v_pk_add_f32 v[72:73], v[66:67], v[230:231]
	v_pk_add_f32 v[66:67], v[64:65], v[228:229]
	v_pk_add_f32 v[70:71], v[70:71], v[226:227]
	v_add_u32_e32 v233, 0x160000, v232
	global_load_dwordx4 v[224:227], v233, s[6:7]
	global_load_dwordx4 v[228:231], v233, s[6:7] offset:16
	v_cvt_pk_bf16_f32 v64, v68, v69
	v_pk_mul_f32 v[68:69], v[100:101], v[68:69]
	v_pk_mul_f32 v[74:75], v[96:97], v[66:67]
	v_cvt_pk_fp8_f32 v80, v68, v69
	v_cvt_pk_fp8_f32 v81, v74, v75
	v_cvt_pk_bf16_f32 v65, v70, v71
	v_pk_mul_f32 v[68:69], v[102:103], v[70:71]
	v_pk_mul_f32 v[70:71], v[98:99], v[72:73]
	v_cvt_pk_fp8_f32 v80, v68, v69 op_sel:[0,0,1]
	v_cvt_pk_fp8_f32 v81, v70, v71 op_sel:[0,0,1]
	v_cvt_pk_bf16_f32 v66, v66, v67
	v_cvt_pk_bf16_f32 v67, v72, v73
	global_store_dwordx4 v[90:91], v[64:67], off offset:256
	global_store_dwordx2 v[92:93], v[80:81], off offset:128
	v_lshl_add_u64 v[74:75], v[82:83], 1, s[14:15]
	v_lshl_add_u64 v[76:77], s[10:11], 0, v[82:83]
	s_waitcnt vmcnt(26)
; __device__ __forceinline__ unsigned cvt_pk_bf16(float lo, float hi) { unsigned r; asm volatile("v_cvt_pk_bf16_f32 %0, %1, %2" : "=v"(r) : "v"(lo), "v"(hi)); return r; }
; __device__ __forceinline__ unsigned cvt_pk4_fp8(float a, float b, float c, float d) { int w; asm("" : "=v"(w));     w = __builtin_amdgcn_cvt_pk_fp8_f32(a, b, w, false); w = __builtin_amdgcn_cvt_pk_fp8_f32(c, d, w, true); return (unsigned)w; }
;     __device__ __forceinline__ void operator()(const f32x4 (&acc)[2][2][4][2], const Unit& u, int wr, int wc, int fr, int fq) const {
;         const int row0 = u.pm * BM + wr * 64 + fr, col0 = u.pn * BM + wc * 32 + 8 * fq;
;         f32x4 gv[2][2];
; #pragma unroll
;         for (int bj = 0; bj < 2; ++bj)
; #pragma unroll
;             for (int n = 0; n < 2; ++n) gv[bj][n] = *(const f32x4*)(g + col0 + bj * HALF + 4 * n);
; #pragma unroll
;         for (int ai = 0; ai < 2; ++ai)
; #pragma unroll
;             for (int m = 0; m < 4; ++m) { const size_t off = (size_t)(row0 + ai * HALF + m * 16) * DM + col0;
; #pragma unroll
;                 for (int bj = 0; bj < 2; ++bj) { const f32x4 v0 = *(const f32x4*)(base + off + bj * HALF) + acc[ai][bj][m][0], v1 = *(const f32x4*)(base + off + bj * HALF + 4) + acc[ai][bj][m][1];
;                     { u32x4 xw; xw.x = cvt_pk_bf16(v0[0], v0[1]); xw.y = cvt_pk_bf16(v0[2], v0[3]); xw.z = cvt_pk_bf16(v1[0], v1[1]); xw.w = cvt_pk_bf16(v1[2], v1[3]); *(u32x4*)(C + off + bj * HALF) = xw; }
;                     const f32x4 h0 = v0 * gv[bj][0], h1 = v1 * gv[bj][1];
;                     u32x2 w; w.x = cvt_pk4_fp8(h0[0], h0[1], h0[2], h0[3]); w.y = cvt_pk4_fp8(h1[0], h1[1], h1[2], h1[3]);
;                     *(u32x2*)(H2 + off + bj * HALF) = w; } }
;     }
	v_pk_add_f32 v[60:61], v[60:61], v[176:177]
	v_pk_add_f32 v[64:65], v[58:59], v[182:183]
	v_pk_add_f32 v[58:59], v[56:57], v[180:181]
	v_pk_add_f32 v[62:63], v[62:63], v[178:179]
	v_add_u32_e32 v233, 0x160000, v232
	global_load_dwordx4 v[176:179], v233, s[6:7] offset:512
	global_load_dwordx4 v[180:183], v233, s[6:7] offset:528
	v_cvt_pk_bf16_f32 v56, v60, v61
	v_pk_mul_f32 v[60:61], v[116:117], v[60:61]
	v_pk_mul_f32 v[66:67], v[112:113], v[58:59]
	v_cvt_pk_fp8_f32 v72, v60, v61
	v_cvt_pk_fp8_f32 v73, v66, v67
	v_cvt_pk_bf16_f32 v57, v62, v63
	v_pk_mul_f32 v[60:61], v[118:119], v[62:63]
	v_pk_mul_f32 v[62:63], v[114:115], v[64:65]
	v_cvt_pk_fp8_f32 v72, v60, v61 op_sel:[0,0,1]
	v_cvt_pk_fp8_f32 v73, v62, v63 op_sel:[0,0,1]
	v_cvt_pk_bf16_f32 v58, v58, v59
	v_cvt_pk_bf16_f32 v59, v64, v65
	global_store_dwordx4 v[74:75], v[56:59], off
	global_store_dwordx2 v[76:77], v[72:73], off
	v_lshl_add_u64 v[66:67], v[146:147], 0, s[22:23]
	v_lshl_add_u64 v[68:69], v[66:67], 2, s[6:7]
	s_waitcnt vmcnt(26)
	v_pk_add_f32 v[52:53], v[52:53], v[184:185]
	v_pk_add_f32 v[56:57], v[50:51], v[190:191]
	v_pk_add_f32 v[50:51], v[48:49], v[188:189]
	v_pk_add_f32 v[54:55], v[54:55], v[186:187]
	v_cvt_pk_bf16_f32 v48, v52, v53
	v_pk_mul_f32 v[52:53], v[100:101], v[52:53]
	v_pk_mul_f32 v[58:59], v[96:97], v[50:51]
	v_cvt_pk_fp8_f32 v64, v52, v53
	v_cvt_pk_fp8_f32 v65, v58, v59
	v_cvt_pk_bf16_f32 v49, v54, v55
	v_pk_mul_f32 v[52:53], v[102:103], v[54:55]
	v_pk_mul_f32 v[54:55], v[98:99], v[56:57]
	v_cvt_pk_fp8_f32 v64, v52, v53 op_sel:[0,0,1]
	v_cvt_pk_fp8_f32 v65, v54, v55 op_sel:[0,0,1]
	v_cvt_pk_bf16_f32 v50, v50, v51
	v_cvt_pk_bf16_f32 v51, v56, v57
	global_store_dwordx4 v[74:75], v[48:51], off offset:256
	global_store_dwordx2 v[76:77], v[64:65], off offset:128
	v_lshl_add_u64 v[58:59], v[66:67], 1, s[14:15]
	v_lshl_add_u64 v[60:61], s[10:11], 0, v[66:67]
	s_waitcnt vmcnt(24)
	v_pk_add_f32 v[44:45], v[44:45], v[192:193]
	v_pk_add_f32 v[48:49], v[42:43], v[198:199]
	v_pk_add_f32 v[42:43], v[40:41], v[196:197]
	v_pk_add_f32 v[46:47], v[46:47], v[194:195]
	v_cvt_pk_bf16_f32 v40, v44, v45
	v_pk_mul_f32 v[44:45], v[116:117], v[44:45]
	v_pk_mul_f32 v[50:51], v[112:113], v[42:43]
	v_cvt_pk_fp8_f32 v56, v44, v45
	v_cvt_pk_fp8_f32 v57, v50, v51
	v_cvt_pk_bf16_f32 v41, v46, v47
	v_pk_mul_f32 v[44:45], v[118:119], v[46:47]
	v_pk_mul_f32 v[46:47], v[114:115], v[48:49]
	v_cvt_pk_fp8_f32 v56, v44, v45 op_sel:[0,0,1]
	v_cvt_pk_fp8_f32 v57, v46, v47 op_sel:[0,0,1]
	v_cvt_pk_bf16_f32 v42, v42, v43
	v_cvt_pk_bf16_f32 v43, v48, v49
	global_store_dwordx4 v[58:59], v[40:43], off
	global_store_dwordx2 v[60:61], v[56:57], off
	v_lshl_add_u64 v[50:51], v[146:147], 0, s[24:25]
	v_lshl_add_u64 v[52:53], v[50:51], 2, s[6:7]
	s_waitcnt vmcnt(22)
	v_pk_add_f32 v[36:37], v[36:37], v[200:201]
	v_pk_add_f32 v[40:41], v[34:35], v[206:207]
	v_pk_add_f32 v[34:35], v[32:33], v[204:205]
	v_pk_add_f32 v[38:39], v[38:39], v[202:203]
	v_cvt_pk_bf16_f32 v32, v36, v37
	v_pk_mul_f32 v[36:37], v[100:101], v[36:37]
	v_pk_mul_f32 v[42:43], v[96:97], v[34:35]
	v_cvt_pk_fp8_f32 v48, v36, v37
	v_cvt_pk_fp8_f32 v49, v42, v43
	v_cvt_pk_bf16_f32 v33, v38, v39
	v_pk_mul_f32 v[36:37], v[102:103], v[38:39]
	v_pk_mul_f32 v[38:39], v[98:99], v[40:41]
	v_cvt_pk_fp8_f32 v48, v36, v37 op_sel:[0,0,1]
	v_cvt_pk_fp8_f32 v49, v38, v39 op_sel:[0,0,1]
	v_cvt_pk_bf16_f32 v34, v34, v35
	v_cvt_pk_bf16_f32 v35, v40, v41
	global_store_dwordx4 v[58:59], v[32:35], off offset:256
	global_store_dwordx2 v[60:61], v[48:49], off offset:128
	v_lshl_add_u64 v[42:43], v[50:51], 1, s[14:15]
	v_lshl_add_u64 v[44:45], s[10:11], 0, v[50:51]
	s_waitcnt vmcnt(20)
	v_pk_add_f32 v[28:29], v[28:29], v[208:209]
	v_pk_add_f32 v[32:33], v[26:27], v[214:215]
	v_pk_add_f32 v[26:27], v[24:25], v[212:213]
	v_pk_add_f32 v[30:31], v[30:31], v[210:211]
	v_cvt_pk_bf16_f32 v24, v28, v29
	v_pk_mul_f32 v[28:29], v[116:117], v[28:29]
	v_pk_mul_f32 v[34:35], v[112:113], v[26:27]
	v_cvt_pk_fp8_f32 v40, v28, v29
	v_cvt_pk_fp8_f32 v41, v34, v35
	v_cvt_pk_bf16_f32 v25, v30, v31
	v_pk_mul_f32 v[28:29], v[118:119], v[30:31]
	v_pk_mul_f32 v[30:31], v[114:115], v[32:33]
	v_cvt_pk_fp8_f32 v40, v28, v29 op_sel:[0,0,1]
	v_cvt_pk_fp8_f32 v41, v30, v31 op_sel:[0,0,1]
	v_cvt_pk_bf16_f32 v26, v26, v27
	v_cvt_pk_bf16_f32 v27, v32, v33
	global_store_dwordx4 v[42:43], v[24:27], off
	global_store_dwordx2 v[44:45], v[40:41], off
	v_lshl_add_u64 v[34:35], v[146:147], 0, s[26:27]
	v_lshl_add_u64 v[36:37], v[34:35], 2, s[6:7]
	s_waitcnt vmcnt(18)
	v_pk_add_f32 v[20:21], v[20:21], v[216:217]
	v_pk_add_f32 v[24:25], v[18:19], v[222:223]
	v_pk_add_f32 v[18:19], v[16:17], v[220:221]
	v_pk_add_f32 v[22:23], v[22:23], v[218:219]
	v_cvt_pk_bf16_f32 v16, v20, v21
	v_pk_mul_f32 v[20:21], v[100:101], v[20:21]
	v_pk_mul_f32 v[26:27], v[96:97], v[18:19]
	v_cvt_pk_fp8_f32 v32, v20, v21
	v_cvt_pk_fp8_f32 v33, v26, v27
	v_cvt_pk_bf16_f32 v17, v22, v23
	v_pk_mul_f32 v[20:21], v[102:103], v[22:23]
	v_pk_mul_f32 v[22:23], v[98:99], v[24:25]
	v_cvt_pk_fp8_f32 v32, v20, v21 op_sel:[0,0,1]
	v_cvt_pk_fp8_f32 v33, v22, v23 op_sel:[0,0,1]
	v_cvt_pk_bf16_f32 v18, v18, v19
	v_cvt_pk_bf16_f32 v19, v24, v25
	global_store_dwordx4 v[42:43], v[16:19], off offset:256
	global_store_dwordx2 v[44:45], v[32:33], off offset:128
	v_lshl_add_u64 v[26:27], v[34:35], 1, s[14:15]
	v_lshl_add_u64 v[28:29], s[10:11], 0, v[34:35]
	s_waitcnt vmcnt(16)
	v_pk_add_f32 v[12:13], v[12:13], v[224:225]
	v_pk_add_f32 v[16:17], v[10:11], v[230:231]
	v_pk_add_f32 v[10:11], v[8:9], v[228:229]
	v_pk_add_f32 v[14:15], v[14:15], v[226:227]
	v_cvt_pk_bf16_f32 v8, v12, v13
	v_pk_mul_f32 v[12:13], v[116:117], v[12:13]
	v_pk_mul_f32 v[18:19], v[112:113], v[10:11]
	v_cvt_pk_fp8_f32 v24, v12, v13
	v_cvt_pk_fp8_f32 v25, v18, v19
	v_cvt_pk_bf16_f32 v9, v14, v15
	v_pk_mul_f32 v[12:13], v[118:119], v[14:15]
	v_pk_mul_f32 v[14:15], v[114:115], v[16:17]
	v_cvt_pk_fp8_f32 v24, v12, v13 op_sel:[0,0,1]
	v_cvt_pk_fp8_f32 v25, v14, v15 op_sel:[0,0,1]
	v_cvt_pk_bf16_f32 v10, v10, v11
	v_cvt_pk_bf16_f32 v11, v16, v17
	global_store_dwordx4 v[26:27], v[8:11], off
	global_store_dwordx2 v[28:29], v[24:25], off
	s_waitcnt vmcnt(14)
	v_pk_add_f32 v[4:5], v[4:5], v[176:177]
	v_pk_add_f32 v[8:9], v[2:3], v[182:183]
	v_pk_add_f32 v[2:3], v[0:1], v[180:181]
	v_pk_add_f32 v[6:7], v[6:7], v[178:179]
	v_cvt_pk_bf16_f32 v0, v4, v5
	v_pk_mul_f32 v[4:5], v[100:101], v[4:5]
	v_pk_mul_f32 v[10:11], v[96:97], v[2:3]
	v_cvt_pk_fp8_f32 v144, v4, v5
	v_cvt_pk_fp8_f32 v145, v10, v11
	v_cvt_pk_bf16_f32 v1, v6, v7
	v_pk_mul_f32 v[4:5], v[102:103], v[6:7]
	v_pk_mul_f32 v[6:7], v[98:99], v[8:9]
	v_cvt_pk_fp8_f32 v144, v4, v5 op_sel:[0,0,1]
	v_cvt_pk_fp8_f32 v145, v6, v7 op_sel:[0,0,1]
	v_cvt_pk_bf16_f32 v2, v2, v3
	v_cvt_pk_bf16_f32 v3, v8, v9
	global_store_dwordx4 v[26:27], v[0:3], off offset:256
	global_store_dwordx2 v[28:29], v[144:145], off offset:128
	s_cbranch_vccnz .LBB0_910
	s_andn2_b64 vcc, exec, s[16:17]
	s_cbranch_vccnz .LBB0_909
	s_barrier
	s_branch .LBB0_909

;     __device__ __forceinline__ void operator()(const f32x4 (&acc)[2][2][4][2], const Unit& u, int wr, int wc, int fr, int fq) const {
;         const int row0 = u.pm * BM + wr * 64 + fr, j0 = u.pn * HALF + wc * 32 + 8 * fq;
;         const float* bg = bgu + (size_t)u.e * 2 * DFF + j0;
;         f32x4 bgv[2], buv[2];
; #pragma unroll
;         for (int n = 0; n < 2; ++n) { bgv[n] = *(const f32x4*)(bg + 4 * n); buv[n] = *(const f32x4*)(bg + DFF + 4 * n); }
;         constexpr float inv = 1.0f / W8_SCALE;
; #pragma unroll
;         for (int ai = 0; ai < 2; ++ai)
; #pragma unroll
;             for (int m = 0; m < 4; ++m) { const int r = row0 + ai * HALF + m * 16; unsigned char* rowp = O + (size_t)r * DFF + j0; const float sc = inv * rs[(size_t)u.e * XCAP + u.lr0 + (r - u.pm * BM)];
;                 float a[8];
; #pragma unroll
;                 for (int n = 0; n < 2; ++n)
; #pragma unroll
;                     for (int h = 0; h < 2; ++h) {
;                         const f32x2 ag = {acc[ai][0][m][n][2 * h], acc[ai][0][m][n][2 * h + 1]}, au = {acc[ai][1][m][n][2 * h], acc[ai][1][m][n][2 * h + 1]};
;                         const f32x2 bg2 = {bgv[n][2 * h], bgv[n][2 * h + 1]}, bu2 = {buv[n][2 * h], buv[n][2 * h + 1]};
;                         f32x2 g = ag * sc + bg2, up = au * sc + bu2;
;                         g.x = fminf(g.x, 7.0f); g.y = fminf(g.y, 7.0f);
;                         up.x = __builtin_amdgcn_fmed3f(up.x, -7.0f, 7.0f); up.y = __builtin_amdgcn_fmed3f(up.y, -7.0f, 7.0f);
;                         const f32x2 t = g * (-1.702f * 1.4426950408889634f);
;                         f32x2 e; e.x = __builtin_amdgcn_exp2f(t.x); e.y = __builtin_amdgcn_exp2f(t.y);
;                         const f32x2 d = e + 1.0f;
;                         f32x2 rr; rr.x = __builtin_amdgcn_rcpf(d.x); rr.y = __builtin_amdgcn_rcpf(d.y);
;                         const f32x2 o2 = (up * ACT8_SCALE + ACT8_SCALE) * (g * rr);
;                         a[4 * n + 2 * h] = o2.x; a[4 * n + 2 * h + 1] = o2.y; }
;                 u32x2 w; w.x = cvt_pk4_fp8(a[0], a[1], a[2], a[3]); w.y = cvt_pk4_fp8(a[4], a[5], a[6], a[7]);
;                 *(u32x2*)rowp = w; }
;     }
.LBB0_1062:
	s_lshl_b32 s39, s50, 7
	s_ashr_i32 s49, s48, 31
	s_lshl_b32 s35, s35, 8
	s_or_b32 s39, s39, s84
	s_lshl_b64 s[54:55], s[48:49], 14
	v_mbcnt_lo_u32_b32 v80, -1, 0
	v_mbcnt_hi_u32_b32 v80, -1, v80
	s_add_u32 s54, s6, s54
	v_ashrrev_i32_e32 v81, 1, v80
	v_and_b32_e32 v81, -8, v81
	s_addc_u32 s55, s7, s55
	s_ashr_i32 s53, s52, 31
	s_lshl_b64 s[48:49], s[48:49], 16
	v_add_u32_e32 v148, s39, v81
	s_add_u32 s39, s26, s48
	s_addc_u32 s43, s27, s49
	s_lshl_b64 s[48:49], s[52:53], 2
	v_ashrrev_i32_e32 v149, 31, v148
	v_and_or_b32 v144, v80, 15, s34
	s_add_u32 s48, s39, s48
	v_lshl_add_u64 v[88:89], v[148:149], 2, s[54:55]
	s_addc_u32 s49, s43, s49
	v_lshlrev_b32_e32 v80, 2, v144
	s_movk_i32 s39, 0x2000
	global_load_dword v164, v80, s[48:49]
	global_load_dword v240, v80, s[48:49] offset:64
	global_load_dword v241, v80, s[48:49] offset:128
	global_load_dword v242, v80, s[48:49] offset:192
	global_load_dword v243, v80, s[48:49] offset:512
	global_load_dword v244, v80, s[48:49] offset:576
	global_load_dword v245, v80, s[48:49] offset:640
	global_load_dword v246, v80, s[48:49] offset:704
	v_add_co_u32_e32 v80, vcc, s39, v88
	s_mov_b64 s[52:53], 0x2000
	s_nop 0
	v_addc_co_u32_e32 v81, vcc, 0, v89, vcc
	global_load_dwordx4 v[84:87], v[80:81], off
	global_load_dwordx4 v[92:95], v[88:89], off
	s_nop 0
	global_load_dwordx4 v[80:83], v[88:89], off offset:16
	v_lshl_add_u64 v[88:89], v[88:89], 0, s[52:53]
	global_load_dwordx4 v[88:91], v[88:89], off offset:16
	v_add_u32_e32 v150, s35, v144
	v_ashrrev_i32_e32 v151, 31, v150
	v_lshlrev_b64 v[146:147], 11, v[150:151]
	s_ashr_i32 s39, s35, 31
	v_lshl_add_u64 v[146:147], s[4:5], 0, v[146:147]
	v_mov_b32_e32 v172, s39
	v_lshl_add_u64 v[146:147], v[146:147], 0, v[148:149]
	s_waitcnt vmcnt(4)
	v_mul_f32_e32 v144, 0x3c800000, v164
	s_waitcnt vmcnt(3)
	v_pk_fma_f32 v[132:133], v[132:133], v[144:145], v[84:85] op_sel_hi:[1,0,1]
	s_waitcnt vmcnt(2)
	v_pk_fma_f32 v[140:141], v[140:141], v[144:145], v[92:93] op_sel_hi:[1,0,1]
	s_waitcnt vmcnt(1)
	v_pk_fma_f32 v[136:137], v[136:137], v[144:145], v[80:81] op_sel_hi:[1,0,1]
	v_min_f32_e32 v140, 0x40e00000, v140
	v_min_f32_e32 v141, 0x40e00000, v141
	v_min_f32_e32 v136, 0x40e00000, v136
	v_min_f32_e32 v137, 0x40e00000, v137
	v_pk_mul_f32 v[164:165], v[140:141], s[36:37] op_sel_hi:[1,0]
	v_pk_mul_f32 v[168:169], v[136:137], s[36:37] op_sel_hi:[1,0]
	v_exp_f32_e32 v164, v164
	v_exp_f32_e32 v165, v165
	v_exp_f32_e32 v168, v168
	v_exp_f32_e32 v169, v169
	v_pk_fma_f32 v[142:143], v[142:143], v[144:145], v[94:95] op_sel_hi:[1,0,1]
	v_pk_fma_f32 v[138:139], v[138:139], v[144:145], v[82:83] op_sel_hi:[1,0,1]
	v_min_f32_e32 v142, 0x40e00000, v142
	v_min_f32_e32 v143, 0x40e00000, v143
	v_min_f32_e32 v138, 0x40e00000, v138
	v_min_f32_e32 v139, 0x40e00000, v139
	v_pk_mul_f32 v[166:167], v[142:143], s[36:37] op_sel_hi:[1,0]
	v_pk_mul_f32 v[170:171], v[138:139], s[36:37] op_sel_hi:[1,0]
	v_exp_f32_e32 v166, v166
	v_exp_f32_e32 v167, v167
	v_exp_f32_e32 v170, v170
	v_exp_f32_e32 v171, v171
	v_pk_add_f32 v[164:165], v[164:165], 1.0 op_sel_hi:[1,0]
	v_pk_add_f32 v[168:169], v[168:169], 1.0 op_sel_hi:[1,0]
	v_rcp_f32_e32 v164, v164
	v_rcp_f32_e32 v165, v165
	v_rcp_f32_e32 v168, v168
	v_rcp_f32_e32 v169, v169
	s_waitcnt vmcnt(0)
	v_pk_fma_f32 v[128:129], v[128:129], v[144:145], v[88:89] op_sel_hi:[1,0,1]
	v_med3_f32 v132, v132, s75, v161
	v_med3_f32 v133, v133, s75, v161
	v_med3_f32 v128, v128, s75, v161
	v_med3_f32 v129, v129, s75, v161
	v_pk_add_f32 v[166:167], v[166:167], 1.0 op_sel_hi:[1,0]
	v_pk_add_f32 v[170:171], v[170:171], 1.0 op_sel_hi:[1,0]
	v_pk_fma_f32 v[132:133], v[132:133], 4.0, 4.0 op_sel_hi:[1,0,0]
	v_pk_fma_f32 v[128:129], v[128:129], 4.0, 4.0 op_sel_hi:[1,0,0]
	v_rcp_f32_e32 v166, v166
	v_rcp_f32_e32 v167, v167
	v_rcp_f32_e32 v170, v170
	v_rcp_f32_e32 v171, v171
	v_pk_mul_f32 v[140:141], v[140:141], v[164:165]
	v_pk_mul_f32 v[136:137], v[136:137], v[168:169]
	v_pk_mul_f32 v[132:133], v[132:133], v[140:141]
	v_pk_mul_f32 v[128:129], v[128:129], v[136:137]
	v_pk_fma_f32 v[134:135], v[134:135], v[144:145], v[86:87] op_sel_hi:[1,0,1]
	v_pk_fma_f32 v[130:131], v[130:131], v[144:145], v[90:91] op_sel_hi:[1,0,1]
	v_cvt_pk_fp8_f32 v162, v132, v133
	v_cvt_pk_fp8_f32 v163, v128, v129
	v_med3_f32 v134, v134, s75, v161
	v_med3_f32 v135, v135, s75, v161
	v_med3_f32 v130, v130, s75, v161
	v_med3_f32 v131, v131, s75, v161
	v_pk_fma_f32 v[134:135], v[134:135], 4.0, 4.0 op_sel_hi:[1,0,0]
	v_pk_fma_f32 v[130:131], v[130:131], 4.0, 4.0 op_sel_hi:[1,0,0]
	v_pk_mul_f32 v[142:143], v[142:143], v[166:167]
	v_pk_mul_f32 v[138:139], v[138:139], v[170:171]
	v_pk_mul_f32 v[128:129], v[134:135], v[142:143]
	v_pk_mul_f32 v[130:131], v[130:131], v[138:139]
	v_cvt_pk_fp8_f32 v162, v128, v129 op_sel:[0,0,1]
	v_cvt_pk_fp8_f32 v163, v130, v131 op_sel:[0,0,1]
	v_subrev_co_u32_e32 v128, vcc, s35, v150
	s_nop 0
	v_subb_co_u32_e32 v129, vcc, v151, v172, vcc
	global_store_dwordx2 v[146:147], v[162:163], off
	v_lshl_add_u64 v[128:129], v[128:129], 2, s[48:49]
	v_mov_b32_e32 v134, v240
	v_or_b32_e32 v132, 16, v150
	v_ashrrev_i32_e32 v133, 31, v132
	s_mov_b32 s35, 0x40000
	v_mov_b32_e32 v144, v145
	v_mul_f32_e32 v134, 0x3c800000, v134
	v_pk_fma_f32 v[124:125], v[124:125], v[134:135], v[92:93] op_sel_hi:[1,0,1]
	v_pk_fma_f32 v[120:121], v[120:121], v[134:135], v[80:81] op_sel_hi:[1,0,1]
	v_min_f32_e32 v124, 0x40e00000, v124
	v_min_f32_e32 v125, 0x40e00000, v125
	v_min_f32_e32 v120, 0x40e00000, v120
	v_min_f32_e32 v121, 0x40e00000, v121
	v_pk_fma_f32 v[116:117], v[116:117], v[134:135], v[84:85] op_sel_hi:[1,0,1]
	v_pk_fma_f32 v[126:127], v[126:127], v[134:135], v[94:95] op_sel_hi:[1,0,1]
;     __device__ __forceinline__ void operator()(const f32x4 (&acc)[2][2][4][2], const Unit& u, int wr, int wc, int fr, int fq) const {
;         const int row0 = u.pm * BM + wr * 64 + fr, j0 = u.pn * HALF + wc * 32 + 8 * fq;
;         const float* bg = bgu + (size_t)u.e * 2 * DFF + j0;
;         f32x4 bgv[2], buv[2];
; #pragma unroll
;         for (int n = 0; n < 2; ++n) { bgv[n] = *(const f32x4*)(bg + 4 * n); buv[n] = *(const f32x4*)(bg + DFF + 4 * n); }
;         constexpr float inv = 1.0f / W8_SCALE;
; #pragma unroll
;         for (int ai = 0; ai < 2; ++ai)
; #pragma unroll
;             for (int m = 0; m < 4; ++m) { const int r = row0 + ai * HALF + m * 16; unsigned char* rowp = O + (size_t)r * DFF + j0; const float sc = inv * rs[(size_t)u.e * XCAP + u.lr0 + (r - u.pm * BM)];
;                 float a[8];
; #pragma unroll
;                 for (int n = 0; n < 2; ++n)
; #pragma unroll
;                     for (int h = 0; h < 2; ++h) {
;                         const f32x2 ag = {acc[ai][0][m][n][2 * h], acc[ai][0][m][n][2 * h + 1]}, au = {acc[ai][1][m][n][2 * h], acc[ai][1][m][n][2 * h + 1]};
;                         const f32x2 bg2 = {bgv[n][2 * h], bgv[n][2 * h + 1]}, bu2 = {buv[n][2 * h], buv[n][2 * h + 1]};
;                         f32x2 g = ag * sc + bg2, up = au * sc + bu2;
;                         g.x = fminf(g.x, 7.0f); g.y = fminf(g.y, 7.0f);
;                         up.x = __builtin_amdgcn_fmed3f(up.x, -7.0f, 7.0f); up.y = __builtin_amdgcn_fmed3f(up.y, -7.0f, 7.0f);
;                         const f32x2 t = g * (-1.702f * 1.4426950408889634f);
;                         f32x2 e; e.x = __builtin_amdgcn_exp2f(t.x); e.y = __builtin_amdgcn_exp2f(t.y);
;                         const f32x2 d = e + 1.0f;
;                         f32x2 rr; rr.x = __builtin_amdgcn_rcpf(d.x); rr.y = __builtin_amdgcn_rcpf(d.y);
;                         const f32x2 o2 = (up * ACT8_SCALE + ACT8_SCALE) * (g * rr);
;                         a[4 * n + 2 * h] = o2.x; a[4 * n + 2 * h + 1] = o2.y; }
;                 u32x2 w; w.x = cvt_pk4_fp8(a[0], a[1], a[2], a[3]); w.y = cvt_pk4_fp8(a[4], a[5], a[6], a[7]);
;                 *(u32x2*)rowp = w; }
;     }
	v_pk_fma_f32 v[118:119], v[118:119], v[134:135], v[86:87] op_sel_hi:[1,0,1]
	v_pk_fma_f32 v[112:113], v[112:113], v[134:135], v[88:89] op_sel_hi:[1,0,1]
	v_pk_fma_f32 v[122:123], v[122:123], v[134:135], v[82:83] op_sel_hi:[1,0,1]
	v_pk_fma_f32 v[114:115], v[114:115], v[134:135], v[90:91] op_sel_hi:[1,0,1]
	v_pk_mul_f32 v[134:135], v[124:125], s[36:37] op_sel_hi:[1,0]
	v_pk_mul_f32 v[138:139], v[120:121], s[36:37] op_sel_hi:[1,0]
	v_exp_f32_e32 v134, v134
	v_exp_f32_e32 v135, v135
	v_exp_f32_e32 v138, v138
	v_exp_f32_e32 v139, v139
	v_min_f32_e32 v126, 0x40e00000, v126
	v_min_f32_e32 v127, 0x40e00000, v127
	v_min_f32_e32 v122, 0x40e00000, v122
	v_min_f32_e32 v123, 0x40e00000, v123
	v_pk_mul_f32 v[136:137], v[126:127], s[36:37] op_sel_hi:[1,0]
	v_pk_mul_f32 v[140:141], v[122:123], s[36:37] op_sel_hi:[1,0]
	v_exp_f32_e32 v136, v136
	v_exp_f32_e32 v137, v137
	v_exp_f32_e32 v140, v140
	v_exp_f32_e32 v141, v141
	v_pk_add_f32 v[134:135], v[134:135], 1.0 op_sel_hi:[1,0]
	v_pk_add_f32 v[138:139], v[138:139], 1.0 op_sel_hi:[1,0]
	v_rcp_f32_e32 v134, v134
	v_rcp_f32_e32 v135, v135
	v_rcp_f32_e32 v138, v138
	v_rcp_f32_e32 v139, v139
	v_med3_f32 v116, v116, s75, v161
	v_med3_f32 v117, v117, s75, v161
	v_med3_f32 v112, v112, s75, v161
	v_med3_f32 v113, v113, s75, v161
	v_pk_add_f32 v[136:137], v[136:137], 1.0 op_sel_hi:[1,0]
	v_pk_add_f32 v[140:141], v[140:141], 1.0 op_sel_hi:[1,0]
	v_pk_fma_f32 v[116:117], v[116:117], 4.0, 4.0 op_sel_hi:[1,0,0]
	v_pk_fma_f32 v[112:113], v[112:113], 4.0, 4.0 op_sel_hi:[1,0,0]
	v_rcp_f32_e32 v136, v136
	v_rcp_f32_e32 v137, v137
	v_rcp_f32_e32 v140, v140
	v_rcp_f32_e32 v141, v141
	v_pk_mul_f32 v[124:125], v[124:125], v[134:135]
	v_pk_mul_f32 v[120:121], v[120:121], v[138:139]
	v_pk_mul_f32 v[116:117], v[116:117], v[124:125]
	v_pk_mul_f32 v[112:113], v[112:113], v[120:121]
	v_cvt_pk_fp8_f32 v130, v116, v117
	v_cvt_pk_fp8_f32 v131, v112, v113
	v_med3_f32 v118, v118, s75, v161
	v_med3_f32 v119, v119, s75, v161
	v_med3_f32 v114, v114, s75, v161
	v_med3_f32 v115, v115, s75, v161
	v_pk_fma_f32 v[118:119], v[118:119], 4.0, 4.0 op_sel_hi:[1,0,0]
	v_pk_fma_f32 v[114:115], v[114:115], 4.0, 4.0 op_sel_hi:[1,0,0]
	v_pk_mul_f32 v[126:127], v[126:127], v[136:137]
	v_pk_mul_f32 v[122:123], v[122:123], v[140:141]
	v_pk_mul_f32 v[112:113], v[118:119], v[126:127]
	v_pk_mul_f32 v[114:115], v[114:115], v[122:123]
	v_cvt_pk_fp8_f32 v130, v112, v113 op_sel:[0,0,1]
	v_cvt_pk_fp8_f32 v131, v114, v115 op_sel:[0,0,1]
	v_lshlrev_b64 v[112:113], 11, v[132:133]
	v_lshl_add_u64 v[112:113], s[4:5], 0, v[112:113]
	v_lshl_add_u64 v[112:113], v[112:113], 0, v[148:149]
	global_store_dwordx2 v[112:113], v[130:131], off
	v_mov_b32_e32 v116, v241
	v_or_b32_e32 v114, 32, v150
	v_ashrrev_i32_e32 v115, 31, v114
	v_mul_f32_e32 v116, 0x3c800000, v116
	v_pk_fma_f32 v[108:109], v[108:109], v[116:117], v[92:93] op_sel_hi:[1,0,1]
	v_pk_fma_f32 v[104:105], v[104:105], v[116:117], v[80:81] op_sel_hi:[1,0,1]
	v_min_f32_e32 v108, 0x40e00000, v108
	v_min_f32_e32 v109, 0x40e00000, v109
	v_min_f32_e32 v104, 0x40e00000, v104
	v_min_f32_e32 v105, 0x40e00000, v105
	v_pk_fma_f32 v[100:101], v[100:101], v[116:117], v[84:85] op_sel_hi:[1,0,1]
	v_pk_fma_f32 v[110:111], v[110:111], v[116:117], v[94:95] op_sel_hi:[1,0,1]
	v_pk_fma_f32 v[102:103], v[102:103], v[116:117], v[86:87] op_sel_hi:[1,0,1]
	v_pk_fma_f32 v[96:97], v[96:97], v[116:117], v[88:89] op_sel_hi:[1,0,1]
	v_pk_fma_f32 v[106:107], v[106:107], v[116:117], v[82:83] op_sel_hi:[1,0,1]
	v_pk_fma_f32 v[98:99], v[98:99], v[116:117], v[90:91] op_sel_hi:[1,0,1]
	v_pk_mul_f32 v[116:117], v[108:109], s[36:37] op_sel_hi:[1,0]
	v_pk_mul_f32 v[120:121], v[104:105], s[36:37] op_sel_hi:[1,0]
	v_exp_f32_e32 v116, v116
	v_exp_f32_e32 v117, v117
	v_exp_f32_e32 v120, v120
	v_exp_f32_e32 v121, v121
	v_min_f32_e32 v110, 0x40e00000, v110
	v_min_f32_e32 v111, 0x40e00000, v111
	v_min_f32_e32 v106, 0x40e00000, v106
	v_min_f32_e32 v107, 0x40e00000, v107
	v_pk_mul_f32 v[118:119], v[110:111], s[36:37] op_sel_hi:[1,0]
	v_pk_mul_f32 v[122:123], v[106:107], s[36:37] op_sel_hi:[1,0]
	v_exp_f32_e32 v118, v118
	v_exp_f32_e32 v119, v119
	v_exp_f32_e32 v122, v122
	v_exp_f32_e32 v123, v123
	v_pk_add_f32 v[116:117], v[116:117], 1.0 op_sel_hi:[1,0]
	v_pk_add_f32 v[120:121], v[120:121], 1.0 op_sel_hi:[1,0]
	v_rcp_f32_e32 v116, v116
	v_rcp_f32_e32 v117, v117
	v_rcp_f32_e32 v120, v120
	v_rcp_f32_e32 v121, v121
	v_med3_f32 v100, v100, s75, v161
	v_med3_f32 v101, v101, s75, v161
	v_med3_f32 v96, v96, s75, v161
	v_med3_f32 v97, v97, s75, v161
	v_pk_add_f32 v[118:119], v[118:119], 1.0 op_sel_hi:[1,0]
	v_pk_add_f32 v[122:123], v[122:123], 1.0 op_sel_hi:[1,0]
	v_pk_fma_f32 v[100:101], v[100:101], 4.0, 4.0 op_sel_hi:[1,0,0]
	v_pk_fma_f32 v[96:97], v[96:97], 4.0, 4.0 op_sel_hi:[1,0,0]
	v_rcp_f32_e32 v118, v118
	v_rcp_f32_e32 v119, v119
	v_rcp_f32_e32 v122, v122
	v_rcp_f32_e32 v123, v123
	v_pk_mul_f32 v[108:109], v[108:109], v[116:117]
	v_pk_mul_f32 v[104:105], v[104:105], v[120:121]
	v_pk_mul_f32 v[100:101], v[100:101], v[108:109]
	v_pk_mul_f32 v[96:97], v[96:97], v[104:105]
	v_cvt_pk_fp8_f32 v112, v100, v101
	v_cvt_pk_fp8_f32 v113, v96, v97
	v_med3_f32 v102, v102, s75, v161
	v_med3_f32 v103, v103, s75, v161
	v_med3_f32 v98, v98, s75, v161
	v_med3_f32 v99, v99, s75, v161
	v_pk_fma_f32 v[102:103], v[102:103], 4.0, 4.0 op_sel_hi:[1,0,0]
	v_pk_fma_f32 v[98:99], v[98:99], 4.0, 4.0 op_sel_hi:[1,0,0]
	v_pk_mul_f32 v[110:111], v[110:111], v[118:119]
	v_pk_mul_f32 v[106:107], v[106:107], v[122:123]
	v_pk_mul_f32 v[96:97], v[102:103], v[110:111]
	v_pk_mul_f32 v[98:99], v[98:99], v[106:107]
	v_cvt_pk_fp8_f32 v112, v96, v97 op_sel:[0,0,1]
	v_cvt_pk_fp8_f32 v113, v98, v99 op_sel:[0,0,1]
;     __device__ __forceinline__ void operator()(const f32x4 (&acc)[2][2][4][2], const Unit& u, int wr, int wc, int fr, int fq) const {
;         const int row0 = u.pm * BM + wr * 64 + fr, j0 = u.pn * HALF + wc * 32 + 8 * fq;
;         const float* bg = bgu + (size_t)u.e * 2 * DFF + j0;
;         f32x4 bgv[2], buv[2];
; #pragma unroll
;         for (int n = 0; n < 2; ++n) { bgv[n] = *(const f32x4*)(bg + 4 * n); buv[n] = *(const f32x4*)(bg + DFF + 4 * n); }
;         constexpr float inv = 1.0f / W8_SCALE;
; #pragma unroll
;         for (int ai = 0; ai < 2; ++ai)
; #pragma unroll
;             for (int m = 0; m < 4; ++m) { const int r = row0 + ai * HALF + m * 16; unsigned char* rowp = O + (size_t)r * DFF + j0; const float sc = inv * rs[(size_t)u.e * XCAP + u.lr0 + (r - u.pm * BM)];
;                 float a[8];
; #pragma unroll
;                 for (int n = 0; n < 2; ++n)
; #pragma unroll
;                     for (int h = 0; h < 2; ++h) {
;                         const f32x2 ag = {acc[ai][0][m][n][2 * h], acc[ai][0][m][n][2 * h + 1]}, au = {acc[ai][1][m][n][2 * h], acc[ai][1][m][n][2 * h + 1]};
;                         const f32x2 bg2 = {bgv[n][2 * h], bgv[n][2 * h + 1]}, bu2 = {buv[n][2 * h], buv[n][2 * h + 1]};
;                         f32x2 g = ag * sc + bg2, up = au * sc + bu2;
;                         g.x = fminf(g.x, 7.0f); g.y = fminf(g.y, 7.0f);
;                         up.x = __builtin_amdgcn_fmed3f(up.x, -7.0f, 7.0f); up.y = __builtin_amdgcn_fmed3f(up.y, -7.0f, 7.0f);
;                         const f32x2 t = g * (-1.702f * 1.4426950408889634f);
;                         f32x2 e; e.x = __builtin_amdgcn_exp2f(t.x); e.y = __builtin_amdgcn_exp2f(t.y);
;                         const f32x2 d = e + 1.0f;
;                         f32x2 rr; rr.x = __builtin_amdgcn_rcpf(d.x); rr.y = __builtin_amdgcn_rcpf(d.y);
;                         const f32x2 o2 = (up * ACT8_SCALE + ACT8_SCALE) * (g * rr);
;                         a[4 * n + 2 * h] = o2.x; a[4 * n + 2 * h + 1] = o2.y; }
;                 u32x2 w; w.x = cvt_pk4_fp8(a[0], a[1], a[2], a[3]); w.y = cvt_pk4_fp8(a[4], a[5], a[6], a[7]);
;                 *(u32x2*)rowp = w; }
;     }
	v_lshlrev_b64 v[96:97], 11, v[114:115]
	v_lshl_add_u64 v[96:97], s[4:5], 0, v[96:97]
	v_lshl_add_u64 v[96:97], v[96:97], 0, v[148:149]
	global_store_dwordx2 v[96:97], v[112:113], off
	v_mov_b32_e32 v100, v242
	v_or_b32_e32 v98, 48, v150
	v_ashrrev_i32_e32 v99, 31, v98
	v_mul_f32_e32 v100, 0x3c800000, v100
	v_pk_fma_f32 v[76:77], v[76:77], v[100:101], v[92:93] op_sel_hi:[1,0,1]
	v_pk_fma_f32 v[72:73], v[72:73], v[100:101], v[80:81] op_sel_hi:[1,0,1]
	v_min_f32_e32 v76, 0x40e00000, v76
	v_min_f32_e32 v77, 0x40e00000, v77
	v_min_f32_e32 v72, 0x40e00000, v72
	v_min_f32_e32 v73, 0x40e00000, v73
	v_pk_fma_f32 v[68:69], v[68:69], v[100:101], v[84:85] op_sel_hi:[1,0,1]
	v_pk_fma_f32 v[78:79], v[78:79], v[100:101], v[94:95] op_sel_hi:[1,0,1]
	v_pk_fma_f32 v[70:71], v[70:71], v[100:101], v[86:87] op_sel_hi:[1,0,1]
	v_pk_fma_f32 v[64:65], v[64:65], v[100:101], v[88:89] op_sel_hi:[1,0,1]
	v_pk_fma_f32 v[74:75], v[74:75], v[100:101], v[82:83] op_sel_hi:[1,0,1]
	v_pk_fma_f32 v[66:67], v[66:67], v[100:101], v[90:91] op_sel_hi:[1,0,1]
	v_pk_mul_f32 v[100:101], v[76:77], s[36:37] op_sel_hi:[1,0]
	v_pk_mul_f32 v[104:105], v[72:73], s[36:37] op_sel_hi:[1,0]
	v_exp_f32_e32 v100, v100
	v_exp_f32_e32 v101, v101
	v_exp_f32_e32 v104, v104
	v_exp_f32_e32 v105, v105
	v_min_f32_e32 v78, 0x40e00000, v78
	v_min_f32_e32 v79, 0x40e00000, v79
	v_min_f32_e32 v74, 0x40e00000, v74
	v_min_f32_e32 v75, 0x40e00000, v75
	v_pk_mul_f32 v[102:103], v[78:79], s[36:37] op_sel_hi:[1,0]
	v_pk_mul_f32 v[106:107], v[74:75], s[36:37] op_sel_hi:[1,0]
	v_exp_f32_e32 v102, v102
	v_exp_f32_e32 v103, v103
	v_exp_f32_e32 v106, v106
	v_exp_f32_e32 v107, v107
	v_pk_add_f32 v[100:101], v[100:101], 1.0 op_sel_hi:[1,0]
	v_pk_add_f32 v[104:105], v[104:105], 1.0 op_sel_hi:[1,0]
	v_rcp_f32_e32 v100, v100
	v_rcp_f32_e32 v101, v101
	v_rcp_f32_e32 v104, v104
	v_rcp_f32_e32 v105, v105
	v_med3_f32 v68, v68, s75, v161
	v_med3_f32 v69, v69, s75, v161
	v_med3_f32 v64, v64, s75, v161
	v_med3_f32 v65, v65, s75, v161
	v_pk_add_f32 v[102:103], v[102:103], 1.0 op_sel_hi:[1,0]
	v_pk_add_f32 v[106:107], v[106:107], 1.0 op_sel_hi:[1,0]
	v_pk_fma_f32 v[68:69], v[68:69], 4.0, 4.0 op_sel_hi:[1,0,0]
	v_pk_fma_f32 v[64:65], v[64:65], 4.0, 4.0 op_sel_hi:[1,0,0]
	v_rcp_f32_e32 v102, v102
	v_rcp_f32_e32 v103, v103
	v_rcp_f32_e32 v106, v106
	v_rcp_f32_e32 v107, v107
	v_pk_mul_f32 v[76:77], v[76:77], v[100:101]
	v_pk_mul_f32 v[72:73], v[72:73], v[104:105]
	v_pk_mul_f32 v[68:69], v[68:69], v[76:77]
	v_pk_mul_f32 v[64:65], v[64:65], v[72:73]
	v_cvt_pk_fp8_f32 v96, v68, v69
	v_cvt_pk_fp8_f32 v97, v64, v65
	v_med3_f32 v70, v70, s75, v161
	v_med3_f32 v71, v71, s75, v161
	v_med3_f32 v66, v66, s75, v161
	v_med3_f32 v67, v67, s75, v161
	v_pk_fma_f32 v[70:71], v[70:71], 4.0, 4.0 op_sel_hi:[1,0,0]
	v_pk_fma_f32 v[66:67], v[66:67], 4.0, 4.0 op_sel_hi:[1,0,0]
	v_pk_mul_f32 v[78:79], v[78:79], v[102:103]
	v_pk_mul_f32 v[74:75], v[74:75], v[106:107]
	v_pk_mul_f32 v[64:65], v[70:71], v[78:79]
	v_pk_mul_f32 v[66:67], v[66:67], v[74:75]
	v_cvt_pk_fp8_f32 v96, v64, v65 op_sel:[0,0,1]
	v_cvt_pk_fp8_f32 v97, v66, v67 op_sel:[0,0,1]
	v_lshlrev_b64 v[64:65], 11, v[98:99]
	v_lshl_add_u64 v[64:65], s[4:5], 0, v[64:65]
	v_lshl_add_u64 v[64:65], v[64:65], 0, v[148:149]
	global_store_dwordx2 v[64:65], v[96:97], off
	v_mov_b32_e32 v66, v243
	v_mul_f32_e32 v66, 0x3c800000, v66
	v_pk_fma_f32 v[60:61], v[60:61], v[66:67], v[92:93] op_sel_hi:[1,0,1]
	v_pk_fma_f32 v[56:57], v[56:57], v[66:67], v[80:81] op_sel_hi:[1,0,1]
	v_min_f32_e32 v60, 0x40e00000, v60
	v_min_f32_e32 v61, 0x40e00000, v61
	v_min_f32_e32 v56, 0x40e00000, v56
	v_min_f32_e32 v57, 0x40e00000, v57
	v_pk_fma_f32 v[52:53], v[52:53], v[66:67], v[84:85] op_sel_hi:[1,0,1]
	v_pk_fma_f32 v[62:63], v[62:63], v[66:67], v[94:95] op_sel_hi:[1,0,1]
	v_pk_fma_f32 v[54:55], v[54:55], v[66:67], v[86:87] op_sel_hi:[1,0,1]
	v_pk_fma_f32 v[48:49], v[48:49], v[66:67], v[88:89] op_sel_hi:[1,0,1]
	v_pk_fma_f32 v[58:59], v[58:59], v[66:67], v[82:83] op_sel_hi:[1,0,1]
	v_pk_fma_f32 v[50:51], v[50:51], v[66:67], v[90:91] op_sel_hi:[1,0,1]
	v_pk_mul_f32 v[66:67], v[60:61], s[36:37] op_sel_hi:[1,0]
	v_pk_mul_f32 v[70:71], v[56:57], s[36:37] op_sel_hi:[1,0]
	v_exp_f32_e32 v66, v66
	v_exp_f32_e32 v67, v67
	v_exp_f32_e32 v70, v70
	v_exp_f32_e32 v71, v71
	v_min_f32_e32 v62, 0x40e00000, v62
	v_min_f32_e32 v63, 0x40e00000, v63
	v_min_f32_e32 v58, 0x40e00000, v58
	v_min_f32_e32 v59, 0x40e00000, v59
	v_pk_mul_f32 v[68:69], v[62:63], s[36:37] op_sel_hi:[1,0]
	v_pk_mul_f32 v[72:73], v[58:59], s[36:37] op_sel_hi:[1,0]
	v_exp_f32_e32 v68, v68
	v_exp_f32_e32 v69, v69
	v_exp_f32_e32 v72, v72
	v_exp_f32_e32 v73, v73
	v_pk_add_f32 v[66:67], v[66:67], 1.0 op_sel_hi:[1,0]
	v_pk_add_f32 v[70:71], v[70:71], 1.0 op_sel_hi:[1,0]
	v_rcp_f32_e32 v66, v66
	v_rcp_f32_e32 v67, v67
	v_rcp_f32_e32 v70, v70
	v_rcp_f32_e32 v71, v71
	v_med3_f32 v52, v52, s75, v161
	v_med3_f32 v53, v53, s75, v161
	v_med3_f32 v48, v48, s75, v161
	v_med3_f32 v49, v49, s75, v161
	v_pk_add_f32 v[68:69], v[68:69], 1.0 op_sel_hi:[1,0]
	v_pk_add_f32 v[72:73], v[72:73], 1.0 op_sel_hi:[1,0]
	v_pk_fma_f32 v[52:53], v[52:53], 4.0, 4.0 op_sel_hi:[1,0,0]
	v_pk_fma_f32 v[48:49], v[48:49], 4.0, 4.0 op_sel_hi:[1,0,0]
	v_rcp_f32_e32 v68, v68
	v_rcp_f32_e32 v69, v69
	v_rcp_f32_e32 v72, v72
	v_rcp_f32_e32 v73, v73
	v_pk_mul_f32 v[60:61], v[60:61], v[66:67]
	v_pk_mul_f32 v[56:57], v[56:57], v[70:71]
	v_pk_mul_f32 v[52:53], v[52:53], v[60:61]
	v_pk_mul_f32 v[48:49], v[48:49], v[56:57]
	v_cvt_pk_fp8_f32 v64, v52, v53
	v_cvt_pk_fp8_f32 v65, v48, v49
	v_med3_f32 v54, v54, s75, v161
	v_med3_f32 v55, v55, s75, v161
	v_med3_f32 v50, v50, s75, v161
	v_med3_f32 v51, v51, s75, v161
;     __device__ __forceinline__ void operator()(const f32x4 (&acc)[2][2][4][2], const Unit& u, int wr, int wc, int fr, int fq) const {
;         const int row0 = u.pm * BM + wr * 64 + fr, j0 = u.pn * HALF + wc * 32 + 8 * fq;
;         const float* bg = bgu + (size_t)u.e * 2 * DFF + j0;
;         f32x4 bgv[2], buv[2];
; #pragma unroll
;         for (int n = 0; n < 2; ++n) { bgv[n] = *(const f32x4*)(bg + 4 * n); buv[n] = *(const f32x4*)(bg + DFF + 4 * n); }
;         constexpr float inv = 1.0f / W8_SCALE;
; #pragma unroll
;         for (int ai = 0; ai < 2; ++ai)
; #pragma unroll
;             for (int m = 0; m < 4; ++m) { const int r = row0 + ai * HALF + m * 16; unsigned char* rowp = O + (size_t)r * DFF + j0; const float sc = inv * rs[(size_t)u.e * XCAP + u.lr0 + (r - u.pm * BM)];
;                 float a[8];
; #pragma unroll
;                 for (int n = 0; n < 2; ++n)
; #pragma unroll
;                     for (int h = 0; h < 2; ++h) {
;                         const f32x2 ag = {acc[ai][0][m][n][2 * h], acc[ai][0][m][n][2 * h + 1]}, au = {acc[ai][1][m][n][2 * h], acc[ai][1][m][n][2 * h + 1]};
;                         const f32x2 bg2 = {bgv[n][2 * h], bgv[n][2 * h + 1]}, bu2 = {buv[n][2 * h], buv[n][2 * h + 1]};
;                         f32x2 g = ag * sc + bg2, up = au * sc + bu2;
;                         g.x = fminf(g.x, 7.0f); g.y = fminf(g.y, 7.0f);
;                         up.x = __builtin_amdgcn_fmed3f(up.x, -7.0f, 7.0f); up.y = __builtin_amdgcn_fmed3f(up.y, -7.0f, 7.0f);
;                         const f32x2 t = g * (-1.702f * 1.4426950408889634f);
;                         f32x2 e; e.x = __builtin_amdgcn_exp2f(t.x); e.y = __builtin_amdgcn_exp2f(t.y);
;                         const f32x2 d = e + 1.0f;
;                         f32x2 rr; rr.x = __builtin_amdgcn_rcpf(d.x); rr.y = __builtin_amdgcn_rcpf(d.y);
;                         const f32x2 o2 = (up * ACT8_SCALE + ACT8_SCALE) * (g * rr);
;                         a[4 * n + 2 * h] = o2.x; a[4 * n + 2 * h + 1] = o2.y; }
;                 u32x2 w; w.x = cvt_pk4_fp8(a[0], a[1], a[2], a[3]); w.y = cvt_pk4_fp8(a[4], a[5], a[6], a[7]);
;                 *(u32x2*)rowp = w; }
;     }
	v_pk_fma_f32 v[54:55], v[54:55], 4.0, 4.0 op_sel_hi:[1,0,0]
	v_pk_fma_f32 v[50:51], v[50:51], 4.0, 4.0 op_sel_hi:[1,0,0]
	v_pk_mul_f32 v[62:63], v[62:63], v[68:69]
	v_pk_mul_f32 v[58:59], v[58:59], v[72:73]
	v_pk_mul_f32 v[48:49], v[54:55], v[62:63]
	v_pk_mul_f32 v[50:51], v[50:51], v[58:59]
	v_cvt_pk_fp8_f32 v64, v48, v49 op_sel:[0,0,1]
	v_cvt_pk_fp8_f32 v65, v50, v51 op_sel:[0,0,1]
	v_add_co_u32_e32 v48, vcc, s35, v146
	s_nop 1
	v_addc_co_u32_e32 v49, vcc, 0, v147, vcc
	global_store_dwordx2 v[48:49], v[64:65], off
	v_mov_b32_e32 v50, v244
	v_mul_f32_e32 v50, 0x3c800000, v50
	v_pk_fma_f32 v[44:45], v[44:45], v[50:51], v[92:93] op_sel_hi:[1,0,1]
	v_pk_fma_f32 v[40:41], v[40:41], v[50:51], v[80:81] op_sel_hi:[1,0,1]
	v_min_f32_e32 v44, 0x40e00000, v44
	v_min_f32_e32 v45, 0x40e00000, v45
	v_min_f32_e32 v40, 0x40e00000, v40
	v_min_f32_e32 v41, 0x40e00000, v41
	v_pk_fma_f32 v[36:37], v[36:37], v[50:51], v[84:85] op_sel_hi:[1,0,1]
	v_pk_fma_f32 v[46:47], v[46:47], v[50:51], v[94:95] op_sel_hi:[1,0,1]
	v_pk_fma_f32 v[38:39], v[38:39], v[50:51], v[86:87] op_sel_hi:[1,0,1]
	v_pk_fma_f32 v[32:33], v[32:33], v[50:51], v[88:89] op_sel_hi:[1,0,1]
	v_pk_fma_f32 v[42:43], v[42:43], v[50:51], v[82:83] op_sel_hi:[1,0,1]
	v_pk_fma_f32 v[34:35], v[34:35], v[50:51], v[90:91] op_sel_hi:[1,0,1]
	v_pk_mul_f32 v[50:51], v[44:45], s[36:37] op_sel_hi:[1,0]
	v_pk_mul_f32 v[54:55], v[40:41], s[36:37] op_sel_hi:[1,0]
	v_exp_f32_e32 v50, v50
	v_exp_f32_e32 v51, v51
	v_exp_f32_e32 v54, v54
	v_exp_f32_e32 v55, v55
	v_min_f32_e32 v46, 0x40e00000, v46
	v_min_f32_e32 v47, 0x40e00000, v47
	v_min_f32_e32 v42, 0x40e00000, v42
	v_min_f32_e32 v43, 0x40e00000, v43
	v_pk_mul_f32 v[52:53], v[46:47], s[36:37] op_sel_hi:[1,0]
	v_pk_mul_f32 v[56:57], v[42:43], s[36:37] op_sel_hi:[1,0]
	v_exp_f32_e32 v52, v52
	v_exp_f32_e32 v53, v53
	v_exp_f32_e32 v56, v56
	v_exp_f32_e32 v57, v57
	v_pk_add_f32 v[50:51], v[50:51], 1.0 op_sel_hi:[1,0]
	v_pk_add_f32 v[54:55], v[54:55], 1.0 op_sel_hi:[1,0]
	v_rcp_f32_e32 v50, v50
	v_rcp_f32_e32 v51, v51
	v_rcp_f32_e32 v54, v54
	v_rcp_f32_e32 v55, v55
	v_med3_f32 v36, v36, s75, v161
	v_med3_f32 v37, v37, s75, v161
	v_med3_f32 v32, v32, s75, v161
	v_med3_f32 v33, v33, s75, v161
	v_pk_add_f32 v[52:53], v[52:53], 1.0 op_sel_hi:[1,0]
	v_pk_add_f32 v[56:57], v[56:57], 1.0 op_sel_hi:[1,0]
	v_pk_fma_f32 v[36:37], v[36:37], 4.0, 4.0 op_sel_hi:[1,0,0]
	v_pk_fma_f32 v[32:33], v[32:33], 4.0, 4.0 op_sel_hi:[1,0,0]
	v_rcp_f32_e32 v52, v52
	v_rcp_f32_e32 v53, v53
	v_rcp_f32_e32 v56, v56
	v_rcp_f32_e32 v57, v57
	v_pk_mul_f32 v[44:45], v[44:45], v[50:51]
	v_pk_mul_f32 v[40:41], v[40:41], v[54:55]
	v_pk_mul_f32 v[36:37], v[36:37], v[44:45]
	v_pk_mul_f32 v[32:33], v[32:33], v[40:41]
	v_cvt_pk_fp8_f32 v48, v36, v37
	v_cvt_pk_fp8_f32 v49, v32, v33
	v_med3_f32 v38, v38, s75, v161
	v_med3_f32 v39, v39, s75, v161
	v_med3_f32 v34, v34, s75, v161
	v_med3_f32 v35, v35, s75, v161
	v_pk_fma_f32 v[38:39], v[38:39], 4.0, 4.0 op_sel_hi:[1,0,0]
	v_pk_fma_f32 v[34:35], v[34:35], 4.0, 4.0 op_sel_hi:[1,0,0]
	v_pk_mul_f32 v[46:47], v[46:47], v[52:53]
	v_pk_mul_f32 v[42:43], v[42:43], v[56:57]
	v_pk_mul_f32 v[32:33], v[38:39], v[46:47]
	v_pk_mul_f32 v[34:35], v[34:35], v[42:43]
	v_cvt_pk_fp8_f32 v48, v32, v33 op_sel:[0,0,1]
	v_cvt_pk_fp8_f32 v49, v34, v35 op_sel:[0,0,1]
	v_add_co_u32_e32 v32, vcc, s76, v146
	s_nop 1
	v_addc_co_u32_e32 v33, vcc, 0, v147, vcc
	global_store_dwordx2 v[32:33], v[48:49], off
	v_mov_b32_e32 v34, v245
	v_mul_f32_e32 v34, 0x3c800000, v34
	v_pk_fma_f32 v[28:29], v[28:29], v[34:35], v[92:93] op_sel_hi:[1,0,1]
	v_pk_fma_f32 v[24:25], v[24:25], v[34:35], v[80:81] op_sel_hi:[1,0,1]
	v_min_f32_e32 v28, 0x40e00000, v28
	v_min_f32_e32 v29, 0x40e00000, v29
	v_min_f32_e32 v24, 0x40e00000, v24
	v_min_f32_e32 v25, 0x40e00000, v25
	v_pk_fma_f32 v[20:21], v[20:21], v[34:35], v[84:85] op_sel_hi:[1,0,1]
	v_pk_fma_f32 v[30:31], v[30:31], v[34:35], v[94:95] op_sel_hi:[1,0,1]
	v_pk_fma_f32 v[22:23], v[22:23], v[34:35], v[86:87] op_sel_hi:[1,0,1]
	v_pk_fma_f32 v[16:17], v[16:17], v[34:35], v[88:89] op_sel_hi:[1,0,1]
	v_pk_fma_f32 v[26:27], v[26:27], v[34:35], v[82:83] op_sel_hi:[1,0,1]
	v_pk_fma_f32 v[18:19], v[18:19], v[34:35], v[90:91] op_sel_hi:[1,0,1]
	v_pk_mul_f32 v[34:35], v[28:29], s[36:37] op_sel_hi:[1,0]
	v_pk_mul_f32 v[38:39], v[24:25], s[36:37] op_sel_hi:[1,0]
	v_exp_f32_e32 v34, v34
	v_exp_f32_e32 v35, v35
	v_exp_f32_e32 v38, v38
	v_exp_f32_e32 v39, v39
	v_min_f32_e32 v30, 0x40e00000, v30
	v_min_f32_e32 v31, 0x40e00000, v31
	v_min_f32_e32 v26, 0x40e00000, v26
	v_min_f32_e32 v27, 0x40e00000, v27
	v_pk_mul_f32 v[36:37], v[30:31], s[36:37] op_sel_hi:[1,0]
	v_pk_mul_f32 v[40:41], v[26:27], s[36:37] op_sel_hi:[1,0]
;     __device__ __forceinline__ void operator()(const f32x4 (&acc)[2][2][4][2], const Unit& u, int wr, int wc, int fr, int fq) const {
;         const int row0 = u.pm * BM + wr * 64 + fr, j0 = u.pn * HALF + wc * 32 + 8 * fq;
;         const float* bg = bgu + (size_t)u.e * 2 * DFF + j0;
;         f32x4 bgv[2], buv[2];
; #pragma unroll
;         for (int n = 0; n < 2; ++n) { bgv[n] = *(const f32x4*)(bg + 4 * n); buv[n] = *(const f32x4*)(bg + DFF + 4 * n); }
;         constexpr float inv = 1.0f / W8_SCALE;
; #pragma unroll
;         for (int ai = 0; ai < 2; ++ai)
; #pragma unroll
;             for (int m = 0; m < 4; ++m) { const int r = row0 + ai * HALF + m * 16; unsigned char* rowp = O + (size_t)r * DFF + j0; const float sc = inv * rs[(size_t)u.e * XCAP + u.lr0 + (r - u.pm * BM)];
;                 float a[8];
; #pragma unroll
;                 for (int n = 0; n < 2; ++n)
; #pragma unroll
;                     for (int h = 0; h < 2; ++h) {
;                         const f32x2 ag = {acc[ai][0][m][n][2 * h], acc[ai][0][m][n][2 * h + 1]}, au = {acc[ai][1][m][n][2 * h], acc[ai][1][m][n][2 * h + 1]};
;                         const f32x2 bg2 = {bgv[n][2 * h], bgv[n][2 * h + 1]}, bu2 = {buv[n][2 * h], buv[n][2 * h + 1]};
;                         f32x2 g = ag * sc + bg2, up = au * sc + bu2;
;                         g.x = fminf(g.x, 7.0f); g.y = fminf(g.y, 7.0f);
;                         up.x = __builtin_amdgcn_fmed3f(up.x, -7.0f, 7.0f); up.y = __builtin_amdgcn_fmed3f(up.y, -7.0f, 7.0f);
;                         const f32x2 t = g * (-1.702f * 1.4426950408889634f);
;                         f32x2 e; e.x = __builtin_amdgcn_exp2f(t.x); e.y = __builtin_amdgcn_exp2f(t.y);
;                         const f32x2 d = e + 1.0f;
;                         f32x2 rr; rr.x = __builtin_amdgcn_rcpf(d.x); rr.y = __builtin_amdgcn_rcpf(d.y);
;                         const f32x2 o2 = (up * ACT8_SCALE + ACT8_SCALE) * (g * rr);
;                         a[4 * n + 2 * h] = o2.x; a[4 * n + 2 * h + 1] = o2.y; }
;                 u32x2 w; w.x = cvt_pk4_fp8(a[0], a[1], a[2], a[3]); w.y = cvt_pk4_fp8(a[4], a[5], a[6], a[7]);
;                 *(u32x2*)rowp = w; }
;     }
	v_exp_f32_e32 v36, v36
	v_exp_f32_e32 v37, v37
	v_exp_f32_e32 v40, v40
	v_exp_f32_e32 v41, v41
	v_pk_add_f32 v[34:35], v[34:35], 1.0 op_sel_hi:[1,0]
	v_pk_add_f32 v[38:39], v[38:39], 1.0 op_sel_hi:[1,0]
	v_rcp_f32_e32 v34, v34
	v_rcp_f32_e32 v35, v35
	v_rcp_f32_e32 v38, v38
	v_rcp_f32_e32 v39, v39
	v_med3_f32 v20, v20, s75, v161
	v_med3_f32 v21, v21, s75, v161
	v_med3_f32 v16, v16, s75, v161
	v_med3_f32 v17, v17, s75, v161
	v_pk_add_f32 v[36:37], v[36:37], 1.0 op_sel_hi:[1,0]
	v_pk_add_f32 v[40:41], v[40:41], 1.0 op_sel_hi:[1,0]
	v_pk_fma_f32 v[20:21], v[20:21], 4.0, 4.0 op_sel_hi:[1,0,0]
	v_pk_fma_f32 v[16:17], v[16:17], 4.0, 4.0 op_sel_hi:[1,0,0]
	v_rcp_f32_e32 v36, v36
	v_rcp_f32_e32 v37, v37
	v_rcp_f32_e32 v40, v40
	v_rcp_f32_e32 v41, v41
	v_pk_mul_f32 v[28:29], v[28:29], v[34:35]
	v_pk_mul_f32 v[24:25], v[24:25], v[38:39]
	v_pk_mul_f32 v[20:21], v[20:21], v[28:29]
	v_pk_mul_f32 v[16:17], v[16:17], v[24:25]
	v_cvt_pk_fp8_f32 v32, v20, v21
	v_cvt_pk_fp8_f32 v33, v16, v17
	v_med3_f32 v22, v22, s75, v161
	v_med3_f32 v23, v23, s75, v161
	v_med3_f32 v18, v18, s75, v161
	v_med3_f32 v19, v19, s75, v161
	v_pk_fma_f32 v[22:23], v[22:23], 4.0, 4.0 op_sel_hi:[1,0,0]
	v_pk_fma_f32 v[18:19], v[18:19], 4.0, 4.0 op_sel_hi:[1,0,0]
	v_pk_mul_f32 v[30:31], v[30:31], v[36:37]
	v_pk_mul_f32 v[26:27], v[26:27], v[40:41]
	v_pk_mul_f32 v[16:17], v[22:23], v[30:31]
	v_pk_mul_f32 v[18:19], v[18:19], v[26:27]
	v_cvt_pk_fp8_f32 v32, v16, v17 op_sel:[0,0,1]
	v_cvt_pk_fp8_f32 v33, v18, v19 op_sel:[0,0,1]
	v_add_co_u32_e32 v16, vcc, s77, v146
	s_nop 1
	v_addc_co_u32_e32 v17, vcc, 0, v147, vcc
	global_store_dwordx2 v[16:17], v[32:33], off
	v_mov_b32_e32 v17, v246
	v_add_co_u32_e32 v16, vcc, 0x58000, v146
	v_mul_f32_e32 v18, 0x3c800000, v17
	v_pk_fma_f32 v[12:13], v[12:13], v[18:19], v[92:93] op_sel_hi:[1,0,1]
	v_pk_fma_f32 v[8:9], v[8:9], v[18:19], v[80:81] op_sel_hi:[1,0,1]
	v_min_f32_e32 v12, 0x40e00000, v12
	v_min_f32_e32 v13, 0x40e00000, v13
	v_min_f32_e32 v8, 0x40e00000, v8
	v_min_f32_e32 v9, 0x40e00000, v9
	v_pk_fma_f32 v[4:5], v[4:5], v[18:19], v[84:85] op_sel_hi:[1,0,1]
	v_pk_fma_f32 v[14:15], v[14:15], v[18:19], v[94:95] op_sel_hi:[1,0,1]
	v_pk_fma_f32 v[6:7], v[6:7], v[18:19], v[86:87] op_sel_hi:[1,0,1]
	v_pk_fma_f32 v[0:1], v[0:1], v[18:19], v[88:89] op_sel_hi:[1,0,1]
	v_pk_fma_f32 v[10:11], v[10:11], v[18:19], v[82:83] op_sel_hi:[1,0,1]
	v_pk_fma_f32 v[2:3], v[2:3], v[18:19], v[90:91] op_sel_hi:[1,0,1]
	v_pk_mul_f32 v[18:19], v[12:13], s[36:37] op_sel_hi:[1,0]
	v_pk_mul_f32 v[22:23], v[8:9], s[36:37] op_sel_hi:[1,0]
	v_exp_f32_e32 v18, v18
	v_exp_f32_e32 v19, v19
	v_exp_f32_e32 v22, v22
	v_exp_f32_e32 v23, v23
	v_min_f32_e32 v14, 0x40e00000, v14
	v_min_f32_e32 v15, 0x40e00000, v15
	v_min_f32_e32 v10, 0x40e00000, v10
	v_min_f32_e32 v11, 0x40e00000, v11
	v_pk_mul_f32 v[20:21], v[14:15], s[36:37] op_sel_hi:[1,0]
	v_pk_mul_f32 v[24:25], v[10:11], s[36:37] op_sel_hi:[1,0]
	v_exp_f32_e32 v20, v20
	v_exp_f32_e32 v21, v21
	v_exp_f32_e32 v24, v24
	v_exp_f32_e32 v25, v25
	v_pk_add_f32 v[18:19], v[18:19], 1.0 op_sel_hi:[1,0]
	v_pk_add_f32 v[22:23], v[22:23], 1.0 op_sel_hi:[1,0]
	v_rcp_f32_e32 v18, v18
	v_rcp_f32_e32 v19, v19
	v_rcp_f32_e32 v22, v22
	v_rcp_f32_e32 v23, v23
	v_med3_f32 v4, v4, s75, v161
	v_med3_f32 v5, v5, s75, v161
	v_med3_f32 v0, v0, s75, v161
	v_med3_f32 v1, v1, s75, v161
	v_pk_add_f32 v[20:21], v[20:21], 1.0 op_sel_hi:[1,0]
	v_pk_add_f32 v[24:25], v[24:25], 1.0 op_sel_hi:[1,0]
	v_pk_fma_f32 v[4:5], v[4:5], 4.0, 4.0 op_sel_hi:[1,0,0]
	v_pk_fma_f32 v[0:1], v[0:1], 4.0, 4.0 op_sel_hi:[1,0,0]
	v_rcp_f32_e32 v20, v20
	v_rcp_f32_e32 v21, v21
	v_rcp_f32_e32 v24, v24
	v_rcp_f32_e32 v25, v25
	v_pk_mul_f32 v[12:13], v[12:13], v[18:19]
	v_pk_mul_f32 v[8:9], v[8:9], v[22:23]
	v_pk_mul_f32 v[4:5], v[4:5], v[12:13]
	v_pk_mul_f32 v[0:1], v[0:1], v[8:9]
	v_cvt_pk_fp8_f32 v144, v4, v5
	v_cvt_pk_fp8_f32 v145, v0, v1
	v_med3_f32 v6, v6, s75, v161
	v_med3_f32 v7, v7, s75, v161
	v_med3_f32 v2, v2, s75, v161
	v_med3_f32 v3, v3, s75, v161
	v_pk_fma_f32 v[6:7], v[6:7], 4.0, 4.0 op_sel_hi:[1,0,0]
	v_pk_fma_f32 v[2:3], v[2:3], 4.0, 4.0 op_sel_hi:[1,0,0]
	v_pk_mul_f32 v[14:15], v[14:15], v[20:21]
	v_pk_mul_f32 v[10:11], v[10:11], v[24:25]
	v_pk_mul_f32 v[0:1], v[6:7], v[14:15]
	v_pk_mul_f32 v[2:3], v[2:3], v[10:11]
	v_cvt_pk_fp8_f32 v144, v0, v1 op_sel:[0,0,1]
	v_cvt_pk_fp8_f32 v145, v2, v3 op_sel:[0,0,1]
	v_addc_co_u32_e32 v17, vcc, 0, v147, vcc
	s_andn2_b64 vcc, exec, s[40:41]
	s_mov_b64 s[40:41], -1
	global_store_dwordx2 v[16:17], v[144:145], off
	s_cbranch_vccnz .LBB0_1055
	s_andn2_b64 vcc, exec, s[10:11]
	s_cbranch_vccnz .LBB0_1054
	s_barrier
	s_branch .LBB0_1054

; __device__ __forceinline__ unsigned cvt_pk4_fp8(float a, float b, float c, float d) { int w; asm("" : "=v"(w));     w = __builtin_amdgcn_cvt_pk_fp8_f32(a, b, w, false); w = __builtin_amdgcn_cvt_pk_fp8_f32(c, d, w, true); return (unsigned)w; }
;     __device__ __forceinline__ void operator()(const f32x4 (&acc)[2][2][4][2], const Unit& u, int wr, int wc, int fr, int fq) const {
;         const int row0 = u.pm * BM + wr * 64 + fr, col0 = u.pn * BM + wc * 32 + 8 * fq;
;         const float* b = bd + (size_t)u.e * DM + col0;
;         f32x4 bv[2][2];
; #pragma unroll
;         for (int bj = 0; bj < 2; ++bj)
; #pragma unroll
;             for (int n = 0; n < 2; ++n) bv[bj][n] = *(const f32x4*)(b + bj * HALF + 4 * n);
; #pragma unroll
;         for (int ai = 0; ai < 2; ++ai)
; #pragma unroll
;             for (int m = 0; m < 4; ++m) { const int r = row0 + ai * HALF + m * 16; const float rw = row_w[(size_t)u.e * XCAP + u.lr0 + (r - u.pm * BM)] * Y8_SCALE; unsigned char* rowp = O + (size_t)r * DM + col0;
; #pragma unroll
;                 for (int bj = 0; bj < 2; ++bj) { const f32x4 v0 = (acc[ai][bj][m][0] * (1.0f / (W8_SCALE * ACT8_SCALE)) + bv[bj][0]) * rw, v1 = (acc[ai][bj][m][1] * (1.0f / (W8_SCALE * ACT8_SCALE)) + bv[bj][1]) * rw;
;                     u32x2 w; w.x = cvt_pk4_fp8(v0[0], v0[1], v0[2], v0[3]); w.y = cvt_pk4_fp8(v1[0], v1[1], v1[2], v1[3]);
;                     *(u32x2*)(rowp + bj * HALF) = w; } }
;     }
.LBB0_1136:
	s_lshl_b32 s49, s58, 8
	v_readlane_b32 s51, v252, 28
	s_ashr_i32 s57, s56, 31
	s_lshl_b32 s45, s60, 8
	s_or_b32 s49, s49, s51
	s_lshl_b64 s[64:65], s[56:57], 13
	v_mbcnt_lo_u32_b32 v144, -1, 0
	v_mbcnt_hi_u32_b32 v144, -1, v144
	s_add_u32 s64, s10, s64
	v_ashrrev_i32_e32 v128, 1, v144
	v_and_b32_e32 v128, -8, v128
	s_addc_u32 s65, s11, s65
	s_ashr_i32 s63, s62, 31
	s_lshl_b64 s[56:57], s[56:57], 16
	v_add_u32_e32 v148, s49, v128
	s_add_u32 s49, s22, s56
	s_addc_u32 s51, s23, s57
	s_lshl_b64 s[56:57], s[62:63], 2
	v_ashrrev_i32_e32 v149, 31, v148
	v_and_or_b32 v144, v144, 15, s34
	s_add_u32 s56, s49, s56
	v_lshl_add_u64 v[136:137], v[148:149], 2, s[64:65]
	s_addc_u32 s57, s51, s57
	v_lshlrev_b32_e32 v145, 2, v144
	global_load_dword v240, v145, s[56:57] offset:64
	global_load_dword v241, v145, s[56:57] offset:128
	global_load_dword v242, v145, s[56:57] offset:192
	global_load_dword v243, v145, s[56:57] offset:512
	global_load_dword v244, v145, s[56:57] offset:576
	global_load_dword v245, v145, s[56:57] offset:640
	global_load_dword v246, v145, s[56:57] offset:704
	global_load_dwordx4 v[132:135], v[136:137], off offset:16
	global_load_dwordx4 v[140:143], v[136:137], off
	global_load_dwordx4 v[128:131], v[136:137], off offset:528
	s_nop 0
	global_load_dwordx4 v[136:139], v[136:137], off offset:512
	v_add_u32_e32 v150, s45, v144
	global_load_dword v161, v145, s[56:57]
	v_ashrrev_i32_e32 v151, 31, v150
	v_lshlrev_b64 v[146:147], 11, v[150:151]
	s_ashr_i32 s49, s45, 31
	v_lshl_add_u64 v[146:147], s[6:7], 0, v[146:147]
	v_mov_b32_e32 v166, s49
	v_lshl_add_u64 v[146:147], v[146:147], 0, v[148:149]
	s_waitcnt vmcnt(4)
	v_pk_fma_f32 v[120:121], v[120:121], s[36:37], v[132:133] op_sel_hi:[1,0,1]
	s_waitcnt vmcnt(3)
	v_pk_fma_f32 v[124:125], v[124:125], s[36:37], v[140:141] op_sel_hi:[1,0,1]
	s_waitcnt vmcnt(2)
	v_pk_fma_f32 v[112:113], v[112:113], s[36:37], v[128:129] op_sel_hi:[1,0,1]
	s_waitcnt vmcnt(1)
	v_pk_fma_f32 v[116:117], v[116:117], s[36:37], v[136:137] op_sel_hi:[1,0,1]
	v_pk_fma_f32 v[126:127], v[126:127], s[36:37], v[142:143] op_sel_hi:[1,0,1]
	s_waitcnt vmcnt(0)
	v_mul_f32_e32 v144, 0x41800000, v161
	v_pk_mul_f32 v[124:125], v[124:125], v[144:145] op_sel_hi:[1,0]
	v_pk_mul_f32 v[120:121], v[120:121], v[144:145] op_sel_hi:[1,0]
	v_pk_mul_f32 v[116:117], v[116:117], v[144:145] op_sel_hi:[1,0]
	v_pk_mul_f32 v[112:113], v[112:113], v[144:145] op_sel_hi:[1,0]
	v_cvt_pk_fp8_f32 v162, v124, v125
	v_cvt_pk_fp8_f32 v163, v120, v121
	v_cvt_pk_fp8_f32 v164, v116, v117
	v_cvt_pk_fp8_f32 v165, v112, v113
	v_pk_fma_f32 v[122:123], v[122:123], s[36:37], v[134:135] op_sel_hi:[1,0,1]
	v_pk_fma_f32 v[118:119], v[118:119], s[36:37], v[138:139] op_sel_hi:[1,0,1]
	v_pk_fma_f32 v[114:115], v[114:115], s[36:37], v[130:131] op_sel_hi:[1,0,1]
	v_pk_mul_f32 v[126:127], v[126:127], v[144:145] op_sel_hi:[1,0]
	v_pk_mul_f32 v[122:123], v[122:123], v[144:145] op_sel_hi:[1,0]
	v_pk_mul_f32 v[118:119], v[118:119], v[144:145] op_sel_hi:[1,0]
	v_pk_mul_f32 v[114:115], v[114:115], v[144:145] op_sel_hi:[1,0]
	v_cvt_pk_fp8_f32 v162, v126, v127 op_sel:[0,0,1]
	v_cvt_pk_fp8_f32 v163, v122, v123 op_sel:[0,0,1]
	v_cvt_pk_fp8_f32 v164, v118, v119 op_sel:[0,0,1]
	v_cvt_pk_fp8_f32 v165, v114, v115 op_sel:[0,0,1]
	v_subrev_co_u32_e32 v112, vcc, s45, v150
	global_store_dwordx2 v[146:147], v[162:163], off
	global_store_dwordx2 v[146:147], v[164:165], off offset:128
	v_subb_co_u32_e32 v113, vcc, v151, v166, vcc
	v_lshl_add_u64 v[112:113], v[112:113], 2, s[56:57]
	v_mov_b32_e32 v120, v240
	v_pk_fma_f32 v[108:109], v[108:109], s[36:37], v[140:141] op_sel_hi:[1,0,1]
	v_pk_fma_f32 v[104:105], v[104:105], s[36:37], v[132:133] op_sel_hi:[1,0,1]
	v_pk_fma_f32 v[100:101], v[100:101], s[36:37], v[136:137] op_sel_hi:[1,0,1]
	v_pk_fma_f32 v[96:97], v[96:97], s[36:37], v[128:129] op_sel_hi:[1,0,1]
	v_pk_fma_f32 v[110:111], v[110:111], s[36:37], v[142:143] op_sel_hi:[1,0,1]
	v_pk_fma_f32 v[106:107], v[106:107], s[36:37], v[134:135] op_sel_hi:[1,0,1]
	v_or_b32_e32 v118, 16, v150
	v_pk_fma_f32 v[102:103], v[102:103], s[36:37], v[138:139] op_sel_hi:[1,0,1]
	v_pk_fma_f32 v[98:99], v[98:99], s[36:37], v[130:131] op_sel_hi:[1,0,1]
	v_ashrrev_i32_e32 v119, 31, v118
	v_lshlrev_b64 v[118:119], 11, v[118:119]
	v_pk_fma_f32 v[92:93], v[92:93], s[36:37], v[140:141] op_sel_hi:[1,0,1]
	v_pk_fma_f32 v[88:89], v[88:89], s[36:37], v[132:133] op_sel_hi:[1,0,1]
	v_pk_fma_f32 v[84:85], v[84:85], s[36:37], v[136:137] op_sel_hi:[1,0,1]
	v_pk_fma_f32 v[80:81], v[80:81], s[36:37], v[128:129] op_sel_hi:[1,0,1]
	v_pk_fma_f32 v[94:95], v[94:95], s[36:37], v[142:143] op_sel_hi:[1,0,1]
	v_pk_fma_f32 v[90:91], v[90:91], s[36:37], v[134:135] op_sel_hi:[1,0,1]
	v_pk_fma_f32 v[86:87], v[86:87], s[36:37], v[138:139] op_sel_hi:[1,0,1]
	v_pk_fma_f32 v[82:83], v[82:83], s[36:37], v[130:131] op_sel_hi:[1,0,1]
	v_pk_fma_f32 v[76:77], v[76:77], s[36:37], v[140:141] op_sel_hi:[1,0,1]
	v_pk_fma_f32 v[72:73], v[72:73], s[36:37], v[132:133] op_sel_hi:[1,0,1]
	v_pk_fma_f32 v[68:69], v[68:69], s[36:37], v[136:137] op_sel_hi:[1,0,1]
	v_pk_fma_f32 v[64:65], v[64:65], s[36:37], v[128:129] op_sel_hi:[1,0,1]
	v_pk_fma_f32 v[78:79], v[78:79], s[36:37], v[142:143] op_sel_hi:[1,0,1]
	v_pk_fma_f32 v[74:75], v[74:75], s[36:37], v[134:135] op_sel_hi:[1,0,1]
	v_pk_fma_f32 v[70:71], v[70:71], s[36:37], v[138:139] op_sel_hi:[1,0,1]
	v_pk_fma_f32 v[66:67], v[66:67], s[36:37], v[130:131] op_sel_hi:[1,0,1]
	v_pk_fma_f32 v[60:61], v[60:61], s[36:37], v[140:141] op_sel_hi:[1,0,1]
	v_pk_fma_f32 v[56:57], v[56:57], s[36:37], v[132:133] op_sel_hi:[1,0,1]
	v_pk_fma_f32 v[52:53], v[52:53], s[36:37], v[136:137] op_sel_hi:[1,0,1]
; __device__ __forceinline__ unsigned cvt_pk4_fp8(float a, float b, float c, float d) { int w; asm("" : "=v"(w));     w = __builtin_amdgcn_cvt_pk_fp8_f32(a, b, w, false); w = __builtin_amdgcn_cvt_pk_fp8_f32(c, d, w, true); return (unsigned)w; }
;     __device__ __forceinline__ void operator()(const f32x4 (&acc)[2][2][4][2], const Unit& u, int wr, int wc, int fr, int fq) const {
;         const int row0 = u.pm * BM + wr * 64 + fr, col0 = u.pn * BM + wc * 32 + 8 * fq;
;         const float* b = bd + (size_t)u.e * DM + col0;
;         f32x4 bv[2][2];
; #pragma unroll
;         for (int bj = 0; bj < 2; ++bj)
; #pragma unroll
;             for (int n = 0; n < 2; ++n) bv[bj][n] = *(const f32x4*)(b + bj * HALF + 4 * n);
; #pragma unroll
;         for (int ai = 0; ai < 2; ++ai)
; #pragma unroll
;             for (int m = 0; m < 4; ++m) { const int r = row0 + ai * HALF + m * 16; const float rw = row_w[(size_t)u.e * XCAP + u.lr0 + (r - u.pm * BM)] * Y8_SCALE; unsigned char* rowp = O + (size_t)r * DM + col0;
; #pragma unroll
;                 for (int bj = 0; bj < 2; ++bj) { const f32x4 v0 = (acc[ai][bj][m][0] * (1.0f / (W8_SCALE * ACT8_SCALE)) + bv[bj][0]) * rw, v1 = (acc[ai][bj][m][1] * (1.0f / (W8_SCALE * ACT8_SCALE)) + bv[bj][1]) * rw;
;                     u32x2 w; w.x = cvt_pk4_fp8(v0[0], v0[1], v0[2], v0[3]); w.y = cvt_pk4_fp8(v1[0], v1[1], v1[2], v1[3]);
;                     *(u32x2*)(rowp + bj * HALF) = w; } }
;     }
	v_pk_fma_f32 v[48:49], v[48:49], s[36:37], v[128:129] op_sel_hi:[1,0,1]
	v_pk_fma_f32 v[62:63], v[62:63], s[36:37], v[142:143] op_sel_hi:[1,0,1]
	v_pk_fma_f32 v[58:59], v[58:59], s[36:37], v[134:135] op_sel_hi:[1,0,1]
	v_pk_fma_f32 v[54:55], v[54:55], s[36:37], v[138:139] op_sel_hi:[1,0,1]
	v_pk_fma_f32 v[50:51], v[50:51], s[36:37], v[130:131] op_sel_hi:[1,0,1]
	v_pk_fma_f32 v[44:45], v[44:45], s[36:37], v[140:141] op_sel_hi:[1,0,1]
	v_pk_fma_f32 v[40:41], v[40:41], s[36:37], v[132:133] op_sel_hi:[1,0,1]
	v_pk_fma_f32 v[36:37], v[36:37], s[36:37], v[136:137] op_sel_hi:[1,0,1]
	v_pk_fma_f32 v[32:33], v[32:33], s[36:37], v[128:129] op_sel_hi:[1,0,1]
	v_pk_fma_f32 v[46:47], v[46:47], s[36:37], v[142:143] op_sel_hi:[1,0,1]
	v_pk_fma_f32 v[42:43], v[42:43], s[36:37], v[134:135] op_sel_hi:[1,0,1]
	v_pk_fma_f32 v[38:39], v[38:39], s[36:37], v[138:139] op_sel_hi:[1,0,1]
	v_pk_fma_f32 v[34:35], v[34:35], s[36:37], v[130:131] op_sel_hi:[1,0,1]
	v_pk_fma_f32 v[28:29], v[28:29], s[36:37], v[140:141] op_sel_hi:[1,0,1]
	v_pk_fma_f32 v[24:25], v[24:25], s[36:37], v[132:133] op_sel_hi:[1,0,1]
	v_pk_fma_f32 v[20:21], v[20:21], s[36:37], v[136:137] op_sel_hi:[1,0,1]
	v_pk_fma_f32 v[16:17], v[16:17], s[36:37], v[128:129] op_sel_hi:[1,0,1]
	v_pk_fma_f32 v[30:31], v[30:31], s[36:37], v[142:143] op_sel_hi:[1,0,1]
	v_pk_fma_f32 v[26:27], v[26:27], s[36:37], v[134:135] op_sel_hi:[1,0,1]
	v_pk_fma_f32 v[22:23], v[22:23], s[36:37], v[138:139] op_sel_hi:[1,0,1]
	v_pk_fma_f32 v[18:19], v[18:19], s[36:37], v[130:131] op_sel_hi:[1,0,1]
	v_pk_fma_f32 v[12:13], v[12:13], s[36:37], v[140:141] op_sel_hi:[1,0,1]
	v_pk_fma_f32 v[8:9], v[8:9], s[36:37], v[132:133] op_sel_hi:[1,0,1]
	v_pk_fma_f32 v[4:5], v[4:5], s[36:37], v[136:137] op_sel_hi:[1,0,1]
	v_pk_fma_f32 v[0:1], v[0:1], s[36:37], v[128:129] op_sel_hi:[1,0,1]
	v_pk_fma_f32 v[14:15], v[14:15], s[36:37], v[142:143] op_sel_hi:[1,0,1]
	v_pk_fma_f32 v[10:11], v[10:11], s[36:37], v[134:135] op_sel_hi:[1,0,1]
	v_pk_fma_f32 v[6:7], v[6:7], s[36:37], v[138:139] op_sel_hi:[1,0,1]
	v_pk_fma_f32 v[2:3], v[2:3], s[36:37], v[130:131] op_sel_hi:[1,0,1]
	v_mul_f32_e32 v120, 0x41800000, v120
	v_pk_mul_f32 v[108:109], v[108:109], v[120:121] op_sel_hi:[1,0]
	v_pk_mul_f32 v[104:105], v[104:105], v[120:121] op_sel_hi:[1,0]
	v_pk_mul_f32 v[100:101], v[100:101], v[120:121] op_sel_hi:[1,0]
	v_pk_mul_f32 v[96:97], v[96:97], v[120:121] op_sel_hi:[1,0]
	v_cvt_pk_fp8_f32 v114, v108, v109
	v_cvt_pk_fp8_f32 v115, v104, v105
	v_cvt_pk_fp8_f32 v116, v100, v101
	v_cvt_pk_fp8_f32 v117, v96, v97
	v_pk_mul_f32 v[110:111], v[110:111], v[120:121] op_sel_hi:[1,0]
	v_pk_mul_f32 v[106:107], v[106:107], v[120:121] op_sel_hi:[1,0]
	v_pk_mul_f32 v[102:103], v[102:103], v[120:121] op_sel_hi:[1,0]
	v_pk_mul_f32 v[98:99], v[98:99], v[120:121] op_sel_hi:[1,0]
	v_cvt_pk_fp8_f32 v114, v110, v111 op_sel:[0,0,1]
	v_cvt_pk_fp8_f32 v115, v106, v107 op_sel:[0,0,1]
	v_cvt_pk_fp8_f32 v116, v102, v103 op_sel:[0,0,1]
	v_cvt_pk_fp8_f32 v117, v98, v99 op_sel:[0,0,1]
	v_lshl_add_u64 v[96:97], s[6:7], 0, v[118:119]
	v_lshl_add_u64 v[96:97], v[96:97], 0, v[148:149]
	global_store_dwordx2 v[96:97], v[114:115], off
	global_store_dwordx2 v[96:97], v[116:117], off offset:128
	v_mov_b32_e32 v102, v241
	v_or_b32_e32 v100, 32, v150
	v_ashrrev_i32_e32 v101, 31, v100
	v_lshlrev_b64 v[100:101], 11, v[100:101]
	v_mul_f32_e32 v102, 0x41800000, v102
	v_pk_mul_f32 v[92:93], v[92:93], v[102:103] op_sel_hi:[1,0]
	v_pk_mul_f32 v[88:89], v[88:89], v[102:103] op_sel_hi:[1,0]
	v_pk_mul_f32 v[84:85], v[84:85], v[102:103] op_sel_hi:[1,0]
	v_pk_mul_f32 v[80:81], v[80:81], v[102:103] op_sel_hi:[1,0]
	v_cvt_pk_fp8_f32 v96, v92, v93
	v_cvt_pk_fp8_f32 v97, v88, v89
	v_cvt_pk_fp8_f32 v98, v84, v85
	v_cvt_pk_fp8_f32 v99, v80, v81
	v_pk_mul_f32 v[94:95], v[94:95], v[102:103] op_sel_hi:[1,0]
	v_pk_mul_f32 v[90:91], v[90:91], v[102:103] op_sel_hi:[1,0]
	v_pk_mul_f32 v[86:87], v[86:87], v[102:103] op_sel_hi:[1,0]
	v_pk_mul_f32 v[82:83], v[82:83], v[102:103] op_sel_hi:[1,0]
	v_cvt_pk_fp8_f32 v96, v94, v95 op_sel:[0,0,1]
	v_cvt_pk_fp8_f32 v97, v90, v91 op_sel:[0,0,1]
	v_cvt_pk_fp8_f32 v98, v86, v87 op_sel:[0,0,1]
	v_cvt_pk_fp8_f32 v99, v82, v83 op_sel:[0,0,1]
	v_lshl_add_u64 v[80:81], s[6:7], 0, v[100:101]
	v_lshl_add_u64 v[80:81], v[80:81], 0, v[148:149]
	global_store_dwordx2 v[80:81], v[96:97], off
	global_store_dwordx2 v[80:81], v[98:99], off offset:128
	v_mov_b32_e32 v86, v242
	v_or_b32_e32 v84, 48, v150
	v_ashrrev_i32_e32 v85, 31, v84
	v_lshlrev_b64 v[84:85], 11, v[84:85]
	v_mul_f32_e32 v86, 0x41800000, v86
	v_pk_mul_f32 v[76:77], v[76:77], v[86:87] op_sel_hi:[1,0]
	v_pk_mul_f32 v[72:73], v[72:73], v[86:87] op_sel_hi:[1,0]
	v_pk_mul_f32 v[68:69], v[68:69], v[86:87] op_sel_hi:[1,0]
	v_pk_mul_f32 v[64:65], v[64:65], v[86:87] op_sel_hi:[1,0]
	v_cvt_pk_fp8_f32 v80, v76, v77
	v_cvt_pk_fp8_f32 v81, v72, v73
	v_cvt_pk_fp8_f32 v82, v68, v69
	v_cvt_pk_fp8_f32 v83, v64, v65
	v_pk_mul_f32 v[78:79], v[78:79], v[86:87] op_sel_hi:[1,0]
	v_pk_mul_f32 v[74:75], v[74:75], v[86:87] op_sel_hi:[1,0]
; __device__ __forceinline__ unsigned cvt_pk4_fp8(float a, float b, float c, float d) { int w; asm("" : "=v"(w));     w = __builtin_amdgcn_cvt_pk_fp8_f32(a, b, w, false); w = __builtin_amdgcn_cvt_pk_fp8_f32(c, d, w, true); return (unsigned)w; }
;     __device__ __forceinline__ void operator()(const f32x4 (&acc)[2][2][4][2], const Unit& u, int wr, int wc, int fr, int fq) const {
;         const int row0 = u.pm * BM + wr * 64 + fr, col0 = u.pn * BM + wc * 32 + 8 * fq;
;         const float* b = bd + (size_t)u.e * DM + col0;
;         f32x4 bv[2][2];
; #pragma unroll
;         for (int bj = 0; bj < 2; ++bj)
; #pragma unroll
;             for (int n = 0; n < 2; ++n) bv[bj][n] = *(const f32x4*)(b + bj * HALF + 4 * n);
; #pragma unroll
;         for (int ai = 0; ai < 2; ++ai)
; #pragma unroll
;             for (int m = 0; m < 4; ++m) { const int r = row0 + ai * HALF + m * 16; const float rw = row_w[(size_t)u.e * XCAP + u.lr0 + (r - u.pm * BM)] * Y8_SCALE; unsigned char* rowp = O + (size_t)r * DM + col0;
; #pragma unroll
;                 for (int bj = 0; bj < 2; ++bj) { const f32x4 v0 = (acc[ai][bj][m][0] * (1.0f / (W8_SCALE * ACT8_SCALE)) + bv[bj][0]) * rw, v1 = (acc[ai][bj][m][1] * (1.0f / (W8_SCALE * ACT8_SCALE)) + bv[bj][1]) * rw;
;                     u32x2 w; w.x = cvt_pk4_fp8(v0[0], v0[1], v0[2], v0[3]); w.y = cvt_pk4_fp8(v1[0], v1[1], v1[2], v1[3]);
;                     *(u32x2*)(rowp + bj * HALF) = w; } }
;     }
	v_pk_mul_f32 v[70:71], v[70:71], v[86:87] op_sel_hi:[1,0]
	v_pk_mul_f32 v[66:67], v[66:67], v[86:87] op_sel_hi:[1,0]
	v_cvt_pk_fp8_f32 v80, v78, v79 op_sel:[0,0,1]
	v_cvt_pk_fp8_f32 v81, v74, v75 op_sel:[0,0,1]
	v_cvt_pk_fp8_f32 v82, v70, v71 op_sel:[0,0,1]
	v_cvt_pk_fp8_f32 v83, v66, v67 op_sel:[0,0,1]
	v_lshl_add_u64 v[64:65], s[6:7], 0, v[84:85]
	v_lshl_add_u64 v[64:65], v[64:65], 0, v[148:149]
	global_store_dwordx2 v[64:65], v[80:81], off
	global_store_dwordx2 v[64:65], v[82:83], off offset:128
	v_mov_b32_e32 v70, v243
	v_lshl_add_u64 v[68:69], v[146:147], 0, s[12:13]
	v_mul_f32_e32 v70, 0x41800000, v70
	v_pk_mul_f32 v[60:61], v[60:61], v[70:71] op_sel_hi:[1,0]
	v_pk_mul_f32 v[56:57], v[56:57], v[70:71] op_sel_hi:[1,0]
	v_pk_mul_f32 v[52:53], v[52:53], v[70:71] op_sel_hi:[1,0]
	v_pk_mul_f32 v[48:49], v[48:49], v[70:71] op_sel_hi:[1,0]
	v_cvt_pk_fp8_f32 v64, v60, v61
	v_cvt_pk_fp8_f32 v65, v56, v57
	v_cvt_pk_fp8_f32 v66, v52, v53
	v_cvt_pk_fp8_f32 v67, v48, v49
	v_pk_mul_f32 v[62:63], v[62:63], v[70:71] op_sel_hi:[1,0]
	v_pk_mul_f32 v[58:59], v[58:59], v[70:71] op_sel_hi:[1,0]
	v_pk_mul_f32 v[54:55], v[54:55], v[70:71] op_sel_hi:[1,0]
	v_pk_mul_f32 v[50:51], v[50:51], v[70:71] op_sel_hi:[1,0]
	v_cvt_pk_fp8_f32 v64, v62, v63 op_sel:[0,0,1]
	v_cvt_pk_fp8_f32 v65, v58, v59 op_sel:[0,0,1]
	v_cvt_pk_fp8_f32 v66, v54, v55 op_sel:[0,0,1]
	v_cvt_pk_fp8_f32 v67, v50, v51 op_sel:[0,0,1]
	v_add_co_u32_e32 v48, vcc, s83, v146
	s_nop 0
	v_addc_co_u32_e32 v49, vcc, 0, v147, vcc
	global_store_dwordx2 v[48:49], v[64:65], off
	global_store_dwordx2 v[68:69], v[66:67], off offset:128
	v_mov_b32_e32 v54, v244
	v_lshl_add_u64 v[52:53], v[146:147], 0, s[38:39]
	v_mul_f32_e32 v54, 0x41800000, v54
	v_pk_mul_f32 v[44:45], v[44:45], v[54:55] op_sel_hi:[1,0]
	v_pk_mul_f32 v[40:41], v[40:41], v[54:55] op_sel_hi:[1,0]
	v_pk_mul_f32 v[36:37], v[36:37], v[54:55] op_sel_hi:[1,0]
	v_pk_mul_f32 v[32:33], v[32:33], v[54:55] op_sel_hi:[1,0]
	v_cvt_pk_fp8_f32 v48, v44, v45
	v_cvt_pk_fp8_f32 v49, v40, v41
	v_cvt_pk_fp8_f32 v50, v36, v37
	v_cvt_pk_fp8_f32 v51, v32, v33
	v_pk_mul_f32 v[46:47], v[46:47], v[54:55] op_sel_hi:[1,0]
	v_pk_mul_f32 v[42:43], v[42:43], v[54:55] op_sel_hi:[1,0]
	v_pk_mul_f32 v[38:39], v[38:39], v[54:55] op_sel_hi:[1,0]
	v_pk_mul_f32 v[34:35], v[34:35], v[54:55] op_sel_hi:[1,0]
	v_cvt_pk_fp8_f32 v48, v46, v47 op_sel:[0,0,1]
	v_cvt_pk_fp8_f32 v49, v42, v43 op_sel:[0,0,1]
	v_cvt_pk_fp8_f32 v50, v38, v39 op_sel:[0,0,1]
	v_cvt_pk_fp8_f32 v51, v34, v35 op_sel:[0,0,1]
	v_add_co_u32_e32 v32, vcc, s84, v146
	s_nop 0
	v_addc_co_u32_e32 v33, vcc, 0, v147, vcc
	global_store_dwordx2 v[32:33], v[48:49], off
	global_store_dwordx2 v[52:53], v[50:51], off offset:128
	v_mov_b32_e32 v38, v245
	v_lshl_add_u64 v[36:37], v[146:147], 0, s[40:41]
	v_mul_f32_e32 v38, 0x41800000, v38
	v_pk_mul_f32 v[28:29], v[28:29], v[38:39] op_sel_hi:[1,0]
	v_pk_mul_f32 v[24:25], v[24:25], v[38:39] op_sel_hi:[1,0]
	v_pk_mul_f32 v[20:21], v[20:21], v[38:39] op_sel_hi:[1,0]
	v_pk_mul_f32 v[16:17], v[16:17], v[38:39] op_sel_hi:[1,0]
	v_cvt_pk_fp8_f32 v32, v28, v29
	v_cvt_pk_fp8_f32 v33, v24, v25
	v_cvt_pk_fp8_f32 v34, v20, v21
	v_cvt_pk_fp8_f32 v35, v16, v17
	v_pk_mul_f32 v[30:31], v[30:31], v[38:39] op_sel_hi:[1,0]
	v_pk_mul_f32 v[26:27], v[26:27], v[38:39] op_sel_hi:[1,0]
	v_pk_mul_f32 v[22:23], v[22:23], v[38:39] op_sel_hi:[1,0]
	v_pk_mul_f32 v[18:19], v[18:19], v[38:39] op_sel_hi:[1,0]
	v_cvt_pk_fp8_f32 v32, v30, v31 op_sel:[0,0,1]
	v_cvt_pk_fp8_f32 v33, v26, v27 op_sel:[0,0,1]
	v_cvt_pk_fp8_f32 v34, v22, v23 op_sel:[0,0,1]
	v_cvt_pk_fp8_f32 v35, v18, v19 op_sel:[0,0,1]
	v_add_co_u32_e32 v16, vcc, s85, v146
	v_lshl_add_u64 v[18:19], v[146:147], 0, s[42:43]
	s_nop 0
	v_addc_co_u32_e32 v17, vcc, 0, v147, vcc
	global_store_dwordx2 v[16:17], v[32:33], off
	global_store_dwordx2 v[36:37], v[34:35], off offset:128
	v_mov_b32_e32 v20, v246
	v_mul_f32_e32 v20, 0x41800000, v20
	v_pk_mul_f32 v[12:13], v[12:13], v[20:21] op_sel_hi:[1,0]
	v_pk_mul_f32 v[8:9], v[8:9], v[20:21] op_sel_hi:[1,0]
	v_pk_mul_f32 v[4:5], v[4:5], v[20:21] op_sel_hi:[1,0]
	v_pk_mul_f32 v[0:1], v[0:1], v[20:21] op_sel_hi:[1,0]
	v_cvt_pk_fp8_f32 v16, v12, v13
	v_cvt_pk_fp8_f32 v17, v8, v9
	v_cvt_pk_fp8_f32 v144, v4, v5
	v_cvt_pk_fp8_f32 v145, v0, v1
	v_pk_mul_f32 v[14:15], v[14:15], v[20:21] op_sel_hi:[1,0]
	v_pk_mul_f32 v[10:11], v[10:11], v[20:21] op_sel_hi:[1,0]
	v_pk_mul_f32 v[6:7], v[6:7], v[20:21] op_sel_hi:[1,0]
	v_pk_mul_f32 v[2:3], v[2:3], v[20:21] op_sel_hi:[1,0]
	v_cvt_pk_fp8_f32 v16, v14, v15 op_sel:[0,0,1]
	v_cvt_pk_fp8_f32 v17, v10, v11 op_sel:[0,0,1]
	v_cvt_pk_fp8_f32 v144, v6, v7 op_sel:[0,0,1]
	v_cvt_pk_fp8_f32 v145, v2, v3 op_sel:[0,0,1]
	v_add_co_u32_e32 v0, vcc, s86, v146
	s_nop 1
	v_addc_co_u32_e32 v1, vcc, 0, v147, vcc
	s_andn2_b64 vcc, exec, s[46:47]
	s_mov_b64 s[46:47], -1
	global_store_dwordx2 v[0:1], v[16:17], off
	global_store_dwordx2 v[18:19], v[144:145], off offset:128
	s_cbranch_vccnz .LBB0_1129
	s_andn2_b64 vcc, exec, s[24:25]
	s_cbranch_vccnz .LBB0_1128
	s_barrier
	s_branch .LBB0_1128
